# PEER gather: two tokens per sweep in one merged ascending-id order (256-key bitonic sort, per-row token dispatch); same f32 math
# speedup vs baseline: 1.0674x; 1.0110x over previous
; #define LAS __attribute__((address_space(3)))
; #define P11_CX(J, ASC0, ASC1) do { const unsigned o0_ = (unsigned)__shfl_xor((int)k0, (J)), o1_ = (unsigned)__shfl_xor((int)k1, (J)); const bool lowl_ = (lane & (J)) == 0; \
;         k0 = (lowl_ == (ASC0)) ? (k0 < o0_ ? k0 : o0_) : (k0 > o0_ ? k0 : o0_); k1 = (lowl_ == (ASC1)) ? (k1 < o1_ ? k1 : o1_) : (k1 > o1_ ? k1 : o1_); } while (0)
; DI void peer_token(LAS unsigned char* ring, const bf16* x1row, float inv2, const float* nffn, const int* ex, const float* pg, const unsigned char* U6, const unsigned char* V6,
;                    const float* usc, const float* vsc, float* orow, int lane) {
;     unsigned k0 = ((unsigned)__hip_atomic_load(ex + lane, __ATOMIC_RELAXED, __HIP_MEMORY_SCOPE_AGENT) << 7) | (unsigned)lane;
;     unsigned k1 = ((unsigned)__hip_atomic_load(ex + 64 + lane, __ATOMIC_RELAXED, __HIP_MEMORY_SCOPE_AGENT) << 7) | (unsigned)(64 + lane);
;     ...
; #pragma unroll
;     for (int kk = 2; kk <= 32; kk <<= 1) { const bool asc = (lane & kk) == 0;
; #pragma unroll
;         for (int j = kk >> 1; j >= 1; j >>= 1) P11_CX(j, asc, asc); }
; __global__ void __launch_bounds__(NTHREADS, 2) fwd(Args args) {
;     ...
;             for (int j = 0; j < 4; ++j) { const int t = tb * 32 + wave * 4 + j;
;                 peer_token(lds + wave * (4 * RSLOT), XB + (size_t)t * DM, inv2[t], norm_ffn, experts + (size_t)t * 128, pgates + (size_t)t * 128, U8, V8, usc, vsc, out + (size_t)t * DM, lane); }
.LBB0_900:
	v_and_b32_e32 v2, 64, v118
	v_add_u32_e32 v2, 64, v2
	v_xor_b32_e32 v3, 1, v118
	v_cmp_lt_i32_e32 vcc, v3, v2
	s_waitcnt vmcnt(0)
	v_readlane_b32 s44, v249, 17
	s_add_i32 s97, s97, s44
	v_cndmask_b32_e32 v3, v118, v3, vcc
	v_lshlrev_b32_e32 v106, 2, v3
	v_xor_b32_e32 v3, 2, v118
	v_cmp_lt_i32_e32 vcc, v3, v2
	s_mov_b32 s76, 0
	s_nop 0
	v_cndmask_b32_e32 v3, v118, v3, vcc
	v_lshlrev_b32_e32 v107, 2, v3
	v_xor_b32_e32 v3, 4, v118
	v_cmp_lt_i32_e32 vcc, v3, v2
	s_barrier
	s_nop 0
	v_cndmask_b32_e32 v3, v118, v3, vcc
	v_lshlrev_b32_e32 v108, 2, v3
	v_xor_b32_e32 v3, 8, v118
	v_cmp_lt_i32_e32 vcc, v3, v2
	s_nop 1
	v_cndmask_b32_e32 v3, v118, v3, vcc
	v_lshlrev_b32_e32 v109, 2, v3
	v_xor_b32_e32 v3, 16, v118
	v_cmp_lt_i32_e32 vcc, v3, v2
	s_nop 1
	v_cndmask_b32_e32 v3, v118, v3, vcc
	v_lshlrev_b32_e32 v110, 2, v3
	v_xor_b32_e32 v3, 32, v118
	v_cmp_lt_i32_e32 vcc, v3, v2
	s_nop 1
	v_cndmask_b32_e32 v2, v118, v3, vcc
	v_lshlrev_b32_e32 v111, 2, v2
	v_readfirstlane_b32 s98, v72
	v_readfirstlane_b32 s47, v74
	s_sub_u32 s98, s47, s98
	v_readfirstlane_b32 s99, v73
	v_readfirstlane_b32 s47, v75
	s_subb_u32 s99, s47, s99
.LBB0_901:
	s_lshl_b32 s46, s76, 1
	s_add_i32 s46, s46, s97
	s_ashr_i32 s47, s46, 31
	s_lshl_b64 s[44:45], s[46:47], 12
	s_lshl_b64 s[74:75], s[46:47], 2
	s_add_u32 s74, s64, s74
	s_addc_u32 s75, s65, s75
	s_lshl_b64 s[78:79], s[46:47], 9
	v_lshl_add_u64 v[2:3], v[78:79], 0, s[78:79]
	s_lshl_b64 s[46:47], s[46:47], 13
	v_lshl_add_u64 v[16:17], v[68:69], 0, s[46:47]
	s_mov_b64 s[46:47], 0x1000
	v_lshl_add_u64 v[18:19], v[16:17], 0, s[46:47]
	s_mov_b64 s[46:47], 0x2000
	v_lshl_add_u64 v[144:145], v[16:17], 0, s[46:47]
	s_mov_b64 s[46:47], 0x3000
	v_lshl_add_u64 v[6:7], v[16:17], 0, s[46:47]
	global_load_dwordx2 v[96:97], v67, s[74:75]
	global_load_dword v112, v[2:3], off sc1
	global_load_dword v113, v[2:3], off offset:256 sc1
	global_load_dword v242, v[2:3], off offset:512 sc1
	global_load_dword v243, v[2:3], off offset:768 sc1
	global_load_dwordx2 v[146:147], v[16:17], off
	global_load_dwordx2 v[148:149], v[16:17], off offset:512
	global_load_dwordx2 v[150:151], v[16:17], off offset:1024
	global_load_dwordx2 v[152:153], v[16:17], off offset:1536
	global_load_dwordx2 v[154:155], v[16:17], off offset:2048
	global_load_dwordx2 v[156:157], v[16:17], off offset:2560
	global_load_dwordx2 v[158:159], v[16:17], off offset:3072
	global_load_dwordx2 v[160:161], v[16:17], off offset:3584
	global_load_dwordx2 v[162:163], v[18:19], off
	global_load_dwordx2 v[164:165], v[18:19], off offset:512
	global_load_dwordx2 v[166:167], v[18:19], off offset:1024
	global_load_dwordx2 v[168:169], v[18:19], off offset:1536
	global_load_dwordx2 v[170:171], v[18:19], off offset:2048
	global_load_dwordx2 v[172:173], v[18:19], off offset:2560
	global_load_dwordx2 v[174:175], v[18:19], off offset:3072
	global_load_dwordx2 v[176:177], v[18:19], off offset:3584
	global_load_dwordx2 v[178:179], v[144:145], off
	global_load_dwordx2 v[180:181], v[144:145], off offset:512
	global_load_dwordx2 v[182:183], v[144:145], off offset:1024
	global_load_dwordx2 v[184:185], v[144:145], off offset:1536
	global_load_dwordx2 v[186:187], v[144:145], off offset:2048
	global_load_dwordx2 v[188:189], v[144:145], off offset:2560
	global_load_dwordx2 v[190:191], v[144:145], off offset:3072
	global_load_dwordx2 v[192:193], v[144:145], off offset:3584
	global_load_dwordx2 v[194:195], v[6:7], off
	global_load_dwordx2 v[196:197], v[6:7], off offset:512
	global_load_dwordx2 v[198:199], v[6:7], off offset:1024
	global_load_dwordx2 v[200:201], v[6:7], off offset:1536
	global_load_dwordx2 v[202:203], v[6:7], off offset:2048
	global_load_dwordx2 v[204:205], v[6:7], off offset:2560
	global_load_dwordx2 v[206:207], v[6:7], off offset:3072
	global_load_dwordx2 v[208:209], v[6:7], off offset:3584
	global_load_dwordx4 v[98:101], v66, s[60:61]
	global_load_dwordx4 v[102:105], v66, s[60:61] offset:1024
	global_load_dwordx4 v[126:129], v66, s[60:61] offset:2048
	global_load_dwordx4 v[130:133], v66, s[60:61] offset:3072
	s_add_u32 s46, s60, 0x1000
	s_addc_u32 s47, s61, 0
	global_load_dwordx4 v[136:139], v66, s[46:47]
	global_load_dwordx4 v[140:143], v66, s[46:47] offset:1024
	global_load_dwordx4 v[8:11], v66, s[46:47] offset:2048
	global_load_dwordx4 v[12:15], v66, s[46:47] offset:3072
	s_add_u32 s46, s60, 0x2000
	s_addc_u32 s47, s61, 0
	global_load_dwordx4 v[210:213], v66, s[46:47]
	global_load_dwordx4 v[214:217], v66, s[46:47] offset:1024
	global_load_dwordx4 v[218:221], v66, s[46:47] offset:2048
	global_load_dwordx4 v[222:225], v66, s[46:47] offset:3072
	s_add_u32 s46, s60, 0x3000
	s_addc_u32 s47, s61, 0
	global_load_dwordx4 v[226:229], v66, s[46:47]
	global_load_dwordx4 v[230:233], v66, s[46:47] offset:1024
	global_load_dwordx4 v[234:237], v66, s[46:47] offset:2048
	global_load_dwordx4 v[238:241], v66, s[46:47] offset:3072
	s_mov_b32 m0, s33
	s_waitcnt vmcnt(48)
	v_lshl_or_b32 v112, v112, 8, v1
	v_lshl_or_b32 v113, v113, 8, v114
	v_or_b32_e32 v6, 0x80, v1
	v_lshl_or_b32 v242, v242, 8, v6
	v_or_b32_e32 v6, 0xc0, v1
	v_lshl_or_b32 v243, v243, 8, v6
	ds_bpermute_b32 v2, v106, v112
	ds_bpermute_b32 v3, v106, v113
	ds_bpermute_b32 v4, v106, v242
	ds_bpermute_b32 v5, v106, v243
	v_and_b32_e32 v6, 3, v118
	v_cmp_eq_u32_e64 s[78:79], 0, v6
	v_cmp_eq_u32_e32 vcc, 3, v6
	s_or_b64 s[74:75], s[78:79], vcc
	s_waitcnt lgkmcnt(3)
	v_min_u32_e32 v6, v112, v2
	v_max_u32_e32 v112, v112, v2
	v_cndmask_b32_e64 v112, v112, v6, s[74:75]
	s_waitcnt lgkmcnt(2)
	v_min_u32_e32 v6, v113, v3
	v_max_u32_e32 v113, v113, v3
	v_cndmask_b32_e64 v113, v113, v6, s[74:75]
	s_waitcnt lgkmcnt(1)
; #define P11_CX(J, ASC0, ASC1) do { const unsigned o0_ = (unsigned)__shfl_xor((int)k0, (J)), o1_ = (unsigned)__shfl_xor((int)k1, (J)); const bool lowl_ = (lane & (J)) == 0; \
;         k0 = (lowl_ == (ASC0)) ? (k0 < o0_ ? k0 : o0_) : (k0 > o0_ ? k0 : o0_); k1 = (lowl_ == (ASC1)) ? (k1 < o1_ ? k1 : o1_) : (k1 > o1_ ? k1 : o1_); } while (0)
; DI void peer_token(LAS unsigned char* ring, const bf16* x1row, float inv2, const float* nffn, const int* ex, const float* pg, const unsigned char* U6, const unsigned char* V6,
;                    const float* usc, const float* vsc, float* orow, int lane) {
;     ...
; #pragma unroll
;     for (int kk = 2; kk <= 32; kk <<= 1) { const bool asc = (lane & kk) == 0;
; #pragma unroll
;         for (int j = kk >> 1; j >= 1; j >>= 1) P11_CX(j, asc, asc); }
; #pragma unroll
;     for (int j = 32; j >= 1; j >>= 1) P11_CX(j, true, false);
;     { const unsigned lo_ = k0 < k1 ? k0 : k1, hi_ = k0 < k1 ? k1 : k0; k0 = lo_; k1 = hi_; }
; #pragma unroll
;     for (int j = 32; j >= 1; j >>= 1) P11_CX(j, true, true);
	v_min_u32_e32 v6, v242, v4
	v_max_u32_e32 v242, v242, v4
	v_cndmask_b32_e64 v242, v242, v6, s[74:75]
	s_waitcnt lgkmcnt(0)
	v_min_u32_e32 v6, v243, v5
	v_max_u32_e32 v243, v243, v5
	v_cndmask_b32_e64 v243, v243, v6, s[74:75]
	ds_bpermute_b32 v2, v107, v112
	ds_bpermute_b32 v3, v107, v113
	ds_bpermute_b32 v4, v107, v242
	ds_bpermute_b32 v5, v107, v243
	v_and_b32_e32 v6, 6, v118
	v_cmp_eq_u32_e64 s[78:79], 0, v6
	v_cmp_eq_u32_e32 vcc, 6, v6
	s_or_b64 s[74:75], s[78:79], vcc
	s_waitcnt lgkmcnt(3)
	v_min_u32_e32 v6, v112, v2
	v_max_u32_e32 v112, v112, v2
	v_cndmask_b32_e64 v112, v112, v6, s[74:75]
	s_waitcnt lgkmcnt(2)
	v_min_u32_e32 v6, v113, v3
	v_max_u32_e32 v113, v113, v3
	v_cndmask_b32_e64 v113, v113, v6, s[74:75]
	s_waitcnt lgkmcnt(1)
	v_min_u32_e32 v6, v242, v4
	v_max_u32_e32 v242, v242, v4
	v_cndmask_b32_e64 v242, v242, v6, s[74:75]
	s_waitcnt lgkmcnt(0)
	v_min_u32_e32 v6, v243, v5
	v_max_u32_e32 v243, v243, v5
	v_cndmask_b32_e64 v243, v243, v6, s[74:75]
	ds_bpermute_b32 v2, v106, v112
	ds_bpermute_b32 v3, v106, v113
	ds_bpermute_b32 v4, v106, v242
	ds_bpermute_b32 v5, v106, v243
	v_and_b32_e32 v6, 5, v118
	v_cmp_eq_u32_e64 s[78:79], 0, v6
	v_cmp_eq_u32_e32 vcc, 5, v6
	s_or_b64 s[74:75], s[78:79], vcc
	s_waitcnt lgkmcnt(3)
	v_min_u32_e32 v6, v112, v2
	v_max_u32_e32 v112, v112, v2
	v_cndmask_b32_e64 v112, v112, v6, s[74:75]
	s_waitcnt lgkmcnt(2)
	v_min_u32_e32 v6, v113, v3
	v_max_u32_e32 v113, v113, v3
	v_cndmask_b32_e64 v113, v113, v6, s[74:75]
	s_waitcnt lgkmcnt(1)
	v_min_u32_e32 v6, v242, v4
	v_max_u32_e32 v242, v242, v4
	v_cndmask_b32_e64 v242, v242, v6, s[74:75]
	s_waitcnt lgkmcnt(0)
	v_min_u32_e32 v6, v243, v5
	v_max_u32_e32 v243, v243, v5
	v_cndmask_b32_e64 v243, v243, v6, s[74:75]
	ds_bpermute_b32 v2, v108, v112
	ds_bpermute_b32 v3, v108, v113
	ds_bpermute_b32 v4, v108, v242
	ds_bpermute_b32 v5, v108, v243
	v_and_b32_e32 v6, 12, v118
	v_cmp_eq_u32_e64 s[78:79], 0, v6
	v_cmp_eq_u32_e32 vcc, 12, v6
	s_or_b64 s[74:75], s[78:79], vcc
	s_waitcnt lgkmcnt(3)
	v_min_u32_e32 v6, v112, v2
	v_max_u32_e32 v112, v112, v2
	v_cndmask_b32_e64 v112, v112, v6, s[74:75]
	s_waitcnt lgkmcnt(2)
	v_min_u32_e32 v6, v113, v3
	v_max_u32_e32 v113, v113, v3
	v_cndmask_b32_e64 v113, v113, v6, s[74:75]
	s_waitcnt lgkmcnt(1)
	v_min_u32_e32 v6, v242, v4
	v_max_u32_e32 v242, v242, v4
	v_cndmask_b32_e64 v242, v242, v6, s[74:75]
	s_waitcnt lgkmcnt(0)
	v_min_u32_e32 v6, v243, v5
	v_max_u32_e32 v243, v243, v5
	v_cndmask_b32_e64 v243, v243, v6, s[74:75]
	ds_bpermute_b32 v2, v107, v112
	ds_bpermute_b32 v3, v107, v113
	ds_bpermute_b32 v4, v107, v242
	ds_bpermute_b32 v5, v107, v243
	v_and_b32_e32 v6, 10, v118
	v_cmp_eq_u32_e64 s[78:79], 0, v6
	v_cmp_eq_u32_e32 vcc, 10, v6
	s_or_b64 s[74:75], s[78:79], vcc
	s_waitcnt lgkmcnt(3)
	v_min_u32_e32 v6, v112, v2
	v_max_u32_e32 v112, v112, v2
	v_cndmask_b32_e64 v112, v112, v6, s[74:75]
	s_waitcnt lgkmcnt(2)
	v_min_u32_e32 v6, v113, v3
	v_max_u32_e32 v113, v113, v3
	v_cndmask_b32_e64 v113, v113, v6, s[74:75]
	s_waitcnt lgkmcnt(1)
	v_min_u32_e32 v6, v242, v4
	v_max_u32_e32 v242, v242, v4
	v_cndmask_b32_e64 v242, v242, v6, s[74:75]
	s_waitcnt lgkmcnt(0)
	v_min_u32_e32 v6, v243, v5
	v_max_u32_e32 v243, v243, v5
	v_cndmask_b32_e64 v243, v243, v6, s[74:75]
	ds_bpermute_b32 v2, v106, v112
	ds_bpermute_b32 v3, v106, v113
	ds_bpermute_b32 v4, v106, v242
	ds_bpermute_b32 v5, v106, v243
	v_and_b32_e32 v6, 9, v118
	v_cmp_eq_u32_e64 s[78:79], 0, v6
	v_cmp_eq_u32_e32 vcc, 9, v6
	s_or_b64 s[74:75], s[78:79], vcc
	s_waitcnt lgkmcnt(3)
	v_min_u32_e32 v6, v112, v2
	v_max_u32_e32 v112, v112, v2
	v_cndmask_b32_e64 v112, v112, v6, s[74:75]
	s_waitcnt lgkmcnt(2)
	v_min_u32_e32 v6, v113, v3
	v_max_u32_e32 v113, v113, v3
	v_cndmask_b32_e64 v113, v113, v6, s[74:75]
	s_waitcnt lgkmcnt(1)
	v_min_u32_e32 v6, v242, v4
	v_max_u32_e32 v242, v242, v4
	v_cndmask_b32_e64 v242, v242, v6, s[74:75]
	s_waitcnt lgkmcnt(0)
	v_min_u32_e32 v6, v243, v5
	v_max_u32_e32 v243, v243, v5
	v_cndmask_b32_e64 v243, v243, v6, s[74:75]
	ds_bpermute_b32 v2, v109, v112
	ds_bpermute_b32 v3, v109, v113
	ds_bpermute_b32 v4, v109, v242
	ds_bpermute_b32 v5, v109, v243
	v_and_b32_e32 v6, 24, v118
	v_cmp_eq_u32_e64 s[78:79], 0, v6
	v_cmp_eq_u32_e32 vcc, 24, v6
	s_or_b64 s[74:75], s[78:79], vcc
	s_waitcnt lgkmcnt(3)
	v_min_u32_e32 v6, v112, v2
	v_max_u32_e32 v112, v112, v2
	v_cndmask_b32_e64 v112, v112, v6, s[74:75]
	s_waitcnt lgkmcnt(2)
	v_min_u32_e32 v6, v113, v3
	v_max_u32_e32 v113, v113, v3
	v_cndmask_b32_e64 v113, v113, v6, s[74:75]
	s_waitcnt lgkmcnt(1)
	v_min_u32_e32 v6, v242, v4
	v_max_u32_e32 v242, v242, v4
	v_cndmask_b32_e64 v242, v242, v6, s[74:75]
	s_waitcnt lgkmcnt(0)
	v_min_u32_e32 v6, v243, v5
	v_max_u32_e32 v243, v243, v5
	v_cndmask_b32_e64 v243, v243, v6, s[74:75]
	ds_bpermute_b32 v2, v108, v112
	ds_bpermute_b32 v3, v108, v113
	ds_bpermute_b32 v4, v108, v242
	ds_bpermute_b32 v5, v108, v243
	v_and_b32_e32 v6, 20, v118
	v_cmp_eq_u32_e64 s[78:79], 0, v6
	v_cmp_eq_u32_e32 vcc, 20, v6
	s_or_b64 s[74:75], s[78:79], vcc
	s_waitcnt lgkmcnt(3)
	v_min_u32_e32 v6, v112, v2
	v_max_u32_e32 v112, v112, v2
	v_cndmask_b32_e64 v112, v112, v6, s[74:75]
	s_waitcnt lgkmcnt(2)
	v_min_u32_e32 v6, v113, v3
	v_max_u32_e32 v113, v113, v3
	v_cndmask_b32_e64 v113, v113, v6, s[74:75]
	s_waitcnt lgkmcnt(1)
	v_min_u32_e32 v6, v242, v4
	v_max_u32_e32 v242, v242, v4
	v_cndmask_b32_e64 v242, v242, v6, s[74:75]
	s_waitcnt lgkmcnt(0)
	v_min_u32_e32 v6, v243, v5
	v_max_u32_e32 v243, v243, v5
	v_cndmask_b32_e64 v243, v243, v6, s[74:75]
	ds_bpermute_b32 v2, v107, v112
	ds_bpermute_b32 v3, v107, v113
	ds_bpermute_b32 v4, v107, v242
	ds_bpermute_b32 v5, v107, v243
	v_and_b32_e32 v6, 18, v118
	v_cmp_eq_u32_e64 s[78:79], 0, v6
	v_cmp_eq_u32_e32 vcc, 18, v6
	s_or_b64 s[74:75], s[78:79], vcc
	s_waitcnt lgkmcnt(3)
; #define P11_CX(J, ASC0, ASC1) do { const unsigned o0_ = (unsigned)__shfl_xor((int)k0, (J)), o1_ = (unsigned)__shfl_xor((int)k1, (J)); const bool lowl_ = (lane & (J)) == 0; \
;         k0 = (lowl_ == (ASC0)) ? (k0 < o0_ ? k0 : o0_) : (k0 > o0_ ? k0 : o0_); k1 = (lowl_ == (ASC1)) ? (k1 < o1_ ? k1 : o1_) : (k1 > o1_ ? k1 : o1_); } while (0)
; DI void peer_token(LAS unsigned char* ring, const bf16* x1row, float inv2, const float* nffn, const int* ex, const float* pg, const unsigned char* U6, const unsigned char* V6,
;                    const float* usc, const float* vsc, float* orow, int lane) {
;     ...
; #pragma unroll
;     for (int kk = 2; kk <= 32; kk <<= 1) { const bool asc = (lane & kk) == 0;
; #pragma unroll
;         for (int j = kk >> 1; j >= 1; j >>= 1) P11_CX(j, asc, asc); }
; #pragma unroll
;     for (int j = 32; j >= 1; j >>= 1) P11_CX(j, true, false);
;     { const unsigned lo_ = k0 < k1 ? k0 : k1, hi_ = k0 < k1 ? k1 : k0; k0 = lo_; k1 = hi_; }
; #pragma unroll
;     for (int j = 32; j >= 1; j >>= 1) P11_CX(j, true, true);
	v_min_u32_e32 v6, v112, v2
	v_max_u32_e32 v112, v112, v2
	v_cndmask_b32_e64 v112, v112, v6, s[74:75]
	s_waitcnt lgkmcnt(2)
	v_min_u32_e32 v6, v113, v3
	v_max_u32_e32 v113, v113, v3
	v_cndmask_b32_e64 v113, v113, v6, s[74:75]
	s_waitcnt lgkmcnt(1)
	v_min_u32_e32 v6, v242, v4
	v_max_u32_e32 v242, v242, v4
	v_cndmask_b32_e64 v242, v242, v6, s[74:75]
	s_waitcnt lgkmcnt(0)
	v_min_u32_e32 v6, v243, v5
	v_max_u32_e32 v243, v243, v5
	v_cndmask_b32_e64 v243, v243, v6, s[74:75]
	ds_bpermute_b32 v2, v106, v112
	ds_bpermute_b32 v3, v106, v113
	ds_bpermute_b32 v4, v106, v242
	ds_bpermute_b32 v5, v106, v243
	v_and_b32_e32 v6, 17, v118
	v_cmp_eq_u32_e64 s[78:79], 0, v6
	v_cmp_eq_u32_e32 vcc, 17, v6
	s_or_b64 s[74:75], s[78:79], vcc
	s_waitcnt lgkmcnt(3)
	v_min_u32_e32 v6, v112, v2
	v_max_u32_e32 v112, v112, v2
	v_cndmask_b32_e64 v112, v112, v6, s[74:75]
	s_waitcnt lgkmcnt(2)
	v_min_u32_e32 v6, v113, v3
	v_max_u32_e32 v113, v113, v3
	v_cndmask_b32_e64 v113, v113, v6, s[74:75]
	s_waitcnt lgkmcnt(1)
	v_min_u32_e32 v6, v242, v4
	v_max_u32_e32 v242, v242, v4
	v_cndmask_b32_e64 v242, v242, v6, s[74:75]
	s_waitcnt lgkmcnt(0)
	v_min_u32_e32 v6, v243, v5
	v_max_u32_e32 v243, v243, v5
	v_cndmask_b32_e64 v243, v243, v6, s[74:75]
	ds_bpermute_b32 v2, v110, v112
	ds_bpermute_b32 v3, v110, v113
	ds_bpermute_b32 v4, v110, v242
	ds_bpermute_b32 v5, v110, v243
	v_and_b32_e32 v6, 48, v118
	v_cmp_eq_u32_e64 s[78:79], 0, v6
	v_cmp_eq_u32_e32 vcc, 48, v6
	s_or_b64 s[74:75], s[78:79], vcc
	s_waitcnt lgkmcnt(3)
	v_min_u32_e32 v6, v112, v2
	v_max_u32_e32 v112, v112, v2
	v_cndmask_b32_e64 v112, v112, v6, s[74:75]
	s_waitcnt lgkmcnt(2)
	v_min_u32_e32 v6, v113, v3
	v_max_u32_e32 v113, v113, v3
	v_cndmask_b32_e64 v113, v113, v6, s[74:75]
	s_waitcnt lgkmcnt(1)
	v_min_u32_e32 v6, v242, v4
	v_max_u32_e32 v242, v242, v4
	v_cndmask_b32_e64 v242, v242, v6, s[74:75]
	s_waitcnt lgkmcnt(0)
	v_min_u32_e32 v6, v243, v5
	v_max_u32_e32 v243, v243, v5
	v_cndmask_b32_e64 v243, v243, v6, s[74:75]
	ds_bpermute_b32 v2, v109, v112
	ds_bpermute_b32 v3, v109, v113
	ds_bpermute_b32 v4, v109, v242
	ds_bpermute_b32 v5, v109, v243
	v_and_b32_e32 v6, 40, v118
	v_cmp_eq_u32_e64 s[78:79], 0, v6
	v_cmp_eq_u32_e32 vcc, 40, v6
	s_or_b64 s[74:75], s[78:79], vcc
	s_waitcnt lgkmcnt(3)
	v_min_u32_e32 v6, v112, v2
	v_max_u32_e32 v112, v112, v2
	v_cndmask_b32_e64 v112, v112, v6, s[74:75]
	s_waitcnt lgkmcnt(2)
	v_min_u32_e32 v6, v113, v3
	v_max_u32_e32 v113, v113, v3
	v_cndmask_b32_e64 v113, v113, v6, s[74:75]
	s_waitcnt lgkmcnt(1)
	v_min_u32_e32 v6, v242, v4
	v_max_u32_e32 v242, v242, v4
	v_cndmask_b32_e64 v242, v242, v6, s[74:75]
	s_waitcnt lgkmcnt(0)
	v_min_u32_e32 v6, v243, v5
	v_max_u32_e32 v243, v243, v5
	v_cndmask_b32_e64 v243, v243, v6, s[74:75]
	ds_bpermute_b32 v2, v108, v112
	ds_bpermute_b32 v3, v108, v113
	ds_bpermute_b32 v4, v108, v242
	ds_bpermute_b32 v5, v108, v243
	v_and_b32_e32 v6, 36, v118
	v_cmp_eq_u32_e64 s[78:79], 0, v6
	v_cmp_eq_u32_e32 vcc, 36, v6
	s_or_b64 s[74:75], s[78:79], vcc
	s_waitcnt lgkmcnt(3)
	v_min_u32_e32 v6, v112, v2
	v_max_u32_e32 v112, v112, v2
	v_cndmask_b32_e64 v112, v112, v6, s[74:75]
	s_waitcnt lgkmcnt(2)
	v_min_u32_e32 v6, v113, v3
	v_max_u32_e32 v113, v113, v3
	v_cndmask_b32_e64 v113, v113, v6, s[74:75]
	s_waitcnt lgkmcnt(1)
	v_min_u32_e32 v6, v242, v4
	v_max_u32_e32 v242, v242, v4
	v_cndmask_b32_e64 v242, v242, v6, s[74:75]
	s_waitcnt lgkmcnt(0)
	v_min_u32_e32 v6, v243, v5
	v_max_u32_e32 v243, v243, v5
	v_cndmask_b32_e64 v243, v243, v6, s[74:75]
	ds_bpermute_b32 v2, v107, v112
	ds_bpermute_b32 v3, v107, v113
	ds_bpermute_b32 v4, v107, v242
	ds_bpermute_b32 v5, v107, v243
	v_and_b32_e32 v6, 34, v118
	v_cmp_eq_u32_e64 s[78:79], 0, v6
	v_cmp_eq_u32_e32 vcc, 34, v6
	s_or_b64 s[74:75], s[78:79], vcc
	s_waitcnt lgkmcnt(3)
	v_min_u32_e32 v6, v112, v2
	v_max_u32_e32 v112, v112, v2
	v_cndmask_b32_e64 v112, v112, v6, s[74:75]
	s_waitcnt lgkmcnt(2)
	v_min_u32_e32 v6, v113, v3
	v_max_u32_e32 v113, v113, v3
	v_cndmask_b32_e64 v113, v113, v6, s[74:75]
	s_waitcnt lgkmcnt(1)
	v_min_u32_e32 v6, v242, v4
	v_max_u32_e32 v242, v242, v4
	v_cndmask_b32_e64 v242, v242, v6, s[74:75]
	s_waitcnt lgkmcnt(0)
	v_min_u32_e32 v6, v243, v5
	v_max_u32_e32 v243, v243, v5
	v_cndmask_b32_e64 v243, v243, v6, s[74:75]
	ds_bpermute_b32 v2, v106, v112
	ds_bpermute_b32 v3, v106, v113
	ds_bpermute_b32 v4, v106, v242
	ds_bpermute_b32 v5, v106, v243
	v_and_b32_e32 v6, 33, v118
	v_cmp_eq_u32_e64 s[78:79], 0, v6
	v_cmp_eq_u32_e32 vcc, 33, v6
	s_or_b64 s[74:75], s[78:79], vcc
	s_waitcnt lgkmcnt(3)
	v_min_u32_e32 v6, v112, v2
	v_max_u32_e32 v112, v112, v2
	v_cndmask_b32_e64 v112, v112, v6, s[74:75]
	s_waitcnt lgkmcnt(2)
	v_min_u32_e32 v6, v113, v3
	v_max_u32_e32 v113, v113, v3
	v_cndmask_b32_e64 v113, v113, v6, s[74:75]
	s_waitcnt lgkmcnt(1)
	v_min_u32_e32 v6, v242, v4
	v_max_u32_e32 v242, v242, v4
	v_cndmask_b32_e64 v242, v242, v6, s[74:75]
	s_waitcnt lgkmcnt(0)
	v_min_u32_e32 v6, v243, v5
	v_max_u32_e32 v243, v243, v5
	v_cndmask_b32_e64 v243, v243, v6, s[74:75]
	ds_bpermute_b32 v2, v111, v112
	ds_bpermute_b32 v3, v111, v113
	ds_bpermute_b32 v4, v111, v242
	ds_bpermute_b32 v5, v111, v243
	v_and_b32_e32 v6, 32, v118
	v_cmp_eq_u32_e64 s[74:75], 0, v6
	s_nop 1
	s_not_b64 s[46:47], s[74:75]
	s_waitcnt lgkmcnt(3)
	v_min_u32_e32 v6, v112, v2
	v_max_u32_e32 v112, v112, v2
	v_cndmask_b32_e64 v112, v112, v6, s[74:75]
	s_waitcnt lgkmcnt(2)
	v_min_u32_e32 v6, v113, v3
	v_max_u32_e32 v113, v113, v3
	v_cndmask_b32_e64 v113, v113, v6, s[46:47]
	s_waitcnt lgkmcnt(1)
	v_min_u32_e32 v6, v242, v4
	v_max_u32_e32 v242, v242, v4
	v_cndmask_b32_e64 v242, v242, v6, s[74:75]
	s_waitcnt lgkmcnt(0)
; #define P11_CX(J, ASC0, ASC1) do { const unsigned o0_ = (unsigned)__shfl_xor((int)k0, (J)), o1_ = (unsigned)__shfl_xor((int)k1, (J)); const bool lowl_ = (lane & (J)) == 0; \
;         k0 = (lowl_ == (ASC0)) ? (k0 < o0_ ? k0 : o0_) : (k0 > o0_ ? k0 : o0_); k1 = (lowl_ == (ASC1)) ? (k1 < o1_ ? k1 : o1_) : (k1 > o1_ ? k1 : o1_); } while (0)
; DI void peer_token(LAS unsigned char* ring, const bf16* x1row, float inv2, const float* nffn, const int* ex, const float* pg, const unsigned char* U6, const unsigned char* V6,
;                    const float* usc, const float* vsc, float* orow, int lane) {
;     ...
; #pragma unroll
;     for (int kk = 2; kk <= 32; kk <<= 1) { const bool asc = (lane & kk) == 0;
; #pragma unroll
;         for (int j = kk >> 1; j >= 1; j >>= 1) P11_CX(j, asc, asc); }
; #pragma unroll
;     for (int j = 32; j >= 1; j >>= 1) P11_CX(j, true, false);
;     { const unsigned lo_ = k0 < k1 ? k0 : k1, hi_ = k0 < k1 ? k1 : k0; k0 = lo_; k1 = hi_; }
; #pragma unroll
;     for (int j = 32; j >= 1; j >>= 1) P11_CX(j, true, true);
	v_min_u32_e32 v6, v243, v5
	v_max_u32_e32 v243, v243, v5
	v_cndmask_b32_e64 v243, v243, v6, s[46:47]
	ds_bpermute_b32 v2, v110, v112
	ds_bpermute_b32 v3, v110, v113
	ds_bpermute_b32 v4, v110, v242
	ds_bpermute_b32 v5, v110, v243
	v_and_b32_e32 v6, 16, v118
	v_cmp_eq_u32_e64 s[74:75], 0, v6
	s_nop 1
	s_not_b64 s[46:47], s[74:75]
	s_waitcnt lgkmcnt(3)
	v_min_u32_e32 v6, v112, v2
	v_max_u32_e32 v112, v112, v2
	v_cndmask_b32_e64 v112, v112, v6, s[74:75]
	s_waitcnt lgkmcnt(2)
	v_min_u32_e32 v6, v113, v3
	v_max_u32_e32 v113, v113, v3
	v_cndmask_b32_e64 v113, v113, v6, s[46:47]
	s_waitcnt lgkmcnt(1)
	v_min_u32_e32 v6, v242, v4
	v_max_u32_e32 v242, v242, v4
	v_cndmask_b32_e64 v242, v242, v6, s[74:75]
	s_waitcnt lgkmcnt(0)
	v_min_u32_e32 v6, v243, v5
	v_max_u32_e32 v243, v243, v5
	v_cndmask_b32_e64 v243, v243, v6, s[46:47]
	ds_bpermute_b32 v2, v109, v112
	ds_bpermute_b32 v3, v109, v113
	ds_bpermute_b32 v4, v109, v242
	ds_bpermute_b32 v5, v109, v243
	v_and_b32_e32 v6, 8, v118
	v_cmp_eq_u32_e64 s[74:75], 0, v6
	s_nop 1
	s_not_b64 s[46:47], s[74:75]
	s_waitcnt lgkmcnt(3)
	v_min_u32_e32 v6, v112, v2
	v_max_u32_e32 v112, v112, v2
	v_cndmask_b32_e64 v112, v112, v6, s[74:75]
	s_waitcnt lgkmcnt(2)
	v_min_u32_e32 v6, v113, v3
	v_max_u32_e32 v113, v113, v3
	v_cndmask_b32_e64 v113, v113, v6, s[46:47]
	s_waitcnt lgkmcnt(1)
	v_min_u32_e32 v6, v242, v4
	v_max_u32_e32 v242, v242, v4
	v_cndmask_b32_e64 v242, v242, v6, s[74:75]
	s_waitcnt lgkmcnt(0)
	v_min_u32_e32 v6, v243, v5
	v_max_u32_e32 v243, v243, v5
	v_cndmask_b32_e64 v243, v243, v6, s[46:47]
	ds_bpermute_b32 v2, v108, v112
	ds_bpermute_b32 v3, v108, v113
	ds_bpermute_b32 v4, v108, v242
	ds_bpermute_b32 v5, v108, v243
	v_and_b32_e32 v6, 4, v118
	v_cmp_eq_u32_e64 s[74:75], 0, v6
	s_nop 1
	s_not_b64 s[46:47], s[74:75]
	s_waitcnt lgkmcnt(3)
	v_min_u32_e32 v6, v112, v2
	v_max_u32_e32 v112, v112, v2
	v_cndmask_b32_e64 v112, v112, v6, s[74:75]
	s_waitcnt lgkmcnt(2)
	v_min_u32_e32 v6, v113, v3
	v_max_u32_e32 v113, v113, v3
	v_cndmask_b32_e64 v113, v113, v6, s[46:47]
	s_waitcnt lgkmcnt(1)
	v_min_u32_e32 v6, v242, v4
	v_max_u32_e32 v242, v242, v4
	v_cndmask_b32_e64 v242, v242, v6, s[74:75]
	s_waitcnt lgkmcnt(0)
	v_min_u32_e32 v6, v243, v5
	v_max_u32_e32 v243, v243, v5
	v_cndmask_b32_e64 v243, v243, v6, s[46:47]
	ds_bpermute_b32 v2, v107, v112
	ds_bpermute_b32 v3, v107, v113
	ds_bpermute_b32 v4, v107, v242
	ds_bpermute_b32 v5, v107, v243
	v_and_b32_e32 v6, 2, v118
	v_cmp_eq_u32_e64 s[74:75], 0, v6
	s_nop 1
	s_not_b64 s[46:47], s[74:75]
	s_waitcnt lgkmcnt(3)
	v_min_u32_e32 v6, v112, v2
	v_max_u32_e32 v112, v112, v2
	v_cndmask_b32_e64 v112, v112, v6, s[74:75]
	s_waitcnt lgkmcnt(2)
	v_min_u32_e32 v6, v113, v3
	v_max_u32_e32 v113, v113, v3
	v_cndmask_b32_e64 v113, v113, v6, s[46:47]
	s_waitcnt lgkmcnt(1)
	v_min_u32_e32 v6, v242, v4
	v_max_u32_e32 v242, v242, v4
	v_cndmask_b32_e64 v242, v242, v6, s[74:75]
	s_waitcnt lgkmcnt(0)
	v_min_u32_e32 v6, v243, v5
	v_max_u32_e32 v243, v243, v5
	v_cndmask_b32_e64 v243, v243, v6, s[46:47]
	ds_bpermute_b32 v2, v106, v112
	ds_bpermute_b32 v3, v106, v113
	ds_bpermute_b32 v4, v106, v242
	ds_bpermute_b32 v5, v106, v243
	v_and_b32_e32 v6, 1, v118
	v_cmp_eq_u32_e64 s[74:75], 0, v6
	s_nop 1
	s_not_b64 s[46:47], s[74:75]
	s_waitcnt lgkmcnt(3)
	v_min_u32_e32 v6, v112, v2
	v_max_u32_e32 v112, v112, v2
	v_cndmask_b32_e64 v112, v112, v6, s[74:75]
	s_waitcnt lgkmcnt(2)
	v_min_u32_e32 v6, v113, v3
	v_max_u32_e32 v113, v113, v3
	v_cndmask_b32_e64 v113, v113, v6, s[46:47]
	s_waitcnt lgkmcnt(1)
	v_min_u32_e32 v6, v242, v4
	v_max_u32_e32 v242, v242, v4
	v_cndmask_b32_e64 v242, v242, v6, s[74:75]
	s_waitcnt lgkmcnt(0)
	v_min_u32_e32 v6, v243, v5
	v_max_u32_e32 v243, v243, v5
	v_cndmask_b32_e64 v243, v243, v6, s[46:47]
	v_min_u32_e32 v6, v112, v113
	v_max_u32_e32 v2, v112, v113
	v_mov_b32_e32 v112, v6
	v_mov_b32_e32 v113, v2
	v_min_u32_e32 v6, v242, v243
	v_max_u32_e32 v2, v242, v243
	v_mov_b32_e32 v242, v2
	v_mov_b32_e32 v243, v6
	ds_bpermute_b32 v2, v111, v112
	ds_bpermute_b32 v3, v111, v113
	ds_bpermute_b32 v4, v111, v242
	ds_bpermute_b32 v5, v111, v243
	v_and_b32_e32 v6, 32, v118
	v_cmp_eq_u32_e64 s[74:75], 0, v6
	s_nop 1
	s_not_b64 s[46:47], s[74:75]
	s_waitcnt lgkmcnt(3)
	v_min_u32_e32 v6, v112, v2
	v_max_u32_e32 v112, v112, v2
	v_cndmask_b32_e64 v112, v112, v6, s[74:75]
	s_waitcnt lgkmcnt(2)
	v_min_u32_e32 v6, v113, v3
	v_max_u32_e32 v113, v113, v3
	v_cndmask_b32_e64 v113, v113, v6, s[74:75]
	s_waitcnt lgkmcnt(1)
	v_min_u32_e32 v6, v242, v4
	v_max_u32_e32 v242, v242, v4
	v_cndmask_b32_e64 v242, v242, v6, s[46:47]
	s_waitcnt lgkmcnt(0)
	v_min_u32_e32 v6, v243, v5
	v_max_u32_e32 v243, v243, v5
	v_cndmask_b32_e64 v243, v243, v6, s[46:47]
	ds_bpermute_b32 v2, v110, v112
	ds_bpermute_b32 v3, v110, v113
	ds_bpermute_b32 v4, v110, v242
	ds_bpermute_b32 v5, v110, v243
	v_and_b32_e32 v6, 16, v118
	v_cmp_eq_u32_e64 s[74:75], 0, v6
	s_nop 1
	s_not_b64 s[46:47], s[74:75]
	s_waitcnt lgkmcnt(3)
	v_min_u32_e32 v6, v112, v2
	v_max_u32_e32 v112, v112, v2
	v_cndmask_b32_e64 v112, v112, v6, s[74:75]
	s_waitcnt lgkmcnt(2)
	v_min_u32_e32 v6, v113, v3
	v_max_u32_e32 v113, v113, v3
	v_cndmask_b32_e64 v113, v113, v6, s[74:75]
	s_waitcnt lgkmcnt(1)
	v_min_u32_e32 v6, v242, v4
	v_max_u32_e32 v242, v242, v4
	v_cndmask_b32_e64 v242, v242, v6, s[46:47]
	s_waitcnt lgkmcnt(0)
	v_min_u32_e32 v6, v243, v5
	v_max_u32_e32 v243, v243, v5
	v_cndmask_b32_e64 v243, v243, v6, s[46:47]
	ds_bpermute_b32 v2, v109, v112
	ds_bpermute_b32 v3, v109, v113
	ds_bpermute_b32 v4, v109, v242
	ds_bpermute_b32 v5, v109, v243
	v_and_b32_e32 v6, 8, v118
	v_cmp_eq_u32_e64 s[74:75], 0, v6
	s_nop 1
	s_not_b64 s[46:47], s[74:75]
	s_waitcnt lgkmcnt(3)
; #define P11_CX(J, ASC0, ASC1) do { const unsigned o0_ = (unsigned)__shfl_xor((int)k0, (J)), o1_ = (unsigned)__shfl_xor((int)k1, (J)); const bool lowl_ = (lane & (J)) == 0; \
;         k0 = (lowl_ == (ASC0)) ? (k0 < o0_ ? k0 : o0_) : (k0 > o0_ ? k0 : o0_); k1 = (lowl_ == (ASC1)) ? (k1 < o1_ ? k1 : o1_) : (k1 > o1_ ? k1 : o1_); } while (0)
; DI void peer_token(LAS unsigned char* ring, const bf16* x1row, float inv2, const float* nffn, const int* ex, const float* pg, const unsigned char* U6, const unsigned char* V6,
;                    const float* usc, const float* vsc, float* orow, int lane) {
;     ...
; #pragma unroll
;     for (int kk = 2; kk <= 32; kk <<= 1) { const bool asc = (lane & kk) == 0;
; #pragma unroll
;         for (int j = kk >> 1; j >= 1; j >>= 1) P11_CX(j, asc, asc); }
; #pragma unroll
;     for (int j = 32; j >= 1; j >>= 1) P11_CX(j, true, false);
;     { const unsigned lo_ = k0 < k1 ? k0 : k1, hi_ = k0 < k1 ? k1 : k0; k0 = lo_; k1 = hi_; }
; #pragma unroll
;     for (int j = 32; j >= 1; j >>= 1) P11_CX(j, true, true);
	v_min_u32_e32 v6, v112, v2
	v_max_u32_e32 v112, v112, v2
	v_cndmask_b32_e64 v112, v112, v6, s[74:75]
	s_waitcnt lgkmcnt(2)
	v_min_u32_e32 v6, v113, v3
	v_max_u32_e32 v113, v113, v3
	v_cndmask_b32_e64 v113, v113, v6, s[74:75]
	s_waitcnt lgkmcnt(1)
	v_min_u32_e32 v6, v242, v4
	v_max_u32_e32 v242, v242, v4
	v_cndmask_b32_e64 v242, v242, v6, s[46:47]
	s_waitcnt lgkmcnt(0)
	v_min_u32_e32 v6, v243, v5
	v_max_u32_e32 v243, v243, v5
	v_cndmask_b32_e64 v243, v243, v6, s[46:47]
	ds_bpermute_b32 v2, v108, v112
	ds_bpermute_b32 v3, v108, v113
	ds_bpermute_b32 v4, v108, v242
	ds_bpermute_b32 v5, v108, v243
	v_and_b32_e32 v6, 4, v118
	v_cmp_eq_u32_e64 s[74:75], 0, v6
	s_nop 1
	s_not_b64 s[46:47], s[74:75]
	s_waitcnt lgkmcnt(3)
	v_min_u32_e32 v6, v112, v2
	v_max_u32_e32 v112, v112, v2
	v_cndmask_b32_e64 v112, v112, v6, s[74:75]
	s_waitcnt lgkmcnt(2)
	v_min_u32_e32 v6, v113, v3
	v_max_u32_e32 v113, v113, v3
	v_cndmask_b32_e64 v113, v113, v6, s[74:75]
	s_waitcnt lgkmcnt(1)
	v_min_u32_e32 v6, v242, v4
	v_max_u32_e32 v242, v242, v4
	v_cndmask_b32_e64 v242, v242, v6, s[46:47]
	s_waitcnt lgkmcnt(0)
	v_min_u32_e32 v6, v243, v5
	v_max_u32_e32 v243, v243, v5
	v_cndmask_b32_e64 v243, v243, v6, s[46:47]
	ds_bpermute_b32 v2, v107, v112
	ds_bpermute_b32 v3, v107, v113
	ds_bpermute_b32 v4, v107, v242
	ds_bpermute_b32 v5, v107, v243
	v_and_b32_e32 v6, 2, v118
	v_cmp_eq_u32_e64 s[74:75], 0, v6
	s_nop 1
	s_not_b64 s[46:47], s[74:75]
	s_waitcnt lgkmcnt(3)
	v_min_u32_e32 v6, v112, v2
	v_max_u32_e32 v112, v112, v2
	v_cndmask_b32_e64 v112, v112, v6, s[74:75]
	s_waitcnt lgkmcnt(2)
	v_min_u32_e32 v6, v113, v3
	v_max_u32_e32 v113, v113, v3
	v_cndmask_b32_e64 v113, v113, v6, s[74:75]
	s_waitcnt lgkmcnt(1)
	v_min_u32_e32 v6, v242, v4
	v_max_u32_e32 v242, v242, v4
	v_cndmask_b32_e64 v242, v242, v6, s[46:47]
	s_waitcnt lgkmcnt(0)
	v_min_u32_e32 v6, v243, v5
	v_max_u32_e32 v243, v243, v5
	v_cndmask_b32_e64 v243, v243, v6, s[46:47]
	ds_bpermute_b32 v2, v106, v112
	ds_bpermute_b32 v3, v106, v113
	ds_bpermute_b32 v4, v106, v242
	ds_bpermute_b32 v5, v106, v243
	v_and_b32_e32 v6, 1, v118
	v_cmp_eq_u32_e64 s[74:75], 0, v6
	s_nop 1
	s_not_b64 s[46:47], s[74:75]
	s_waitcnt lgkmcnt(3)
	v_min_u32_e32 v6, v112, v2
	v_max_u32_e32 v112, v112, v2
	v_cndmask_b32_e64 v112, v112, v6, s[74:75]
	s_waitcnt lgkmcnt(2)
	v_min_u32_e32 v6, v113, v3
	v_max_u32_e32 v113, v113, v3
	v_cndmask_b32_e64 v113, v113, v6, s[74:75]
	s_waitcnt lgkmcnt(1)
	v_min_u32_e32 v6, v242, v4
	v_max_u32_e32 v242, v242, v4
	v_cndmask_b32_e64 v242, v242, v6, s[46:47]
	s_waitcnt lgkmcnt(0)
	v_min_u32_e32 v6, v243, v5
	v_max_u32_e32 v243, v243, v5
	v_cndmask_b32_e64 v243, v243, v6, s[46:47]
	v_min_u32_e32 v6, v112, v242
	v_max_u32_e32 v2, v112, v242
	v_mov_b32_e32 v112, v6
	v_mov_b32_e32 v242, v2
	v_min_u32_e32 v6, v113, v243
	v_max_u32_e32 v2, v113, v243
	v_mov_b32_e32 v113, v6
	v_mov_b32_e32 v243, v2
	v_min_u32_e32 v6, v112, v113
	v_max_u32_e32 v2, v112, v113
	v_mov_b32_e32 v112, v6
	v_mov_b32_e32 v113, v2
	v_min_u32_e32 v6, v242, v243
	v_max_u32_e32 v2, v242, v243
	v_mov_b32_e32 v242, v6
	v_mov_b32_e32 v243, v2
	ds_bpermute_b32 v2, v111, v112
	ds_bpermute_b32 v3, v111, v113
	ds_bpermute_b32 v4, v111, v242
	ds_bpermute_b32 v5, v111, v243
	v_and_b32_e32 v6, 32, v118
	v_cmp_eq_u32_e64 s[74:75], 0, v6
	s_nop 1
	s_not_b64 s[46:47], s[74:75]
	s_waitcnt lgkmcnt(3)
	v_min_u32_e32 v6, v112, v2
	v_max_u32_e32 v112, v112, v2
	v_cndmask_b32_e64 v112, v112, v6, s[74:75]
	s_waitcnt lgkmcnt(2)
	v_min_u32_e32 v6, v113, v3
	v_max_u32_e32 v113, v113, v3
	v_cndmask_b32_e64 v113, v113, v6, s[74:75]
	s_waitcnt lgkmcnt(1)
	v_min_u32_e32 v6, v242, v4
	v_max_u32_e32 v242, v242, v4
	v_cndmask_b32_e64 v242, v242, v6, s[74:75]
	s_waitcnt lgkmcnt(0)
	v_min_u32_e32 v6, v243, v5
	v_max_u32_e32 v243, v243, v5
	v_cndmask_b32_e64 v243, v243, v6, s[74:75]
	ds_bpermute_b32 v2, v110, v112
	ds_bpermute_b32 v3, v110, v113
	ds_bpermute_b32 v4, v110, v242
	ds_bpermute_b32 v5, v110, v243
	v_and_b32_e32 v6, 16, v118
	v_cmp_eq_u32_e64 s[74:75], 0, v6
	s_nop 1
	s_not_b64 s[46:47], s[74:75]
	s_waitcnt lgkmcnt(3)
	v_min_u32_e32 v6, v112, v2
	v_max_u32_e32 v112, v112, v2
	v_cndmask_b32_e64 v112, v112, v6, s[74:75]
	s_waitcnt lgkmcnt(2)
	v_min_u32_e32 v6, v113, v3
	v_max_u32_e32 v113, v113, v3
	v_cndmask_b32_e64 v113, v113, v6, s[74:75]
	s_waitcnt lgkmcnt(1)
	v_min_u32_e32 v6, v242, v4
	v_max_u32_e32 v242, v242, v4
	v_cndmask_b32_e64 v242, v242, v6, s[74:75]
	s_waitcnt lgkmcnt(0)
	v_min_u32_e32 v6, v243, v5
	v_max_u32_e32 v243, v243, v5
	v_cndmask_b32_e64 v243, v243, v6, s[74:75]
	ds_bpermute_b32 v2, v109, v112
	ds_bpermute_b32 v3, v109, v113
	ds_bpermute_b32 v4, v109, v242
	ds_bpermute_b32 v5, v109, v243
	v_and_b32_e32 v6, 8, v118
	v_cmp_eq_u32_e64 s[74:75], 0, v6
	s_nop 1
	s_not_b64 s[46:47], s[74:75]
	s_waitcnt lgkmcnt(3)
	v_min_u32_e32 v6, v112, v2
	v_max_u32_e32 v112, v112, v2
	v_cndmask_b32_e64 v112, v112, v6, s[74:75]
	s_waitcnt lgkmcnt(2)
	v_min_u32_e32 v6, v113, v3
	v_max_u32_e32 v113, v113, v3
	v_cndmask_b32_e64 v113, v113, v6, s[74:75]
	s_waitcnt lgkmcnt(1)
	v_min_u32_e32 v6, v242, v4
	v_max_u32_e32 v242, v242, v4
	v_cndmask_b32_e64 v242, v242, v6, s[74:75]
	s_waitcnt lgkmcnt(0)
	v_min_u32_e32 v6, v243, v5
	v_max_u32_e32 v243, v243, v5
	v_cndmask_b32_e64 v243, v243, v6, s[74:75]
	ds_bpermute_b32 v2, v108, v112
	ds_bpermute_b32 v3, v108, v113
	ds_bpermute_b32 v4, v108, v242
	ds_bpermute_b32 v5, v108, v243
	v_and_b32_e32 v6, 4, v118
	v_cmp_eq_u32_e64 s[74:75], 0, v6
	s_nop 1
	s_not_b64 s[46:47], s[74:75]
	s_waitcnt lgkmcnt(3)
	v_min_u32_e32 v6, v112, v2
	v_max_u32_e32 v112, v112, v2
	v_cndmask_b32_e64 v112, v112, v6, s[74:75]
	s_waitcnt lgkmcnt(2)
; #define P11_CX(J, ASC0, ASC1) do { const unsigned o0_ = (unsigned)__shfl_xor((int)k0, (J)), o1_ = (unsigned)__shfl_xor((int)k1, (J)); const bool lowl_ = (lane & (J)) == 0; \
;         k0 = (lowl_ == (ASC0)) ? (k0 < o0_ ? k0 : o0_) : (k0 > o0_ ? k0 : o0_); k1 = (lowl_ == (ASC1)) ? (k1 < o1_ ? k1 : o1_) : (k1 > o1_ ? k1 : o1_); } while (0)
; DI void peer_token(LAS unsigned char* ring, const bf16* x1row, float inv2, const float* nffn, const int* ex, const float* pg, const unsigned char* U6, const unsigned char* V6,
;                    const float* usc, const float* vsc, float* orow, int lane) {
;     ...
;     for (int j = 32; j >= 1; j >>= 1) P11_CX(j, true, false);
;     { const unsigned lo_ = k0 < k1 ? k0 : k1, hi_ = k0 < k1 ? k1 : k0; k0 = lo_; k1 = hi_; }
; #pragma unroll
;     for (int j = 32; j >= 1; j >>= 1) P11_CX(j, true, true);
;     ...
;     const int e_lo = (int)(k0 >> 7), e_hi = (int)(k1 >> 7);
;     const float us_lo = usc[e_lo], us_hi = usc[e_hi];
;     const float gv_lo = __hip_atomic_load(pg + (k0 & 127u), __ATOMIC_RELAXED, __HIP_MEMORY_SCOPE_AGENT) * vsc[e_lo], gv_hi = __hip_atomic_load(pg + (k1 & 127u), __ATOMIC_RELAXED, __HIP_MEMORY_SCOPE_AGENT) * vsc[e_hi];
;     f32x2 h2[32], y[32];
;     asm volatile("" : "+s"(nffn));
; #pragma unroll
;     for (int i = 0; i < 16; ++i) {
;         const v2u aw = *(const v2u*)(x1row + i * 256 + lane * 4); const f32x4 g = *(const f32x4*)(nffn + i * 256 + lane * 4);
;         h2[2 * i] = (f32x2){bflo(aw.x) * inv2 * g.x, bfhi(aw.x) * inv2 * g.y}; h2[2 * i + 1] = (f32x2){bflo(aw.y) * inv2 * g.z, bfhi(aw.y) * inv2 * g.w};
	v_min_u32_e32 v6, v113, v3
	v_max_u32_e32 v113, v113, v3
	v_cndmask_b32_e64 v113, v113, v6, s[74:75]
	s_waitcnt lgkmcnt(1)
	v_min_u32_e32 v6, v242, v4
	v_max_u32_e32 v242, v242, v4
	v_cndmask_b32_e64 v242, v242, v6, s[74:75]
	s_waitcnt lgkmcnt(0)
	v_min_u32_e32 v6, v243, v5
	v_max_u32_e32 v243, v243, v5
	v_cndmask_b32_e64 v243, v243, v6, s[74:75]
	ds_bpermute_b32 v2, v107, v112
	ds_bpermute_b32 v3, v107, v113
	ds_bpermute_b32 v4, v107, v242
	ds_bpermute_b32 v5, v107, v243
	v_and_b32_e32 v6, 2, v118
	v_cmp_eq_u32_e64 s[74:75], 0, v6
	s_nop 1
	s_not_b64 s[46:47], s[74:75]
	s_waitcnt lgkmcnt(3)
	v_min_u32_e32 v6, v112, v2
	v_max_u32_e32 v112, v112, v2
	v_cndmask_b32_e64 v112, v112, v6, s[74:75]
	s_waitcnt lgkmcnt(2)
	v_min_u32_e32 v6, v113, v3
	v_max_u32_e32 v113, v113, v3
	v_cndmask_b32_e64 v113, v113, v6, s[74:75]
	s_waitcnt lgkmcnt(1)
	v_min_u32_e32 v6, v242, v4
	v_max_u32_e32 v242, v242, v4
	v_cndmask_b32_e64 v242, v242, v6, s[74:75]
	s_waitcnt lgkmcnt(0)
	v_min_u32_e32 v6, v243, v5
	v_max_u32_e32 v243, v243, v5
	v_cndmask_b32_e64 v243, v243, v6, s[74:75]
	ds_bpermute_b32 v2, v106, v112
	ds_bpermute_b32 v3, v106, v113
	ds_bpermute_b32 v4, v106, v242
	ds_bpermute_b32 v5, v106, v243
	v_and_b32_e32 v6, 1, v118
	v_cmp_eq_u32_e64 s[74:75], 0, v6
	s_nop 1
	s_not_b64 s[46:47], s[74:75]
	s_waitcnt lgkmcnt(3)
	v_min_u32_e32 v6, v112, v2
	v_max_u32_e32 v112, v112, v2
	v_cndmask_b32_e64 v112, v112, v6, s[74:75]
	s_waitcnt lgkmcnt(2)
	v_min_u32_e32 v6, v113, v3
	v_max_u32_e32 v113, v113, v3
	v_cndmask_b32_e64 v113, v113, v6, s[74:75]
	s_waitcnt lgkmcnt(1)
	v_min_u32_e32 v6, v242, v4
	v_max_u32_e32 v242, v242, v4
	v_cndmask_b32_e64 v242, v242, v6, s[74:75]
	s_waitcnt lgkmcnt(0)
	v_min_u32_e32 v6, v243, v5
	v_max_u32_e32 v243, v243, v5
	v_cndmask_b32_e64 v243, v243, v6, s[74:75]
	v_and_b32_e32 v6, 0x80, v112
	v_cmp_ne_u32_e64 s[100:101], 0, v6
	v_and_b32_e32 v6, 0x80, v113
	v_cmp_ne_u32_e64 s[50:51], 0, v6
	v_and_b32_e32 v6, 0x80, v242
	v_cmp_ne_u32_e64 s[82:83], 0, v6
	v_and_b32_e32 v6, 0x80, v243
	v_cmp_ne_u32_e64 s[70:71], 0, v6
	s_lshl_b32 s46, s76, 1
	s_add_i32 s46, s46, s97
	s_ashr_i32 s47, s46, 31
	s_lshl_b64 s[78:79], s[46:47], 9
	s_add_u32 s74, s56, s78
	s_addc_u32 s75, s57, s79
	v_lshrrev_b32_e32 v2, 6, v112
	v_and_b32_e32 v2, -4, v2
	v_and_b32_e32 v16, 0xff, v112
	v_lshlrev_b32_e32 v16, 2, v16
	v_lshrrev_b32_e32 v3, 6, v113
	v_and_b32_e32 v3, -4, v3
	v_and_b32_e32 v17, 0xff, v113
	v_lshlrev_b32_e32 v17, 2, v17
	v_lshrrev_b32_e32 v4, 6, v242
	v_and_b32_e32 v4, -4, v4
	v_and_b32_e32 v18, 0xff, v242
	v_lshlrev_b32_e32 v18, 2, v18
	v_lshrrev_b32_e32 v5, 6, v243
	v_and_b32_e32 v5, -4, v5
	v_and_b32_e32 v19, 0xff, v243
	v_lshlrev_b32_e32 v19, 2, v19
	global_load_dword v121, v2, s[52:53]
	global_load_dword v124, v16, s[74:75] sc1
	global_load_dword v115, v2, s[54:55]
	global_load_dword v119, v3, s[52:53]
	global_load_dword v122, v17, s[74:75] sc1
	global_load_dword v116, v3, s[54:55]
	global_load_dword v244, v4, s[52:53]
	global_load_dword v246, v18, s[74:75] sc1
	global_load_dword v71, v4, s[54:55]
	global_load_dword v245, v5, s[52:53]
	global_load_dword v247, v19, s[74:75] sc1
	global_load_dword v135, v5, s[54:55]
	s_waitcnt vmcnt(12)
	v_mov_b32_e32 v134, v97
	v_lshlrev_b32_e32 v2, 16, v146
	v_and_b32_e32 v3, 0xffff0000, v146
	v_lshlrev_b32_e32 v4, 16, v147
	v_and_b32_e32 v5, 0xffff0000, v147
	v_pk_mul_f32 v[2:3], v[96:97], v[2:3] op_sel_hi:[0,1]
	v_pk_mul_f32 v[4:5], v[96:97], v[4:5] op_sel_hi:[0,1]
	v_pk_mul_f32 v[20:21], v[98:99], v[2:3]
	v_pk_mul_f32 v[22:23], v[100:101], v[4:5]
	v_lshlrev_b32_e32 v16, 16, v148
	v_and_b32_e32 v17, 0xffff0000, v148
	v_lshlrev_b32_e32 v18, 16, v149
	v_and_b32_e32 v19, 0xffff0000, v149
	v_pk_mul_f32 v[16:17], v[96:97], v[16:17] op_sel_hi:[0,1]
	v_pk_mul_f32 v[18:19], v[96:97], v[18:19] op_sel_hi:[0,1]
	v_pk_mul_f32 v[24:25], v[102:103], v[16:17]
	v_pk_mul_f32 v[26:27], v[104:105], v[18:19]
	v_lshlrev_b32_e32 v2, 16, v150
	v_and_b32_e32 v3, 0xffff0000, v150
	v_lshlrev_b32_e32 v4, 16, v151
	v_and_b32_e32 v5, 0xffff0000, v151
	v_pk_mul_f32 v[2:3], v[96:97], v[2:3] op_sel_hi:[0,1]
	v_pk_mul_f32 v[4:5], v[96:97], v[4:5] op_sel_hi:[0,1]
	v_pk_mul_f32 v[28:29], v[126:127], v[2:3]
	v_pk_mul_f32 v[30:31], v[128:129], v[4:5]
	v_lshlrev_b32_e32 v16, 16, v152
	v_and_b32_e32 v17, 0xffff0000, v152
	v_lshlrev_b32_e32 v18, 16, v153
	v_and_b32_e32 v19, 0xffff0000, v153
	v_pk_mul_f32 v[16:17], v[96:97], v[16:17] op_sel_hi:[0,1]
	v_pk_mul_f32 v[18:19], v[96:97], v[18:19] op_sel_hi:[0,1]
	v_pk_mul_f32 v[32:33], v[130:131], v[16:17]
	v_pk_mul_f32 v[34:35], v[132:133], v[18:19]
	v_lshlrev_b32_e32 v2, 16, v154
	v_and_b32_e32 v3, 0xffff0000, v154
	v_lshlrev_b32_e32 v4, 16, v155
	v_and_b32_e32 v5, 0xffff0000, v155
	v_pk_mul_f32 v[2:3], v[96:97], v[2:3] op_sel_hi:[0,1]
	v_pk_mul_f32 v[4:5], v[96:97], v[4:5] op_sel_hi:[0,1]
	v_pk_mul_f32 v[36:37], v[136:137], v[2:3]
	v_pk_mul_f32 v[38:39], v[138:139], v[4:5]
	v_lshlrev_b32_e32 v16, 16, v156
	v_and_b32_e32 v17, 0xffff0000, v156
	v_lshlrev_b32_e32 v18, 16, v157
	v_and_b32_e32 v19, 0xffff0000, v157
	v_pk_mul_f32 v[16:17], v[96:97], v[16:17] op_sel_hi:[0,1]
	v_pk_mul_f32 v[18:19], v[96:97], v[18:19] op_sel_hi:[0,1]
	v_pk_mul_f32 v[40:41], v[140:141], v[16:17]
	v_pk_mul_f32 v[42:43], v[142:143], v[18:19]
	v_lshlrev_b32_e32 v2, 16, v158
	v_and_b32_e32 v3, 0xffff0000, v158
	v_lshlrev_b32_e32 v4, 16, v159
	v_and_b32_e32 v5, 0xffff0000, v159
	v_pk_mul_f32 v[2:3], v[96:97], v[2:3] op_sel_hi:[0,1]
	v_pk_mul_f32 v[4:5], v[96:97], v[4:5] op_sel_hi:[0,1]
	v_pk_mul_f32 v[44:45], v[8:9], v[2:3]
	v_pk_mul_f32 v[46:47], v[10:11], v[4:5]
	v_lshlrev_b32_e32 v16, 16, v160
	v_and_b32_e32 v17, 0xffff0000, v160
; DI void peer_token(LAS unsigned char* ring, const bf16* x1row, float inv2, const float* nffn, const int* ex, const float* pg, const unsigned char* U6, const unsigned char* V6,
;                    const float* usc, const float* vsc, float* orow, int lane) {
;     ...
; #pragma unroll
;     for (int i = 0; i < 16; ++i) {
;         const v2u aw = *(const v2u*)(x1row + i * 256 + lane * 4); const f32x4 g = *(const f32x4*)(nffn + i * 256 + lane * 4);
;         h2[2 * i] = (f32x2){bflo(aw.x) * inv2 * g.x, bfhi(aw.x) * inv2 * g.y}; h2[2 * i + 1] = (f32x2){bflo(aw.y) * inv2 * g.z, bfhi(aw.y) * inv2 * g.w};
;     }
	v_lshlrev_b32_e32 v18, 16, v161
	v_and_b32_e32 v19, 0xffff0000, v161
	v_pk_mul_f32 v[16:17], v[96:97], v[16:17] op_sel_hi:[0,1]
	v_pk_mul_f32 v[18:19], v[96:97], v[18:19] op_sel_hi:[0,1]
	v_pk_mul_f32 v[48:49], v[12:13], v[16:17]
	v_pk_mul_f32 v[50:51], v[14:15], v[18:19]
	v_lshlrev_b32_e32 v2, 16, v162
	v_and_b32_e32 v3, 0xffff0000, v162
	v_lshlrev_b32_e32 v4, 16, v163
	v_and_b32_e32 v5, 0xffff0000, v163
	v_pk_mul_f32 v[2:3], v[96:97], v[2:3] op_sel_hi:[0,1]
	v_pk_mul_f32 v[4:5], v[96:97], v[4:5] op_sel_hi:[0,1]
	v_pk_mul_f32 v[52:53], v[210:211], v[2:3]
	v_pk_mul_f32 v[54:55], v[212:213], v[4:5]
	v_lshlrev_b32_e32 v16, 16, v164
	v_and_b32_e32 v17, 0xffff0000, v164
	v_lshlrev_b32_e32 v18, 16, v165
	v_and_b32_e32 v19, 0xffff0000, v165
	v_pk_mul_f32 v[16:17], v[96:97], v[16:17] op_sel_hi:[0,1]
	v_pk_mul_f32 v[18:19], v[96:97], v[18:19] op_sel_hi:[0,1]
	v_pk_mul_f32 v[56:57], v[214:215], v[16:17]
	v_pk_mul_f32 v[58:59], v[216:217], v[18:19]
	v_lshlrev_b32_e32 v2, 16, v166
	v_and_b32_e32 v3, 0xffff0000, v166
	v_lshlrev_b32_e32 v4, 16, v167
	v_and_b32_e32 v5, 0xffff0000, v167
	v_pk_mul_f32 v[2:3], v[96:97], v[2:3] op_sel_hi:[0,1]
	v_pk_mul_f32 v[4:5], v[96:97], v[4:5] op_sel_hi:[0,1]
	v_pk_mul_f32 v[60:61], v[218:219], v[2:3]
	v_pk_mul_f32 v[62:63], v[220:221], v[4:5]
	v_lshlrev_b32_e32 v16, 16, v168
	v_and_b32_e32 v17, 0xffff0000, v168
	v_lshlrev_b32_e32 v18, 16, v169
	v_and_b32_e32 v19, 0xffff0000, v169
	v_pk_mul_f32 v[16:17], v[96:97], v[16:17] op_sel_hi:[0,1]
	v_pk_mul_f32 v[18:19], v[96:97], v[18:19] op_sel_hi:[0,1]
	v_pk_mul_f32 v[64:65], v[222:223], v[16:17]
	v_pk_mul_f32 v[80:81], v[224:225], v[18:19]
	v_lshlrev_b32_e32 v2, 16, v170
	v_and_b32_e32 v3, 0xffff0000, v170
	v_lshlrev_b32_e32 v4, 16, v171
	v_and_b32_e32 v5, 0xffff0000, v171
	v_pk_mul_f32 v[2:3], v[96:97], v[2:3] op_sel_hi:[0,1]
	v_pk_mul_f32 v[4:5], v[96:97], v[4:5] op_sel_hi:[0,1]
	v_pk_mul_f32 v[82:83], v[226:227], v[2:3]
	v_pk_mul_f32 v[84:85], v[228:229], v[4:5]
	v_lshlrev_b32_e32 v16, 16, v172
	v_and_b32_e32 v17, 0xffff0000, v172
	v_lshlrev_b32_e32 v18, 16, v173
	v_and_b32_e32 v19, 0xffff0000, v173
	v_pk_mul_f32 v[16:17], v[96:97], v[16:17] op_sel_hi:[0,1]
	v_pk_mul_f32 v[18:19], v[96:97], v[18:19] op_sel_hi:[0,1]
	v_pk_mul_f32 v[86:87], v[230:231], v[16:17]
	v_pk_mul_f32 v[88:89], v[232:233], v[18:19]
	v_lshlrev_b32_e32 v2, 16, v174
	v_and_b32_e32 v3, 0xffff0000, v174
	v_lshlrev_b32_e32 v4, 16, v175
	v_and_b32_e32 v5, 0xffff0000, v175
	v_pk_mul_f32 v[2:3], v[96:97], v[2:3] op_sel_hi:[0,1]
	v_pk_mul_f32 v[4:5], v[96:97], v[4:5] op_sel_hi:[0,1]
	v_pk_mul_f32 v[90:91], v[234:235], v[2:3]
	v_pk_mul_f32 v[92:93], v[236:237], v[4:5]
	v_lshlrev_b32_e32 v16, 16, v176
	v_and_b32_e32 v17, 0xffff0000, v176
	v_lshlrev_b32_e32 v18, 16, v177
	v_and_b32_e32 v19, 0xffff0000, v177
	v_pk_mul_f32 v[16:17], v[96:97], v[16:17] op_sel_hi:[0,1]
	v_pk_mul_f32 v[18:19], v[96:97], v[18:19] op_sel_hi:[0,1]
	v_pk_mul_f32 v[94:95], v[238:239], v[16:17]
	v_pk_mul_f32 v[96:97], v[240:241], v[18:19]
	v_lshlrev_b32_e32 v16, 16, v208
	v_and_b32_e32 v17, 0xffff0000, v208
	v_lshlrev_b32_e32 v18, 16, v209
	v_and_b32_e32 v19, 0xffff0000, v209
	v_pk_mul_f32 v[16:17], v[134:135], v[16:17] op_sel_hi:[0,1]
	v_pk_mul_f32 v[18:19], v[134:135], v[18:19] op_sel_hi:[0,1]
	v_pk_mul_f32 v[238:239], v[238:239], v[16:17]
	v_pk_mul_f32 v[240:241], v[240:241], v[18:19]
	v_lshlrev_b32_e32 v2, 16, v206
	v_and_b32_e32 v3, 0xffff0000, v206
	v_lshlrev_b32_e32 v4, 16, v207
	v_and_b32_e32 v5, 0xffff0000, v207
	v_pk_mul_f32 v[2:3], v[134:135], v[2:3] op_sel_hi:[0,1]
	v_pk_mul_f32 v[4:5], v[134:135], v[4:5] op_sel_hi:[0,1]
	v_pk_mul_f32 v[234:235], v[234:235], v[2:3]
	v_pk_mul_f32 v[236:237], v[236:237], v[4:5]
	v_lshlrev_b32_e32 v16, 16, v204
	v_and_b32_e32 v17, 0xffff0000, v204
	v_lshlrev_b32_e32 v18, 16, v205
	v_and_b32_e32 v19, 0xffff0000, v205
	v_pk_mul_f32 v[16:17], v[134:135], v[16:17] op_sel_hi:[0,1]
	v_pk_mul_f32 v[18:19], v[134:135], v[18:19] op_sel_hi:[0,1]
	v_pk_mul_f32 v[230:231], v[230:231], v[16:17]
	v_pk_mul_f32 v[232:233], v[232:233], v[18:19]
	v_lshlrev_b32_e32 v2, 16, v202
	v_and_b32_e32 v3, 0xffff0000, v202
	v_lshlrev_b32_e32 v4, 16, v203
	v_and_b32_e32 v5, 0xffff0000, v203
	v_pk_mul_f32 v[2:3], v[134:135], v[2:3] op_sel_hi:[0,1]
	v_pk_mul_f32 v[4:5], v[134:135], v[4:5] op_sel_hi:[0,1]
	v_pk_mul_f32 v[226:227], v[226:227], v[2:3]
	v_pk_mul_f32 v[228:229], v[228:229], v[4:5]
	v_lshlrev_b32_e32 v16, 16, v200
	v_and_b32_e32 v17, 0xffff0000, v200
	v_lshlrev_b32_e32 v18, 16, v201
	v_and_b32_e32 v19, 0xffff0000, v201
	v_pk_mul_f32 v[16:17], v[134:135], v[16:17] op_sel_hi:[0,1]
	v_pk_mul_f32 v[18:19], v[134:135], v[18:19] op_sel_hi:[0,1]
	v_pk_mul_f32 v[222:223], v[222:223], v[16:17]
	v_pk_mul_f32 v[224:225], v[224:225], v[18:19]
	v_lshlrev_b32_e32 v2, 16, v198
	v_and_b32_e32 v3, 0xffff0000, v198
	v_lshlrev_b32_e32 v4, 16, v199
	v_and_b32_e32 v5, 0xffff0000, v199
	v_pk_mul_f32 v[2:3], v[134:135], v[2:3] op_sel_hi:[0,1]
	v_pk_mul_f32 v[4:5], v[134:135], v[4:5] op_sel_hi:[0,1]
	v_pk_mul_f32 v[218:219], v[218:219], v[2:3]
	v_pk_mul_f32 v[220:221], v[220:221], v[4:5]
	v_lshlrev_b32_e32 v16, 16, v196
	v_and_b32_e32 v17, 0xffff0000, v196
	v_lshlrev_b32_e32 v18, 16, v197
	v_and_b32_e32 v19, 0xffff0000, v197
	v_pk_mul_f32 v[16:17], v[134:135], v[16:17] op_sel_hi:[0,1]
	v_pk_mul_f32 v[18:19], v[134:135], v[18:19] op_sel_hi:[0,1]
	v_pk_mul_f32 v[214:215], v[214:215], v[16:17]
	v_pk_mul_f32 v[216:217], v[216:217], v[18:19]
	v_lshlrev_b32_e32 v2, 16, v194
	v_and_b32_e32 v3, 0xffff0000, v194
	v_lshlrev_b32_e32 v4, 16, v195
	v_and_b32_e32 v5, 0xffff0000, v195
	v_pk_mul_f32 v[2:3], v[134:135], v[2:3] op_sel_hi:[0,1]
; #define P11_DMA(gsrc, ldst, NP) do { _Pragma("unroll") for (int _i = 0; _i < (NP); ++_i) \
;     __builtin_amdgcn_global_load_lds((const unsigned*)((gsrc) + _i * 1024), (LAS unsigned*)((ldst) + _i * 1024), 16, 0, 0); } while (0)
; DI void peer_token(LAS unsigned char* ring, const bf16* x1row, float inv2, const float* nffn, const int* ex, const float* pg, const unsigned char* U6, const unsigned char* V6,
;                    const float* usc, const float* vsc, float* orow, int lane) {
;     ...
;     const float us_lo = usc[e_lo], us_hi = usc[e_hi];
;     const float gv_lo = __hip_atomic_load(pg + (k0 & 127u), __ATOMIC_RELAXED, __HIP_MEMORY_SCOPE_AGENT) * vsc[e_lo], gv_hi = __hip_atomic_load(pg + (k1 & 127u), __ATOMIC_RELAXED, __HIP_MEMORY_SCOPE_AGENT) * vsc[e_hi];
;     f32x2 h2[32], y[32];
;     asm volatile("" : "+s"(nffn));
; #pragma unroll
;     for (int i = 0; i < 16; ++i) {
;         const v2u aw = *(const v2u*)(x1row + i * 256 + lane * 4); const f32x4 g = *(const f32x4*)(nffn + i * 256 + lane * 4);
;         h2[2 * i] = (f32x2){bflo(aw.x) * inv2 * g.x, bfhi(aw.x) * inv2 * g.y}; h2[2 * i + 1] = (f32x2){bflo(aw.y) * inv2 * g.z, bfhi(aw.y) * inv2 * g.w};
;     }
; #pragma unroll
;     for (int i = 0; i < 32; ++i) y[i] = (f32x2){0.f, 0.f};
;     asm volatile("s_waitcnt vmcnt(0)" ::: "memory");
;     const unsigned char* ul = U6 + lane * 16; const unsigned char* vl = V6 + lane * 16;
;     {
; #pragma unroll
;         for (int j = 0; j < 8; ++j) { const int ej = __builtin_amdgcn_readlane(e_lo, j); P11_DMA(ul + (size_t)ej * ROW4, ring + j * ROW4, 2); }
;     }
	v_pk_mul_f32 v[4:5], v[134:135], v[4:5] op_sel_hi:[0,1]
	v_pk_mul_f32 v[210:211], v[210:211], v[2:3]
	v_pk_mul_f32 v[212:213], v[212:213], v[4:5]
	v_lshlrev_b32_e32 v16, 16, v192
	v_and_b32_e32 v17, 0xffff0000, v192
	v_lshlrev_b32_e32 v18, 16, v193
	v_and_b32_e32 v19, 0xffff0000, v193
	v_pk_mul_f32 v[16:17], v[134:135], v[16:17] op_sel_hi:[0,1]
	v_pk_mul_f32 v[18:19], v[134:135], v[18:19] op_sel_hi:[0,1]
	v_pk_mul_f32 v[206:207], v[12:13], v[16:17]
	v_pk_mul_f32 v[208:209], v[14:15], v[18:19]
	v_lshlrev_b32_e32 v2, 16, v190
	v_and_b32_e32 v3, 0xffff0000, v190
	v_lshlrev_b32_e32 v4, 16, v191
	v_and_b32_e32 v5, 0xffff0000, v191
	v_pk_mul_f32 v[2:3], v[134:135], v[2:3] op_sel_hi:[0,1]
	v_pk_mul_f32 v[4:5], v[134:135], v[4:5] op_sel_hi:[0,1]
	v_pk_mul_f32 v[202:203], v[8:9], v[2:3]
	v_pk_mul_f32 v[204:205], v[10:11], v[4:5]
	v_lshlrev_b32_e32 v16, 16, v188
	v_and_b32_e32 v17, 0xffff0000, v188
	v_lshlrev_b32_e32 v18, 16, v189
	v_and_b32_e32 v19, 0xffff0000, v189
	v_pk_mul_f32 v[16:17], v[134:135], v[16:17] op_sel_hi:[0,1]
	v_pk_mul_f32 v[18:19], v[134:135], v[18:19] op_sel_hi:[0,1]
	v_pk_mul_f32 v[198:199], v[140:141], v[16:17]
	v_pk_mul_f32 v[200:201], v[142:143], v[18:19]
	v_lshlrev_b32_e32 v2, 16, v186
	v_and_b32_e32 v3, 0xffff0000, v186
	v_lshlrev_b32_e32 v4, 16, v187
	v_and_b32_e32 v5, 0xffff0000, v187
	v_pk_mul_f32 v[2:3], v[134:135], v[2:3] op_sel_hi:[0,1]
	v_pk_mul_f32 v[4:5], v[134:135], v[4:5] op_sel_hi:[0,1]
	v_pk_mul_f32 v[194:195], v[136:137], v[2:3]
	v_pk_mul_f32 v[196:197], v[138:139], v[4:5]
	v_lshlrev_b32_e32 v16, 16, v184
	v_and_b32_e32 v17, 0xffff0000, v184
	v_lshlrev_b32_e32 v18, 16, v185
	v_and_b32_e32 v19, 0xffff0000, v185
	v_pk_mul_f32 v[16:17], v[134:135], v[16:17] op_sel_hi:[0,1]
	v_pk_mul_f32 v[18:19], v[134:135], v[18:19] op_sel_hi:[0,1]
	v_pk_mul_f32 v[190:191], v[130:131], v[16:17]
	v_pk_mul_f32 v[192:193], v[132:133], v[18:19]
	v_lshlrev_b32_e32 v2, 16, v182
	v_and_b32_e32 v3, 0xffff0000, v182
	v_lshlrev_b32_e32 v4, 16, v183
	v_and_b32_e32 v5, 0xffff0000, v183
	v_pk_mul_f32 v[2:3], v[134:135], v[2:3] op_sel_hi:[0,1]
	v_pk_mul_f32 v[4:5], v[134:135], v[4:5] op_sel_hi:[0,1]
	v_pk_mul_f32 v[186:187], v[126:127], v[2:3]
	v_pk_mul_f32 v[188:189], v[128:129], v[4:5]
	v_lshlrev_b32_e32 v16, 16, v180
	v_and_b32_e32 v17, 0xffff0000, v180
	v_lshlrev_b32_e32 v18, 16, v181
	v_and_b32_e32 v19, 0xffff0000, v181
	v_pk_mul_f32 v[16:17], v[134:135], v[16:17] op_sel_hi:[0,1]
	v_pk_mul_f32 v[18:19], v[134:135], v[18:19] op_sel_hi:[0,1]
	v_pk_mul_f32 v[182:183], v[102:103], v[16:17]
	v_pk_mul_f32 v[184:185], v[104:105], v[18:19]
	v_lshlrev_b32_e32 v2, 16, v178
	v_and_b32_e32 v3, 0xffff0000, v178
	v_lshlrev_b32_e32 v4, 16, v179
	v_and_b32_e32 v5, 0xffff0000, v179
	v_pk_mul_f32 v[2:3], v[134:135], v[2:3] op_sel_hi:[0,1]
	v_pk_mul_f32 v[4:5], v[134:135], v[4:5] op_sel_hi:[0,1]
	v_pk_mul_f32 v[178:179], v[98:99], v[2:3]
	v_pk_mul_f32 v[180:181], v[100:101], v[4:5]
	s_waitcnt vmcnt(0)
	v_mul_f32_e32 v124, v115, v124
	v_mul_f32_e32 v122, v116, v122
	v_mul_f32_e32 v246, v71, v246
	v_mul_f32_e32 v247, v135, v247
	v_readlane_b32 s74, v112, 0
	s_lshr_b32 s74, s74, 8
	s_lshl_b32 s74, s74, 11
	s_mov_b32 s75, 0
	v_lshl_add_u64 v[2:3], v[72:73], 0, s[74:75]
	s_mov_b32 m0, s33
	s_nop 0
	global_load_lds_dwordx4 v[2:3], off
	global_load_lds_dwordx4 v[2:3], off offset:1024
	v_readlane_b32 s74, v112, 1
	s_lshr_b32 s74, s74, 8
	s_lshl_b32 s74, s74, 11
	s_mov_b32 s75, 0
	v_lshl_add_u64 v[2:3], v[72:73], 0, s[74:75]
	s_add_i32 m0, s33, 0x800
	s_nop 0
	global_load_lds_dwordx4 v[2:3], off
	global_load_lds_dwordx4 v[2:3], off offset:1024
	v_readlane_b32 s74, v112, 2
	s_lshr_b32 s74, s74, 8
	s_lshl_b32 s74, s74, 11
	s_mov_b32 s75, 0
	v_lshl_add_u64 v[2:3], v[72:73], 0, s[74:75]
	s_add_i32 m0, s33, 0x1000
	s_nop 0
	global_load_lds_dwordx4 v[2:3], off
	global_load_lds_dwordx4 v[2:3], off offset:1024
	v_readlane_b32 s74, v112, 3
	s_lshr_b32 s74, s74, 8
	s_lshl_b32 s74, s74, 11
	s_mov_b32 s75, 0
	v_lshl_add_u64 v[2:3], v[72:73], 0, s[74:75]
	s_add_i32 m0, s33, 0x1800
	s_nop 0
	global_load_lds_dwordx4 v[2:3], off
	global_load_lds_dwordx4 v[2:3], off offset:1024
	v_readlane_b32 s74, v112, 4
	s_lshr_b32 s74, s74, 8
	s_lshl_b32 s74, s74, 11
	s_mov_b32 s75, 0
	v_lshl_add_u64 v[2:3], v[72:73], 0, s[74:75]
	s_add_i32 m0, s33, 0x2000
	s_nop 0
	global_load_lds_dwordx4 v[2:3], off
	global_load_lds_dwordx4 v[2:3], off offset:1024
	v_readlane_b32 s74, v112, 5
	s_lshr_b32 s74, s74, 8
	s_lshl_b32 s74, s74, 11
	s_mov_b32 s75, 0
	v_lshl_add_u64 v[2:3], v[72:73], 0, s[74:75]
	s_add_i32 m0, s33, 0x2800
	s_nop 0
	global_load_lds_dwordx4 v[2:3], off
	global_load_lds_dwordx4 v[2:3], off offset:1024
	v_readlane_b32 s74, v112, 6
	s_lshr_b32 s74, s74, 8
	s_lshl_b32 s74, s74, 11
	s_mov_b32 s75, 0
	v_lshl_add_u64 v[2:3], v[72:73], 0, s[74:75]
	s_add_i32 m0, s33, 0x3000
	s_nop 0
	global_load_lds_dwordx4 v[2:3], off
	global_load_lds_dwordx4 v[2:3], off offset:1024
	v_readlane_b32 s74, v112, 7
	s_lshr_b32 s74, s74, 8
	s_lshl_b32 s74, s74, 11
	s_mov_b32 s75, 0
	v_lshl_add_u64 v[2:3], v[72:73], 0, s[74:75]
	s_add_i32 m0, s33, 0x3800
	s_nop 0
	global_load_lds_dwordx4 v[2:3], off
	global_load_lds_dwordx4 v[2:3], off offset:1024
	s_mov_b32 s46, 0
	s_waitcnt vmcnt(14)
	v_add_u32_e32 v4, s33, v70
	ds_read_b128 v[98:101], v4
	ds_read_b128 v[102:105], v4 offset:1024
	v_readlane_b32 s78, v112, 8
	s_lshr_b32 s78, s78, 8
	s_lshl_b32 s78, s78, 11
	s_mov_b32 s79, 0
	v_lshl_add_u64 v[2:3], v[72:73], 0, s[78:79]
	s_waitcnt lgkmcnt(0)
	s_mov_b32 m0, s33
	s_nop 0
	global_load_lds_dwordx4 v[2:3], off
	global_load_lds_dwordx4 v[2:3], off offset:1024
	v_mov_b32_e32 v6, 0
; DI void peer_token(LAS unsigned char* ring, const bf16* x1row, float inv2, const float* nffn, const int* ex, const float* pg, const unsigned char* U6, const unsigned char* V6,
;                    const float* usc, const float* vsc, float* orow, int lane) {
;     ...
; #pragma unroll 2
;     for (int k = 0; k < 56; ++k) P11_U(k, us_lo, gv_lo, cf_lo, ul, e_lo, k + 8);
; #pragma unroll 1
;     for (int k = 56; k < 64; ++k) P11_U(k, us_lo, gv_lo, cf_lo, ul, e_hi, k - 56);
; #pragma unroll 2
;     for (int k = 64; k < 120; ++k) P11_U(k, us_hi, gv_hi, cf_hi, ul, e_hi, k - 56);
; #pragma unroll 1
;     for (int k = 120; k < 128; ++k) P11_U(k, us_hi, gv_hi, cf_hi, vl, e_lo, k - 120);
.Lpu0_even:
	s_bitcmp1_b64 s[100:101], s46
	s_cbranch_scc1 .Lpu0_evenB
	s_add_i32 s47, s46, 1
	s_and_b32 s47, s47, 7
	s_lshl_b32 s47, s47, 11
	s_add_i32 s77, s33, s47
	v_add_u32_e32 v4, s77, v70
	s_add_i32 s78, s46, 9
	s_and_b32 s75, s78, 63
	v_readlane_b32 s79, v113, s75
	v_readlane_b32 s47, v112, s75
	s_bitcmp1_b32 s78, 6
	s_cselect_b32 s47, s79, s47
	s_lshr_b32 s47, s47, 8
	s_lshl_b32 s47, s47, 11
	s_bitcmp1_b32 s78, 8
	s_cselect_b32 s78, s98, 0
	s_cselect_b32 s79, s99, 0
	s_add_u32 s78, s78, s47
	s_addc_u32 s79, s79, 0
	s_add_i32 s32, s46, 0
	s_waitcnt vmcnt(14)
	ds_read_b128 v[126:129], v4
	ds_read_b128 v[130:133], v4 offset:1024
	v_lshl_add_u64 v[2:3], v[72:73], 0, s[78:79]
	v_cvt_scalef32_pk_f32_fp4 v[136:137], v98, 1.0
	v_cvt_scalef32_pk_f32_fp4 v[138:139], v98, 1.0 op_sel:[1,0,0]
	v_cvt_scalef32_pk_f32_fp4 v[140:141], v98, 1.0 op_sel:[0,1,0]
	v_cvt_scalef32_pk_f32_fp4 v[142:143], v98, 1.0 op_sel:[1,1,0]
	v_add_f32_dpp v6, v6, v6 quad_perm:[1,0,3,2] row_mask:0xf bank_mask:0xf bound_ctrl:1
	v_pk_fma_f32 v[8:9], v[20:21], v[136:137], 0 op_sel_hi:[1,1,0]
	v_pk_fma_f32 v[10:11], v[22:23], v[138:139], 0 op_sel_hi:[1,1,0]
	v_pk_fma_f32 v[12:13], v[24:25], v[140:141], 0 op_sel_hi:[1,1,0]
	v_pk_fma_f32 v[14:15], v[26:27], v[142:143], 0 op_sel_hi:[1,1,0]
	v_add_f32_dpp v6, v6, v6 quad_perm:[2,3,0,1] row_mask:0xf bank_mask:0xf bound_ctrl:1
	v_cvt_scalef32_pk_f32_fp4 v[136:137], v99, 1.0
	v_cvt_scalef32_pk_f32_fp4 v[138:139], v99, 1.0 op_sel:[1,0,0]
	v_cvt_scalef32_pk_f32_fp4 v[140:141], v99, 1.0 op_sel:[0,1,0]
	v_cvt_scalef32_pk_f32_fp4 v[142:143], v99, 1.0 op_sel:[1,1,0]
	v_add_f32_dpp v6, v6, v6 row_half_mirror row_mask:0xf bank_mask:0xf bound_ctrl:1
	v_pk_fma_f32 v[8:9], v[28:29], v[136:137], v[8:9]
	v_pk_fma_f32 v[10:11], v[30:31], v[138:139], v[10:11]
	v_pk_fma_f32 v[12:13], v[32:33], v[140:141], v[12:13]
	v_pk_fma_f32 v[14:15], v[34:35], v[142:143], v[14:15]
	v_mov_b32_e32 v7, 0
	v_cvt_scalef32_pk_f32_fp4 v[136:137], v100, 1.0
	v_cvt_scalef32_pk_f32_fp4 v[138:139], v100, 1.0 op_sel:[1,0,0]
	v_cvt_scalef32_pk_f32_fp4 v[140:141], v100, 1.0 op_sel:[0,1,0]
	v_cvt_scalef32_pk_f32_fp4 v[142:143], v100, 1.0 op_sel:[1,1,0]
	v_add_f32_dpp v6, v6, v6 row_mirror row_mask:0xf bank_mask:0xf bound_ctrl:1
	v_pk_fma_f32 v[8:9], v[36:37], v[136:137], v[8:9]
	v_pk_fma_f32 v[10:11], v[38:39], v[138:139], v[10:11]
	v_pk_fma_f32 v[12:13], v[40:41], v[140:141], v[12:13]
	v_pk_fma_f32 v[14:15], v[42:43], v[142:143], v[14:15]
	s_waitcnt lgkmcnt(0)
	s_mov_b32 m0, s77
	s_nop 0
	global_load_lds_dwordx4 v[2:3], off
	global_load_lds_dwordx4 v[2:3], off offset:1024
	v_cvt_scalef32_pk_f32_fp4 v[136:137], v101, 1.0
	v_cvt_scalef32_pk_f32_fp4 v[138:139], v101, 1.0 op_sel:[1,0,0]
	v_cvt_scalef32_pk_f32_fp4 v[140:141], v101, 1.0 op_sel:[0,1,0]
	v_cvt_scalef32_pk_f32_fp4 v[142:143], v101, 1.0 op_sel:[1,1,0]
	v_mov_b32_dpp v7, v6 row_bcast:15 row_mask:0xa bank_mask:0xf
	v_pk_fma_f32 v[8:9], v[44:45], v[136:137], v[8:9]
	v_pk_fma_f32 v[10:11], v[46:47], v[138:139], v[10:11]
	v_pk_fma_f32 v[12:13], v[48:49], v[140:141], v[12:13]
	v_pk_fma_f32 v[14:15], v[50:51], v[142:143], v[14:15]
	v_add_f32_e32 v6, v6, v7
	v_cvt_scalef32_pk_f32_fp4 v[136:137], v102, 1.0
	v_cvt_scalef32_pk_f32_fp4 v[138:139], v102, 1.0 op_sel:[1,0,0]
	v_cvt_scalef32_pk_f32_fp4 v[140:141], v102, 1.0 op_sel:[0,1,0]
	v_cvt_scalef32_pk_f32_fp4 v[142:143], v102, 1.0 op_sel:[1,1,0]
	v_mov_b32_e32 v7, 0
	v_pk_fma_f32 v[8:9], v[52:53], v[136:137], v[8:9]
	v_pk_fma_f32 v[10:11], v[54:55], v[138:139], v[10:11]
	v_pk_fma_f32 v[12:13], v[56:57], v[140:141], v[12:13]
	v_pk_fma_f32 v[14:15], v[58:59], v[142:143], v[14:15]
	v_mov_b32_dpp v7, v6 row_bcast:31 row_mask:0xc bank_mask:0xf
	v_cvt_scalef32_pk_f32_fp4 v[136:137], v103, 1.0
	v_cvt_scalef32_pk_f32_fp4 v[138:139], v103, 1.0 op_sel:[1,0,0]
	v_cvt_scalef32_pk_f32_fp4 v[140:141], v103, 1.0 op_sel:[0,1,0]
	v_cvt_scalef32_pk_f32_fp4 v[142:143], v103, 1.0 op_sel:[1,1,0]
	v_add_f32_e32 v6, v6, v7
	v_pk_fma_f32 v[8:9], v[60:61], v[136:137], v[8:9]
	v_pk_fma_f32 v[10:11], v[62:63], v[138:139], v[10:11]
	v_pk_fma_f32 v[12:13], v[64:65], v[140:141], v[12:13]
	v_pk_fma_f32 v[14:15], v[80:81], v[142:143], v[14:15]
	v_readlane_b32 s74, v6, 63
	v_cvt_scalef32_pk_f32_fp4 v[136:137], v104, 1.0
	v_cvt_scalef32_pk_f32_fp4 v[138:139], v104, 1.0 op_sel:[1,0,0]
	v_cvt_scalef32_pk_f32_fp4 v[140:141], v104, 1.0 op_sel:[0,1,0]
	v_cvt_scalef32_pk_f32_fp4 v[142:143], v104, 1.0 op_sel:[1,1,0]
	s_lshl_b64 exec, 1, s32
	v_mov_b32_e32 v120, s74
	s_mov_b64 exec, -1
	v_pk_fma_f32 v[8:9], v[82:83], v[136:137], v[8:9]
	v_pk_fma_f32 v[10:11], v[84:85], v[138:139], v[10:11]
	v_pk_fma_f32 v[12:13], v[86:87], v[140:141], v[12:13]
	v_pk_fma_f32 v[14:15], v[88:89], v[142:143], v[14:15]
	v_cvt_scalef32_pk_f32_fp4 v[136:137], v105, 1.0
	v_cvt_scalef32_pk_f32_fp4 v[138:139], v105, 1.0 op_sel:[1,0,0]
	v_cvt_scalef32_pk_f32_fp4 v[140:141], v105, 1.0 op_sel:[0,1,0]
	v_cvt_scalef32_pk_f32_fp4 v[142:143], v105, 1.0 op_sel:[1,1,0]
	v_pk_fma_f32 v[8:9], v[90:91], v[136:137], v[8:9]
	v_pk_fma_f32 v[10:11], v[92:93], v[138:139], v[10:11]
	v_pk_fma_f32 v[12:13], v[94:95], v[140:141], v[12:13]
	v_pk_fma_f32 v[14:15], v[96:97], v[142:143], v[14:15]
	v_pk_add_f32 v[8:9], v[8:9], v[10:11]
	v_pk_add_f32 v[12:13], v[12:13], v[14:15]
	v_pk_add_f32 v[8:9], v[8:9], v[12:13]
	v_add_f32_e32 v5, v8, v9
	s_branch .Lpu0_odd
; DI void peer_token(LAS unsigned char* ring, const bf16* x1row, float inv2, const float* nffn, const int* ex, const float* pg, const unsigned char* U6, const unsigned char* V6,
;                    const float* usc, const float* vsc, float* orow, int lane) {
;     ...
; #pragma unroll 2
;     for (int k = 0; k < 56; ++k) P11_U(k, us_lo, gv_lo, cf_lo, ul, e_lo, k + 8);
; #pragma unroll 1
;     for (int k = 56; k < 64; ++k) P11_U(k, us_lo, gv_lo, cf_lo, ul, e_hi, k - 56);
; #pragma unroll 2
;     for (int k = 64; k < 120; ++k) P11_U(k, us_hi, gv_hi, cf_hi, ul, e_hi, k - 56);
; #pragma unroll 1
;     for (int k = 120; k < 128; ++k) P11_U(k, us_hi, gv_hi, cf_hi, vl, e_lo, k - 120);
.Lpu0_evenB:
	s_add_i32 s47, s46, 1
	s_and_b32 s47, s47, 7
	s_lshl_b32 s47, s47, 11
	s_add_i32 s77, s33, s47
	v_add_u32_e32 v4, s77, v70
	s_add_i32 s78, s46, 9
	s_and_b32 s75, s78, 63
	v_readlane_b32 s79, v113, s75
	v_readlane_b32 s47, v112, s75
	s_bitcmp1_b32 s78, 6
	s_cselect_b32 s47, s79, s47
	s_lshr_b32 s47, s47, 8
	s_lshl_b32 s47, s47, 11
	s_bitcmp1_b32 s78, 8
	s_cselect_b32 s78, s98, 0
	s_cselect_b32 s79, s99, 0
	s_add_u32 s78, s78, s47
	s_addc_u32 s79, s79, 0
	s_add_i32 s32, s46, 0
	s_waitcnt vmcnt(14)
	ds_read_b128 v[126:129], v4
	ds_read_b128 v[130:133], v4 offset:1024
	v_lshl_add_u64 v[2:3], v[72:73], 0, s[78:79]
	v_cvt_scalef32_pk_f32_fp4 v[136:137], v98, 1.0
	v_cvt_scalef32_pk_f32_fp4 v[138:139], v98, 1.0 op_sel:[1,0,0]
	v_cvt_scalef32_pk_f32_fp4 v[140:141], v98, 1.0 op_sel:[0,1,0]
	v_cvt_scalef32_pk_f32_fp4 v[142:143], v98, 1.0 op_sel:[1,1,0]
	v_add_f32_dpp v6, v6, v6 quad_perm:[1,0,3,2] row_mask:0xf bank_mask:0xf bound_ctrl:1
	v_pk_fma_f32 v[8:9], v[178:179], v[136:137], 0 op_sel_hi:[1,1,0]
	v_pk_fma_f32 v[10:11], v[180:181], v[138:139], 0 op_sel_hi:[1,1,0]
	v_pk_fma_f32 v[12:13], v[182:183], v[140:141], 0 op_sel_hi:[1,1,0]
	v_pk_fma_f32 v[14:15], v[184:185], v[142:143], 0 op_sel_hi:[1,1,0]
	v_add_f32_dpp v6, v6, v6 quad_perm:[2,3,0,1] row_mask:0xf bank_mask:0xf bound_ctrl:1
	v_cvt_scalef32_pk_f32_fp4 v[136:137], v99, 1.0
	v_cvt_scalef32_pk_f32_fp4 v[138:139], v99, 1.0 op_sel:[1,0,0]
	v_cvt_scalef32_pk_f32_fp4 v[140:141], v99, 1.0 op_sel:[0,1,0]
	v_cvt_scalef32_pk_f32_fp4 v[142:143], v99, 1.0 op_sel:[1,1,0]
	v_add_f32_dpp v6, v6, v6 row_half_mirror row_mask:0xf bank_mask:0xf bound_ctrl:1
	v_pk_fma_f32 v[8:9], v[186:187], v[136:137], v[8:9]
	v_pk_fma_f32 v[10:11], v[188:189], v[138:139], v[10:11]
	v_pk_fma_f32 v[12:13], v[190:191], v[140:141], v[12:13]
	v_pk_fma_f32 v[14:15], v[192:193], v[142:143], v[14:15]
	v_mov_b32_e32 v7, 0
	v_cvt_scalef32_pk_f32_fp4 v[136:137], v100, 1.0
	v_cvt_scalef32_pk_f32_fp4 v[138:139], v100, 1.0 op_sel:[1,0,0]
	v_cvt_scalef32_pk_f32_fp4 v[140:141], v100, 1.0 op_sel:[0,1,0]
	v_cvt_scalef32_pk_f32_fp4 v[142:143], v100, 1.0 op_sel:[1,1,0]
	v_add_f32_dpp v6, v6, v6 row_mirror row_mask:0xf bank_mask:0xf bound_ctrl:1
	v_pk_fma_f32 v[8:9], v[194:195], v[136:137], v[8:9]
	v_pk_fma_f32 v[10:11], v[196:197], v[138:139], v[10:11]
	v_pk_fma_f32 v[12:13], v[198:199], v[140:141], v[12:13]
	v_pk_fma_f32 v[14:15], v[200:201], v[142:143], v[14:15]
	s_waitcnt lgkmcnt(0)
	s_mov_b32 m0, s77
	s_nop 0
	global_load_lds_dwordx4 v[2:3], off
	global_load_lds_dwordx4 v[2:3], off offset:1024
	v_cvt_scalef32_pk_f32_fp4 v[136:137], v101, 1.0
	v_cvt_scalef32_pk_f32_fp4 v[138:139], v101, 1.0 op_sel:[1,0,0]
	v_cvt_scalef32_pk_f32_fp4 v[140:141], v101, 1.0 op_sel:[0,1,0]
	v_cvt_scalef32_pk_f32_fp4 v[142:143], v101, 1.0 op_sel:[1,1,0]
	v_mov_b32_dpp v7, v6 row_bcast:15 row_mask:0xa bank_mask:0xf
	v_pk_fma_f32 v[8:9], v[202:203], v[136:137], v[8:9]
	v_pk_fma_f32 v[10:11], v[204:205], v[138:139], v[10:11]
	v_pk_fma_f32 v[12:13], v[206:207], v[140:141], v[12:13]
	v_pk_fma_f32 v[14:15], v[208:209], v[142:143], v[14:15]
	v_add_f32_e32 v6, v6, v7
	v_cvt_scalef32_pk_f32_fp4 v[136:137], v102, 1.0
	v_cvt_scalef32_pk_f32_fp4 v[138:139], v102, 1.0 op_sel:[1,0,0]
	v_cvt_scalef32_pk_f32_fp4 v[140:141], v102, 1.0 op_sel:[0,1,0]
	v_cvt_scalef32_pk_f32_fp4 v[142:143], v102, 1.0 op_sel:[1,1,0]
	v_mov_b32_e32 v7, 0
	v_pk_fma_f32 v[8:9], v[210:211], v[136:137], v[8:9]
	v_pk_fma_f32 v[10:11], v[212:213], v[138:139], v[10:11]
	v_pk_fma_f32 v[12:13], v[214:215], v[140:141], v[12:13]
	v_pk_fma_f32 v[14:15], v[216:217], v[142:143], v[14:15]
	v_mov_b32_dpp v7, v6 row_bcast:31 row_mask:0xc bank_mask:0xf
	v_cvt_scalef32_pk_f32_fp4 v[136:137], v103, 1.0
	v_cvt_scalef32_pk_f32_fp4 v[138:139], v103, 1.0 op_sel:[1,0,0]
	v_cvt_scalef32_pk_f32_fp4 v[140:141], v103, 1.0 op_sel:[0,1,0]
	v_cvt_scalef32_pk_f32_fp4 v[142:143], v103, 1.0 op_sel:[1,1,0]
	v_add_f32_e32 v6, v6, v7
	v_pk_fma_f32 v[8:9], v[218:219], v[136:137], v[8:9]
	v_pk_fma_f32 v[10:11], v[220:221], v[138:139], v[10:11]
	v_pk_fma_f32 v[12:13], v[222:223], v[140:141], v[12:13]
	v_pk_fma_f32 v[14:15], v[224:225], v[142:143], v[14:15]
	v_readlane_b32 s74, v6, 63
	v_cvt_scalef32_pk_f32_fp4 v[136:137], v104, 1.0
	v_cvt_scalef32_pk_f32_fp4 v[138:139], v104, 1.0 op_sel:[1,0,0]
	v_cvt_scalef32_pk_f32_fp4 v[140:141], v104, 1.0 op_sel:[0,1,0]
	v_cvt_scalef32_pk_f32_fp4 v[142:143], v104, 1.0 op_sel:[1,1,0]
	s_lshl_b64 exec, 1, s32
	v_mov_b32_e32 v120, s74
	s_mov_b64 exec, -1
	v_pk_fma_f32 v[8:9], v[226:227], v[136:137], v[8:9]
	v_pk_fma_f32 v[10:11], v[228:229], v[138:139], v[10:11]
	v_pk_fma_f32 v[12:13], v[230:231], v[140:141], v[12:13]
	v_pk_fma_f32 v[14:15], v[232:233], v[142:143], v[14:15]
	v_cvt_scalef32_pk_f32_fp4 v[136:137], v105, 1.0
	v_cvt_scalef32_pk_f32_fp4 v[138:139], v105, 1.0 op_sel:[1,0,0]
	v_cvt_scalef32_pk_f32_fp4 v[140:141], v105, 1.0 op_sel:[0,1,0]
	v_cvt_scalef32_pk_f32_fp4 v[142:143], v105, 1.0 op_sel:[1,1,0]
	v_pk_fma_f32 v[8:9], v[234:235], v[136:137], v[8:9]
	v_pk_fma_f32 v[10:11], v[236:237], v[138:139], v[10:11]
	v_pk_fma_f32 v[12:13], v[238:239], v[140:141], v[12:13]
	v_pk_fma_f32 v[14:15], v[240:241], v[142:143], v[14:15]
	v_pk_add_f32 v[8:9], v[8:9], v[10:11]
	v_pk_add_f32 v[12:13], v[12:13], v[14:15]
	v_pk_add_f32 v[8:9], v[8:9], v[12:13]
	v_add_f32_e32 v5, v8, v9
; DI void peer_token(LAS unsigned char* ring, const bf16* x1row, float inv2, const float* nffn, const int* ex, const float* pg, const unsigned char* U6, const unsigned char* V6,
;                    const float* usc, const float* vsc, float* orow, int lane) {
;     ...
; #pragma unroll 2
;     for (int k = 0; k < 56; ++k) P11_U(k, us_lo, gv_lo, cf_lo, ul, e_lo, k + 8);
; #pragma unroll 1
;     for (int k = 56; k < 64; ++k) P11_U(k, us_lo, gv_lo, cf_lo, ul, e_hi, k - 56);
; #pragma unroll 2
;     for (int k = 64; k < 120; ++k) P11_U(k, us_hi, gv_hi, cf_hi, ul, e_hi, k - 56);
; #pragma unroll 1
;     for (int k = 120; k < 128; ++k) P11_U(k, us_hi, gv_hi, cf_hi, vl, e_lo, k - 120);
.Lpu0_odd:
	s_add_i32 s32, s46, 1
	s_bitcmp1_b64 s[100:101], s32
	s_cbranch_scc1 .Lpu0_oddB
	s_add_i32 s47, s46, 2
	s_and_b32 s47, s47, 7
	s_lshl_b32 s47, s47, 11
	s_add_i32 s77, s33, s47
	v_add_u32_e32 v4, s77, v70
	s_add_i32 s78, s46, 10
	s_and_b32 s75, s78, 63
	v_readlane_b32 s79, v113, s75
	v_readlane_b32 s47, v112, s75
	s_bitcmp1_b32 s78, 6
	s_cselect_b32 s47, s79, s47
	s_lshr_b32 s47, s47, 8
	s_lshl_b32 s47, s47, 11
	s_bitcmp1_b32 s78, 8
	s_cselect_b32 s78, s98, 0
	s_cselect_b32 s79, s99, 0
	s_add_u32 s78, s78, s47
	s_addc_u32 s79, s79, 0
	s_add_i32 s32, s46, 1
	s_waitcnt vmcnt(14)
	ds_read_b128 v[98:101], v4
	ds_read_b128 v[102:105], v4 offset:1024
	v_lshl_add_u64 v[2:3], v[72:73], 0, s[78:79]
	v_cvt_scalef32_pk_f32_fp4 v[136:137], v126, 1.0
	v_cvt_scalef32_pk_f32_fp4 v[138:139], v126, 1.0 op_sel:[1,0,0]
	v_cvt_scalef32_pk_f32_fp4 v[140:141], v126, 1.0 op_sel:[0,1,0]
	v_cvt_scalef32_pk_f32_fp4 v[142:143], v126, 1.0 op_sel:[1,1,0]
	v_add_f32_dpp v5, v5, v5 quad_perm:[1,0,3,2] row_mask:0xf bank_mask:0xf bound_ctrl:1
	v_pk_fma_f32 v[8:9], v[20:21], v[136:137], 0 op_sel_hi:[1,1,0]
	v_pk_fma_f32 v[10:11], v[22:23], v[138:139], 0 op_sel_hi:[1,1,0]
	v_pk_fma_f32 v[12:13], v[24:25], v[140:141], 0 op_sel_hi:[1,1,0]
	v_pk_fma_f32 v[14:15], v[26:27], v[142:143], 0 op_sel_hi:[1,1,0]
	v_add_f32_dpp v5, v5, v5 quad_perm:[2,3,0,1] row_mask:0xf bank_mask:0xf bound_ctrl:1
	v_cvt_scalef32_pk_f32_fp4 v[136:137], v127, 1.0
	v_cvt_scalef32_pk_f32_fp4 v[138:139], v127, 1.0 op_sel:[1,0,0]
	v_cvt_scalef32_pk_f32_fp4 v[140:141], v127, 1.0 op_sel:[0,1,0]
	v_cvt_scalef32_pk_f32_fp4 v[142:143], v127, 1.0 op_sel:[1,1,0]
	v_add_f32_dpp v5, v5, v5 row_half_mirror row_mask:0xf bank_mask:0xf bound_ctrl:1
	v_pk_fma_f32 v[8:9], v[28:29], v[136:137], v[8:9]
	v_pk_fma_f32 v[10:11], v[30:31], v[138:139], v[10:11]
	v_pk_fma_f32 v[12:13], v[32:33], v[140:141], v[12:13]
	v_pk_fma_f32 v[14:15], v[34:35], v[142:143], v[14:15]
	v_mov_b32_e32 v7, 0
	v_cvt_scalef32_pk_f32_fp4 v[136:137], v128, 1.0
	v_cvt_scalef32_pk_f32_fp4 v[138:139], v128, 1.0 op_sel:[1,0,0]
	v_cvt_scalef32_pk_f32_fp4 v[140:141], v128, 1.0 op_sel:[0,1,0]
	v_cvt_scalef32_pk_f32_fp4 v[142:143], v128, 1.0 op_sel:[1,1,0]
	v_add_f32_dpp v5, v5, v5 row_mirror row_mask:0xf bank_mask:0xf bound_ctrl:1
	v_pk_fma_f32 v[8:9], v[36:37], v[136:137], v[8:9]
	v_pk_fma_f32 v[10:11], v[38:39], v[138:139], v[10:11]
	v_pk_fma_f32 v[12:13], v[40:41], v[140:141], v[12:13]
	v_pk_fma_f32 v[14:15], v[42:43], v[142:143], v[14:15]
	s_waitcnt lgkmcnt(0)
	s_mov_b32 m0, s77
	s_nop 0
	global_load_lds_dwordx4 v[2:3], off
	global_load_lds_dwordx4 v[2:3], off offset:1024
	v_cvt_scalef32_pk_f32_fp4 v[136:137], v129, 1.0
	v_cvt_scalef32_pk_f32_fp4 v[138:139], v129, 1.0 op_sel:[1,0,0]
	v_cvt_scalef32_pk_f32_fp4 v[140:141], v129, 1.0 op_sel:[0,1,0]
	v_cvt_scalef32_pk_f32_fp4 v[142:143], v129, 1.0 op_sel:[1,1,0]
	v_mov_b32_dpp v7, v5 row_bcast:15 row_mask:0xa bank_mask:0xf
	v_pk_fma_f32 v[8:9], v[44:45], v[136:137], v[8:9]
	v_pk_fma_f32 v[10:11], v[46:47], v[138:139], v[10:11]
	v_pk_fma_f32 v[12:13], v[48:49], v[140:141], v[12:13]
	v_pk_fma_f32 v[14:15], v[50:51], v[142:143], v[14:15]
	v_add_f32_e32 v5, v5, v7
	v_cvt_scalef32_pk_f32_fp4 v[136:137], v130, 1.0
	v_cvt_scalef32_pk_f32_fp4 v[138:139], v130, 1.0 op_sel:[1,0,0]
	v_cvt_scalef32_pk_f32_fp4 v[140:141], v130, 1.0 op_sel:[0,1,0]
	v_cvt_scalef32_pk_f32_fp4 v[142:143], v130, 1.0 op_sel:[1,1,0]
	v_mov_b32_e32 v7, 0
	v_pk_fma_f32 v[8:9], v[52:53], v[136:137], v[8:9]
	v_pk_fma_f32 v[10:11], v[54:55], v[138:139], v[10:11]
	v_pk_fma_f32 v[12:13], v[56:57], v[140:141], v[12:13]
	v_pk_fma_f32 v[14:15], v[58:59], v[142:143], v[14:15]
	v_mov_b32_dpp v7, v5 row_bcast:31 row_mask:0xc bank_mask:0xf
	v_cvt_scalef32_pk_f32_fp4 v[136:137], v131, 1.0
	v_cvt_scalef32_pk_f32_fp4 v[138:139], v131, 1.0 op_sel:[1,0,0]
	v_cvt_scalef32_pk_f32_fp4 v[140:141], v131, 1.0 op_sel:[0,1,0]
	v_cvt_scalef32_pk_f32_fp4 v[142:143], v131, 1.0 op_sel:[1,1,0]
	v_add_f32_e32 v5, v5, v7
	v_pk_fma_f32 v[8:9], v[60:61], v[136:137], v[8:9]
	v_pk_fma_f32 v[10:11], v[62:63], v[138:139], v[10:11]
	v_pk_fma_f32 v[12:13], v[64:65], v[140:141], v[12:13]
	v_pk_fma_f32 v[14:15], v[80:81], v[142:143], v[14:15]
	v_readlane_b32 s74, v5, 63
	v_cvt_scalef32_pk_f32_fp4 v[136:137], v132, 1.0
	v_cvt_scalef32_pk_f32_fp4 v[138:139], v132, 1.0 op_sel:[1,0,0]
	v_cvt_scalef32_pk_f32_fp4 v[140:141], v132, 1.0 op_sel:[0,1,0]
	v_cvt_scalef32_pk_f32_fp4 v[142:143], v132, 1.0 op_sel:[1,1,0]
	s_lshl_b64 exec, 1, s32
	v_mov_b32_e32 v120, s74
	s_mov_b64 exec, -1
	v_pk_fma_f32 v[8:9], v[82:83], v[136:137], v[8:9]
	v_pk_fma_f32 v[10:11], v[84:85], v[138:139], v[10:11]
	v_pk_fma_f32 v[12:13], v[86:87], v[140:141], v[12:13]
	v_pk_fma_f32 v[14:15], v[88:89], v[142:143], v[14:15]
	v_cvt_scalef32_pk_f32_fp4 v[136:137], v133, 1.0
	v_cvt_scalef32_pk_f32_fp4 v[138:139], v133, 1.0 op_sel:[1,0,0]
	v_cvt_scalef32_pk_f32_fp4 v[140:141], v133, 1.0 op_sel:[0,1,0]
	v_cvt_scalef32_pk_f32_fp4 v[142:143], v133, 1.0 op_sel:[1,1,0]
	v_pk_fma_f32 v[8:9], v[90:91], v[136:137], v[8:9]
	v_pk_fma_f32 v[10:11], v[92:93], v[138:139], v[10:11]
	v_pk_fma_f32 v[12:13], v[94:95], v[140:141], v[12:13]
	v_pk_fma_f32 v[14:15], v[96:97], v[142:143], v[14:15]
	v_pk_add_f32 v[8:9], v[8:9], v[10:11]
	v_pk_add_f32 v[12:13], v[12:13], v[14:15]
	v_pk_add_f32 v[8:9], v[8:9], v[12:13]
	v_add_f32_e32 v6, v8, v9
	s_branch .Lpu0_next
; DI void peer_token(LAS unsigned char* ring, const bf16* x1row, float inv2, const float* nffn, const int* ex, const float* pg, const unsigned char* U6, const unsigned char* V6,
;                    const float* usc, const float* vsc, float* orow, int lane) {
;     ...
; #pragma unroll 2
;     for (int k = 0; k < 56; ++k) P11_U(k, us_lo, gv_lo, cf_lo, ul, e_lo, k + 8);
; #pragma unroll 1
;     for (int k = 56; k < 64; ++k) P11_U(k, us_lo, gv_lo, cf_lo, ul, e_hi, k - 56);
; #pragma unroll 2
;     for (int k = 64; k < 120; ++k) P11_U(k, us_hi, gv_hi, cf_hi, ul, e_hi, k - 56);
; #pragma unroll 1
;     for (int k = 120; k < 128; ++k) P11_U(k, us_hi, gv_hi, cf_hi, vl, e_lo, k - 120);
.Lpu0_oddB:
	s_add_i32 s47, s46, 2
	s_and_b32 s47, s47, 7
	s_lshl_b32 s47, s47, 11
	s_add_i32 s77, s33, s47
	v_add_u32_e32 v4, s77, v70
	s_add_i32 s78, s46, 10
	s_and_b32 s75, s78, 63
	v_readlane_b32 s79, v113, s75
	v_readlane_b32 s47, v112, s75
	s_bitcmp1_b32 s78, 6
	s_cselect_b32 s47, s79, s47
	s_lshr_b32 s47, s47, 8
	s_lshl_b32 s47, s47, 11
	s_bitcmp1_b32 s78, 8
	s_cselect_b32 s78, s98, 0
	s_cselect_b32 s79, s99, 0
	s_add_u32 s78, s78, s47
	s_addc_u32 s79, s79, 0
	s_add_i32 s32, s46, 1
	s_waitcnt vmcnt(14)
	ds_read_b128 v[98:101], v4
	ds_read_b128 v[102:105], v4 offset:1024
	v_lshl_add_u64 v[2:3], v[72:73], 0, s[78:79]
	v_cvt_scalef32_pk_f32_fp4 v[136:137], v126, 1.0
	v_cvt_scalef32_pk_f32_fp4 v[138:139], v126, 1.0 op_sel:[1,0,0]
	v_cvt_scalef32_pk_f32_fp4 v[140:141], v126, 1.0 op_sel:[0,1,0]
	v_cvt_scalef32_pk_f32_fp4 v[142:143], v126, 1.0 op_sel:[1,1,0]
	v_add_f32_dpp v5, v5, v5 quad_perm:[1,0,3,2] row_mask:0xf bank_mask:0xf bound_ctrl:1
	v_pk_fma_f32 v[8:9], v[178:179], v[136:137], 0 op_sel_hi:[1,1,0]
	v_pk_fma_f32 v[10:11], v[180:181], v[138:139], 0 op_sel_hi:[1,1,0]
	v_pk_fma_f32 v[12:13], v[182:183], v[140:141], 0 op_sel_hi:[1,1,0]
	v_pk_fma_f32 v[14:15], v[184:185], v[142:143], 0 op_sel_hi:[1,1,0]
	v_add_f32_dpp v5, v5, v5 quad_perm:[2,3,0,1] row_mask:0xf bank_mask:0xf bound_ctrl:1
	v_cvt_scalef32_pk_f32_fp4 v[136:137], v127, 1.0
	v_cvt_scalef32_pk_f32_fp4 v[138:139], v127, 1.0 op_sel:[1,0,0]
	v_cvt_scalef32_pk_f32_fp4 v[140:141], v127, 1.0 op_sel:[0,1,0]
	v_cvt_scalef32_pk_f32_fp4 v[142:143], v127, 1.0 op_sel:[1,1,0]
	v_add_f32_dpp v5, v5, v5 row_half_mirror row_mask:0xf bank_mask:0xf bound_ctrl:1
	v_pk_fma_f32 v[8:9], v[186:187], v[136:137], v[8:9]
	v_pk_fma_f32 v[10:11], v[188:189], v[138:139], v[10:11]
	v_pk_fma_f32 v[12:13], v[190:191], v[140:141], v[12:13]
	v_pk_fma_f32 v[14:15], v[192:193], v[142:143], v[14:15]
	v_mov_b32_e32 v7, 0
	v_cvt_scalef32_pk_f32_fp4 v[136:137], v128, 1.0
	v_cvt_scalef32_pk_f32_fp4 v[138:139], v128, 1.0 op_sel:[1,0,0]
	v_cvt_scalef32_pk_f32_fp4 v[140:141], v128, 1.0 op_sel:[0,1,0]
	v_cvt_scalef32_pk_f32_fp4 v[142:143], v128, 1.0 op_sel:[1,1,0]
	v_add_f32_dpp v5, v5, v5 row_mirror row_mask:0xf bank_mask:0xf bound_ctrl:1
	v_pk_fma_f32 v[8:9], v[194:195], v[136:137], v[8:9]
	v_pk_fma_f32 v[10:11], v[196:197], v[138:139], v[10:11]
	v_pk_fma_f32 v[12:13], v[198:199], v[140:141], v[12:13]
	v_pk_fma_f32 v[14:15], v[200:201], v[142:143], v[14:15]
	s_waitcnt lgkmcnt(0)
	s_mov_b32 m0, s77
	s_nop 0
	global_load_lds_dwordx4 v[2:3], off
	global_load_lds_dwordx4 v[2:3], off offset:1024
	v_cvt_scalef32_pk_f32_fp4 v[136:137], v129, 1.0
	v_cvt_scalef32_pk_f32_fp4 v[138:139], v129, 1.0 op_sel:[1,0,0]
	v_cvt_scalef32_pk_f32_fp4 v[140:141], v129, 1.0 op_sel:[0,1,0]
	v_cvt_scalef32_pk_f32_fp4 v[142:143], v129, 1.0 op_sel:[1,1,0]
	v_mov_b32_dpp v7, v5 row_bcast:15 row_mask:0xa bank_mask:0xf
	v_pk_fma_f32 v[8:9], v[202:203], v[136:137], v[8:9]
	v_pk_fma_f32 v[10:11], v[204:205], v[138:139], v[10:11]
	v_pk_fma_f32 v[12:13], v[206:207], v[140:141], v[12:13]
	v_pk_fma_f32 v[14:15], v[208:209], v[142:143], v[14:15]
	v_add_f32_e32 v5, v5, v7
	v_cvt_scalef32_pk_f32_fp4 v[136:137], v130, 1.0
	v_cvt_scalef32_pk_f32_fp4 v[138:139], v130, 1.0 op_sel:[1,0,0]
	v_cvt_scalef32_pk_f32_fp4 v[140:141], v130, 1.0 op_sel:[0,1,0]
	v_cvt_scalef32_pk_f32_fp4 v[142:143], v130, 1.0 op_sel:[1,1,0]
	v_mov_b32_e32 v7, 0
	v_pk_fma_f32 v[8:9], v[210:211], v[136:137], v[8:9]
	v_pk_fma_f32 v[10:11], v[212:213], v[138:139], v[10:11]
	v_pk_fma_f32 v[12:13], v[214:215], v[140:141], v[12:13]
	v_pk_fma_f32 v[14:15], v[216:217], v[142:143], v[14:15]
	v_mov_b32_dpp v7, v5 row_bcast:31 row_mask:0xc bank_mask:0xf
	v_cvt_scalef32_pk_f32_fp4 v[136:137], v131, 1.0
	v_cvt_scalef32_pk_f32_fp4 v[138:139], v131, 1.0 op_sel:[1,0,0]
	v_cvt_scalef32_pk_f32_fp4 v[140:141], v131, 1.0 op_sel:[0,1,0]
	v_cvt_scalef32_pk_f32_fp4 v[142:143], v131, 1.0 op_sel:[1,1,0]
	v_add_f32_e32 v5, v5, v7
	v_pk_fma_f32 v[8:9], v[218:219], v[136:137], v[8:9]
	v_pk_fma_f32 v[10:11], v[220:221], v[138:139], v[10:11]
	v_pk_fma_f32 v[12:13], v[222:223], v[140:141], v[12:13]
	v_pk_fma_f32 v[14:15], v[224:225], v[142:143], v[14:15]
	v_readlane_b32 s74, v5, 63
	v_cvt_scalef32_pk_f32_fp4 v[136:137], v132, 1.0
	v_cvt_scalef32_pk_f32_fp4 v[138:139], v132, 1.0 op_sel:[1,0,0]
	v_cvt_scalef32_pk_f32_fp4 v[140:141], v132, 1.0 op_sel:[0,1,0]
	v_cvt_scalef32_pk_f32_fp4 v[142:143], v132, 1.0 op_sel:[1,1,0]
	s_lshl_b64 exec, 1, s32
	v_mov_b32_e32 v120, s74
	s_mov_b64 exec, -1
	v_pk_fma_f32 v[8:9], v[226:227], v[136:137], v[8:9]
	v_pk_fma_f32 v[10:11], v[228:229], v[138:139], v[10:11]
	v_pk_fma_f32 v[12:13], v[230:231], v[140:141], v[12:13]
	v_pk_fma_f32 v[14:15], v[232:233], v[142:143], v[14:15]
	v_cvt_scalef32_pk_f32_fp4 v[136:137], v133, 1.0
	v_cvt_scalef32_pk_f32_fp4 v[138:139], v133, 1.0 op_sel:[1,0,0]
	v_cvt_scalef32_pk_f32_fp4 v[140:141], v133, 1.0 op_sel:[0,1,0]
	v_cvt_scalef32_pk_f32_fp4 v[142:143], v133, 1.0 op_sel:[1,1,0]
	v_pk_fma_f32 v[8:9], v[234:235], v[136:137], v[8:9]
	v_pk_fma_f32 v[10:11], v[236:237], v[138:139], v[10:11]
	v_pk_fma_f32 v[12:13], v[238:239], v[140:141], v[12:13]
	v_pk_fma_f32 v[14:15], v[240:241], v[142:143], v[14:15]
	v_pk_add_f32 v[8:9], v[8:9], v[10:11]
	v_pk_add_f32 v[12:13], v[12:13], v[14:15]
	v_pk_add_f32 v[8:9], v[8:9], v[12:13]
	v_add_f32_e32 v6, v8, v9
.Lpu0_next:
	s_add_i32 s46, s46, 2
	s_cmp_lg_u32 s46, 64
	s_cbranch_scc1 .Lpu0_even
; DI void peer_token(LAS unsigned char* ring, const bf16* x1row, float inv2, const float* nffn, const int* ex, const float* pg, const unsigned char* U6, const unsigned char* V6,
;                    const float* usc, const float* vsc, float* orow, int lane) {
;     ...
; #pragma unroll 2
;     for (int k = 0; k < 56; ++k) P11_U(k, us_lo, gv_lo, cf_lo, ul, e_lo, k + 8);
; #pragma unroll 1
;     for (int k = 56; k < 64; ++k) P11_U(k, us_lo, gv_lo, cf_lo, ul, e_hi, k - 56);
; #pragma unroll 2
;     for (int k = 64; k < 120; ++k) P11_U(k, us_hi, gv_hi, cf_hi, ul, e_hi, k - 56);
; #pragma unroll 1
;     for (int k = 120; k < 128; ++k) P11_U(k, us_hi, gv_hi, cf_hi, vl, e_lo, k - 120);
.Lpu1_even:
	s_bitcmp1_b64 s[50:51], s46
	s_cbranch_scc1 .Lpu1_evenB
	s_add_i32 s47, s46, 1
	s_and_b32 s47, s47, 7
	s_lshl_b32 s47, s47, 11
	s_add_i32 s77, s33, s47
	v_add_u32_e32 v4, s77, v70
	s_add_i32 s78, s46, 9
	s_and_b32 s75, s78, 63
	v_readlane_b32 s79, v242, s75
	v_readlane_b32 s47, v113, s75
	s_bitcmp1_b32 s78, 6
	s_cselect_b32 s47, s47, s79
	s_lshr_b32 s47, s47, 8
	s_lshl_b32 s47, s47, 11
	s_bitcmp1_b32 s78, 8
	s_cselect_b32 s78, s98, 0
	s_cselect_b32 s79, s99, 0
	s_add_u32 s78, s78, s47
	s_addc_u32 s79, s79, 0
	s_add_i32 s32, s46, 0
	s_waitcnt vmcnt(14)
	ds_read_b128 v[126:129], v4
	ds_read_b128 v[130:133], v4 offset:1024
	v_lshl_add_u64 v[2:3], v[72:73], 0, s[78:79]
	v_cvt_scalef32_pk_f32_fp4 v[136:137], v98, 1.0
	v_cvt_scalef32_pk_f32_fp4 v[138:139], v98, 1.0 op_sel:[1,0,0]
	v_cvt_scalef32_pk_f32_fp4 v[140:141], v98, 1.0 op_sel:[0,1,0]
	v_cvt_scalef32_pk_f32_fp4 v[142:143], v98, 1.0 op_sel:[1,1,0]
	v_add_f32_dpp v6, v6, v6 quad_perm:[1,0,3,2] row_mask:0xf bank_mask:0xf bound_ctrl:1
	v_pk_fma_f32 v[8:9], v[20:21], v[136:137], 0 op_sel_hi:[1,1,0]
	v_pk_fma_f32 v[10:11], v[22:23], v[138:139], 0 op_sel_hi:[1,1,0]
	v_pk_fma_f32 v[12:13], v[24:25], v[140:141], 0 op_sel_hi:[1,1,0]
	v_pk_fma_f32 v[14:15], v[26:27], v[142:143], 0 op_sel_hi:[1,1,0]
	v_add_f32_dpp v6, v6, v6 quad_perm:[2,3,0,1] row_mask:0xf bank_mask:0xf bound_ctrl:1
	v_cvt_scalef32_pk_f32_fp4 v[136:137], v99, 1.0
	v_cvt_scalef32_pk_f32_fp4 v[138:139], v99, 1.0 op_sel:[1,0,0]
	v_cvt_scalef32_pk_f32_fp4 v[140:141], v99, 1.0 op_sel:[0,1,0]
	v_cvt_scalef32_pk_f32_fp4 v[142:143], v99, 1.0 op_sel:[1,1,0]
	v_add_f32_dpp v6, v6, v6 row_half_mirror row_mask:0xf bank_mask:0xf bound_ctrl:1
	v_pk_fma_f32 v[8:9], v[28:29], v[136:137], v[8:9]
	v_pk_fma_f32 v[10:11], v[30:31], v[138:139], v[10:11]
	v_pk_fma_f32 v[12:13], v[32:33], v[140:141], v[12:13]
	v_pk_fma_f32 v[14:15], v[34:35], v[142:143], v[14:15]
	v_mov_b32_e32 v7, 0
	v_cvt_scalef32_pk_f32_fp4 v[136:137], v100, 1.0
	v_cvt_scalef32_pk_f32_fp4 v[138:139], v100, 1.0 op_sel:[1,0,0]
	v_cvt_scalef32_pk_f32_fp4 v[140:141], v100, 1.0 op_sel:[0,1,0]
	v_cvt_scalef32_pk_f32_fp4 v[142:143], v100, 1.0 op_sel:[1,1,0]
	v_add_f32_dpp v6, v6, v6 row_mirror row_mask:0xf bank_mask:0xf bound_ctrl:1
	v_pk_fma_f32 v[8:9], v[36:37], v[136:137], v[8:9]
	v_pk_fma_f32 v[10:11], v[38:39], v[138:139], v[10:11]
	v_pk_fma_f32 v[12:13], v[40:41], v[140:141], v[12:13]
	v_pk_fma_f32 v[14:15], v[42:43], v[142:143], v[14:15]
	s_waitcnt lgkmcnt(0)
	s_mov_b32 m0, s77
	s_nop 0
	global_load_lds_dwordx4 v[2:3], off
	global_load_lds_dwordx4 v[2:3], off offset:1024
	v_cvt_scalef32_pk_f32_fp4 v[136:137], v101, 1.0
	v_cvt_scalef32_pk_f32_fp4 v[138:139], v101, 1.0 op_sel:[1,0,0]
	v_cvt_scalef32_pk_f32_fp4 v[140:141], v101, 1.0 op_sel:[0,1,0]
	v_cvt_scalef32_pk_f32_fp4 v[142:143], v101, 1.0 op_sel:[1,1,0]
	v_mov_b32_dpp v7, v6 row_bcast:15 row_mask:0xa bank_mask:0xf
	v_pk_fma_f32 v[8:9], v[44:45], v[136:137], v[8:9]
	v_pk_fma_f32 v[10:11], v[46:47], v[138:139], v[10:11]
	v_pk_fma_f32 v[12:13], v[48:49], v[140:141], v[12:13]
	v_pk_fma_f32 v[14:15], v[50:51], v[142:143], v[14:15]
	v_add_f32_e32 v6, v6, v7
	v_cvt_scalef32_pk_f32_fp4 v[136:137], v102, 1.0
	v_cvt_scalef32_pk_f32_fp4 v[138:139], v102, 1.0 op_sel:[1,0,0]
	v_cvt_scalef32_pk_f32_fp4 v[140:141], v102, 1.0 op_sel:[0,1,0]
	v_cvt_scalef32_pk_f32_fp4 v[142:143], v102, 1.0 op_sel:[1,1,0]
	v_mov_b32_e32 v7, 0
	v_pk_fma_f32 v[8:9], v[52:53], v[136:137], v[8:9]
	v_pk_fma_f32 v[10:11], v[54:55], v[138:139], v[10:11]
	v_pk_fma_f32 v[12:13], v[56:57], v[140:141], v[12:13]
	v_pk_fma_f32 v[14:15], v[58:59], v[142:143], v[14:15]
	v_mov_b32_dpp v7, v6 row_bcast:31 row_mask:0xc bank_mask:0xf
	v_cvt_scalef32_pk_f32_fp4 v[136:137], v103, 1.0
	v_cvt_scalef32_pk_f32_fp4 v[138:139], v103, 1.0 op_sel:[1,0,0]
	v_cvt_scalef32_pk_f32_fp4 v[140:141], v103, 1.0 op_sel:[0,1,0]
	v_cvt_scalef32_pk_f32_fp4 v[142:143], v103, 1.0 op_sel:[1,1,0]
	v_add_f32_e32 v6, v6, v7
	v_pk_fma_f32 v[8:9], v[60:61], v[136:137], v[8:9]
	v_pk_fma_f32 v[10:11], v[62:63], v[138:139], v[10:11]
	v_pk_fma_f32 v[12:13], v[64:65], v[140:141], v[12:13]
	v_pk_fma_f32 v[14:15], v[80:81], v[142:143], v[14:15]
	v_readlane_b32 s74, v6, 63
	v_cvt_scalef32_pk_f32_fp4 v[136:137], v104, 1.0
	v_cvt_scalef32_pk_f32_fp4 v[138:139], v104, 1.0 op_sel:[1,0,0]
	v_cvt_scalef32_pk_f32_fp4 v[140:141], v104, 1.0 op_sel:[0,1,0]
	v_cvt_scalef32_pk_f32_fp4 v[142:143], v104, 1.0 op_sel:[1,1,0]
	s_lshl_b64 exec, 1, s32
	v_mov_b32_e32 v125, s74
	s_mov_b64 exec, -1
	v_pk_fma_f32 v[8:9], v[82:83], v[136:137], v[8:9]
	v_pk_fma_f32 v[10:11], v[84:85], v[138:139], v[10:11]
	v_pk_fma_f32 v[12:13], v[86:87], v[140:141], v[12:13]
	v_pk_fma_f32 v[14:15], v[88:89], v[142:143], v[14:15]
	v_cvt_scalef32_pk_f32_fp4 v[136:137], v105, 1.0
	v_cvt_scalef32_pk_f32_fp4 v[138:139], v105, 1.0 op_sel:[1,0,0]
	v_cvt_scalef32_pk_f32_fp4 v[140:141], v105, 1.0 op_sel:[0,1,0]
	v_cvt_scalef32_pk_f32_fp4 v[142:143], v105, 1.0 op_sel:[1,1,0]
	v_pk_fma_f32 v[8:9], v[90:91], v[136:137], v[8:9]
	v_pk_fma_f32 v[10:11], v[92:93], v[138:139], v[10:11]
	v_pk_fma_f32 v[12:13], v[94:95], v[140:141], v[12:13]
	v_pk_fma_f32 v[14:15], v[96:97], v[142:143], v[14:15]
	v_pk_add_f32 v[8:9], v[8:9], v[10:11]
	v_pk_add_f32 v[12:13], v[12:13], v[14:15]
	v_pk_add_f32 v[8:9], v[8:9], v[12:13]
	v_add_f32_e32 v5, v8, v9
	s_branch .Lpu1_odd
; DI void peer_token(LAS unsigned char* ring, const bf16* x1row, float inv2, const float* nffn, const int* ex, const float* pg, const unsigned char* U6, const unsigned char* V6,
;                    const float* usc, const float* vsc, float* orow, int lane) {
;     ...
; #pragma unroll 2
;     for (int k = 0; k < 56; ++k) P11_U(k, us_lo, gv_lo, cf_lo, ul, e_lo, k + 8);
; #pragma unroll 1
;     for (int k = 56; k < 64; ++k) P11_U(k, us_lo, gv_lo, cf_lo, ul, e_hi, k - 56);
; #pragma unroll 2
;     for (int k = 64; k < 120; ++k) P11_U(k, us_hi, gv_hi, cf_hi, ul, e_hi, k - 56);
; #pragma unroll 1
;     for (int k = 120; k < 128; ++k) P11_U(k, us_hi, gv_hi, cf_hi, vl, e_lo, k - 120);
.Lpu1_evenB:
	s_add_i32 s47, s46, 1
	s_and_b32 s47, s47, 7
	s_lshl_b32 s47, s47, 11
	s_add_i32 s77, s33, s47
	v_add_u32_e32 v4, s77, v70
	s_add_i32 s78, s46, 9
	s_and_b32 s75, s78, 63
	v_readlane_b32 s79, v242, s75
	v_readlane_b32 s47, v113, s75
	s_bitcmp1_b32 s78, 6
	s_cselect_b32 s47, s47, s79
	s_lshr_b32 s47, s47, 8
	s_lshl_b32 s47, s47, 11
	s_bitcmp1_b32 s78, 8
	s_cselect_b32 s78, s98, 0
	s_cselect_b32 s79, s99, 0
	s_add_u32 s78, s78, s47
	s_addc_u32 s79, s79, 0
	s_add_i32 s32, s46, 0
	s_waitcnt vmcnt(14)
	ds_read_b128 v[126:129], v4
	ds_read_b128 v[130:133], v4 offset:1024
	v_lshl_add_u64 v[2:3], v[72:73], 0, s[78:79]
	v_cvt_scalef32_pk_f32_fp4 v[136:137], v98, 1.0
	v_cvt_scalef32_pk_f32_fp4 v[138:139], v98, 1.0 op_sel:[1,0,0]
	v_cvt_scalef32_pk_f32_fp4 v[140:141], v98, 1.0 op_sel:[0,1,0]
	v_cvt_scalef32_pk_f32_fp4 v[142:143], v98, 1.0 op_sel:[1,1,0]
	v_add_f32_dpp v6, v6, v6 quad_perm:[1,0,3,2] row_mask:0xf bank_mask:0xf bound_ctrl:1
	v_pk_fma_f32 v[8:9], v[178:179], v[136:137], 0 op_sel_hi:[1,1,0]
	v_pk_fma_f32 v[10:11], v[180:181], v[138:139], 0 op_sel_hi:[1,1,0]
	v_pk_fma_f32 v[12:13], v[182:183], v[140:141], 0 op_sel_hi:[1,1,0]
	v_pk_fma_f32 v[14:15], v[184:185], v[142:143], 0 op_sel_hi:[1,1,0]
	v_add_f32_dpp v6, v6, v6 quad_perm:[2,3,0,1] row_mask:0xf bank_mask:0xf bound_ctrl:1
	v_cvt_scalef32_pk_f32_fp4 v[136:137], v99, 1.0
	v_cvt_scalef32_pk_f32_fp4 v[138:139], v99, 1.0 op_sel:[1,0,0]
	v_cvt_scalef32_pk_f32_fp4 v[140:141], v99, 1.0 op_sel:[0,1,0]
	v_cvt_scalef32_pk_f32_fp4 v[142:143], v99, 1.0 op_sel:[1,1,0]
	v_add_f32_dpp v6, v6, v6 row_half_mirror row_mask:0xf bank_mask:0xf bound_ctrl:1
	v_pk_fma_f32 v[8:9], v[186:187], v[136:137], v[8:9]
	v_pk_fma_f32 v[10:11], v[188:189], v[138:139], v[10:11]
	v_pk_fma_f32 v[12:13], v[190:191], v[140:141], v[12:13]
	v_pk_fma_f32 v[14:15], v[192:193], v[142:143], v[14:15]
	v_mov_b32_e32 v7, 0
	v_cvt_scalef32_pk_f32_fp4 v[136:137], v100, 1.0
	v_cvt_scalef32_pk_f32_fp4 v[138:139], v100, 1.0 op_sel:[1,0,0]
	v_cvt_scalef32_pk_f32_fp4 v[140:141], v100, 1.0 op_sel:[0,1,0]
	v_cvt_scalef32_pk_f32_fp4 v[142:143], v100, 1.0 op_sel:[1,1,0]
	v_add_f32_dpp v6, v6, v6 row_mirror row_mask:0xf bank_mask:0xf bound_ctrl:1
	v_pk_fma_f32 v[8:9], v[194:195], v[136:137], v[8:9]
	v_pk_fma_f32 v[10:11], v[196:197], v[138:139], v[10:11]
	v_pk_fma_f32 v[12:13], v[198:199], v[140:141], v[12:13]
	v_pk_fma_f32 v[14:15], v[200:201], v[142:143], v[14:15]
	s_waitcnt lgkmcnt(0)
	s_mov_b32 m0, s77
	s_nop 0
	global_load_lds_dwordx4 v[2:3], off
	global_load_lds_dwordx4 v[2:3], off offset:1024
	v_cvt_scalef32_pk_f32_fp4 v[136:137], v101, 1.0
	v_cvt_scalef32_pk_f32_fp4 v[138:139], v101, 1.0 op_sel:[1,0,0]
	v_cvt_scalef32_pk_f32_fp4 v[140:141], v101, 1.0 op_sel:[0,1,0]
	v_cvt_scalef32_pk_f32_fp4 v[142:143], v101, 1.0 op_sel:[1,1,0]
	v_mov_b32_dpp v7, v6 row_bcast:15 row_mask:0xa bank_mask:0xf
	v_pk_fma_f32 v[8:9], v[202:203], v[136:137], v[8:9]
	v_pk_fma_f32 v[10:11], v[204:205], v[138:139], v[10:11]
	v_pk_fma_f32 v[12:13], v[206:207], v[140:141], v[12:13]
	v_pk_fma_f32 v[14:15], v[208:209], v[142:143], v[14:15]
	v_add_f32_e32 v6, v6, v7
	v_cvt_scalef32_pk_f32_fp4 v[136:137], v102, 1.0
	v_cvt_scalef32_pk_f32_fp4 v[138:139], v102, 1.0 op_sel:[1,0,0]
	v_cvt_scalef32_pk_f32_fp4 v[140:141], v102, 1.0 op_sel:[0,1,0]
	v_cvt_scalef32_pk_f32_fp4 v[142:143], v102, 1.0 op_sel:[1,1,0]
	v_mov_b32_e32 v7, 0
	v_pk_fma_f32 v[8:9], v[210:211], v[136:137], v[8:9]
	v_pk_fma_f32 v[10:11], v[212:213], v[138:139], v[10:11]
	v_pk_fma_f32 v[12:13], v[214:215], v[140:141], v[12:13]
	v_pk_fma_f32 v[14:15], v[216:217], v[142:143], v[14:15]
	v_mov_b32_dpp v7, v6 row_bcast:31 row_mask:0xc bank_mask:0xf
	v_cvt_scalef32_pk_f32_fp4 v[136:137], v103, 1.0
	v_cvt_scalef32_pk_f32_fp4 v[138:139], v103, 1.0 op_sel:[1,0,0]
	v_cvt_scalef32_pk_f32_fp4 v[140:141], v103, 1.0 op_sel:[0,1,0]
	v_cvt_scalef32_pk_f32_fp4 v[142:143], v103, 1.0 op_sel:[1,1,0]
	v_add_f32_e32 v6, v6, v7
	v_pk_fma_f32 v[8:9], v[218:219], v[136:137], v[8:9]
	v_pk_fma_f32 v[10:11], v[220:221], v[138:139], v[10:11]
	v_pk_fma_f32 v[12:13], v[222:223], v[140:141], v[12:13]
	v_pk_fma_f32 v[14:15], v[224:225], v[142:143], v[14:15]
	v_readlane_b32 s74, v6, 63
	v_cvt_scalef32_pk_f32_fp4 v[136:137], v104, 1.0
	v_cvt_scalef32_pk_f32_fp4 v[138:139], v104, 1.0 op_sel:[1,0,0]
	v_cvt_scalef32_pk_f32_fp4 v[140:141], v104, 1.0 op_sel:[0,1,0]
	v_cvt_scalef32_pk_f32_fp4 v[142:143], v104, 1.0 op_sel:[1,1,0]
	s_lshl_b64 exec, 1, s32
	v_mov_b32_e32 v125, s74
	s_mov_b64 exec, -1
	v_pk_fma_f32 v[8:9], v[226:227], v[136:137], v[8:9]
	v_pk_fma_f32 v[10:11], v[228:229], v[138:139], v[10:11]
	v_pk_fma_f32 v[12:13], v[230:231], v[140:141], v[12:13]
	v_pk_fma_f32 v[14:15], v[232:233], v[142:143], v[14:15]
	v_cvt_scalef32_pk_f32_fp4 v[136:137], v105, 1.0
	v_cvt_scalef32_pk_f32_fp4 v[138:139], v105, 1.0 op_sel:[1,0,0]
	v_cvt_scalef32_pk_f32_fp4 v[140:141], v105, 1.0 op_sel:[0,1,0]
	v_cvt_scalef32_pk_f32_fp4 v[142:143], v105, 1.0 op_sel:[1,1,0]
	v_pk_fma_f32 v[8:9], v[234:235], v[136:137], v[8:9]
	v_pk_fma_f32 v[10:11], v[236:237], v[138:139], v[10:11]
	v_pk_fma_f32 v[12:13], v[238:239], v[140:141], v[12:13]
	v_pk_fma_f32 v[14:15], v[240:241], v[142:143], v[14:15]
	v_pk_add_f32 v[8:9], v[8:9], v[10:11]
	v_pk_add_f32 v[12:13], v[12:13], v[14:15]
	v_pk_add_f32 v[8:9], v[8:9], v[12:13]
	v_add_f32_e32 v5, v8, v9
; DI void peer_token(LAS unsigned char* ring, const bf16* x1row, float inv2, const float* nffn, const int* ex, const float* pg, const unsigned char* U6, const unsigned char* V6,
;                    const float* usc, const float* vsc, float* orow, int lane) {
;     ...
; #pragma unroll 2
;     for (int k = 0; k < 56; ++k) P11_U(k, us_lo, gv_lo, cf_lo, ul, e_lo, k + 8);
; #pragma unroll 1
;     for (int k = 56; k < 64; ++k) P11_U(k, us_lo, gv_lo, cf_lo, ul, e_hi, k - 56);
; #pragma unroll 2
;     for (int k = 64; k < 120; ++k) P11_U(k, us_hi, gv_hi, cf_hi, ul, e_hi, k - 56);
; #pragma unroll 1
;     for (int k = 120; k < 128; ++k) P11_U(k, us_hi, gv_hi, cf_hi, vl, e_lo, k - 120);
.Lpu1_odd:
	s_add_i32 s32, s46, 1
	s_bitcmp1_b64 s[50:51], s32
	s_cbranch_scc1 .Lpu1_oddB
	s_add_i32 s47, s46, 2
	s_and_b32 s47, s47, 7
	s_lshl_b32 s47, s47, 11
	s_add_i32 s77, s33, s47
	v_add_u32_e32 v4, s77, v70
	s_add_i32 s78, s46, 10
	s_and_b32 s75, s78, 63
	v_readlane_b32 s79, v242, s75
	v_readlane_b32 s47, v113, s75
	s_bitcmp1_b32 s78, 6
	s_cselect_b32 s47, s47, s79
	s_lshr_b32 s47, s47, 8
	s_lshl_b32 s47, s47, 11
	s_bitcmp1_b32 s78, 8
	s_cselect_b32 s78, s98, 0
	s_cselect_b32 s79, s99, 0
	s_add_u32 s78, s78, s47
	s_addc_u32 s79, s79, 0
	s_add_i32 s32, s46, 1
	s_waitcnt vmcnt(14)
	ds_read_b128 v[98:101], v4
	ds_read_b128 v[102:105], v4 offset:1024
	v_lshl_add_u64 v[2:3], v[72:73], 0, s[78:79]
	v_cvt_scalef32_pk_f32_fp4 v[136:137], v126, 1.0
	v_cvt_scalef32_pk_f32_fp4 v[138:139], v126, 1.0 op_sel:[1,0,0]
	v_cvt_scalef32_pk_f32_fp4 v[140:141], v126, 1.0 op_sel:[0,1,0]
	v_cvt_scalef32_pk_f32_fp4 v[142:143], v126, 1.0 op_sel:[1,1,0]
	v_add_f32_dpp v5, v5, v5 quad_perm:[1,0,3,2] row_mask:0xf bank_mask:0xf bound_ctrl:1
	v_pk_fma_f32 v[8:9], v[20:21], v[136:137], 0 op_sel_hi:[1,1,0]
	v_pk_fma_f32 v[10:11], v[22:23], v[138:139], 0 op_sel_hi:[1,1,0]
	v_pk_fma_f32 v[12:13], v[24:25], v[140:141], 0 op_sel_hi:[1,1,0]
	v_pk_fma_f32 v[14:15], v[26:27], v[142:143], 0 op_sel_hi:[1,1,0]
	v_add_f32_dpp v5, v5, v5 quad_perm:[2,3,0,1] row_mask:0xf bank_mask:0xf bound_ctrl:1
	v_cvt_scalef32_pk_f32_fp4 v[136:137], v127, 1.0
	v_cvt_scalef32_pk_f32_fp4 v[138:139], v127, 1.0 op_sel:[1,0,0]
	v_cvt_scalef32_pk_f32_fp4 v[140:141], v127, 1.0 op_sel:[0,1,0]
	v_cvt_scalef32_pk_f32_fp4 v[142:143], v127, 1.0 op_sel:[1,1,0]
	v_add_f32_dpp v5, v5, v5 row_half_mirror row_mask:0xf bank_mask:0xf bound_ctrl:1
	v_pk_fma_f32 v[8:9], v[28:29], v[136:137], v[8:9]
	v_pk_fma_f32 v[10:11], v[30:31], v[138:139], v[10:11]
	v_pk_fma_f32 v[12:13], v[32:33], v[140:141], v[12:13]
	v_pk_fma_f32 v[14:15], v[34:35], v[142:143], v[14:15]
	v_mov_b32_e32 v7, 0
	v_cvt_scalef32_pk_f32_fp4 v[136:137], v128, 1.0
	v_cvt_scalef32_pk_f32_fp4 v[138:139], v128, 1.0 op_sel:[1,0,0]
	v_cvt_scalef32_pk_f32_fp4 v[140:141], v128, 1.0 op_sel:[0,1,0]
	v_cvt_scalef32_pk_f32_fp4 v[142:143], v128, 1.0 op_sel:[1,1,0]
	v_add_f32_dpp v5, v5, v5 row_mirror row_mask:0xf bank_mask:0xf bound_ctrl:1
	v_pk_fma_f32 v[8:9], v[36:37], v[136:137], v[8:9]
	v_pk_fma_f32 v[10:11], v[38:39], v[138:139], v[10:11]
	v_pk_fma_f32 v[12:13], v[40:41], v[140:141], v[12:13]
	v_pk_fma_f32 v[14:15], v[42:43], v[142:143], v[14:15]
	s_waitcnt lgkmcnt(0)
	s_mov_b32 m0, s77
	s_nop 0
	global_load_lds_dwordx4 v[2:3], off
	global_load_lds_dwordx4 v[2:3], off offset:1024
	v_cvt_scalef32_pk_f32_fp4 v[136:137], v129, 1.0
	v_cvt_scalef32_pk_f32_fp4 v[138:139], v129, 1.0 op_sel:[1,0,0]
	v_cvt_scalef32_pk_f32_fp4 v[140:141], v129, 1.0 op_sel:[0,1,0]
	v_cvt_scalef32_pk_f32_fp4 v[142:143], v129, 1.0 op_sel:[1,1,0]
	v_mov_b32_dpp v7, v5 row_bcast:15 row_mask:0xa bank_mask:0xf
	v_pk_fma_f32 v[8:9], v[44:45], v[136:137], v[8:9]
	v_pk_fma_f32 v[10:11], v[46:47], v[138:139], v[10:11]
	v_pk_fma_f32 v[12:13], v[48:49], v[140:141], v[12:13]
	v_pk_fma_f32 v[14:15], v[50:51], v[142:143], v[14:15]
	v_add_f32_e32 v5, v5, v7
	v_cvt_scalef32_pk_f32_fp4 v[136:137], v130, 1.0
	v_cvt_scalef32_pk_f32_fp4 v[138:139], v130, 1.0 op_sel:[1,0,0]
	v_cvt_scalef32_pk_f32_fp4 v[140:141], v130, 1.0 op_sel:[0,1,0]
	v_cvt_scalef32_pk_f32_fp4 v[142:143], v130, 1.0 op_sel:[1,1,0]
	v_mov_b32_e32 v7, 0
	v_pk_fma_f32 v[8:9], v[52:53], v[136:137], v[8:9]
	v_pk_fma_f32 v[10:11], v[54:55], v[138:139], v[10:11]
	v_pk_fma_f32 v[12:13], v[56:57], v[140:141], v[12:13]
	v_pk_fma_f32 v[14:15], v[58:59], v[142:143], v[14:15]
	v_mov_b32_dpp v7, v5 row_bcast:31 row_mask:0xc bank_mask:0xf
	v_cvt_scalef32_pk_f32_fp4 v[136:137], v131, 1.0
	v_cvt_scalef32_pk_f32_fp4 v[138:139], v131, 1.0 op_sel:[1,0,0]
	v_cvt_scalef32_pk_f32_fp4 v[140:141], v131, 1.0 op_sel:[0,1,0]
	v_cvt_scalef32_pk_f32_fp4 v[142:143], v131, 1.0 op_sel:[1,1,0]
	v_add_f32_e32 v5, v5, v7
	v_pk_fma_f32 v[8:9], v[60:61], v[136:137], v[8:9]
	v_pk_fma_f32 v[10:11], v[62:63], v[138:139], v[10:11]
	v_pk_fma_f32 v[12:13], v[64:65], v[140:141], v[12:13]
	v_pk_fma_f32 v[14:15], v[80:81], v[142:143], v[14:15]
	v_readlane_b32 s74, v5, 63
	v_cvt_scalef32_pk_f32_fp4 v[136:137], v132, 1.0
	v_cvt_scalef32_pk_f32_fp4 v[138:139], v132, 1.0 op_sel:[1,0,0]
	v_cvt_scalef32_pk_f32_fp4 v[140:141], v132, 1.0 op_sel:[0,1,0]
	v_cvt_scalef32_pk_f32_fp4 v[142:143], v132, 1.0 op_sel:[1,1,0]
	s_lshl_b64 exec, 1, s32
	v_mov_b32_e32 v125, s74
	s_mov_b64 exec, -1
	v_pk_fma_f32 v[8:9], v[82:83], v[136:137], v[8:9]
	v_pk_fma_f32 v[10:11], v[84:85], v[138:139], v[10:11]
	v_pk_fma_f32 v[12:13], v[86:87], v[140:141], v[12:13]
	v_pk_fma_f32 v[14:15], v[88:89], v[142:143], v[14:15]
	v_cvt_scalef32_pk_f32_fp4 v[136:137], v133, 1.0
	v_cvt_scalef32_pk_f32_fp4 v[138:139], v133, 1.0 op_sel:[1,0,0]
	v_cvt_scalef32_pk_f32_fp4 v[140:141], v133, 1.0 op_sel:[0,1,0]
	v_cvt_scalef32_pk_f32_fp4 v[142:143], v133, 1.0 op_sel:[1,1,0]
	v_pk_fma_f32 v[8:9], v[90:91], v[136:137], v[8:9]
	v_pk_fma_f32 v[10:11], v[92:93], v[138:139], v[10:11]
	v_pk_fma_f32 v[12:13], v[94:95], v[140:141], v[12:13]
	v_pk_fma_f32 v[14:15], v[96:97], v[142:143], v[14:15]
	v_pk_add_f32 v[8:9], v[8:9], v[10:11]
	v_pk_add_f32 v[12:13], v[12:13], v[14:15]
	v_pk_add_f32 v[8:9], v[8:9], v[12:13]
	v_add_f32_e32 v6, v8, v9
	s_branch .Lpu1_next
; DI void peer_token(LAS unsigned char* ring, const bf16* x1row, float inv2, const float* nffn, const int* ex, const float* pg, const unsigned char* U6, const unsigned char* V6,
;                    const float* usc, const float* vsc, float* orow, int lane) {
;     ...
; #pragma unroll 2
;     for (int k = 0; k < 56; ++k) P11_U(k, us_lo, gv_lo, cf_lo, ul, e_lo, k + 8);
; #pragma unroll 1
;     for (int k = 56; k < 64; ++k) P11_U(k, us_lo, gv_lo, cf_lo, ul, e_hi, k - 56);
; #pragma unroll 2
;     for (int k = 64; k < 120; ++k) P11_U(k, us_hi, gv_hi, cf_hi, ul, e_hi, k - 56);
; #pragma unroll 1
;     for (int k = 120; k < 128; ++k) P11_U(k, us_hi, gv_hi, cf_hi, vl, e_lo, k - 120);
.Lpu1_oddB:
	s_add_i32 s47, s46, 2
	s_and_b32 s47, s47, 7
	s_lshl_b32 s47, s47, 11
	s_add_i32 s77, s33, s47
	v_add_u32_e32 v4, s77, v70
	s_add_i32 s78, s46, 10
	s_and_b32 s75, s78, 63
	v_readlane_b32 s79, v242, s75
	v_readlane_b32 s47, v113, s75
	s_bitcmp1_b32 s78, 6
	s_cselect_b32 s47, s47, s79
	s_lshr_b32 s47, s47, 8
	s_lshl_b32 s47, s47, 11
	s_bitcmp1_b32 s78, 8
	s_cselect_b32 s78, s98, 0
	s_cselect_b32 s79, s99, 0
	s_add_u32 s78, s78, s47
	s_addc_u32 s79, s79, 0
	s_add_i32 s32, s46, 1
	s_waitcnt vmcnt(14)
	ds_read_b128 v[98:101], v4
	ds_read_b128 v[102:105], v4 offset:1024
	v_lshl_add_u64 v[2:3], v[72:73], 0, s[78:79]
	v_cvt_scalef32_pk_f32_fp4 v[136:137], v126, 1.0
	v_cvt_scalef32_pk_f32_fp4 v[138:139], v126, 1.0 op_sel:[1,0,0]
	v_cvt_scalef32_pk_f32_fp4 v[140:141], v126, 1.0 op_sel:[0,1,0]
	v_cvt_scalef32_pk_f32_fp4 v[142:143], v126, 1.0 op_sel:[1,1,0]
	v_add_f32_dpp v5, v5, v5 quad_perm:[1,0,3,2] row_mask:0xf bank_mask:0xf bound_ctrl:1
	v_pk_fma_f32 v[8:9], v[178:179], v[136:137], 0 op_sel_hi:[1,1,0]
	v_pk_fma_f32 v[10:11], v[180:181], v[138:139], 0 op_sel_hi:[1,1,0]
	v_pk_fma_f32 v[12:13], v[182:183], v[140:141], 0 op_sel_hi:[1,1,0]
	v_pk_fma_f32 v[14:15], v[184:185], v[142:143], 0 op_sel_hi:[1,1,0]
	v_add_f32_dpp v5, v5, v5 quad_perm:[2,3,0,1] row_mask:0xf bank_mask:0xf bound_ctrl:1
	v_cvt_scalef32_pk_f32_fp4 v[136:137], v127, 1.0
	v_cvt_scalef32_pk_f32_fp4 v[138:139], v127, 1.0 op_sel:[1,0,0]
	v_cvt_scalef32_pk_f32_fp4 v[140:141], v127, 1.0 op_sel:[0,1,0]
	v_cvt_scalef32_pk_f32_fp4 v[142:143], v127, 1.0 op_sel:[1,1,0]
	v_add_f32_dpp v5, v5, v5 row_half_mirror row_mask:0xf bank_mask:0xf bound_ctrl:1
	v_pk_fma_f32 v[8:9], v[186:187], v[136:137], v[8:9]
	v_pk_fma_f32 v[10:11], v[188:189], v[138:139], v[10:11]
	v_pk_fma_f32 v[12:13], v[190:191], v[140:141], v[12:13]
	v_pk_fma_f32 v[14:15], v[192:193], v[142:143], v[14:15]
	v_mov_b32_e32 v7, 0
	v_cvt_scalef32_pk_f32_fp4 v[136:137], v128, 1.0
	v_cvt_scalef32_pk_f32_fp4 v[138:139], v128, 1.0 op_sel:[1,0,0]
	v_cvt_scalef32_pk_f32_fp4 v[140:141], v128, 1.0 op_sel:[0,1,0]
	v_cvt_scalef32_pk_f32_fp4 v[142:143], v128, 1.0 op_sel:[1,1,0]
	v_add_f32_dpp v5, v5, v5 row_mirror row_mask:0xf bank_mask:0xf bound_ctrl:1
	v_pk_fma_f32 v[8:9], v[194:195], v[136:137], v[8:9]
	v_pk_fma_f32 v[10:11], v[196:197], v[138:139], v[10:11]
	v_pk_fma_f32 v[12:13], v[198:199], v[140:141], v[12:13]
	v_pk_fma_f32 v[14:15], v[200:201], v[142:143], v[14:15]
	s_waitcnt lgkmcnt(0)
	s_mov_b32 m0, s77
	s_nop 0
	global_load_lds_dwordx4 v[2:3], off
	global_load_lds_dwordx4 v[2:3], off offset:1024
	v_cvt_scalef32_pk_f32_fp4 v[136:137], v129, 1.0
	v_cvt_scalef32_pk_f32_fp4 v[138:139], v129, 1.0 op_sel:[1,0,0]
	v_cvt_scalef32_pk_f32_fp4 v[140:141], v129, 1.0 op_sel:[0,1,0]
	v_cvt_scalef32_pk_f32_fp4 v[142:143], v129, 1.0 op_sel:[1,1,0]
	v_mov_b32_dpp v7, v5 row_bcast:15 row_mask:0xa bank_mask:0xf
	v_pk_fma_f32 v[8:9], v[202:203], v[136:137], v[8:9]
	v_pk_fma_f32 v[10:11], v[204:205], v[138:139], v[10:11]
	v_pk_fma_f32 v[12:13], v[206:207], v[140:141], v[12:13]
	v_pk_fma_f32 v[14:15], v[208:209], v[142:143], v[14:15]
	v_add_f32_e32 v5, v5, v7
	v_cvt_scalef32_pk_f32_fp4 v[136:137], v130, 1.0
	v_cvt_scalef32_pk_f32_fp4 v[138:139], v130, 1.0 op_sel:[1,0,0]
	v_cvt_scalef32_pk_f32_fp4 v[140:141], v130, 1.0 op_sel:[0,1,0]
	v_cvt_scalef32_pk_f32_fp4 v[142:143], v130, 1.0 op_sel:[1,1,0]
	v_mov_b32_e32 v7, 0
	v_pk_fma_f32 v[8:9], v[210:211], v[136:137], v[8:9]
	v_pk_fma_f32 v[10:11], v[212:213], v[138:139], v[10:11]
	v_pk_fma_f32 v[12:13], v[214:215], v[140:141], v[12:13]
	v_pk_fma_f32 v[14:15], v[216:217], v[142:143], v[14:15]
	v_mov_b32_dpp v7, v5 row_bcast:31 row_mask:0xc bank_mask:0xf
	v_cvt_scalef32_pk_f32_fp4 v[136:137], v131, 1.0
	v_cvt_scalef32_pk_f32_fp4 v[138:139], v131, 1.0 op_sel:[1,0,0]
	v_cvt_scalef32_pk_f32_fp4 v[140:141], v131, 1.0 op_sel:[0,1,0]
	v_cvt_scalef32_pk_f32_fp4 v[142:143], v131, 1.0 op_sel:[1,1,0]
	v_add_f32_e32 v5, v5, v7
	v_pk_fma_f32 v[8:9], v[218:219], v[136:137], v[8:9]
	v_pk_fma_f32 v[10:11], v[220:221], v[138:139], v[10:11]
	v_pk_fma_f32 v[12:13], v[222:223], v[140:141], v[12:13]
	v_pk_fma_f32 v[14:15], v[224:225], v[142:143], v[14:15]
	v_readlane_b32 s74, v5, 63
	v_cvt_scalef32_pk_f32_fp4 v[136:137], v132, 1.0
	v_cvt_scalef32_pk_f32_fp4 v[138:139], v132, 1.0 op_sel:[1,0,0]
	v_cvt_scalef32_pk_f32_fp4 v[140:141], v132, 1.0 op_sel:[0,1,0]
	v_cvt_scalef32_pk_f32_fp4 v[142:143], v132, 1.0 op_sel:[1,1,0]
	s_lshl_b64 exec, 1, s32
	v_mov_b32_e32 v125, s74
	s_mov_b64 exec, -1
	v_pk_fma_f32 v[8:9], v[226:227], v[136:137], v[8:9]
	v_pk_fma_f32 v[10:11], v[228:229], v[138:139], v[10:11]
	v_pk_fma_f32 v[12:13], v[230:231], v[140:141], v[12:13]
	v_pk_fma_f32 v[14:15], v[232:233], v[142:143], v[14:15]
	v_cvt_scalef32_pk_f32_fp4 v[136:137], v133, 1.0
	v_cvt_scalef32_pk_f32_fp4 v[138:139], v133, 1.0 op_sel:[1,0,0]
	v_cvt_scalef32_pk_f32_fp4 v[140:141], v133, 1.0 op_sel:[0,1,0]
	v_cvt_scalef32_pk_f32_fp4 v[142:143], v133, 1.0 op_sel:[1,1,0]
	v_pk_fma_f32 v[8:9], v[234:235], v[136:137], v[8:9]
	v_pk_fma_f32 v[10:11], v[236:237], v[138:139], v[10:11]
	v_pk_fma_f32 v[12:13], v[238:239], v[140:141], v[12:13]
	v_pk_fma_f32 v[14:15], v[240:241], v[142:143], v[14:15]
	v_pk_add_f32 v[8:9], v[8:9], v[10:11]
	v_pk_add_f32 v[12:13], v[12:13], v[14:15]
	v_pk_add_f32 v[8:9], v[8:9], v[12:13]
	v_add_f32_e32 v6, v8, v9
.Lpu1_next:
	s_add_i32 s46, s46, 2
	s_cmp_lg_u32 s46, 128
	s_cbranch_scc1 .Lpu1_even
; DI void peer_token(LAS unsigned char* ring, const bf16* x1row, float inv2, const float* nffn, const int* ex, const float* pg, const unsigned char* U6, const unsigned char* V6,
;                    const float* usc, const float* vsc, float* orow, int lane) {
;     ...
; #pragma unroll 2
;     for (int k = 0; k < 56; ++k) P11_U(k, us_lo, gv_lo, cf_lo, ul, e_lo, k + 8);
; #pragma unroll 1
;     for (int k = 56; k < 64; ++k) P11_U(k, us_lo, gv_lo, cf_lo, ul, e_hi, k - 56);
; #pragma unroll 2
;     for (int k = 64; k < 120; ++k) P11_U(k, us_hi, gv_hi, cf_hi, ul, e_hi, k - 56);
; #pragma unroll 1
;     for (int k = 120; k < 128; ++k) P11_U(k, us_hi, gv_hi, cf_hi, vl, e_lo, k - 120);
.Lpu2_even:
	s_bitcmp1_b64 s[82:83], s46
	s_cbranch_scc1 .Lpu2_evenB
	s_add_i32 s47, s46, 1
	s_and_b32 s47, s47, 7
	s_lshl_b32 s47, s47, 11
	s_add_i32 s77, s33, s47
	v_add_u32_e32 v4, s77, v70
	s_add_i32 s78, s46, 9
	s_and_b32 s75, s78, 63
	v_readlane_b32 s79, v243, s75
	v_readlane_b32 s47, v242, s75
	s_bitcmp1_b32 s78, 6
	s_cselect_b32 s47, s79, s47
	s_lshr_b32 s47, s47, 8
	s_lshl_b32 s47, s47, 11
	s_bitcmp1_b32 s78, 8
	s_cselect_b32 s78, s98, 0
	s_cselect_b32 s79, s99, 0
	s_add_u32 s78, s78, s47
	s_addc_u32 s79, s79, 0
	s_add_i32 s32, s46, 0
	s_waitcnt vmcnt(14)
	ds_read_b128 v[126:129], v4
	ds_read_b128 v[130:133], v4 offset:1024
	v_lshl_add_u64 v[2:3], v[72:73], 0, s[78:79]
	v_cvt_scalef32_pk_f32_fp4 v[136:137], v98, 1.0
	v_cvt_scalef32_pk_f32_fp4 v[138:139], v98, 1.0 op_sel:[1,0,0]
	v_cvt_scalef32_pk_f32_fp4 v[140:141], v98, 1.0 op_sel:[0,1,0]
	v_cvt_scalef32_pk_f32_fp4 v[142:143], v98, 1.0 op_sel:[1,1,0]
	v_add_f32_dpp v6, v6, v6 quad_perm:[1,0,3,2] row_mask:0xf bank_mask:0xf bound_ctrl:1
	v_pk_fma_f32 v[8:9], v[20:21], v[136:137], 0 op_sel_hi:[1,1,0]
	v_pk_fma_f32 v[10:11], v[22:23], v[138:139], 0 op_sel_hi:[1,1,0]
	v_pk_fma_f32 v[12:13], v[24:25], v[140:141], 0 op_sel_hi:[1,1,0]
	v_pk_fma_f32 v[14:15], v[26:27], v[142:143], 0 op_sel_hi:[1,1,0]
	v_add_f32_dpp v6, v6, v6 quad_perm:[2,3,0,1] row_mask:0xf bank_mask:0xf bound_ctrl:1
	v_cvt_scalef32_pk_f32_fp4 v[136:137], v99, 1.0
	v_cvt_scalef32_pk_f32_fp4 v[138:139], v99, 1.0 op_sel:[1,0,0]
	v_cvt_scalef32_pk_f32_fp4 v[140:141], v99, 1.0 op_sel:[0,1,0]
	v_cvt_scalef32_pk_f32_fp4 v[142:143], v99, 1.0 op_sel:[1,1,0]
	v_add_f32_dpp v6, v6, v6 row_half_mirror row_mask:0xf bank_mask:0xf bound_ctrl:1
	v_pk_fma_f32 v[8:9], v[28:29], v[136:137], v[8:9]
	v_pk_fma_f32 v[10:11], v[30:31], v[138:139], v[10:11]
	v_pk_fma_f32 v[12:13], v[32:33], v[140:141], v[12:13]
	v_pk_fma_f32 v[14:15], v[34:35], v[142:143], v[14:15]
	v_mov_b32_e32 v7, 0
	v_cvt_scalef32_pk_f32_fp4 v[136:137], v100, 1.0
	v_cvt_scalef32_pk_f32_fp4 v[138:139], v100, 1.0 op_sel:[1,0,0]
	v_cvt_scalef32_pk_f32_fp4 v[140:141], v100, 1.0 op_sel:[0,1,0]
	v_cvt_scalef32_pk_f32_fp4 v[142:143], v100, 1.0 op_sel:[1,1,0]
	v_add_f32_dpp v6, v6, v6 row_mirror row_mask:0xf bank_mask:0xf bound_ctrl:1
	v_pk_fma_f32 v[8:9], v[36:37], v[136:137], v[8:9]
	v_pk_fma_f32 v[10:11], v[38:39], v[138:139], v[10:11]
	v_pk_fma_f32 v[12:13], v[40:41], v[140:141], v[12:13]
	v_pk_fma_f32 v[14:15], v[42:43], v[142:143], v[14:15]
	s_waitcnt lgkmcnt(0)
	s_mov_b32 m0, s77
	s_nop 0
	global_load_lds_dwordx4 v[2:3], off
	global_load_lds_dwordx4 v[2:3], off offset:1024
	v_cvt_scalef32_pk_f32_fp4 v[136:137], v101, 1.0
	v_cvt_scalef32_pk_f32_fp4 v[138:139], v101, 1.0 op_sel:[1,0,0]
	v_cvt_scalef32_pk_f32_fp4 v[140:141], v101, 1.0 op_sel:[0,1,0]
	v_cvt_scalef32_pk_f32_fp4 v[142:143], v101, 1.0 op_sel:[1,1,0]
	v_mov_b32_dpp v7, v6 row_bcast:15 row_mask:0xa bank_mask:0xf
	v_pk_fma_f32 v[8:9], v[44:45], v[136:137], v[8:9]
	v_pk_fma_f32 v[10:11], v[46:47], v[138:139], v[10:11]
	v_pk_fma_f32 v[12:13], v[48:49], v[140:141], v[12:13]
	v_pk_fma_f32 v[14:15], v[50:51], v[142:143], v[14:15]
	v_add_f32_e32 v6, v6, v7
	v_cvt_scalef32_pk_f32_fp4 v[136:137], v102, 1.0
	v_cvt_scalef32_pk_f32_fp4 v[138:139], v102, 1.0 op_sel:[1,0,0]
	v_cvt_scalef32_pk_f32_fp4 v[140:141], v102, 1.0 op_sel:[0,1,0]
	v_cvt_scalef32_pk_f32_fp4 v[142:143], v102, 1.0 op_sel:[1,1,0]
	v_mov_b32_e32 v7, 0
	v_pk_fma_f32 v[8:9], v[52:53], v[136:137], v[8:9]
	v_pk_fma_f32 v[10:11], v[54:55], v[138:139], v[10:11]
	v_pk_fma_f32 v[12:13], v[56:57], v[140:141], v[12:13]
	v_pk_fma_f32 v[14:15], v[58:59], v[142:143], v[14:15]
	v_mov_b32_dpp v7, v6 row_bcast:31 row_mask:0xc bank_mask:0xf
	v_cvt_scalef32_pk_f32_fp4 v[136:137], v103, 1.0
	v_cvt_scalef32_pk_f32_fp4 v[138:139], v103, 1.0 op_sel:[1,0,0]
	v_cvt_scalef32_pk_f32_fp4 v[140:141], v103, 1.0 op_sel:[0,1,0]
	v_cvt_scalef32_pk_f32_fp4 v[142:143], v103, 1.0 op_sel:[1,1,0]
	v_add_f32_e32 v6, v6, v7
	v_pk_fma_f32 v[8:9], v[60:61], v[136:137], v[8:9]
	v_pk_fma_f32 v[10:11], v[62:63], v[138:139], v[10:11]
	v_pk_fma_f32 v[12:13], v[64:65], v[140:141], v[12:13]
	v_pk_fma_f32 v[14:15], v[80:81], v[142:143], v[14:15]
	v_readlane_b32 s74, v6, 63
	v_cvt_scalef32_pk_f32_fp4 v[136:137], v104, 1.0
	v_cvt_scalef32_pk_f32_fp4 v[138:139], v104, 1.0 op_sel:[1,0,0]
	v_cvt_scalef32_pk_f32_fp4 v[140:141], v104, 1.0 op_sel:[0,1,0]
	v_cvt_scalef32_pk_f32_fp4 v[142:143], v104, 1.0 op_sel:[1,1,0]
	s_lshl_b64 exec, 1, s32
	v_mov_b32_e32 v248, s74
	s_mov_b64 exec, -1
	v_pk_fma_f32 v[8:9], v[82:83], v[136:137], v[8:9]
	v_pk_fma_f32 v[10:11], v[84:85], v[138:139], v[10:11]
	v_pk_fma_f32 v[12:13], v[86:87], v[140:141], v[12:13]
	v_pk_fma_f32 v[14:15], v[88:89], v[142:143], v[14:15]
	v_cvt_scalef32_pk_f32_fp4 v[136:137], v105, 1.0
	v_cvt_scalef32_pk_f32_fp4 v[138:139], v105, 1.0 op_sel:[1,0,0]
	v_cvt_scalef32_pk_f32_fp4 v[140:141], v105, 1.0 op_sel:[0,1,0]
	v_cvt_scalef32_pk_f32_fp4 v[142:143], v105, 1.0 op_sel:[1,1,0]
	v_pk_fma_f32 v[8:9], v[90:91], v[136:137], v[8:9]
	v_pk_fma_f32 v[10:11], v[92:93], v[138:139], v[10:11]
	v_pk_fma_f32 v[12:13], v[94:95], v[140:141], v[12:13]
	v_pk_fma_f32 v[14:15], v[96:97], v[142:143], v[14:15]
	v_pk_add_f32 v[8:9], v[8:9], v[10:11]
	v_pk_add_f32 v[12:13], v[12:13], v[14:15]
	v_pk_add_f32 v[8:9], v[8:9], v[12:13]
	v_add_f32_e32 v5, v8, v9
	s_branch .Lpu2_odd
; DI void peer_token(LAS unsigned char* ring, const bf16* x1row, float inv2, const float* nffn, const int* ex, const float* pg, const unsigned char* U6, const unsigned char* V6,
;                    const float* usc, const float* vsc, float* orow, int lane) {
;     ...
; #pragma unroll 2
;     for (int k = 0; k < 56; ++k) P11_U(k, us_lo, gv_lo, cf_lo, ul, e_lo, k + 8);
; #pragma unroll 1
;     for (int k = 56; k < 64; ++k) P11_U(k, us_lo, gv_lo, cf_lo, ul, e_hi, k - 56);
; #pragma unroll 2
;     for (int k = 64; k < 120; ++k) P11_U(k, us_hi, gv_hi, cf_hi, ul, e_hi, k - 56);
; #pragma unroll 1
;     for (int k = 120; k < 128; ++k) P11_U(k, us_hi, gv_hi, cf_hi, vl, e_lo, k - 120);
.Lpu2_evenB:
	s_add_i32 s47, s46, 1
	s_and_b32 s47, s47, 7
	s_lshl_b32 s47, s47, 11
	s_add_i32 s77, s33, s47
	v_add_u32_e32 v4, s77, v70
	s_add_i32 s78, s46, 9
	s_and_b32 s75, s78, 63
	v_readlane_b32 s79, v243, s75
	v_readlane_b32 s47, v242, s75
	s_bitcmp1_b32 s78, 6
	s_cselect_b32 s47, s79, s47
	s_lshr_b32 s47, s47, 8
	s_lshl_b32 s47, s47, 11
	s_bitcmp1_b32 s78, 8
	s_cselect_b32 s78, s98, 0
	s_cselect_b32 s79, s99, 0
	s_add_u32 s78, s78, s47
	s_addc_u32 s79, s79, 0
	s_add_i32 s32, s46, 0
	s_waitcnt vmcnt(14)
	ds_read_b128 v[126:129], v4
	ds_read_b128 v[130:133], v4 offset:1024
	v_lshl_add_u64 v[2:3], v[72:73], 0, s[78:79]
	v_cvt_scalef32_pk_f32_fp4 v[136:137], v98, 1.0
	v_cvt_scalef32_pk_f32_fp4 v[138:139], v98, 1.0 op_sel:[1,0,0]
	v_cvt_scalef32_pk_f32_fp4 v[140:141], v98, 1.0 op_sel:[0,1,0]
	v_cvt_scalef32_pk_f32_fp4 v[142:143], v98, 1.0 op_sel:[1,1,0]
	v_add_f32_dpp v6, v6, v6 quad_perm:[1,0,3,2] row_mask:0xf bank_mask:0xf bound_ctrl:1
	v_pk_fma_f32 v[8:9], v[178:179], v[136:137], 0 op_sel_hi:[1,1,0]
	v_pk_fma_f32 v[10:11], v[180:181], v[138:139], 0 op_sel_hi:[1,1,0]
	v_pk_fma_f32 v[12:13], v[182:183], v[140:141], 0 op_sel_hi:[1,1,0]
	v_pk_fma_f32 v[14:15], v[184:185], v[142:143], 0 op_sel_hi:[1,1,0]
	v_add_f32_dpp v6, v6, v6 quad_perm:[2,3,0,1] row_mask:0xf bank_mask:0xf bound_ctrl:1
	v_cvt_scalef32_pk_f32_fp4 v[136:137], v99, 1.0
	v_cvt_scalef32_pk_f32_fp4 v[138:139], v99, 1.0 op_sel:[1,0,0]
	v_cvt_scalef32_pk_f32_fp4 v[140:141], v99, 1.0 op_sel:[0,1,0]
	v_cvt_scalef32_pk_f32_fp4 v[142:143], v99, 1.0 op_sel:[1,1,0]
	v_add_f32_dpp v6, v6, v6 row_half_mirror row_mask:0xf bank_mask:0xf bound_ctrl:1
	v_pk_fma_f32 v[8:9], v[186:187], v[136:137], v[8:9]
	v_pk_fma_f32 v[10:11], v[188:189], v[138:139], v[10:11]
	v_pk_fma_f32 v[12:13], v[190:191], v[140:141], v[12:13]
	v_pk_fma_f32 v[14:15], v[192:193], v[142:143], v[14:15]
	v_mov_b32_e32 v7, 0
	v_cvt_scalef32_pk_f32_fp4 v[136:137], v100, 1.0
	v_cvt_scalef32_pk_f32_fp4 v[138:139], v100, 1.0 op_sel:[1,0,0]
	v_cvt_scalef32_pk_f32_fp4 v[140:141], v100, 1.0 op_sel:[0,1,0]
	v_cvt_scalef32_pk_f32_fp4 v[142:143], v100, 1.0 op_sel:[1,1,0]
	v_add_f32_dpp v6, v6, v6 row_mirror row_mask:0xf bank_mask:0xf bound_ctrl:1
	v_pk_fma_f32 v[8:9], v[194:195], v[136:137], v[8:9]
	v_pk_fma_f32 v[10:11], v[196:197], v[138:139], v[10:11]
	v_pk_fma_f32 v[12:13], v[198:199], v[140:141], v[12:13]
	v_pk_fma_f32 v[14:15], v[200:201], v[142:143], v[14:15]
	s_waitcnt lgkmcnt(0)
	s_mov_b32 m0, s77
	s_nop 0
	global_load_lds_dwordx4 v[2:3], off
	global_load_lds_dwordx4 v[2:3], off offset:1024
	v_cvt_scalef32_pk_f32_fp4 v[136:137], v101, 1.0
	v_cvt_scalef32_pk_f32_fp4 v[138:139], v101, 1.0 op_sel:[1,0,0]
	v_cvt_scalef32_pk_f32_fp4 v[140:141], v101, 1.0 op_sel:[0,1,0]
	v_cvt_scalef32_pk_f32_fp4 v[142:143], v101, 1.0 op_sel:[1,1,0]
	v_mov_b32_dpp v7, v6 row_bcast:15 row_mask:0xa bank_mask:0xf
	v_pk_fma_f32 v[8:9], v[202:203], v[136:137], v[8:9]
	v_pk_fma_f32 v[10:11], v[204:205], v[138:139], v[10:11]
	v_pk_fma_f32 v[12:13], v[206:207], v[140:141], v[12:13]
	v_pk_fma_f32 v[14:15], v[208:209], v[142:143], v[14:15]
	v_add_f32_e32 v6, v6, v7
	v_cvt_scalef32_pk_f32_fp4 v[136:137], v102, 1.0
	v_cvt_scalef32_pk_f32_fp4 v[138:139], v102, 1.0 op_sel:[1,0,0]
	v_cvt_scalef32_pk_f32_fp4 v[140:141], v102, 1.0 op_sel:[0,1,0]
	v_cvt_scalef32_pk_f32_fp4 v[142:143], v102, 1.0 op_sel:[1,1,0]
	v_mov_b32_e32 v7, 0
	v_pk_fma_f32 v[8:9], v[210:211], v[136:137], v[8:9]
	v_pk_fma_f32 v[10:11], v[212:213], v[138:139], v[10:11]
	v_pk_fma_f32 v[12:13], v[214:215], v[140:141], v[12:13]
	v_pk_fma_f32 v[14:15], v[216:217], v[142:143], v[14:15]
	v_mov_b32_dpp v7, v6 row_bcast:31 row_mask:0xc bank_mask:0xf
	v_cvt_scalef32_pk_f32_fp4 v[136:137], v103, 1.0
	v_cvt_scalef32_pk_f32_fp4 v[138:139], v103, 1.0 op_sel:[1,0,0]
	v_cvt_scalef32_pk_f32_fp4 v[140:141], v103, 1.0 op_sel:[0,1,0]
	v_cvt_scalef32_pk_f32_fp4 v[142:143], v103, 1.0 op_sel:[1,1,0]
	v_add_f32_e32 v6, v6, v7
	v_pk_fma_f32 v[8:9], v[218:219], v[136:137], v[8:9]
	v_pk_fma_f32 v[10:11], v[220:221], v[138:139], v[10:11]
	v_pk_fma_f32 v[12:13], v[222:223], v[140:141], v[12:13]
	v_pk_fma_f32 v[14:15], v[224:225], v[142:143], v[14:15]
	v_readlane_b32 s74, v6, 63
	v_cvt_scalef32_pk_f32_fp4 v[136:137], v104, 1.0
	v_cvt_scalef32_pk_f32_fp4 v[138:139], v104, 1.0 op_sel:[1,0,0]
	v_cvt_scalef32_pk_f32_fp4 v[140:141], v104, 1.0 op_sel:[0,1,0]
	v_cvt_scalef32_pk_f32_fp4 v[142:143], v104, 1.0 op_sel:[1,1,0]
	s_lshl_b64 exec, 1, s32
	v_mov_b32_e32 v248, s74
	s_mov_b64 exec, -1
	v_pk_fma_f32 v[8:9], v[226:227], v[136:137], v[8:9]
	v_pk_fma_f32 v[10:11], v[228:229], v[138:139], v[10:11]
	v_pk_fma_f32 v[12:13], v[230:231], v[140:141], v[12:13]
	v_pk_fma_f32 v[14:15], v[232:233], v[142:143], v[14:15]
	v_cvt_scalef32_pk_f32_fp4 v[136:137], v105, 1.0
	v_cvt_scalef32_pk_f32_fp4 v[138:139], v105, 1.0 op_sel:[1,0,0]
	v_cvt_scalef32_pk_f32_fp4 v[140:141], v105, 1.0 op_sel:[0,1,0]
	v_cvt_scalef32_pk_f32_fp4 v[142:143], v105, 1.0 op_sel:[1,1,0]
	v_pk_fma_f32 v[8:9], v[234:235], v[136:137], v[8:9]
	v_pk_fma_f32 v[10:11], v[236:237], v[138:139], v[10:11]
	v_pk_fma_f32 v[12:13], v[238:239], v[140:141], v[12:13]
	v_pk_fma_f32 v[14:15], v[240:241], v[142:143], v[14:15]
	v_pk_add_f32 v[8:9], v[8:9], v[10:11]
	v_pk_add_f32 v[12:13], v[12:13], v[14:15]
	v_pk_add_f32 v[8:9], v[8:9], v[12:13]
	v_add_f32_e32 v5, v8, v9
; DI void peer_token(LAS unsigned char* ring, const bf16* x1row, float inv2, const float* nffn, const int* ex, const float* pg, const unsigned char* U6, const unsigned char* V6,
;                    const float* usc, const float* vsc, float* orow, int lane) {
;     ...
; #pragma unroll 2
;     for (int k = 0; k < 56; ++k) P11_U(k, us_lo, gv_lo, cf_lo, ul, e_lo, k + 8);
; #pragma unroll 1
;     for (int k = 56; k < 64; ++k) P11_U(k, us_lo, gv_lo, cf_lo, ul, e_hi, k - 56);
; #pragma unroll 2
;     for (int k = 64; k < 120; ++k) P11_U(k, us_hi, gv_hi, cf_hi, ul, e_hi, k - 56);
; #pragma unroll 1
;     for (int k = 120; k < 128; ++k) P11_U(k, us_hi, gv_hi, cf_hi, vl, e_lo, k - 120);
.Lpu2_odd:
	s_add_i32 s32, s46, 1
	s_bitcmp1_b64 s[82:83], s32
	s_cbranch_scc1 .Lpu2_oddB
	s_add_i32 s47, s46, 2
	s_and_b32 s47, s47, 7
	s_lshl_b32 s47, s47, 11
	s_add_i32 s77, s33, s47
	v_add_u32_e32 v4, s77, v70
	s_add_i32 s78, s46, 10
	s_and_b32 s75, s78, 63
	v_readlane_b32 s79, v243, s75
	v_readlane_b32 s47, v242, s75
	s_bitcmp1_b32 s78, 6
	s_cselect_b32 s47, s79, s47
	s_lshr_b32 s47, s47, 8
	s_lshl_b32 s47, s47, 11
	s_bitcmp1_b32 s78, 8
	s_cselect_b32 s78, s98, 0
	s_cselect_b32 s79, s99, 0
	s_add_u32 s78, s78, s47
	s_addc_u32 s79, s79, 0
	s_add_i32 s32, s46, 1
	s_waitcnt vmcnt(14)
	ds_read_b128 v[98:101], v4
	ds_read_b128 v[102:105], v4 offset:1024
	v_lshl_add_u64 v[2:3], v[72:73], 0, s[78:79]
	v_cvt_scalef32_pk_f32_fp4 v[136:137], v126, 1.0
	v_cvt_scalef32_pk_f32_fp4 v[138:139], v126, 1.0 op_sel:[1,0,0]
	v_cvt_scalef32_pk_f32_fp4 v[140:141], v126, 1.0 op_sel:[0,1,0]
	v_cvt_scalef32_pk_f32_fp4 v[142:143], v126, 1.0 op_sel:[1,1,0]
	v_add_f32_dpp v5, v5, v5 quad_perm:[1,0,3,2] row_mask:0xf bank_mask:0xf bound_ctrl:1
	v_pk_fma_f32 v[8:9], v[20:21], v[136:137], 0 op_sel_hi:[1,1,0]
	v_pk_fma_f32 v[10:11], v[22:23], v[138:139], 0 op_sel_hi:[1,1,0]
	v_pk_fma_f32 v[12:13], v[24:25], v[140:141], 0 op_sel_hi:[1,1,0]
	v_pk_fma_f32 v[14:15], v[26:27], v[142:143], 0 op_sel_hi:[1,1,0]
	v_add_f32_dpp v5, v5, v5 quad_perm:[2,3,0,1] row_mask:0xf bank_mask:0xf bound_ctrl:1
	v_cvt_scalef32_pk_f32_fp4 v[136:137], v127, 1.0
	v_cvt_scalef32_pk_f32_fp4 v[138:139], v127, 1.0 op_sel:[1,0,0]
	v_cvt_scalef32_pk_f32_fp4 v[140:141], v127, 1.0 op_sel:[0,1,0]
	v_cvt_scalef32_pk_f32_fp4 v[142:143], v127, 1.0 op_sel:[1,1,0]
	v_add_f32_dpp v5, v5, v5 row_half_mirror row_mask:0xf bank_mask:0xf bound_ctrl:1
	v_pk_fma_f32 v[8:9], v[28:29], v[136:137], v[8:9]
	v_pk_fma_f32 v[10:11], v[30:31], v[138:139], v[10:11]
	v_pk_fma_f32 v[12:13], v[32:33], v[140:141], v[12:13]
	v_pk_fma_f32 v[14:15], v[34:35], v[142:143], v[14:15]
	v_mov_b32_e32 v7, 0
	v_cvt_scalef32_pk_f32_fp4 v[136:137], v128, 1.0
	v_cvt_scalef32_pk_f32_fp4 v[138:139], v128, 1.0 op_sel:[1,0,0]
	v_cvt_scalef32_pk_f32_fp4 v[140:141], v128, 1.0 op_sel:[0,1,0]
	v_cvt_scalef32_pk_f32_fp4 v[142:143], v128, 1.0 op_sel:[1,1,0]
	v_add_f32_dpp v5, v5, v5 row_mirror row_mask:0xf bank_mask:0xf bound_ctrl:1
	v_pk_fma_f32 v[8:9], v[36:37], v[136:137], v[8:9]
	v_pk_fma_f32 v[10:11], v[38:39], v[138:139], v[10:11]
	v_pk_fma_f32 v[12:13], v[40:41], v[140:141], v[12:13]
	v_pk_fma_f32 v[14:15], v[42:43], v[142:143], v[14:15]
	s_waitcnt lgkmcnt(0)
	s_mov_b32 m0, s77
	s_nop 0
	global_load_lds_dwordx4 v[2:3], off
	global_load_lds_dwordx4 v[2:3], off offset:1024
	v_cvt_scalef32_pk_f32_fp4 v[136:137], v129, 1.0
	v_cvt_scalef32_pk_f32_fp4 v[138:139], v129, 1.0 op_sel:[1,0,0]
	v_cvt_scalef32_pk_f32_fp4 v[140:141], v129, 1.0 op_sel:[0,1,0]
	v_cvt_scalef32_pk_f32_fp4 v[142:143], v129, 1.0 op_sel:[1,1,0]
	v_mov_b32_dpp v7, v5 row_bcast:15 row_mask:0xa bank_mask:0xf
	v_pk_fma_f32 v[8:9], v[44:45], v[136:137], v[8:9]
	v_pk_fma_f32 v[10:11], v[46:47], v[138:139], v[10:11]
	v_pk_fma_f32 v[12:13], v[48:49], v[140:141], v[12:13]
	v_pk_fma_f32 v[14:15], v[50:51], v[142:143], v[14:15]
	v_add_f32_e32 v5, v5, v7
	v_cvt_scalef32_pk_f32_fp4 v[136:137], v130, 1.0
	v_cvt_scalef32_pk_f32_fp4 v[138:139], v130, 1.0 op_sel:[1,0,0]
	v_cvt_scalef32_pk_f32_fp4 v[140:141], v130, 1.0 op_sel:[0,1,0]
	v_cvt_scalef32_pk_f32_fp4 v[142:143], v130, 1.0 op_sel:[1,1,0]
	v_mov_b32_e32 v7, 0
	v_pk_fma_f32 v[8:9], v[52:53], v[136:137], v[8:9]
	v_pk_fma_f32 v[10:11], v[54:55], v[138:139], v[10:11]
	v_pk_fma_f32 v[12:13], v[56:57], v[140:141], v[12:13]
	v_pk_fma_f32 v[14:15], v[58:59], v[142:143], v[14:15]
	v_mov_b32_dpp v7, v5 row_bcast:31 row_mask:0xc bank_mask:0xf
	v_cvt_scalef32_pk_f32_fp4 v[136:137], v131, 1.0
	v_cvt_scalef32_pk_f32_fp4 v[138:139], v131, 1.0 op_sel:[1,0,0]
	v_cvt_scalef32_pk_f32_fp4 v[140:141], v131, 1.0 op_sel:[0,1,0]
	v_cvt_scalef32_pk_f32_fp4 v[142:143], v131, 1.0 op_sel:[1,1,0]
	v_add_f32_e32 v5, v5, v7
	v_pk_fma_f32 v[8:9], v[60:61], v[136:137], v[8:9]
	v_pk_fma_f32 v[10:11], v[62:63], v[138:139], v[10:11]
	v_pk_fma_f32 v[12:13], v[64:65], v[140:141], v[12:13]
	v_pk_fma_f32 v[14:15], v[80:81], v[142:143], v[14:15]
	v_readlane_b32 s74, v5, 63
	v_cvt_scalef32_pk_f32_fp4 v[136:137], v132, 1.0
	v_cvt_scalef32_pk_f32_fp4 v[138:139], v132, 1.0 op_sel:[1,0,0]
	v_cvt_scalef32_pk_f32_fp4 v[140:141], v132, 1.0 op_sel:[0,1,0]
	v_cvt_scalef32_pk_f32_fp4 v[142:143], v132, 1.0 op_sel:[1,1,0]
	s_lshl_b64 exec, 1, s32
	v_mov_b32_e32 v248, s74
	s_mov_b64 exec, -1
	v_pk_fma_f32 v[8:9], v[82:83], v[136:137], v[8:9]
	v_pk_fma_f32 v[10:11], v[84:85], v[138:139], v[10:11]
	v_pk_fma_f32 v[12:13], v[86:87], v[140:141], v[12:13]
	v_pk_fma_f32 v[14:15], v[88:89], v[142:143], v[14:15]
	v_cvt_scalef32_pk_f32_fp4 v[136:137], v133, 1.0
	v_cvt_scalef32_pk_f32_fp4 v[138:139], v133, 1.0 op_sel:[1,0,0]
	v_cvt_scalef32_pk_f32_fp4 v[140:141], v133, 1.0 op_sel:[0,1,0]
	v_cvt_scalef32_pk_f32_fp4 v[142:143], v133, 1.0 op_sel:[1,1,0]
	v_pk_fma_f32 v[8:9], v[90:91], v[136:137], v[8:9]
	v_pk_fma_f32 v[10:11], v[92:93], v[138:139], v[10:11]
	v_pk_fma_f32 v[12:13], v[94:95], v[140:141], v[12:13]
	v_pk_fma_f32 v[14:15], v[96:97], v[142:143], v[14:15]
	v_pk_add_f32 v[8:9], v[8:9], v[10:11]
	v_pk_add_f32 v[12:13], v[12:13], v[14:15]
	v_pk_add_f32 v[8:9], v[8:9], v[12:13]
	v_add_f32_e32 v6, v8, v9
	s_branch .Lpu2_next
.Lpu2_oddB:
	s_add_i32 s47, s46, 2
	s_and_b32 s47, s47, 7
	s_lshl_b32 s47, s47, 11
	s_add_i32 s77, s33, s47
	v_add_u32_e32 v4, s77, v70
	s_add_i32 s78, s46, 10
	s_and_b32 s75, s78, 63
	v_readlane_b32 s79, v243, s75
	v_readlane_b32 s47, v242, s75
	s_bitcmp1_b32 s78, 6
	s_cselect_b32 s47, s79, s47
	s_lshr_b32 s47, s47, 8
	s_lshl_b32 s47, s47, 11
	s_bitcmp1_b32 s78, 8
	s_cselect_b32 s78, s98, 0
	s_cselect_b32 s79, s99, 0
	s_add_u32 s78, s78, s47
	s_addc_u32 s79, s79, 0
	s_add_i32 s32, s46, 1
	s_waitcnt vmcnt(14)
	ds_read_b128 v[98:101], v4
	ds_read_b128 v[102:105], v4 offset:1024
	v_lshl_add_u64 v[2:3], v[72:73], 0, s[78:79]
	v_cvt_scalef32_pk_f32_fp4 v[136:137], v126, 1.0
	v_cvt_scalef32_pk_f32_fp4 v[138:139], v126, 1.0 op_sel:[1,0,0]
	v_cvt_scalef32_pk_f32_fp4 v[140:141], v126, 1.0 op_sel:[0,1,0]
	v_cvt_scalef32_pk_f32_fp4 v[142:143], v126, 1.0 op_sel:[1,1,0]
	v_add_f32_dpp v5, v5, v5 quad_perm:[1,0,3,2] row_mask:0xf bank_mask:0xf bound_ctrl:1
	v_pk_fma_f32 v[8:9], v[178:179], v[136:137], 0 op_sel_hi:[1,1,0]
	v_pk_fma_f32 v[10:11], v[180:181], v[138:139], 0 op_sel_hi:[1,1,0]
	v_pk_fma_f32 v[12:13], v[182:183], v[140:141], 0 op_sel_hi:[1,1,0]
	v_pk_fma_f32 v[14:15], v[184:185], v[142:143], 0 op_sel_hi:[1,1,0]
	v_add_f32_dpp v5, v5, v5 quad_perm:[2,3,0,1] row_mask:0xf bank_mask:0xf bound_ctrl:1
	v_cvt_scalef32_pk_f32_fp4 v[136:137], v127, 1.0
	v_cvt_scalef32_pk_f32_fp4 v[138:139], v127, 1.0 op_sel:[1,0,0]
	v_cvt_scalef32_pk_f32_fp4 v[140:141], v127, 1.0 op_sel:[0,1,0]
	v_cvt_scalef32_pk_f32_fp4 v[142:143], v127, 1.0 op_sel:[1,1,0]
	v_add_f32_dpp v5, v5, v5 row_half_mirror row_mask:0xf bank_mask:0xf bound_ctrl:1
	v_pk_fma_f32 v[8:9], v[186:187], v[136:137], v[8:9]
	v_pk_fma_f32 v[10:11], v[188:189], v[138:139], v[10:11]
	v_pk_fma_f32 v[12:13], v[190:191], v[140:141], v[12:13]
	v_pk_fma_f32 v[14:15], v[192:193], v[142:143], v[14:15]
	v_mov_b32_e32 v7, 0
	v_cvt_scalef32_pk_f32_fp4 v[136:137], v128, 1.0
	v_cvt_scalef32_pk_f32_fp4 v[138:139], v128, 1.0 op_sel:[1,0,0]
	v_cvt_scalef32_pk_f32_fp4 v[140:141], v128, 1.0 op_sel:[0,1,0]
	v_cvt_scalef32_pk_f32_fp4 v[142:143], v128, 1.0 op_sel:[1,1,0]
	v_add_f32_dpp v5, v5, v5 row_mirror row_mask:0xf bank_mask:0xf bound_ctrl:1
	v_pk_fma_f32 v[8:9], v[194:195], v[136:137], v[8:9]
	v_pk_fma_f32 v[10:11], v[196:197], v[138:139], v[10:11]
	v_pk_fma_f32 v[12:13], v[198:199], v[140:141], v[12:13]
	v_pk_fma_f32 v[14:15], v[200:201], v[142:143], v[14:15]
	s_waitcnt lgkmcnt(0)
	s_mov_b32 m0, s77
	s_nop 0
	global_load_lds_dwordx4 v[2:3], off
	global_load_lds_dwordx4 v[2:3], off offset:1024
	v_cvt_scalef32_pk_f32_fp4 v[136:137], v129, 1.0
	v_cvt_scalef32_pk_f32_fp4 v[138:139], v129, 1.0 op_sel:[1,0,0]
	v_cvt_scalef32_pk_f32_fp4 v[140:141], v129, 1.0 op_sel:[0,1,0]
	v_cvt_scalef32_pk_f32_fp4 v[142:143], v129, 1.0 op_sel:[1,1,0]
	v_mov_b32_dpp v7, v5 row_bcast:15 row_mask:0xa bank_mask:0xf
	v_pk_fma_f32 v[8:9], v[202:203], v[136:137], v[8:9]
	v_pk_fma_f32 v[10:11], v[204:205], v[138:139], v[10:11]
	v_pk_fma_f32 v[12:13], v[206:207], v[140:141], v[12:13]
	v_pk_fma_f32 v[14:15], v[208:209], v[142:143], v[14:15]
	v_add_f32_e32 v5, v5, v7
	v_cvt_scalef32_pk_f32_fp4 v[136:137], v130, 1.0
	v_cvt_scalef32_pk_f32_fp4 v[138:139], v130, 1.0 op_sel:[1,0,0]
	v_cvt_scalef32_pk_f32_fp4 v[140:141], v130, 1.0 op_sel:[0,1,0]
	v_cvt_scalef32_pk_f32_fp4 v[142:143], v130, 1.0 op_sel:[1,1,0]
	v_mov_b32_e32 v7, 0
	v_pk_fma_f32 v[8:9], v[210:211], v[136:137], v[8:9]
	v_pk_fma_f32 v[10:11], v[212:213], v[138:139], v[10:11]
	v_pk_fma_f32 v[12:13], v[214:215], v[140:141], v[12:13]
	v_pk_fma_f32 v[14:15], v[216:217], v[142:143], v[14:15]
	v_mov_b32_dpp v7, v5 row_bcast:31 row_mask:0xc bank_mask:0xf
	v_cvt_scalef32_pk_f32_fp4 v[136:137], v131, 1.0
	v_cvt_scalef32_pk_f32_fp4 v[138:139], v131, 1.0 op_sel:[1,0,0]
	v_cvt_scalef32_pk_f32_fp4 v[140:141], v131, 1.0 op_sel:[0,1,0]
	v_cvt_scalef32_pk_f32_fp4 v[142:143], v131, 1.0 op_sel:[1,1,0]
	v_add_f32_e32 v5, v5, v7
	v_pk_fma_f32 v[8:9], v[218:219], v[136:137], v[8:9]
	v_pk_fma_f32 v[10:11], v[220:221], v[138:139], v[10:11]
	v_pk_fma_f32 v[12:13], v[222:223], v[140:141], v[12:13]
	v_pk_fma_f32 v[14:15], v[224:225], v[142:143], v[14:15]
	v_readlane_b32 s74, v5, 63
	v_cvt_scalef32_pk_f32_fp4 v[136:137], v132, 1.0
	v_cvt_scalef32_pk_f32_fp4 v[138:139], v132, 1.0 op_sel:[1,0,0]
	v_cvt_scalef32_pk_f32_fp4 v[140:141], v132, 1.0 op_sel:[0,1,0]
	v_cvt_scalef32_pk_f32_fp4 v[142:143], v132, 1.0 op_sel:[1,1,0]
	s_lshl_b64 exec, 1, s32
	v_mov_b32_e32 v248, s74
	s_mov_b64 exec, -1
	v_pk_fma_f32 v[8:9], v[226:227], v[136:137], v[8:9]
	v_pk_fma_f32 v[10:11], v[228:229], v[138:139], v[10:11]
	v_pk_fma_f32 v[12:13], v[230:231], v[140:141], v[12:13]
	v_pk_fma_f32 v[14:15], v[232:233], v[142:143], v[14:15]
	v_cvt_scalef32_pk_f32_fp4 v[136:137], v133, 1.0
	v_cvt_scalef32_pk_f32_fp4 v[138:139], v133, 1.0 op_sel:[1,0,0]
	v_cvt_scalef32_pk_f32_fp4 v[140:141], v133, 1.0 op_sel:[0,1,0]
	v_cvt_scalef32_pk_f32_fp4 v[142:143], v133, 1.0 op_sel:[1,1,0]
	v_pk_fma_f32 v[8:9], v[234:235], v[136:137], v[8:9]
	v_pk_fma_f32 v[10:11], v[236:237], v[138:139], v[10:11]
	v_pk_fma_f32 v[12:13], v[238:239], v[140:141], v[12:13]
	v_pk_fma_f32 v[14:15], v[240:241], v[142:143], v[14:15]
	v_pk_add_f32 v[8:9], v[8:9], v[10:11]
	v_pk_add_f32 v[12:13], v[12:13], v[14:15]
	v_pk_add_f32 v[8:9], v[8:9], v[12:13]
	v_add_f32_e32 v6, v8, v9
.Lpu2_next:
	s_add_i32 s46, s46, 2
	s_cmp_lg_u32 s46, 192
	s_cbranch_scc1 .Lpu2_even
; DI void peer_token(LAS unsigned char* ring, const bf16* x1row, float inv2, const float* nffn, const int* ex, const float* pg, const unsigned char* U6, const unsigned char* V6,
;                    const float* usc, const float* vsc, float* orow, int lane) {
;     ...
;     for (int k = 120; k < 128; ++k) P11_U(k, us_hi, gv_hi, cf_hi, vl, e_lo, k - 120);
.Lpu3_even:
	s_bitcmp1_b64 s[70:71], s46
	s_cbranch_scc1 .Lpu3_evenB
	s_add_i32 s47, s46, 1
	s_and_b32 s47, s47, 7
	s_lshl_b32 s47, s47, 11
	s_add_i32 s77, s33, s47
	v_add_u32_e32 v4, s77, v70
	s_add_i32 s78, s46, 9
	s_and_b32 s75, s78, 63
	v_readlane_b32 s79, v112, s75
	v_readlane_b32 s47, v243, s75
	s_bitcmp1_b32 s78, 6
	s_cselect_b32 s47, s47, s79
	s_lshr_b32 s47, s47, 8
	s_lshl_b32 s47, s47, 11
	s_bitcmp1_b32 s78, 8
	s_cselect_b32 s78, s98, 0
	s_cselect_b32 s79, s99, 0
	s_add_u32 s78, s78, s47
	s_addc_u32 s79, s79, 0
	s_add_i32 s32, s46, 0
	s_waitcnt vmcnt(14)
	ds_read_b128 v[126:129], v4
	ds_read_b128 v[130:133], v4 offset:1024
	v_lshl_add_u64 v[2:3], v[72:73], 0, s[78:79]
	v_cvt_scalef32_pk_f32_fp4 v[136:137], v98, 1.0
	v_cvt_scalef32_pk_f32_fp4 v[138:139], v98, 1.0 op_sel:[1,0,0]
	v_cvt_scalef32_pk_f32_fp4 v[140:141], v98, 1.0 op_sel:[0,1,0]
	v_cvt_scalef32_pk_f32_fp4 v[142:143], v98, 1.0 op_sel:[1,1,0]
	v_add_f32_dpp v6, v6, v6 quad_perm:[1,0,3,2] row_mask:0xf bank_mask:0xf bound_ctrl:1
	v_pk_fma_f32 v[8:9], v[20:21], v[136:137], 0 op_sel_hi:[1,1,0]
	v_pk_fma_f32 v[10:11], v[22:23], v[138:139], 0 op_sel_hi:[1,1,0]
	v_pk_fma_f32 v[12:13], v[24:25], v[140:141], 0 op_sel_hi:[1,1,0]
	v_pk_fma_f32 v[14:15], v[26:27], v[142:143], 0 op_sel_hi:[1,1,0]
	v_add_f32_dpp v6, v6, v6 quad_perm:[2,3,0,1] row_mask:0xf bank_mask:0xf bound_ctrl:1
	v_cvt_scalef32_pk_f32_fp4 v[136:137], v99, 1.0
	v_cvt_scalef32_pk_f32_fp4 v[138:139], v99, 1.0 op_sel:[1,0,0]
	v_cvt_scalef32_pk_f32_fp4 v[140:141], v99, 1.0 op_sel:[0,1,0]
	v_cvt_scalef32_pk_f32_fp4 v[142:143], v99, 1.0 op_sel:[1,1,0]
	v_add_f32_dpp v6, v6, v6 row_half_mirror row_mask:0xf bank_mask:0xf bound_ctrl:1
	v_pk_fma_f32 v[8:9], v[28:29], v[136:137], v[8:9]
	v_pk_fma_f32 v[10:11], v[30:31], v[138:139], v[10:11]
	v_pk_fma_f32 v[12:13], v[32:33], v[140:141], v[12:13]
	v_pk_fma_f32 v[14:15], v[34:35], v[142:143], v[14:15]
	v_mov_b32_e32 v7, 0
	v_cvt_scalef32_pk_f32_fp4 v[136:137], v100, 1.0
	v_cvt_scalef32_pk_f32_fp4 v[138:139], v100, 1.0 op_sel:[1,0,0]
	v_cvt_scalef32_pk_f32_fp4 v[140:141], v100, 1.0 op_sel:[0,1,0]
	v_cvt_scalef32_pk_f32_fp4 v[142:143], v100, 1.0 op_sel:[1,1,0]
	v_add_f32_dpp v6, v6, v6 row_mirror row_mask:0xf bank_mask:0xf bound_ctrl:1
	v_pk_fma_f32 v[8:9], v[36:37], v[136:137], v[8:9]
	v_pk_fma_f32 v[10:11], v[38:39], v[138:139], v[10:11]
	v_pk_fma_f32 v[12:13], v[40:41], v[140:141], v[12:13]
	v_pk_fma_f32 v[14:15], v[42:43], v[142:143], v[14:15]
	s_waitcnt lgkmcnt(0)
	s_mov_b32 m0, s77
	s_nop 0
	global_load_lds_dwordx4 v[2:3], off
	global_load_lds_dwordx4 v[2:3], off offset:1024
	v_cvt_scalef32_pk_f32_fp4 v[136:137], v101, 1.0
	v_cvt_scalef32_pk_f32_fp4 v[138:139], v101, 1.0 op_sel:[1,0,0]
	v_cvt_scalef32_pk_f32_fp4 v[140:141], v101, 1.0 op_sel:[0,1,0]
	v_cvt_scalef32_pk_f32_fp4 v[142:143], v101, 1.0 op_sel:[1,1,0]
	v_mov_b32_dpp v7, v6 row_bcast:15 row_mask:0xa bank_mask:0xf
	v_pk_fma_f32 v[8:9], v[44:45], v[136:137], v[8:9]
	v_pk_fma_f32 v[10:11], v[46:47], v[138:139], v[10:11]
	v_pk_fma_f32 v[12:13], v[48:49], v[140:141], v[12:13]
	v_pk_fma_f32 v[14:15], v[50:51], v[142:143], v[14:15]
	v_add_f32_e32 v6, v6, v7
	v_cvt_scalef32_pk_f32_fp4 v[136:137], v102, 1.0
	v_cvt_scalef32_pk_f32_fp4 v[138:139], v102, 1.0 op_sel:[1,0,0]
	v_cvt_scalef32_pk_f32_fp4 v[140:141], v102, 1.0 op_sel:[0,1,0]
	v_cvt_scalef32_pk_f32_fp4 v[142:143], v102, 1.0 op_sel:[1,1,0]
	v_mov_b32_e32 v7, 0
	v_pk_fma_f32 v[8:9], v[52:53], v[136:137], v[8:9]
	v_pk_fma_f32 v[10:11], v[54:55], v[138:139], v[10:11]
	v_pk_fma_f32 v[12:13], v[56:57], v[140:141], v[12:13]
	v_pk_fma_f32 v[14:15], v[58:59], v[142:143], v[14:15]
	v_mov_b32_dpp v7, v6 row_bcast:31 row_mask:0xc bank_mask:0xf
	v_cvt_scalef32_pk_f32_fp4 v[136:137], v103, 1.0
	v_cvt_scalef32_pk_f32_fp4 v[138:139], v103, 1.0 op_sel:[1,0,0]
	v_cvt_scalef32_pk_f32_fp4 v[140:141], v103, 1.0 op_sel:[0,1,0]
	v_cvt_scalef32_pk_f32_fp4 v[142:143], v103, 1.0 op_sel:[1,1,0]
	v_add_f32_e32 v6, v6, v7
	v_pk_fma_f32 v[8:9], v[60:61], v[136:137], v[8:9]
	v_pk_fma_f32 v[10:11], v[62:63], v[138:139], v[10:11]
	v_pk_fma_f32 v[12:13], v[64:65], v[140:141], v[12:13]
	v_pk_fma_f32 v[14:15], v[80:81], v[142:143], v[14:15]
	v_readlane_b32 s74, v6, 63
	v_cvt_scalef32_pk_f32_fp4 v[136:137], v104, 1.0
	v_cvt_scalef32_pk_f32_fp4 v[138:139], v104, 1.0 op_sel:[1,0,0]
	v_cvt_scalef32_pk_f32_fp4 v[140:141], v104, 1.0 op_sel:[0,1,0]
	v_cvt_scalef32_pk_f32_fp4 v[142:143], v104, 1.0 op_sel:[1,1,0]
	s_lshl_b64 exec, 1, s32
	v_mov_b32_e32 v123, s74
	s_mov_b64 exec, -1
	v_pk_fma_f32 v[8:9], v[82:83], v[136:137], v[8:9]
	v_pk_fma_f32 v[10:11], v[84:85], v[138:139], v[10:11]
	v_pk_fma_f32 v[12:13], v[86:87], v[140:141], v[12:13]
	v_pk_fma_f32 v[14:15], v[88:89], v[142:143], v[14:15]
	v_cvt_scalef32_pk_f32_fp4 v[136:137], v105, 1.0
	v_cvt_scalef32_pk_f32_fp4 v[138:139], v105, 1.0 op_sel:[1,0,0]
	v_cvt_scalef32_pk_f32_fp4 v[140:141], v105, 1.0 op_sel:[0,1,0]
	v_cvt_scalef32_pk_f32_fp4 v[142:143], v105, 1.0 op_sel:[1,1,0]
	v_pk_fma_f32 v[8:9], v[90:91], v[136:137], v[8:9]
	v_pk_fma_f32 v[10:11], v[92:93], v[138:139], v[10:11]
	v_pk_fma_f32 v[12:13], v[94:95], v[140:141], v[12:13]
	v_pk_fma_f32 v[14:15], v[96:97], v[142:143], v[14:15]
	v_pk_add_f32 v[8:9], v[8:9], v[10:11]
	v_pk_add_f32 v[12:13], v[12:13], v[14:15]
	v_pk_add_f32 v[8:9], v[8:9], v[12:13]
	v_add_f32_e32 v5, v8, v9
	s_branch .Lpu3_odd
; DI void peer_token(LAS unsigned char* ring, const bf16* x1row, float inv2, const float* nffn, const int* ex, const float* pg, const unsigned char* U6, const unsigned char* V6,
;                    const float* usc, const float* vsc, float* orow, int lane) {
;     ...
;     for (int k = 120; k < 128; ++k) P11_U(k, us_hi, gv_hi, cf_hi, vl, e_lo, k - 120);
.Lpu3_evenB:
	s_add_i32 s47, s46, 1
	s_and_b32 s47, s47, 7
	s_lshl_b32 s47, s47, 11
	s_add_i32 s77, s33, s47
	v_add_u32_e32 v4, s77, v70
	s_add_i32 s78, s46, 9
	s_and_b32 s75, s78, 63
	v_readlane_b32 s79, v112, s75
	v_readlane_b32 s47, v243, s75
	s_bitcmp1_b32 s78, 6
	s_cselect_b32 s47, s47, s79
	s_lshr_b32 s47, s47, 8
	s_lshl_b32 s47, s47, 11
	s_bitcmp1_b32 s78, 8
	s_cselect_b32 s78, s98, 0
	s_cselect_b32 s79, s99, 0
	s_add_u32 s78, s78, s47
	s_addc_u32 s79, s79, 0
	s_add_i32 s32, s46, 0
	s_waitcnt vmcnt(14)
	ds_read_b128 v[126:129], v4
	ds_read_b128 v[130:133], v4 offset:1024
	v_lshl_add_u64 v[2:3], v[72:73], 0, s[78:79]
	v_cvt_scalef32_pk_f32_fp4 v[136:137], v98, 1.0
	v_cvt_scalef32_pk_f32_fp4 v[138:139], v98, 1.0 op_sel:[1,0,0]
	v_cvt_scalef32_pk_f32_fp4 v[140:141], v98, 1.0 op_sel:[0,1,0]
	v_cvt_scalef32_pk_f32_fp4 v[142:143], v98, 1.0 op_sel:[1,1,0]
	v_add_f32_dpp v6, v6, v6 quad_perm:[1,0,3,2] row_mask:0xf bank_mask:0xf bound_ctrl:1
	v_pk_fma_f32 v[8:9], v[178:179], v[136:137], 0 op_sel_hi:[1,1,0]
	v_pk_fma_f32 v[10:11], v[180:181], v[138:139], 0 op_sel_hi:[1,1,0]
	v_pk_fma_f32 v[12:13], v[182:183], v[140:141], 0 op_sel_hi:[1,1,0]
	v_pk_fma_f32 v[14:15], v[184:185], v[142:143], 0 op_sel_hi:[1,1,0]
	v_add_f32_dpp v6, v6, v6 quad_perm:[2,3,0,1] row_mask:0xf bank_mask:0xf bound_ctrl:1
	v_cvt_scalef32_pk_f32_fp4 v[136:137], v99, 1.0
	v_cvt_scalef32_pk_f32_fp4 v[138:139], v99, 1.0 op_sel:[1,0,0]
	v_cvt_scalef32_pk_f32_fp4 v[140:141], v99, 1.0 op_sel:[0,1,0]
	v_cvt_scalef32_pk_f32_fp4 v[142:143], v99, 1.0 op_sel:[1,1,0]
	v_add_f32_dpp v6, v6, v6 row_half_mirror row_mask:0xf bank_mask:0xf bound_ctrl:1
	v_pk_fma_f32 v[8:9], v[186:187], v[136:137], v[8:9]
	v_pk_fma_f32 v[10:11], v[188:189], v[138:139], v[10:11]
	v_pk_fma_f32 v[12:13], v[190:191], v[140:141], v[12:13]
	v_pk_fma_f32 v[14:15], v[192:193], v[142:143], v[14:15]
	v_mov_b32_e32 v7, 0
	v_cvt_scalef32_pk_f32_fp4 v[136:137], v100, 1.0
	v_cvt_scalef32_pk_f32_fp4 v[138:139], v100, 1.0 op_sel:[1,0,0]
	v_cvt_scalef32_pk_f32_fp4 v[140:141], v100, 1.0 op_sel:[0,1,0]
	v_cvt_scalef32_pk_f32_fp4 v[142:143], v100, 1.0 op_sel:[1,1,0]
	v_add_f32_dpp v6, v6, v6 row_mirror row_mask:0xf bank_mask:0xf bound_ctrl:1
	v_pk_fma_f32 v[8:9], v[194:195], v[136:137], v[8:9]
	v_pk_fma_f32 v[10:11], v[196:197], v[138:139], v[10:11]
	v_pk_fma_f32 v[12:13], v[198:199], v[140:141], v[12:13]
	v_pk_fma_f32 v[14:15], v[200:201], v[142:143], v[14:15]
	s_waitcnt lgkmcnt(0)
	s_mov_b32 m0, s77
	s_nop 0
	global_load_lds_dwordx4 v[2:3], off
	global_load_lds_dwordx4 v[2:3], off offset:1024
	v_cvt_scalef32_pk_f32_fp4 v[136:137], v101, 1.0
	v_cvt_scalef32_pk_f32_fp4 v[138:139], v101, 1.0 op_sel:[1,0,0]
	v_cvt_scalef32_pk_f32_fp4 v[140:141], v101, 1.0 op_sel:[0,1,0]
	v_cvt_scalef32_pk_f32_fp4 v[142:143], v101, 1.0 op_sel:[1,1,0]
	v_mov_b32_dpp v7, v6 row_bcast:15 row_mask:0xa bank_mask:0xf
	v_pk_fma_f32 v[8:9], v[202:203], v[136:137], v[8:9]
	v_pk_fma_f32 v[10:11], v[204:205], v[138:139], v[10:11]
	v_pk_fma_f32 v[12:13], v[206:207], v[140:141], v[12:13]
	v_pk_fma_f32 v[14:15], v[208:209], v[142:143], v[14:15]
	v_add_f32_e32 v6, v6, v7
	v_cvt_scalef32_pk_f32_fp4 v[136:137], v102, 1.0
	v_cvt_scalef32_pk_f32_fp4 v[138:139], v102, 1.0 op_sel:[1,0,0]
	v_cvt_scalef32_pk_f32_fp4 v[140:141], v102, 1.0 op_sel:[0,1,0]
	v_cvt_scalef32_pk_f32_fp4 v[142:143], v102, 1.0 op_sel:[1,1,0]
	v_mov_b32_e32 v7, 0
	v_pk_fma_f32 v[8:9], v[210:211], v[136:137], v[8:9]
	v_pk_fma_f32 v[10:11], v[212:213], v[138:139], v[10:11]
	v_pk_fma_f32 v[12:13], v[214:215], v[140:141], v[12:13]
	v_pk_fma_f32 v[14:15], v[216:217], v[142:143], v[14:15]
	v_mov_b32_dpp v7, v6 row_bcast:31 row_mask:0xc bank_mask:0xf
	v_cvt_scalef32_pk_f32_fp4 v[136:137], v103, 1.0
	v_cvt_scalef32_pk_f32_fp4 v[138:139], v103, 1.0 op_sel:[1,0,0]
	v_cvt_scalef32_pk_f32_fp4 v[140:141], v103, 1.0 op_sel:[0,1,0]
	v_cvt_scalef32_pk_f32_fp4 v[142:143], v103, 1.0 op_sel:[1,1,0]
	v_add_f32_e32 v6, v6, v7
	v_pk_fma_f32 v[8:9], v[218:219], v[136:137], v[8:9]
	v_pk_fma_f32 v[10:11], v[220:221], v[138:139], v[10:11]
	v_pk_fma_f32 v[12:13], v[222:223], v[140:141], v[12:13]
	v_pk_fma_f32 v[14:15], v[224:225], v[142:143], v[14:15]
	v_readlane_b32 s74, v6, 63
	v_cvt_scalef32_pk_f32_fp4 v[136:137], v104, 1.0
	v_cvt_scalef32_pk_f32_fp4 v[138:139], v104, 1.0 op_sel:[1,0,0]
	v_cvt_scalef32_pk_f32_fp4 v[140:141], v104, 1.0 op_sel:[0,1,0]
	v_cvt_scalef32_pk_f32_fp4 v[142:143], v104, 1.0 op_sel:[1,1,0]
	s_lshl_b64 exec, 1, s32
	v_mov_b32_e32 v123, s74
	s_mov_b64 exec, -1
	v_pk_fma_f32 v[8:9], v[226:227], v[136:137], v[8:9]
	v_pk_fma_f32 v[10:11], v[228:229], v[138:139], v[10:11]
	v_pk_fma_f32 v[12:13], v[230:231], v[140:141], v[12:13]
	v_pk_fma_f32 v[14:15], v[232:233], v[142:143], v[14:15]
	v_cvt_scalef32_pk_f32_fp4 v[136:137], v105, 1.0
	v_cvt_scalef32_pk_f32_fp4 v[138:139], v105, 1.0 op_sel:[1,0,0]
	v_cvt_scalef32_pk_f32_fp4 v[140:141], v105, 1.0 op_sel:[0,1,0]
	v_cvt_scalef32_pk_f32_fp4 v[142:143], v105, 1.0 op_sel:[1,1,0]
	v_pk_fma_f32 v[8:9], v[234:235], v[136:137], v[8:9]
	v_pk_fma_f32 v[10:11], v[236:237], v[138:139], v[10:11]
	v_pk_fma_f32 v[12:13], v[238:239], v[140:141], v[12:13]
	v_pk_fma_f32 v[14:15], v[240:241], v[142:143], v[14:15]
	v_pk_add_f32 v[8:9], v[8:9], v[10:11]
	v_pk_add_f32 v[12:13], v[12:13], v[14:15]
	v_pk_add_f32 v[8:9], v[8:9], v[12:13]
	v_add_f32_e32 v5, v8, v9
; DI void peer_token(LAS unsigned char* ring, const bf16* x1row, float inv2, const float* nffn, const int* ex, const float* pg, const unsigned char* U6, const unsigned char* V6,
;                    const float* usc, const float* vsc, float* orow, int lane) {
;     ...
;     for (int k = 120; k < 128; ++k) P11_U(k, us_hi, gv_hi, cf_hi, vl, e_lo, k - 120);
.Lpu3_odd:
	s_add_i32 s32, s46, 1
	s_bitcmp1_b64 s[70:71], s32
	s_cbranch_scc1 .Lpu3_oddB
	s_add_i32 s47, s46, 2
	s_and_b32 s47, s47, 7
	s_lshl_b32 s47, s47, 11
	s_add_i32 s77, s33, s47
	v_add_u32_e32 v4, s77, v70
	s_add_i32 s78, s46, 10
	s_and_b32 s75, s78, 63
	v_readlane_b32 s79, v112, s75
	v_readlane_b32 s47, v243, s75
	s_bitcmp1_b32 s78, 6
	s_cselect_b32 s47, s47, s79
	s_lshr_b32 s47, s47, 8
	s_lshl_b32 s47, s47, 11
	s_bitcmp1_b32 s78, 8
	s_cselect_b32 s78, s98, 0
	s_cselect_b32 s79, s99, 0
	s_add_u32 s78, s78, s47
	s_addc_u32 s79, s79, 0
	s_add_i32 s32, s46, 1
	s_waitcnt vmcnt(14)
	ds_read_b128 v[98:101], v4
	ds_read_b128 v[102:105], v4 offset:1024
	v_lshl_add_u64 v[2:3], v[72:73], 0, s[78:79]
	v_cvt_scalef32_pk_f32_fp4 v[136:137], v126, 1.0
	v_cvt_scalef32_pk_f32_fp4 v[138:139], v126, 1.0 op_sel:[1,0,0]
	v_cvt_scalef32_pk_f32_fp4 v[140:141], v126, 1.0 op_sel:[0,1,0]
	v_cvt_scalef32_pk_f32_fp4 v[142:143], v126, 1.0 op_sel:[1,1,0]
	v_add_f32_dpp v5, v5, v5 quad_perm:[1,0,3,2] row_mask:0xf bank_mask:0xf bound_ctrl:1
	v_pk_fma_f32 v[8:9], v[20:21], v[136:137], 0 op_sel_hi:[1,1,0]
	v_pk_fma_f32 v[10:11], v[22:23], v[138:139], 0 op_sel_hi:[1,1,0]
	v_pk_fma_f32 v[12:13], v[24:25], v[140:141], 0 op_sel_hi:[1,1,0]
	v_pk_fma_f32 v[14:15], v[26:27], v[142:143], 0 op_sel_hi:[1,1,0]
	v_add_f32_dpp v5, v5, v5 quad_perm:[2,3,0,1] row_mask:0xf bank_mask:0xf bound_ctrl:1
	v_cvt_scalef32_pk_f32_fp4 v[136:137], v127, 1.0
	v_cvt_scalef32_pk_f32_fp4 v[138:139], v127, 1.0 op_sel:[1,0,0]
	v_cvt_scalef32_pk_f32_fp4 v[140:141], v127, 1.0 op_sel:[0,1,0]
	v_cvt_scalef32_pk_f32_fp4 v[142:143], v127, 1.0 op_sel:[1,1,0]
	v_add_f32_dpp v5, v5, v5 row_half_mirror row_mask:0xf bank_mask:0xf bound_ctrl:1
	v_pk_fma_f32 v[8:9], v[28:29], v[136:137], v[8:9]
	v_pk_fma_f32 v[10:11], v[30:31], v[138:139], v[10:11]
	v_pk_fma_f32 v[12:13], v[32:33], v[140:141], v[12:13]
	v_pk_fma_f32 v[14:15], v[34:35], v[142:143], v[14:15]
	v_mov_b32_e32 v7, 0
	v_cvt_scalef32_pk_f32_fp4 v[136:137], v128, 1.0
	v_cvt_scalef32_pk_f32_fp4 v[138:139], v128, 1.0 op_sel:[1,0,0]
	v_cvt_scalef32_pk_f32_fp4 v[140:141], v128, 1.0 op_sel:[0,1,0]
	v_cvt_scalef32_pk_f32_fp4 v[142:143], v128, 1.0 op_sel:[1,1,0]
	v_add_f32_dpp v5, v5, v5 row_mirror row_mask:0xf bank_mask:0xf bound_ctrl:1
	v_pk_fma_f32 v[8:9], v[36:37], v[136:137], v[8:9]
	v_pk_fma_f32 v[10:11], v[38:39], v[138:139], v[10:11]
	v_pk_fma_f32 v[12:13], v[40:41], v[140:141], v[12:13]
	v_pk_fma_f32 v[14:15], v[42:43], v[142:143], v[14:15]
	s_waitcnt lgkmcnt(0)
	s_mov_b32 m0, s77
	s_nop 0
	global_load_lds_dwordx4 v[2:3], off
	global_load_lds_dwordx4 v[2:3], off offset:1024
	v_cvt_scalef32_pk_f32_fp4 v[136:137], v129, 1.0
	v_cvt_scalef32_pk_f32_fp4 v[138:139], v129, 1.0 op_sel:[1,0,0]
	v_cvt_scalef32_pk_f32_fp4 v[140:141], v129, 1.0 op_sel:[0,1,0]
	v_cvt_scalef32_pk_f32_fp4 v[142:143], v129, 1.0 op_sel:[1,1,0]
	v_mov_b32_dpp v7, v5 row_bcast:15 row_mask:0xa bank_mask:0xf
	v_pk_fma_f32 v[8:9], v[44:45], v[136:137], v[8:9]
	v_pk_fma_f32 v[10:11], v[46:47], v[138:139], v[10:11]
	v_pk_fma_f32 v[12:13], v[48:49], v[140:141], v[12:13]
	v_pk_fma_f32 v[14:15], v[50:51], v[142:143], v[14:15]
	v_add_f32_e32 v5, v5, v7
	v_cvt_scalef32_pk_f32_fp4 v[136:137], v130, 1.0
	v_cvt_scalef32_pk_f32_fp4 v[138:139], v130, 1.0 op_sel:[1,0,0]
	v_cvt_scalef32_pk_f32_fp4 v[140:141], v130, 1.0 op_sel:[0,1,0]
	v_cvt_scalef32_pk_f32_fp4 v[142:143], v130, 1.0 op_sel:[1,1,0]
	v_mov_b32_e32 v7, 0
	v_pk_fma_f32 v[8:9], v[52:53], v[136:137], v[8:9]
	v_pk_fma_f32 v[10:11], v[54:55], v[138:139], v[10:11]
	v_pk_fma_f32 v[12:13], v[56:57], v[140:141], v[12:13]
	v_pk_fma_f32 v[14:15], v[58:59], v[142:143], v[14:15]
	v_mov_b32_dpp v7, v5 row_bcast:31 row_mask:0xc bank_mask:0xf
	v_cvt_scalef32_pk_f32_fp4 v[136:137], v131, 1.0
	v_cvt_scalef32_pk_f32_fp4 v[138:139], v131, 1.0 op_sel:[1,0,0]
	v_cvt_scalef32_pk_f32_fp4 v[140:141], v131, 1.0 op_sel:[0,1,0]
	v_cvt_scalef32_pk_f32_fp4 v[142:143], v131, 1.0 op_sel:[1,1,0]
	v_add_f32_e32 v5, v5, v7
	v_pk_fma_f32 v[8:9], v[60:61], v[136:137], v[8:9]
	v_pk_fma_f32 v[10:11], v[62:63], v[138:139], v[10:11]
	v_pk_fma_f32 v[12:13], v[64:65], v[140:141], v[12:13]
	v_pk_fma_f32 v[14:15], v[80:81], v[142:143], v[14:15]
	v_readlane_b32 s74, v5, 63
	v_cvt_scalef32_pk_f32_fp4 v[136:137], v132, 1.0
	v_cvt_scalef32_pk_f32_fp4 v[138:139], v132, 1.0 op_sel:[1,0,0]
	v_cvt_scalef32_pk_f32_fp4 v[140:141], v132, 1.0 op_sel:[0,1,0]
	v_cvt_scalef32_pk_f32_fp4 v[142:143], v132, 1.0 op_sel:[1,1,0]
	s_lshl_b64 exec, 1, s32
	v_mov_b32_e32 v123, s74
	s_mov_b64 exec, -1
	v_pk_fma_f32 v[8:9], v[82:83], v[136:137], v[8:9]
	v_pk_fma_f32 v[10:11], v[84:85], v[138:139], v[10:11]
	v_pk_fma_f32 v[12:13], v[86:87], v[140:141], v[12:13]
	v_pk_fma_f32 v[14:15], v[88:89], v[142:143], v[14:15]
	v_cvt_scalef32_pk_f32_fp4 v[136:137], v133, 1.0
	v_cvt_scalef32_pk_f32_fp4 v[138:139], v133, 1.0 op_sel:[1,0,0]
	v_cvt_scalef32_pk_f32_fp4 v[140:141], v133, 1.0 op_sel:[0,1,0]
	v_cvt_scalef32_pk_f32_fp4 v[142:143], v133, 1.0 op_sel:[1,1,0]
	v_pk_fma_f32 v[8:9], v[90:91], v[136:137], v[8:9]
	v_pk_fma_f32 v[10:11], v[92:93], v[138:139], v[10:11]
	v_pk_fma_f32 v[12:13], v[94:95], v[140:141], v[12:13]
	v_pk_fma_f32 v[14:15], v[96:97], v[142:143], v[14:15]
	v_pk_add_f32 v[8:9], v[8:9], v[10:11]
	v_pk_add_f32 v[12:13], v[12:13], v[14:15]
	v_pk_add_f32 v[8:9], v[8:9], v[12:13]
	v_add_f32_e32 v6, v8, v9
	s_branch .Lpu3_next
; DI void peer_token(LAS unsigned char* ring, const bf16* x1row, float inv2, const float* nffn, const int* ex, const float* pg, const unsigned char* U6, const unsigned char* V6,
;                    const float* usc, const float* vsc, float* orow, int lane) {
;     ...
;     for (int k = 120; k < 128; ++k) P11_U(k, us_hi, gv_hi, cf_hi, vl, e_lo, k - 120);
.Lpu3_oddB:
	s_add_i32 s47, s46, 2
	s_and_b32 s47, s47, 7
	s_lshl_b32 s47, s47, 11
	s_add_i32 s77, s33, s47
	v_add_u32_e32 v4, s77, v70
	s_add_i32 s78, s46, 10
	s_and_b32 s75, s78, 63
	v_readlane_b32 s79, v112, s75
	v_readlane_b32 s47, v243, s75
	s_bitcmp1_b32 s78, 6
	s_cselect_b32 s47, s47, s79
	s_lshr_b32 s47, s47, 8
	s_lshl_b32 s47, s47, 11
	s_bitcmp1_b32 s78, 8
	s_cselect_b32 s78, s98, 0
	s_cselect_b32 s79, s99, 0
	s_add_u32 s78, s78, s47
	s_addc_u32 s79, s79, 0
	s_add_i32 s32, s46, 1
	s_waitcnt vmcnt(14)
	ds_read_b128 v[98:101], v4
	ds_read_b128 v[102:105], v4 offset:1024
	v_lshl_add_u64 v[2:3], v[72:73], 0, s[78:79]
	v_cvt_scalef32_pk_f32_fp4 v[136:137], v126, 1.0
	v_cvt_scalef32_pk_f32_fp4 v[138:139], v126, 1.0 op_sel:[1,0,0]
	v_cvt_scalef32_pk_f32_fp4 v[140:141], v126, 1.0 op_sel:[0,1,0]
	v_cvt_scalef32_pk_f32_fp4 v[142:143], v126, 1.0 op_sel:[1,1,0]
	v_add_f32_dpp v5, v5, v5 quad_perm:[1,0,3,2] row_mask:0xf bank_mask:0xf bound_ctrl:1
	v_pk_fma_f32 v[8:9], v[178:179], v[136:137], 0 op_sel_hi:[1,1,0]
	v_pk_fma_f32 v[10:11], v[180:181], v[138:139], 0 op_sel_hi:[1,1,0]
	v_pk_fma_f32 v[12:13], v[182:183], v[140:141], 0 op_sel_hi:[1,1,0]
	v_pk_fma_f32 v[14:15], v[184:185], v[142:143], 0 op_sel_hi:[1,1,0]
	v_add_f32_dpp v5, v5, v5 quad_perm:[2,3,0,1] row_mask:0xf bank_mask:0xf bound_ctrl:1
	v_cvt_scalef32_pk_f32_fp4 v[136:137], v127, 1.0
	v_cvt_scalef32_pk_f32_fp4 v[138:139], v127, 1.0 op_sel:[1,0,0]
	v_cvt_scalef32_pk_f32_fp4 v[140:141], v127, 1.0 op_sel:[0,1,0]
	v_cvt_scalef32_pk_f32_fp4 v[142:143], v127, 1.0 op_sel:[1,1,0]
	v_add_f32_dpp v5, v5, v5 row_half_mirror row_mask:0xf bank_mask:0xf bound_ctrl:1
	v_pk_fma_f32 v[8:9], v[186:187], v[136:137], v[8:9]
	v_pk_fma_f32 v[10:11], v[188:189], v[138:139], v[10:11]
	v_pk_fma_f32 v[12:13], v[190:191], v[140:141], v[12:13]
	v_pk_fma_f32 v[14:15], v[192:193], v[142:143], v[14:15]
	v_mov_b32_e32 v7, 0
	v_cvt_scalef32_pk_f32_fp4 v[136:137], v128, 1.0
	v_cvt_scalef32_pk_f32_fp4 v[138:139], v128, 1.0 op_sel:[1,0,0]
	v_cvt_scalef32_pk_f32_fp4 v[140:141], v128, 1.0 op_sel:[0,1,0]
	v_cvt_scalef32_pk_f32_fp4 v[142:143], v128, 1.0 op_sel:[1,1,0]
	v_add_f32_dpp v5, v5, v5 row_mirror row_mask:0xf bank_mask:0xf bound_ctrl:1
	v_pk_fma_f32 v[8:9], v[194:195], v[136:137], v[8:9]
	v_pk_fma_f32 v[10:11], v[196:197], v[138:139], v[10:11]
	v_pk_fma_f32 v[12:13], v[198:199], v[140:141], v[12:13]
	v_pk_fma_f32 v[14:15], v[200:201], v[142:143], v[14:15]
	s_waitcnt lgkmcnt(0)
	s_mov_b32 m0, s77
	s_nop 0
	global_load_lds_dwordx4 v[2:3], off
	global_load_lds_dwordx4 v[2:3], off offset:1024
	v_cvt_scalef32_pk_f32_fp4 v[136:137], v129, 1.0
	v_cvt_scalef32_pk_f32_fp4 v[138:139], v129, 1.0 op_sel:[1,0,0]
	v_cvt_scalef32_pk_f32_fp4 v[140:141], v129, 1.0 op_sel:[0,1,0]
	v_cvt_scalef32_pk_f32_fp4 v[142:143], v129, 1.0 op_sel:[1,1,0]
	v_mov_b32_dpp v7, v5 row_bcast:15 row_mask:0xa bank_mask:0xf
	v_pk_fma_f32 v[8:9], v[202:203], v[136:137], v[8:9]
	v_pk_fma_f32 v[10:11], v[204:205], v[138:139], v[10:11]
	v_pk_fma_f32 v[12:13], v[206:207], v[140:141], v[12:13]
	v_pk_fma_f32 v[14:15], v[208:209], v[142:143], v[14:15]
	v_add_f32_e32 v5, v5, v7
	v_cvt_scalef32_pk_f32_fp4 v[136:137], v130, 1.0
	v_cvt_scalef32_pk_f32_fp4 v[138:139], v130, 1.0 op_sel:[1,0,0]
	v_cvt_scalef32_pk_f32_fp4 v[140:141], v130, 1.0 op_sel:[0,1,0]
	v_cvt_scalef32_pk_f32_fp4 v[142:143], v130, 1.0 op_sel:[1,1,0]
	v_mov_b32_e32 v7, 0
	v_pk_fma_f32 v[8:9], v[210:211], v[136:137], v[8:9]
	v_pk_fma_f32 v[10:11], v[212:213], v[138:139], v[10:11]
	v_pk_fma_f32 v[12:13], v[214:215], v[140:141], v[12:13]
	v_pk_fma_f32 v[14:15], v[216:217], v[142:143], v[14:15]
	v_mov_b32_dpp v7, v5 row_bcast:31 row_mask:0xc bank_mask:0xf
	v_cvt_scalef32_pk_f32_fp4 v[136:137], v131, 1.0
	v_cvt_scalef32_pk_f32_fp4 v[138:139], v131, 1.0 op_sel:[1,0,0]
	v_cvt_scalef32_pk_f32_fp4 v[140:141], v131, 1.0 op_sel:[0,1,0]
	v_cvt_scalef32_pk_f32_fp4 v[142:143], v131, 1.0 op_sel:[1,1,0]
	v_add_f32_e32 v5, v5, v7
	v_pk_fma_f32 v[8:9], v[218:219], v[136:137], v[8:9]
	v_pk_fma_f32 v[10:11], v[220:221], v[138:139], v[10:11]
	v_pk_fma_f32 v[12:13], v[222:223], v[140:141], v[12:13]
	v_pk_fma_f32 v[14:15], v[224:225], v[142:143], v[14:15]
	v_readlane_b32 s74, v5, 63
	v_cvt_scalef32_pk_f32_fp4 v[136:137], v132, 1.0
	v_cvt_scalef32_pk_f32_fp4 v[138:139], v132, 1.0 op_sel:[1,0,0]
	v_cvt_scalef32_pk_f32_fp4 v[140:141], v132, 1.0 op_sel:[0,1,0]
	v_cvt_scalef32_pk_f32_fp4 v[142:143], v132, 1.0 op_sel:[1,1,0]
	s_lshl_b64 exec, 1, s32
	v_mov_b32_e32 v123, s74
	s_mov_b64 exec, -1
	v_pk_fma_f32 v[8:9], v[226:227], v[136:137], v[8:9]
	v_pk_fma_f32 v[10:11], v[228:229], v[138:139], v[10:11]
	v_pk_fma_f32 v[12:13], v[230:231], v[140:141], v[12:13]
	v_pk_fma_f32 v[14:15], v[232:233], v[142:143], v[14:15]
	v_cvt_scalef32_pk_f32_fp4 v[136:137], v133, 1.0
	v_cvt_scalef32_pk_f32_fp4 v[138:139], v133, 1.0 op_sel:[1,0,0]
	v_cvt_scalef32_pk_f32_fp4 v[140:141], v133, 1.0 op_sel:[0,1,0]
	v_cvt_scalef32_pk_f32_fp4 v[142:143], v133, 1.0 op_sel:[1,1,0]
	v_pk_fma_f32 v[8:9], v[234:235], v[136:137], v[8:9]
	v_pk_fma_f32 v[10:11], v[236:237], v[138:139], v[10:11]
	v_pk_fma_f32 v[12:13], v[238:239], v[140:141], v[12:13]
	v_pk_fma_f32 v[14:15], v[240:241], v[142:143], v[14:15]
	v_pk_add_f32 v[8:9], v[8:9], v[10:11]
	v_pk_add_f32 v[12:13], v[12:13], v[14:15]
	v_pk_add_f32 v[8:9], v[8:9], v[12:13]
	v_add_f32_e32 v6, v8, v9
; DI float gelu_exact(float v) {
;     const float av = fabsf(v), t = __builtin_amdgcn_rcpf(av * 0.2316418882f + 1.0f);
;     float q = t * 0.5307027145f + (-0.7265760135f); q = q * t + 0.7107068705f; q = q * t + (-0.142248368f); q = q * t + 0.127414796f; q = q * t;
;     const float e = __builtin_amdgcn_exp2f((v * v) * (-0.72134752044f));
;     const float m = v * (q * e);
;     return v < 0.f ? m : v - m;
; }
; DI void peer_token(LAS unsigned char* ring, const bf16* x1row, float inv2, const float* nffn, const int* ex, const float* pg, const unsigned char* U6, const unsigned char* V6,
;                    const float* usc, const float* vsc, float* orow, int lane) {
;     ...
; #pragma unroll
;     for (int i = 0; i < 32; ++i) y[i] = (f32x2){0.f, 0.f};
.Lpu3_next:
	s_add_i32 s46, s46, 2
	s_cmp_lg_u32 s46, 256
	s_cbranch_scc1 .Lpu3_even
	s_mov_b32 s32, 0
	v_add_f32_dpp v6, v6, v6 quad_perm:[1,0,3,2] row_mask:0xf bank_mask:0xf bound_ctrl:1
	s_nop 1
	v_add_f32_dpp v6, v6, v6 quad_perm:[2,3,0,1] row_mask:0xf bank_mask:0xf bound_ctrl:1
	s_nop 1
	v_add_f32_dpp v6, v6, v6 row_half_mirror row_mask:0xf bank_mask:0xf bound_ctrl:1
	s_nop 1
	v_mov_b32_e32 v7, 0
	s_nop 1
	v_add_f32_dpp v6, v6, v6 row_mirror row_mask:0xf bank_mask:0xf bound_ctrl:1
	s_nop 1
	v_mov_b32_dpp v7, v6 row_bcast:15 row_mask:0xa bank_mask:0xf
	s_nop 1
	v_add_f32_e32 v6, v6, v7
	s_nop 1
	v_mov_b32_e32 v7, 0
	s_nop 1
	v_mov_b32_dpp v7, v6 row_bcast:31 row_mask:0xc bank_mask:0xf
	s_nop 1
	v_add_f32_e32 v6, v6, v7
	s_nop 1
	v_readlane_b32 s74, v6, 63
	s_nop 1
	s_lshl_b64 exec, 1, s32
	v_mov_b32_e32 v120, s74
	s_mov_b64 exec, -1
	s_nop 1
	s_nop 1
	v_add_u32_e32 v4, 1, v118
	v_lshlrev_b32_e32 v4, 2, v4
	ds_bpermute_b32 v8, v4, v120
	ds_bpermute_b32 v9, v4, v125
	ds_bpermute_b32 v10, v4, v248
	ds_bpermute_b32 v11, v4, v123
	s_waitcnt lgkmcnt(0)
	v_readlane_b32 s74, v125, 0
	s_nop 3
	v_writelane_b32 v8, s74, 63
	v_readlane_b32 s74, v248, 0
	s_nop 3
	v_writelane_b32 v9, s74, 63
	v_readlane_b32 s74, v123, 0
	s_nop 3
	v_writelane_b32 v10, s74, 63
	v_readlane_b32 s74, v120, 0
	s_nop 3
	v_writelane_b32 v11, s74, 63
	v_mov_b32_e32 v120, v8
	v_mov_b32_e32 v125, v9
	v_mov_b32_e32 v248, v10
	v_mov_b32_e32 v123, v11
	v_mul_f32_e32 v16, v121, v120
	v_fma_f32 v17, |v16|, s96, 1.0
	v_rcp_f32_e32 v17, v17
	v_cmp_gt_f32_e32 vcc, 0, v16
	v_mul_f32_e32 v18, v16, v16
	v_mul_f32_e32 v18, 0xbf38aa3b, v18
	v_exp_f32_e32 v18, v18
	v_fmamk_f32 v120, v17, 0x3f07dc22, v117
	v_fmaak_f32 v120, v17, v120, 0x3f35f0e3
	v_fmaak_f32 v120, v17, v120, 0xbe11a98e
	v_fmaak_f32 v120, v17, v120, 0x3e027906
	v_mul_f32_e32 v17, v17, v120
	v_mul_f32_e32 v17, v18, v17
	v_mul_f32_e32 v18, v16, v17
	v_fma_f32 v16, -v16, v17, v16
	v_cndmask_b32_e32 v16, v16, v18, vcc
	v_mul_f32_e32 v120, v124, v16
	v_mul_f32_e32 v16, v119, v125
	v_fma_f32 v17, |v16|, s96, 1.0
	v_rcp_f32_e32 v17, v17
	v_cmp_gt_f32_e32 vcc, 0, v16
	v_mul_f32_e32 v18, v16, v16
	v_mul_f32_e32 v18, 0xbf38aa3b, v18
	v_exp_f32_e32 v18, v18
	v_fmamk_f32 v125, v17, 0x3f07dc22, v117
	v_fmaak_f32 v125, v17, v125, 0x3f35f0e3
	v_fmaak_f32 v125, v17, v125, 0xbe11a98e
	v_fmaak_f32 v125, v17, v125, 0x3e027906
	v_mul_f32_e32 v17, v17, v125
	v_mul_f32_e32 v17, v18, v17
	v_mul_f32_e32 v18, v16, v17
	v_fma_f32 v16, -v16, v17, v16
	v_cndmask_b32_e32 v16, v16, v18, vcc
	v_mul_f32_e32 v125, v122, v16
	v_mul_f32_e32 v16, v244, v248
	v_fma_f32 v17, |v16|, s96, 1.0
	v_rcp_f32_e32 v17, v17
	v_cmp_gt_f32_e32 vcc, 0, v16
	v_mul_f32_e32 v18, v16, v16
	v_mul_f32_e32 v18, 0xbf38aa3b, v18
	v_exp_f32_e32 v18, v18
	v_fmamk_f32 v248, v17, 0x3f07dc22, v117
	v_fmaak_f32 v248, v17, v248, 0x3f35f0e3
	v_fmaak_f32 v248, v17, v248, 0xbe11a98e
	v_fmaak_f32 v248, v17, v248, 0x3e027906
	v_mul_f32_e32 v17, v17, v248
	v_mul_f32_e32 v17, v18, v17
	v_mul_f32_e32 v18, v16, v17
	v_fma_f32 v16, -v16, v17, v16
	v_cndmask_b32_e32 v16, v16, v18, vcc
	v_mul_f32_e32 v248, v246, v16
	v_mul_f32_e32 v16, v245, v123
	v_fma_f32 v17, |v16|, s96, 1.0
	v_rcp_f32_e32 v17, v17
	v_cmp_gt_f32_e32 vcc, 0, v16
	v_mul_f32_e32 v18, v16, v16
	v_mul_f32_e32 v18, 0xbf38aa3b, v18
	v_exp_f32_e32 v18, v18
	v_fmamk_f32 v123, v17, 0x3f07dc22, v117
	v_fmaak_f32 v123, v17, v123, 0x3f35f0e3
	v_fmaak_f32 v123, v17, v123, 0xbe11a98e
	v_fmaak_f32 v123, v17, v123, 0x3e027906
	v_mul_f32_e32 v17, v17, v123
	v_mul_f32_e32 v17, v18, v17
	v_mul_f32_e32 v18, v16, v17
	v_fma_f32 v16, -v16, v17, v16
	v_cndmask_b32_e32 v16, v16, v18, vcc
	v_mul_f32_e32 v123, v247, v16
	v_mov_b32_e32 v20, 0
	v_mov_b32_e32 v21, 0
	v_mov_b32_e32 v178, 0
	v_mov_b32_e32 v179, 0
	v_mov_b32_e32 v22, 0
	v_mov_b32_e32 v23, 0
	v_mov_b32_e32 v180, 0
	v_mov_b32_e32 v181, 0
	v_mov_b32_e32 v24, 0
	v_mov_b32_e32 v25, 0
	v_mov_b32_e32 v182, 0
	v_mov_b32_e32 v183, 0
	v_mov_b32_e32 v26, 0
	v_mov_b32_e32 v27, 0
	v_mov_b32_e32 v184, 0
	v_mov_b32_e32 v185, 0
	v_mov_b32_e32 v28, 0
	v_mov_b32_e32 v29, 0
	v_mov_b32_e32 v186, 0
	v_mov_b32_e32 v187, 0
	v_mov_b32_e32 v30, 0
	v_mov_b32_e32 v31, 0
	v_mov_b32_e32 v188, 0
	v_mov_b32_e32 v189, 0
	v_mov_b32_e32 v32, 0
	v_mov_b32_e32 v33, 0
	v_mov_b32_e32 v190, 0
	v_mov_b32_e32 v191, 0
	v_mov_b32_e32 v34, 0
	v_mov_b32_e32 v35, 0
	v_mov_b32_e32 v192, 0
	v_mov_b32_e32 v193, 0
	v_mov_b32_e32 v36, 0
	v_mov_b32_e32 v37, 0
	v_mov_b32_e32 v194, 0
	v_mov_b32_e32 v195, 0
	v_mov_b32_e32 v38, 0
	v_mov_b32_e32 v39, 0
	v_mov_b32_e32 v196, 0
	v_mov_b32_e32 v197, 0
	v_mov_b32_e32 v40, 0
	v_mov_b32_e32 v41, 0
	v_mov_b32_e32 v198, 0
	v_mov_b32_e32 v199, 0
	v_mov_b32_e32 v42, 0
	v_mov_b32_e32 v43, 0
	v_mov_b32_e32 v200, 0
	v_mov_b32_e32 v201, 0
	v_mov_b32_e32 v44, 0
	v_mov_b32_e32 v45, 0
	v_mov_b32_e32 v202, 0
	v_mov_b32_e32 v203, 0
	v_mov_b32_e32 v46, 0
	v_mov_b32_e32 v47, 0
	v_mov_b32_e32 v204, 0
	v_mov_b32_e32 v205, 0
	v_mov_b32_e32 v48, 0
	v_mov_b32_e32 v49, 0
	v_mov_b32_e32 v206, 0
	v_mov_b32_e32 v207, 0
	v_mov_b32_e32 v50, 0
	v_mov_b32_e32 v51, 0
	v_mov_b32_e32 v208, 0
	v_mov_b32_e32 v209, 0
	v_mov_b32_e32 v52, 0
	v_mov_b32_e32 v53, 0
	v_mov_b32_e32 v210, 0
	v_mov_b32_e32 v211, 0
	v_mov_b32_e32 v54, 0
	v_mov_b32_e32 v55, 0
	v_mov_b32_e32 v212, 0
	v_mov_b32_e32 v213, 0
	v_mov_b32_e32 v56, 0
	v_mov_b32_e32 v57, 0
	v_mov_b32_e32 v214, 0
	v_mov_b32_e32 v215, 0
	v_mov_b32_e32 v58, 0
	v_mov_b32_e32 v59, 0
	v_mov_b32_e32 v216, 0
	v_mov_b32_e32 v217, 0
	v_mov_b32_e32 v60, 0
	v_mov_b32_e32 v61, 0
	v_mov_b32_e32 v218, 0
	v_mov_b32_e32 v219, 0
	v_mov_b32_e32 v62, 0
	v_mov_b32_e32 v63, 0
	v_mov_b32_e32 v220, 0
	v_mov_b32_e32 v221, 0
	v_mov_b32_e32 v64, 0
	v_mov_b32_e32 v65, 0
	v_mov_b32_e32 v222, 0
	v_mov_b32_e32 v223, 0
	v_mov_b32_e32 v80, 0
	v_mov_b32_e32 v81, 0
	v_mov_b32_e32 v224, 0
	v_mov_b32_e32 v225, 0
	v_mov_b32_e32 v82, 0
	v_mov_b32_e32 v83, 0
	v_mov_b32_e32 v226, 0
	v_mov_b32_e32 v227, 0
	v_mov_b32_e32 v84, 0
	v_mov_b32_e32 v85, 0
	v_mov_b32_e32 v228, 0
	v_mov_b32_e32 v229, 0
	v_mov_b32_e32 v86, 0
	v_mov_b32_e32 v87, 0
	v_mov_b32_e32 v230, 0
	v_mov_b32_e32 v231, 0
	v_mov_b32_e32 v88, 0
	v_mov_b32_e32 v89, 0
	v_mov_b32_e32 v232, 0
	v_mov_b32_e32 v233, 0
	v_mov_b32_e32 v90, 0
	v_mov_b32_e32 v91, 0
	v_mov_b32_e32 v234, 0
	v_mov_b32_e32 v235, 0
	v_mov_b32_e32 v92, 0
	v_mov_b32_e32 v93, 0
	v_mov_b32_e32 v236, 0
	v_mov_b32_e32 v237, 0
	v_mov_b32_e32 v94, 0
	v_mov_b32_e32 v95, 0
	v_mov_b32_e32 v238, 0
	v_mov_b32_e32 v239, 0
	v_mov_b32_e32 v96, 0
	v_mov_b32_e32 v97, 0
	v_mov_b32_e32 v240, 0
	v_mov_b32_e32 v241, 0
	s_movk_i32 s46, 0x100
; DI void peer_token(LAS unsigned char* ring, const bf16* x1row, float inv2, const float* nffn, const int* ex, const float* pg, const unsigned char* U6, const unsigned char* V6,
;                    const float* usc, const float* vsc, float* orow, int lane) {
;     ...
;     for (int k = 0; k < 56; ++k) P11_V(k, cf_lo, vl, e_lo, k + 8);
; #pragma unroll 1
;     for (int k = 56; k < 64; ++k) P11_V(k, cf_lo, vl, e_hi, k - 56);
; #pragma unroll 1
;     for (int k = 64; k < 120; ++k) P11_V(k, cf_hi, vl, e_hi, k - 56);
; #pragma unroll 1
;     for (int k = 120; k < 128; ++k) P11_V(k, cf_hi, vl, e_lo, k - 120);
.Lpv0_even:
	s_bitcmp1_b64 s[100:101], s46
	s_cbranch_scc1 .Lpv0_evenB
	s_add_i32 s47, s46, 1
	s_and_b32 s47, s47, 7
	s_lshl_b32 s47, s47, 11
	s_add_i32 s77, s33, s47
	v_add_u32_e32 v4, s77, v70
	s_add_i32 s78, s46, 9
	s_and_b32 s75, s78, 63
	v_readlane_b32 s79, v113, s75
	v_readlane_b32 s47, v112, s75
	s_bitcmp1_b32 s78, 6
	s_cselect_b32 s47, s79, s47
	s_lshr_b32 s47, s47, 8
	s_lshl_b32 s47, s47, 11
	s_bitcmp1_b32 s78, 8
	s_cselect_b32 s78, s98, 0
	s_cselect_b32 s79, s99, 0
	s_add_u32 s78, s78, s47
	s_addc_u32 s79, s79, 0
	s_add_i32 s32, s46, 0
	v_readlane_b32 s74, v120, s32
	s_waitcnt vmcnt(14)
	ds_read_b128 v[126:129], v4
	ds_read_b128 v[130:133], v4 offset:1024
	v_lshl_add_u64 v[2:3], v[72:73], 0, s[78:79]
	v_cvt_scalef32_pk_f32_fp4 v[136:137], v98, 1.0
	v_cvt_scalef32_pk_f32_fp4 v[138:139], v98, 1.0 op_sel:[1,0,0]
	v_cvt_scalef32_pk_f32_fp4 v[140:141], v98, 1.0 op_sel:[0,1,0]
	v_cvt_scalef32_pk_f32_fp4 v[142:143], v98, 1.0 op_sel:[1,1,0]
	v_pk_fma_f32 v[94:95], s[74:75], v[136:137], v[94:95] op_sel_hi:[0,1,1]
	v_pk_fma_f32 v[96:97], s[74:75], v[138:139], v[96:97] op_sel_hi:[0,1,1]
	v_pk_fma_f32 v[92:93], s[74:75], v[140:141], v[92:93] op_sel_hi:[0,1,1]
	v_pk_fma_f32 v[90:91], s[74:75], v[142:143], v[90:91] op_sel_hi:[0,1,1]
	v_cvt_scalef32_pk_f32_fp4 v[136:137], v99, 1.0
	v_cvt_scalef32_pk_f32_fp4 v[138:139], v99, 1.0 op_sel:[1,0,0]
	v_cvt_scalef32_pk_f32_fp4 v[140:141], v99, 1.0 op_sel:[0,1,0]
	v_cvt_scalef32_pk_f32_fp4 v[142:143], v99, 1.0 op_sel:[1,1,0]
	v_pk_fma_f32 v[88:89], s[74:75], v[136:137], v[88:89] op_sel_hi:[0,1,1]
	v_pk_fma_f32 v[86:87], s[74:75], v[138:139], v[86:87] op_sel_hi:[0,1,1]
	v_pk_fma_f32 v[84:85], s[74:75], v[140:141], v[84:85] op_sel_hi:[0,1,1]
	v_pk_fma_f32 v[82:83], s[74:75], v[142:143], v[82:83] op_sel_hi:[0,1,1]
	v_cvt_scalef32_pk_f32_fp4 v[136:137], v100, 1.0
	v_cvt_scalef32_pk_f32_fp4 v[138:139], v100, 1.0 op_sel:[1,0,0]
	v_cvt_scalef32_pk_f32_fp4 v[140:141], v100, 1.0 op_sel:[0,1,0]
	v_cvt_scalef32_pk_f32_fp4 v[142:143], v100, 1.0 op_sel:[1,1,0]
	v_pk_fma_f32 v[64:65], s[74:75], v[136:137], v[64:65] op_sel_hi:[0,1,1]
	v_pk_fma_f32 v[80:81], s[74:75], v[138:139], v[80:81] op_sel_hi:[0,1,1]
	v_pk_fma_f32 v[62:63], s[74:75], v[140:141], v[62:63] op_sel_hi:[0,1,1]
	v_pk_fma_f32 v[60:61], s[74:75], v[142:143], v[60:61] op_sel_hi:[0,1,1]
	s_waitcnt lgkmcnt(0)
	s_mov_b32 m0, s77
	s_nop 0
	global_load_lds_dwordx4 v[2:3], off
	global_load_lds_dwordx4 v[2:3], off offset:1024
	v_cvt_scalef32_pk_f32_fp4 v[136:137], v101, 1.0
	v_cvt_scalef32_pk_f32_fp4 v[138:139], v101, 1.0 op_sel:[1,0,0]
	v_cvt_scalef32_pk_f32_fp4 v[140:141], v101, 1.0 op_sel:[0,1,0]
	v_cvt_scalef32_pk_f32_fp4 v[142:143], v101, 1.0 op_sel:[1,1,0]
	v_pk_fma_f32 v[58:59], s[74:75], v[136:137], v[58:59] op_sel_hi:[0,1,1]
	v_pk_fma_f32 v[56:57], s[74:75], v[138:139], v[56:57] op_sel_hi:[0,1,1]
	v_pk_fma_f32 v[54:55], s[74:75], v[140:141], v[54:55] op_sel_hi:[0,1,1]
	v_pk_fma_f32 v[52:53], s[74:75], v[142:143], v[52:53] op_sel_hi:[0,1,1]
	v_cvt_scalef32_pk_f32_fp4 v[136:137], v102, 1.0
	v_cvt_scalef32_pk_f32_fp4 v[138:139], v102, 1.0 op_sel:[1,0,0]
	v_cvt_scalef32_pk_f32_fp4 v[140:141], v102, 1.0 op_sel:[0,1,0]
	v_cvt_scalef32_pk_f32_fp4 v[142:143], v102, 1.0 op_sel:[1,1,0]
	v_pk_fma_f32 v[50:51], s[74:75], v[136:137], v[50:51] op_sel_hi:[0,1,1]
	v_pk_fma_f32 v[48:49], s[74:75], v[138:139], v[48:49] op_sel_hi:[0,1,1]
	v_pk_fma_f32 v[46:47], s[74:75], v[140:141], v[46:47] op_sel_hi:[0,1,1]
	v_pk_fma_f32 v[44:45], s[74:75], v[142:143], v[44:45] op_sel_hi:[0,1,1]
	v_cvt_scalef32_pk_f32_fp4 v[136:137], v103, 1.0
	v_cvt_scalef32_pk_f32_fp4 v[138:139], v103, 1.0 op_sel:[1,0,0]
	v_cvt_scalef32_pk_f32_fp4 v[140:141], v103, 1.0 op_sel:[0,1,0]
	v_cvt_scalef32_pk_f32_fp4 v[142:143], v103, 1.0 op_sel:[1,1,0]
	v_pk_fma_f32 v[42:43], s[74:75], v[136:137], v[42:43] op_sel_hi:[0,1,1]
	v_pk_fma_f32 v[40:41], s[74:75], v[138:139], v[40:41] op_sel_hi:[0,1,1]
	v_pk_fma_f32 v[38:39], s[74:75], v[140:141], v[38:39] op_sel_hi:[0,1,1]
	v_pk_fma_f32 v[36:37], s[74:75], v[142:143], v[36:37] op_sel_hi:[0,1,1]
	v_cvt_scalef32_pk_f32_fp4 v[136:137], v104, 1.0
	v_cvt_scalef32_pk_f32_fp4 v[138:139], v104, 1.0 op_sel:[1,0,0]
	v_cvt_scalef32_pk_f32_fp4 v[140:141], v104, 1.0 op_sel:[0,1,0]
	v_cvt_scalef32_pk_f32_fp4 v[142:143], v104, 1.0 op_sel:[1,1,0]
	v_pk_fma_f32 v[32:33], s[74:75], v[136:137], v[32:33] op_sel_hi:[0,1,1]
	v_pk_fma_f32 v[34:35], s[74:75], v[138:139], v[34:35] op_sel_hi:[0,1,1]
	v_pk_fma_f32 v[30:31], s[74:75], v[140:141], v[30:31] op_sel_hi:[0,1,1]
	v_pk_fma_f32 v[28:29], s[74:75], v[142:143], v[28:29] op_sel_hi:[0,1,1]
	v_cvt_scalef32_pk_f32_fp4 v[136:137], v105, 1.0
	v_cvt_scalef32_pk_f32_fp4 v[138:139], v105, 1.0 op_sel:[1,0,0]
	v_cvt_scalef32_pk_f32_fp4 v[140:141], v105, 1.0 op_sel:[0,1,0]
	v_cvt_scalef32_pk_f32_fp4 v[142:143], v105, 1.0 op_sel:[1,1,0]
	v_pk_fma_f32 v[26:27], s[74:75], v[136:137], v[26:27] op_sel_hi:[0,1,1]
	v_pk_fma_f32 v[24:25], s[74:75], v[138:139], v[24:25] op_sel_hi:[0,1,1]
	v_pk_fma_f32 v[20:21], s[74:75], v[140:141], v[20:21] op_sel_hi:[0,1,1]
	v_pk_fma_f32 v[22:23], s[74:75], v[142:143], v[22:23] op_sel_hi:[0,1,1]
	s_branch .Lpv0_odd
; DI void peer_token(LAS unsigned char* ring, const bf16* x1row, float inv2, const float* nffn, const int* ex, const float* pg, const unsigned char* U6, const unsigned char* V6,
;                    const float* usc, const float* vsc, float* orow, int lane) {
;     ...
;     for (int k = 0; k < 56; ++k) P11_V(k, cf_lo, vl, e_lo, k + 8);
; #pragma unroll 1
;     for (int k = 56; k < 64; ++k) P11_V(k, cf_lo, vl, e_hi, k - 56);
; #pragma unroll 1
;     for (int k = 64; k < 120; ++k) P11_V(k, cf_hi, vl, e_hi, k - 56);
; #pragma unroll 1
;     for (int k = 120; k < 128; ++k) P11_V(k, cf_hi, vl, e_lo, k - 120);
.Lpv0_evenB:
	s_add_i32 s47, s46, 1
	s_and_b32 s47, s47, 7
	s_lshl_b32 s47, s47, 11
	s_add_i32 s77, s33, s47
	v_add_u32_e32 v4, s77, v70
	s_add_i32 s78, s46, 9
	s_and_b32 s75, s78, 63
	v_readlane_b32 s79, v113, s75
	v_readlane_b32 s47, v112, s75
	s_bitcmp1_b32 s78, 6
	s_cselect_b32 s47, s79, s47
	s_lshr_b32 s47, s47, 8
	s_lshl_b32 s47, s47, 11
	s_bitcmp1_b32 s78, 8
	s_cselect_b32 s78, s98, 0
	s_cselect_b32 s79, s99, 0
	s_add_u32 s78, s78, s47
	s_addc_u32 s79, s79, 0
	s_add_i32 s32, s46, 0
	v_readlane_b32 s74, v120, s32
	s_waitcnt vmcnt(14)
	ds_read_b128 v[126:129], v4
	ds_read_b128 v[130:133], v4 offset:1024
	v_lshl_add_u64 v[2:3], v[72:73], 0, s[78:79]
	v_cvt_scalef32_pk_f32_fp4 v[136:137], v98, 1.0
	v_cvt_scalef32_pk_f32_fp4 v[138:139], v98, 1.0 op_sel:[1,0,0]
	v_cvt_scalef32_pk_f32_fp4 v[140:141], v98, 1.0 op_sel:[0,1,0]
	v_cvt_scalef32_pk_f32_fp4 v[142:143], v98, 1.0 op_sel:[1,1,0]
	v_pk_fma_f32 v[178:179], s[74:75], v[136:137], v[178:179] op_sel_hi:[0,1,1]
	v_pk_fma_f32 v[180:181], s[74:75], v[138:139], v[180:181] op_sel_hi:[0,1,1]
	v_pk_fma_f32 v[182:183], s[74:75], v[140:141], v[182:183] op_sel_hi:[0,1,1]
	v_pk_fma_f32 v[184:185], s[74:75], v[142:143], v[184:185] op_sel_hi:[0,1,1]
	v_cvt_scalef32_pk_f32_fp4 v[136:137], v99, 1.0
	v_cvt_scalef32_pk_f32_fp4 v[138:139], v99, 1.0 op_sel:[1,0,0]
	v_cvt_scalef32_pk_f32_fp4 v[140:141], v99, 1.0 op_sel:[0,1,0]
	v_cvt_scalef32_pk_f32_fp4 v[142:143], v99, 1.0 op_sel:[1,1,0]
	v_pk_fma_f32 v[186:187], s[74:75], v[136:137], v[186:187] op_sel_hi:[0,1,1]
	v_pk_fma_f32 v[188:189], s[74:75], v[138:139], v[188:189] op_sel_hi:[0,1,1]
	v_pk_fma_f32 v[190:191], s[74:75], v[140:141], v[190:191] op_sel_hi:[0,1,1]
	v_pk_fma_f32 v[192:193], s[74:75], v[142:143], v[192:193] op_sel_hi:[0,1,1]
	v_cvt_scalef32_pk_f32_fp4 v[136:137], v100, 1.0
	v_cvt_scalef32_pk_f32_fp4 v[138:139], v100, 1.0 op_sel:[1,0,0]
	v_cvt_scalef32_pk_f32_fp4 v[140:141], v100, 1.0 op_sel:[0,1,0]
	v_cvt_scalef32_pk_f32_fp4 v[142:143], v100, 1.0 op_sel:[1,1,0]
	v_pk_fma_f32 v[194:195], s[74:75], v[136:137], v[194:195] op_sel_hi:[0,1,1]
	v_pk_fma_f32 v[196:197], s[74:75], v[138:139], v[196:197] op_sel_hi:[0,1,1]
	v_pk_fma_f32 v[198:199], s[74:75], v[140:141], v[198:199] op_sel_hi:[0,1,1]
	v_pk_fma_f32 v[200:201], s[74:75], v[142:143], v[200:201] op_sel_hi:[0,1,1]
	s_waitcnt lgkmcnt(0)
	s_mov_b32 m0, s77
	s_nop 0
	global_load_lds_dwordx4 v[2:3], off
	global_load_lds_dwordx4 v[2:3], off offset:1024
	v_cvt_scalef32_pk_f32_fp4 v[136:137], v101, 1.0
	v_cvt_scalef32_pk_f32_fp4 v[138:139], v101, 1.0 op_sel:[1,0,0]
	v_cvt_scalef32_pk_f32_fp4 v[140:141], v101, 1.0 op_sel:[0,1,0]
	v_cvt_scalef32_pk_f32_fp4 v[142:143], v101, 1.0 op_sel:[1,1,0]
	v_pk_fma_f32 v[202:203], s[74:75], v[136:137], v[202:203] op_sel_hi:[0,1,1]
	v_pk_fma_f32 v[204:205], s[74:75], v[138:139], v[204:205] op_sel_hi:[0,1,1]
	v_pk_fma_f32 v[206:207], s[74:75], v[140:141], v[206:207] op_sel_hi:[0,1,1]
	v_pk_fma_f32 v[208:209], s[74:75], v[142:143], v[208:209] op_sel_hi:[0,1,1]
	v_cvt_scalef32_pk_f32_fp4 v[136:137], v102, 1.0
	v_cvt_scalef32_pk_f32_fp4 v[138:139], v102, 1.0 op_sel:[1,0,0]
	v_cvt_scalef32_pk_f32_fp4 v[140:141], v102, 1.0 op_sel:[0,1,0]
	v_cvt_scalef32_pk_f32_fp4 v[142:143], v102, 1.0 op_sel:[1,1,0]
	v_pk_fma_f32 v[210:211], s[74:75], v[136:137], v[210:211] op_sel_hi:[0,1,1]
	v_pk_fma_f32 v[212:213], s[74:75], v[138:139], v[212:213] op_sel_hi:[0,1,1]
	v_pk_fma_f32 v[214:215], s[74:75], v[140:141], v[214:215] op_sel_hi:[0,1,1]
	v_pk_fma_f32 v[216:217], s[74:75], v[142:143], v[216:217] op_sel_hi:[0,1,1]
	v_cvt_scalef32_pk_f32_fp4 v[136:137], v103, 1.0
	v_cvt_scalef32_pk_f32_fp4 v[138:139], v103, 1.0 op_sel:[1,0,0]
	v_cvt_scalef32_pk_f32_fp4 v[140:141], v103, 1.0 op_sel:[0,1,0]
	v_cvt_scalef32_pk_f32_fp4 v[142:143], v103, 1.0 op_sel:[1,1,0]
	v_pk_fma_f32 v[218:219], s[74:75], v[136:137], v[218:219] op_sel_hi:[0,1,1]
	v_pk_fma_f32 v[220:221], s[74:75], v[138:139], v[220:221] op_sel_hi:[0,1,1]
	v_pk_fma_f32 v[222:223], s[74:75], v[140:141], v[222:223] op_sel_hi:[0,1,1]
	v_pk_fma_f32 v[224:225], s[74:75], v[142:143], v[224:225] op_sel_hi:[0,1,1]
	v_cvt_scalef32_pk_f32_fp4 v[136:137], v104, 1.0
	v_cvt_scalef32_pk_f32_fp4 v[138:139], v104, 1.0 op_sel:[1,0,0]
	v_cvt_scalef32_pk_f32_fp4 v[140:141], v104, 1.0 op_sel:[0,1,0]
	v_cvt_scalef32_pk_f32_fp4 v[142:143], v104, 1.0 op_sel:[1,1,0]
	v_pk_fma_f32 v[226:227], s[74:75], v[136:137], v[226:227] op_sel_hi:[0,1,1]
	v_pk_fma_f32 v[228:229], s[74:75], v[138:139], v[228:229] op_sel_hi:[0,1,1]
	v_pk_fma_f32 v[230:231], s[74:75], v[140:141], v[230:231] op_sel_hi:[0,1,1]
	v_pk_fma_f32 v[232:233], s[74:75], v[142:143], v[232:233] op_sel_hi:[0,1,1]
	v_cvt_scalef32_pk_f32_fp4 v[136:137], v105, 1.0
	v_cvt_scalef32_pk_f32_fp4 v[138:139], v105, 1.0 op_sel:[1,0,0]
	v_cvt_scalef32_pk_f32_fp4 v[140:141], v105, 1.0 op_sel:[0,1,0]
	v_cvt_scalef32_pk_f32_fp4 v[142:143], v105, 1.0 op_sel:[1,1,0]
	v_pk_fma_f32 v[234:235], s[74:75], v[136:137], v[234:235] op_sel_hi:[0,1,1]
	v_pk_fma_f32 v[236:237], s[74:75], v[138:139], v[236:237] op_sel_hi:[0,1,1]
	v_pk_fma_f32 v[238:239], s[74:75], v[140:141], v[238:239] op_sel_hi:[0,1,1]
	v_pk_fma_f32 v[240:241], s[74:75], v[142:143], v[240:241] op_sel_hi:[0,1,1]
; DI void peer_token(LAS unsigned char* ring, const bf16* x1row, float inv2, const float* nffn, const int* ex, const float* pg, const unsigned char* U6, const unsigned char* V6,
;                    const float* usc, const float* vsc, float* orow, int lane) {
;     ...
;     for (int k = 0; k < 56; ++k) P11_V(k, cf_lo, vl, e_lo, k + 8);
; #pragma unroll 1
;     for (int k = 56; k < 64; ++k) P11_V(k, cf_lo, vl, e_hi, k - 56);
; #pragma unroll 1
;     for (int k = 64; k < 120; ++k) P11_V(k, cf_hi, vl, e_hi, k - 56);
; #pragma unroll 1
;     for (int k = 120; k < 128; ++k) P11_V(k, cf_hi, vl, e_lo, k - 120);
.Lpv0_odd:
	s_add_i32 s32, s46, 1
	s_bitcmp1_b64 s[100:101], s32
	s_cbranch_scc1 .Lpv0_oddB
	s_add_i32 s47, s46, 2
	s_and_b32 s47, s47, 7
	s_lshl_b32 s47, s47, 11
	s_add_i32 s77, s33, s47
	v_add_u32_e32 v4, s77, v70
	s_add_i32 s78, s46, 10
	s_and_b32 s75, s78, 63
	v_readlane_b32 s79, v113, s75
	v_readlane_b32 s47, v112, s75
	s_bitcmp1_b32 s78, 6
	s_cselect_b32 s47, s79, s47
	s_lshr_b32 s47, s47, 8
	s_lshl_b32 s47, s47, 11
	s_bitcmp1_b32 s78, 8
	s_cselect_b32 s78, s98, 0
	s_cselect_b32 s79, s99, 0
	s_add_u32 s78, s78, s47
	s_addc_u32 s79, s79, 0
	s_add_i32 s32, s46, 1
	v_readlane_b32 s74, v120, s32
	s_waitcnt vmcnt(14)
	ds_read_b128 v[98:101], v4
	ds_read_b128 v[102:105], v4 offset:1024
	v_lshl_add_u64 v[2:3], v[72:73], 0, s[78:79]
	v_cvt_scalef32_pk_f32_fp4 v[136:137], v126, 1.0
	v_cvt_scalef32_pk_f32_fp4 v[138:139], v126, 1.0 op_sel:[1,0,0]
	v_cvt_scalef32_pk_f32_fp4 v[140:141], v126, 1.0 op_sel:[0,1,0]
	v_cvt_scalef32_pk_f32_fp4 v[142:143], v126, 1.0 op_sel:[1,1,0]
	v_pk_fma_f32 v[94:95], s[74:75], v[136:137], v[94:95] op_sel_hi:[0,1,1]
	v_pk_fma_f32 v[96:97], s[74:75], v[138:139], v[96:97] op_sel_hi:[0,1,1]
	v_pk_fma_f32 v[92:93], s[74:75], v[140:141], v[92:93] op_sel_hi:[0,1,1]
	v_pk_fma_f32 v[90:91], s[74:75], v[142:143], v[90:91] op_sel_hi:[0,1,1]
	v_cvt_scalef32_pk_f32_fp4 v[136:137], v127, 1.0
	v_cvt_scalef32_pk_f32_fp4 v[138:139], v127, 1.0 op_sel:[1,0,0]
	v_cvt_scalef32_pk_f32_fp4 v[140:141], v127, 1.0 op_sel:[0,1,0]
	v_cvt_scalef32_pk_f32_fp4 v[142:143], v127, 1.0 op_sel:[1,1,0]
	v_pk_fma_f32 v[88:89], s[74:75], v[136:137], v[88:89] op_sel_hi:[0,1,1]
	v_pk_fma_f32 v[86:87], s[74:75], v[138:139], v[86:87] op_sel_hi:[0,1,1]
	v_pk_fma_f32 v[84:85], s[74:75], v[140:141], v[84:85] op_sel_hi:[0,1,1]
	v_pk_fma_f32 v[82:83], s[74:75], v[142:143], v[82:83] op_sel_hi:[0,1,1]
	v_cvt_scalef32_pk_f32_fp4 v[136:137], v128, 1.0
	v_cvt_scalef32_pk_f32_fp4 v[138:139], v128, 1.0 op_sel:[1,0,0]
	v_cvt_scalef32_pk_f32_fp4 v[140:141], v128, 1.0 op_sel:[0,1,0]
	v_cvt_scalef32_pk_f32_fp4 v[142:143], v128, 1.0 op_sel:[1,1,0]
	v_pk_fma_f32 v[64:65], s[74:75], v[136:137], v[64:65] op_sel_hi:[0,1,1]
	v_pk_fma_f32 v[80:81], s[74:75], v[138:139], v[80:81] op_sel_hi:[0,1,1]
	v_pk_fma_f32 v[62:63], s[74:75], v[140:141], v[62:63] op_sel_hi:[0,1,1]
	v_pk_fma_f32 v[60:61], s[74:75], v[142:143], v[60:61] op_sel_hi:[0,1,1]
	s_waitcnt lgkmcnt(0)
	s_mov_b32 m0, s77
	s_nop 0
	global_load_lds_dwordx4 v[2:3], off
	global_load_lds_dwordx4 v[2:3], off offset:1024
	v_cvt_scalef32_pk_f32_fp4 v[136:137], v129, 1.0
	v_cvt_scalef32_pk_f32_fp4 v[138:139], v129, 1.0 op_sel:[1,0,0]
	v_cvt_scalef32_pk_f32_fp4 v[140:141], v129, 1.0 op_sel:[0,1,0]
	v_cvt_scalef32_pk_f32_fp4 v[142:143], v129, 1.0 op_sel:[1,1,0]
	v_pk_fma_f32 v[58:59], s[74:75], v[136:137], v[58:59] op_sel_hi:[0,1,1]
	v_pk_fma_f32 v[56:57], s[74:75], v[138:139], v[56:57] op_sel_hi:[0,1,1]
	v_pk_fma_f32 v[54:55], s[74:75], v[140:141], v[54:55] op_sel_hi:[0,1,1]
	v_pk_fma_f32 v[52:53], s[74:75], v[142:143], v[52:53] op_sel_hi:[0,1,1]
	v_cvt_scalef32_pk_f32_fp4 v[136:137], v130, 1.0
	v_cvt_scalef32_pk_f32_fp4 v[138:139], v130, 1.0 op_sel:[1,0,0]
	v_cvt_scalef32_pk_f32_fp4 v[140:141], v130, 1.0 op_sel:[0,1,0]
	v_cvt_scalef32_pk_f32_fp4 v[142:143], v130, 1.0 op_sel:[1,1,0]
	v_pk_fma_f32 v[50:51], s[74:75], v[136:137], v[50:51] op_sel_hi:[0,1,1]
	v_pk_fma_f32 v[48:49], s[74:75], v[138:139], v[48:49] op_sel_hi:[0,1,1]
	v_pk_fma_f32 v[46:47], s[74:75], v[140:141], v[46:47] op_sel_hi:[0,1,1]
	v_pk_fma_f32 v[44:45], s[74:75], v[142:143], v[44:45] op_sel_hi:[0,1,1]
	v_cvt_scalef32_pk_f32_fp4 v[136:137], v131, 1.0
	v_cvt_scalef32_pk_f32_fp4 v[138:139], v131, 1.0 op_sel:[1,0,0]
	v_cvt_scalef32_pk_f32_fp4 v[140:141], v131, 1.0 op_sel:[0,1,0]
	v_cvt_scalef32_pk_f32_fp4 v[142:143], v131, 1.0 op_sel:[1,1,0]
	v_pk_fma_f32 v[42:43], s[74:75], v[136:137], v[42:43] op_sel_hi:[0,1,1]
	v_pk_fma_f32 v[40:41], s[74:75], v[138:139], v[40:41] op_sel_hi:[0,1,1]
	v_pk_fma_f32 v[38:39], s[74:75], v[140:141], v[38:39] op_sel_hi:[0,1,1]
	v_pk_fma_f32 v[36:37], s[74:75], v[142:143], v[36:37] op_sel_hi:[0,1,1]
	v_cvt_scalef32_pk_f32_fp4 v[136:137], v132, 1.0
	v_cvt_scalef32_pk_f32_fp4 v[138:139], v132, 1.0 op_sel:[1,0,0]
	v_cvt_scalef32_pk_f32_fp4 v[140:141], v132, 1.0 op_sel:[0,1,0]
	v_cvt_scalef32_pk_f32_fp4 v[142:143], v132, 1.0 op_sel:[1,1,0]
	v_pk_fma_f32 v[32:33], s[74:75], v[136:137], v[32:33] op_sel_hi:[0,1,1]
	v_pk_fma_f32 v[34:35], s[74:75], v[138:139], v[34:35] op_sel_hi:[0,1,1]
	v_pk_fma_f32 v[30:31], s[74:75], v[140:141], v[30:31] op_sel_hi:[0,1,1]
	v_pk_fma_f32 v[28:29], s[74:75], v[142:143], v[28:29] op_sel_hi:[0,1,1]
	v_cvt_scalef32_pk_f32_fp4 v[136:137], v133, 1.0
	v_cvt_scalef32_pk_f32_fp4 v[138:139], v133, 1.0 op_sel:[1,0,0]
	v_cvt_scalef32_pk_f32_fp4 v[140:141], v133, 1.0 op_sel:[0,1,0]
	v_cvt_scalef32_pk_f32_fp4 v[142:143], v133, 1.0 op_sel:[1,1,0]
	v_pk_fma_f32 v[26:27], s[74:75], v[136:137], v[26:27] op_sel_hi:[0,1,1]
	v_pk_fma_f32 v[24:25], s[74:75], v[138:139], v[24:25] op_sel_hi:[0,1,1]
	v_pk_fma_f32 v[20:21], s[74:75], v[140:141], v[20:21] op_sel_hi:[0,1,1]
	v_pk_fma_f32 v[22:23], s[74:75], v[142:143], v[22:23] op_sel_hi:[0,1,1]
	s_branch .Lpv0_next
; DI void peer_token(LAS unsigned char* ring, const bf16* x1row, float inv2, const float* nffn, const int* ex, const float* pg, const unsigned char* U6, const unsigned char* V6,
;                    const float* usc, const float* vsc, float* orow, int lane) {
;     ...
;     for (int k = 0; k < 56; ++k) P11_V(k, cf_lo, vl, e_lo, k + 8);
; #pragma unroll 1
;     for (int k = 56; k < 64; ++k) P11_V(k, cf_lo, vl, e_hi, k - 56);
; #pragma unroll 1
;     for (int k = 64; k < 120; ++k) P11_V(k, cf_hi, vl, e_hi, k - 56);
; #pragma unroll 1
;     for (int k = 120; k < 128; ++k) P11_V(k, cf_hi, vl, e_lo, k - 120);
.Lpv0_oddB:
	s_add_i32 s47, s46, 2
	s_and_b32 s47, s47, 7
	s_lshl_b32 s47, s47, 11
	s_add_i32 s77, s33, s47
	v_add_u32_e32 v4, s77, v70
	s_add_i32 s78, s46, 10
	s_and_b32 s75, s78, 63
	v_readlane_b32 s79, v113, s75
	v_readlane_b32 s47, v112, s75
	s_bitcmp1_b32 s78, 6
	s_cselect_b32 s47, s79, s47
	s_lshr_b32 s47, s47, 8
	s_lshl_b32 s47, s47, 11
	s_bitcmp1_b32 s78, 8
	s_cselect_b32 s78, s98, 0
	s_cselect_b32 s79, s99, 0
	s_add_u32 s78, s78, s47
	s_addc_u32 s79, s79, 0
	s_add_i32 s32, s46, 1
	v_readlane_b32 s74, v120, s32
	s_waitcnt vmcnt(14)
	ds_read_b128 v[98:101], v4
	ds_read_b128 v[102:105], v4 offset:1024
	v_lshl_add_u64 v[2:3], v[72:73], 0, s[78:79]
	v_cvt_scalef32_pk_f32_fp4 v[136:137], v126, 1.0
	v_cvt_scalef32_pk_f32_fp4 v[138:139], v126, 1.0 op_sel:[1,0,0]
	v_cvt_scalef32_pk_f32_fp4 v[140:141], v126, 1.0 op_sel:[0,1,0]
	v_cvt_scalef32_pk_f32_fp4 v[142:143], v126, 1.0 op_sel:[1,1,0]
	v_pk_fma_f32 v[178:179], s[74:75], v[136:137], v[178:179] op_sel_hi:[0,1,1]
	v_pk_fma_f32 v[180:181], s[74:75], v[138:139], v[180:181] op_sel_hi:[0,1,1]
	v_pk_fma_f32 v[182:183], s[74:75], v[140:141], v[182:183] op_sel_hi:[0,1,1]
	v_pk_fma_f32 v[184:185], s[74:75], v[142:143], v[184:185] op_sel_hi:[0,1,1]
	v_cvt_scalef32_pk_f32_fp4 v[136:137], v127, 1.0
	v_cvt_scalef32_pk_f32_fp4 v[138:139], v127, 1.0 op_sel:[1,0,0]
	v_cvt_scalef32_pk_f32_fp4 v[140:141], v127, 1.0 op_sel:[0,1,0]
	v_cvt_scalef32_pk_f32_fp4 v[142:143], v127, 1.0 op_sel:[1,1,0]
	v_pk_fma_f32 v[186:187], s[74:75], v[136:137], v[186:187] op_sel_hi:[0,1,1]
	v_pk_fma_f32 v[188:189], s[74:75], v[138:139], v[188:189] op_sel_hi:[0,1,1]
	v_pk_fma_f32 v[190:191], s[74:75], v[140:141], v[190:191] op_sel_hi:[0,1,1]
	v_pk_fma_f32 v[192:193], s[74:75], v[142:143], v[192:193] op_sel_hi:[0,1,1]
	v_cvt_scalef32_pk_f32_fp4 v[136:137], v128, 1.0
	v_cvt_scalef32_pk_f32_fp4 v[138:139], v128, 1.0 op_sel:[1,0,0]
	v_cvt_scalef32_pk_f32_fp4 v[140:141], v128, 1.0 op_sel:[0,1,0]
	v_cvt_scalef32_pk_f32_fp4 v[142:143], v128, 1.0 op_sel:[1,1,0]
	v_pk_fma_f32 v[194:195], s[74:75], v[136:137], v[194:195] op_sel_hi:[0,1,1]
	v_pk_fma_f32 v[196:197], s[74:75], v[138:139], v[196:197] op_sel_hi:[0,1,1]
	v_pk_fma_f32 v[198:199], s[74:75], v[140:141], v[198:199] op_sel_hi:[0,1,1]
	v_pk_fma_f32 v[200:201], s[74:75], v[142:143], v[200:201] op_sel_hi:[0,1,1]
	s_waitcnt lgkmcnt(0)
	s_mov_b32 m0, s77
	s_nop 0
	global_load_lds_dwordx4 v[2:3], off
	global_load_lds_dwordx4 v[2:3], off offset:1024
	v_cvt_scalef32_pk_f32_fp4 v[136:137], v129, 1.0
	v_cvt_scalef32_pk_f32_fp4 v[138:139], v129, 1.0 op_sel:[1,0,0]
	v_cvt_scalef32_pk_f32_fp4 v[140:141], v129, 1.0 op_sel:[0,1,0]
	v_cvt_scalef32_pk_f32_fp4 v[142:143], v129, 1.0 op_sel:[1,1,0]
	v_pk_fma_f32 v[202:203], s[74:75], v[136:137], v[202:203] op_sel_hi:[0,1,1]
	v_pk_fma_f32 v[204:205], s[74:75], v[138:139], v[204:205] op_sel_hi:[0,1,1]
	v_pk_fma_f32 v[206:207], s[74:75], v[140:141], v[206:207] op_sel_hi:[0,1,1]
	v_pk_fma_f32 v[208:209], s[74:75], v[142:143], v[208:209] op_sel_hi:[0,1,1]
	v_cvt_scalef32_pk_f32_fp4 v[136:137], v130, 1.0
	v_cvt_scalef32_pk_f32_fp4 v[138:139], v130, 1.0 op_sel:[1,0,0]
	v_cvt_scalef32_pk_f32_fp4 v[140:141], v130, 1.0 op_sel:[0,1,0]
	v_cvt_scalef32_pk_f32_fp4 v[142:143], v130, 1.0 op_sel:[1,1,0]
	v_pk_fma_f32 v[210:211], s[74:75], v[136:137], v[210:211] op_sel_hi:[0,1,1]
	v_pk_fma_f32 v[212:213], s[74:75], v[138:139], v[212:213] op_sel_hi:[0,1,1]
	v_pk_fma_f32 v[214:215], s[74:75], v[140:141], v[214:215] op_sel_hi:[0,1,1]
	v_pk_fma_f32 v[216:217], s[74:75], v[142:143], v[216:217] op_sel_hi:[0,1,1]
	v_cvt_scalef32_pk_f32_fp4 v[136:137], v131, 1.0
	v_cvt_scalef32_pk_f32_fp4 v[138:139], v131, 1.0 op_sel:[1,0,0]
	v_cvt_scalef32_pk_f32_fp4 v[140:141], v131, 1.0 op_sel:[0,1,0]
	v_cvt_scalef32_pk_f32_fp4 v[142:143], v131, 1.0 op_sel:[1,1,0]
	v_pk_fma_f32 v[218:219], s[74:75], v[136:137], v[218:219] op_sel_hi:[0,1,1]
	v_pk_fma_f32 v[220:221], s[74:75], v[138:139], v[220:221] op_sel_hi:[0,1,1]
	v_pk_fma_f32 v[222:223], s[74:75], v[140:141], v[222:223] op_sel_hi:[0,1,1]
	v_pk_fma_f32 v[224:225], s[74:75], v[142:143], v[224:225] op_sel_hi:[0,1,1]
	v_cvt_scalef32_pk_f32_fp4 v[136:137], v132, 1.0
	v_cvt_scalef32_pk_f32_fp4 v[138:139], v132, 1.0 op_sel:[1,0,0]
	v_cvt_scalef32_pk_f32_fp4 v[140:141], v132, 1.0 op_sel:[0,1,0]
	v_cvt_scalef32_pk_f32_fp4 v[142:143], v132, 1.0 op_sel:[1,1,0]
	v_pk_fma_f32 v[226:227], s[74:75], v[136:137], v[226:227] op_sel_hi:[0,1,1]
	v_pk_fma_f32 v[228:229], s[74:75], v[138:139], v[228:229] op_sel_hi:[0,1,1]
	v_pk_fma_f32 v[230:231], s[74:75], v[140:141], v[230:231] op_sel_hi:[0,1,1]
	v_pk_fma_f32 v[232:233], s[74:75], v[142:143], v[232:233] op_sel_hi:[0,1,1]
	v_cvt_scalef32_pk_f32_fp4 v[136:137], v133, 1.0
	v_cvt_scalef32_pk_f32_fp4 v[138:139], v133, 1.0 op_sel:[1,0,0]
	v_cvt_scalef32_pk_f32_fp4 v[140:141], v133, 1.0 op_sel:[0,1,0]
	v_cvt_scalef32_pk_f32_fp4 v[142:143], v133, 1.0 op_sel:[1,1,0]
	v_pk_fma_f32 v[234:235], s[74:75], v[136:137], v[234:235] op_sel_hi:[0,1,1]
	v_pk_fma_f32 v[236:237], s[74:75], v[138:139], v[236:237] op_sel_hi:[0,1,1]
	v_pk_fma_f32 v[238:239], s[74:75], v[140:141], v[238:239] op_sel_hi:[0,1,1]
	v_pk_fma_f32 v[240:241], s[74:75], v[142:143], v[240:241] op_sel_hi:[0,1,1]
.Lpv0_next:
	s_add_i32 s46, s46, 2
	s_cmp_lg_u32 s46, 320
	s_cbranch_scc1 .Lpv0_even
; DI void peer_token(LAS unsigned char* ring, const bf16* x1row, float inv2, const float* nffn, const int* ex, const float* pg, const unsigned char* U6, const unsigned char* V6,
;                    const float* usc, const float* vsc, float* orow, int lane) {
;     ...
;     for (int k = 0; k < 56; ++k) P11_V(k, cf_lo, vl, e_lo, k + 8);
; #pragma unroll 1
;     for (int k = 56; k < 64; ++k) P11_V(k, cf_lo, vl, e_hi, k - 56);
; #pragma unroll 1
;     for (int k = 64; k < 120; ++k) P11_V(k, cf_hi, vl, e_hi, k - 56);
; #pragma unroll 1
;     for (int k = 120; k < 128; ++k) P11_V(k, cf_hi, vl, e_lo, k - 120);
.Lpv1_even:
	s_bitcmp1_b64 s[50:51], s46
	s_cbranch_scc1 .Lpv1_evenB
	s_add_i32 s47, s46, 1
	s_and_b32 s47, s47, 7
	s_lshl_b32 s47, s47, 11
	s_add_i32 s77, s33, s47
	v_add_u32_e32 v4, s77, v70
	s_add_i32 s78, s46, 9
	s_and_b32 s75, s78, 63
	v_readlane_b32 s79, v242, s75
	v_readlane_b32 s47, v113, s75
	s_bitcmp1_b32 s78, 6
	s_cselect_b32 s47, s47, s79
	s_lshr_b32 s47, s47, 8
	s_lshl_b32 s47, s47, 11
	s_bitcmp1_b32 s78, 8
	s_cselect_b32 s78, s98, 0
	s_cselect_b32 s79, s99, 0
	s_add_u32 s78, s78, s47
	s_addc_u32 s79, s79, 0
	s_add_i32 s32, s46, 0
	v_readlane_b32 s74, v125, s32
	s_waitcnt vmcnt(14)
	ds_read_b128 v[126:129], v4
	ds_read_b128 v[130:133], v4 offset:1024
	v_lshl_add_u64 v[2:3], v[72:73], 0, s[78:79]
	v_cvt_scalef32_pk_f32_fp4 v[136:137], v98, 1.0
	v_cvt_scalef32_pk_f32_fp4 v[138:139], v98, 1.0 op_sel:[1,0,0]
	v_cvt_scalef32_pk_f32_fp4 v[140:141], v98, 1.0 op_sel:[0,1,0]
	v_cvt_scalef32_pk_f32_fp4 v[142:143], v98, 1.0 op_sel:[1,1,0]
	v_pk_fma_f32 v[94:95], s[74:75], v[136:137], v[94:95] op_sel_hi:[0,1,1]
	v_pk_fma_f32 v[96:97], s[74:75], v[138:139], v[96:97] op_sel_hi:[0,1,1]
	v_pk_fma_f32 v[92:93], s[74:75], v[140:141], v[92:93] op_sel_hi:[0,1,1]
	v_pk_fma_f32 v[90:91], s[74:75], v[142:143], v[90:91] op_sel_hi:[0,1,1]
	v_cvt_scalef32_pk_f32_fp4 v[136:137], v99, 1.0
	v_cvt_scalef32_pk_f32_fp4 v[138:139], v99, 1.0 op_sel:[1,0,0]
	v_cvt_scalef32_pk_f32_fp4 v[140:141], v99, 1.0 op_sel:[0,1,0]
	v_cvt_scalef32_pk_f32_fp4 v[142:143], v99, 1.0 op_sel:[1,1,0]
	v_pk_fma_f32 v[88:89], s[74:75], v[136:137], v[88:89] op_sel_hi:[0,1,1]
	v_pk_fma_f32 v[86:87], s[74:75], v[138:139], v[86:87] op_sel_hi:[0,1,1]
	v_pk_fma_f32 v[84:85], s[74:75], v[140:141], v[84:85] op_sel_hi:[0,1,1]
	v_pk_fma_f32 v[82:83], s[74:75], v[142:143], v[82:83] op_sel_hi:[0,1,1]
	v_cvt_scalef32_pk_f32_fp4 v[136:137], v100, 1.0
	v_cvt_scalef32_pk_f32_fp4 v[138:139], v100, 1.0 op_sel:[1,0,0]
	v_cvt_scalef32_pk_f32_fp4 v[140:141], v100, 1.0 op_sel:[0,1,0]
	v_cvt_scalef32_pk_f32_fp4 v[142:143], v100, 1.0 op_sel:[1,1,0]
	v_pk_fma_f32 v[64:65], s[74:75], v[136:137], v[64:65] op_sel_hi:[0,1,1]
	v_pk_fma_f32 v[80:81], s[74:75], v[138:139], v[80:81] op_sel_hi:[0,1,1]
	v_pk_fma_f32 v[62:63], s[74:75], v[140:141], v[62:63] op_sel_hi:[0,1,1]
	v_pk_fma_f32 v[60:61], s[74:75], v[142:143], v[60:61] op_sel_hi:[0,1,1]
	s_waitcnt lgkmcnt(0)
	s_mov_b32 m0, s77
	s_nop 0
	global_load_lds_dwordx4 v[2:3], off
	global_load_lds_dwordx4 v[2:3], off offset:1024
	v_cvt_scalef32_pk_f32_fp4 v[136:137], v101, 1.0
	v_cvt_scalef32_pk_f32_fp4 v[138:139], v101, 1.0 op_sel:[1,0,0]
	v_cvt_scalef32_pk_f32_fp4 v[140:141], v101, 1.0 op_sel:[0,1,0]
	v_cvt_scalef32_pk_f32_fp4 v[142:143], v101, 1.0 op_sel:[1,1,0]
	v_pk_fma_f32 v[58:59], s[74:75], v[136:137], v[58:59] op_sel_hi:[0,1,1]
	v_pk_fma_f32 v[56:57], s[74:75], v[138:139], v[56:57] op_sel_hi:[0,1,1]
	v_pk_fma_f32 v[54:55], s[74:75], v[140:141], v[54:55] op_sel_hi:[0,1,1]
	v_pk_fma_f32 v[52:53], s[74:75], v[142:143], v[52:53] op_sel_hi:[0,1,1]
	v_cvt_scalef32_pk_f32_fp4 v[136:137], v102, 1.0
	v_cvt_scalef32_pk_f32_fp4 v[138:139], v102, 1.0 op_sel:[1,0,0]
	v_cvt_scalef32_pk_f32_fp4 v[140:141], v102, 1.0 op_sel:[0,1,0]
	v_cvt_scalef32_pk_f32_fp4 v[142:143], v102, 1.0 op_sel:[1,1,0]
	v_pk_fma_f32 v[50:51], s[74:75], v[136:137], v[50:51] op_sel_hi:[0,1,1]
	v_pk_fma_f32 v[48:49], s[74:75], v[138:139], v[48:49] op_sel_hi:[0,1,1]
	v_pk_fma_f32 v[46:47], s[74:75], v[140:141], v[46:47] op_sel_hi:[0,1,1]
	v_pk_fma_f32 v[44:45], s[74:75], v[142:143], v[44:45] op_sel_hi:[0,1,1]
	v_cvt_scalef32_pk_f32_fp4 v[136:137], v103, 1.0
	v_cvt_scalef32_pk_f32_fp4 v[138:139], v103, 1.0 op_sel:[1,0,0]
	v_cvt_scalef32_pk_f32_fp4 v[140:141], v103, 1.0 op_sel:[0,1,0]
	v_cvt_scalef32_pk_f32_fp4 v[142:143], v103, 1.0 op_sel:[1,1,0]
	v_pk_fma_f32 v[42:43], s[74:75], v[136:137], v[42:43] op_sel_hi:[0,1,1]
	v_pk_fma_f32 v[40:41], s[74:75], v[138:139], v[40:41] op_sel_hi:[0,1,1]
	v_pk_fma_f32 v[38:39], s[74:75], v[140:141], v[38:39] op_sel_hi:[0,1,1]
	v_pk_fma_f32 v[36:37], s[74:75], v[142:143], v[36:37] op_sel_hi:[0,1,1]
	v_cvt_scalef32_pk_f32_fp4 v[136:137], v104, 1.0
	v_cvt_scalef32_pk_f32_fp4 v[138:139], v104, 1.0 op_sel:[1,0,0]
	v_cvt_scalef32_pk_f32_fp4 v[140:141], v104, 1.0 op_sel:[0,1,0]
	v_cvt_scalef32_pk_f32_fp4 v[142:143], v104, 1.0 op_sel:[1,1,0]
	v_pk_fma_f32 v[32:33], s[74:75], v[136:137], v[32:33] op_sel_hi:[0,1,1]
	v_pk_fma_f32 v[34:35], s[74:75], v[138:139], v[34:35] op_sel_hi:[0,1,1]
	v_pk_fma_f32 v[30:31], s[74:75], v[140:141], v[30:31] op_sel_hi:[0,1,1]
	v_pk_fma_f32 v[28:29], s[74:75], v[142:143], v[28:29] op_sel_hi:[0,1,1]
	v_cvt_scalef32_pk_f32_fp4 v[136:137], v105, 1.0
	v_cvt_scalef32_pk_f32_fp4 v[138:139], v105, 1.0 op_sel:[1,0,0]
	v_cvt_scalef32_pk_f32_fp4 v[140:141], v105, 1.0 op_sel:[0,1,0]
	v_cvt_scalef32_pk_f32_fp4 v[142:143], v105, 1.0 op_sel:[1,1,0]
	v_pk_fma_f32 v[26:27], s[74:75], v[136:137], v[26:27] op_sel_hi:[0,1,1]
	v_pk_fma_f32 v[24:25], s[74:75], v[138:139], v[24:25] op_sel_hi:[0,1,1]
	v_pk_fma_f32 v[20:21], s[74:75], v[140:141], v[20:21] op_sel_hi:[0,1,1]
	v_pk_fma_f32 v[22:23], s[74:75], v[142:143], v[22:23] op_sel_hi:[0,1,1]
	s_branch .Lpv1_odd
; DI void peer_token(LAS unsigned char* ring, const bf16* x1row, float inv2, const float* nffn, const int* ex, const float* pg, const unsigned char* U6, const unsigned char* V6,
;                    const float* usc, const float* vsc, float* orow, int lane) {
;     ...
;     for (int k = 0; k < 56; ++k) P11_V(k, cf_lo, vl, e_lo, k + 8);
; #pragma unroll 1
;     for (int k = 56; k < 64; ++k) P11_V(k, cf_lo, vl, e_hi, k - 56);
; #pragma unroll 1
;     for (int k = 64; k < 120; ++k) P11_V(k, cf_hi, vl, e_hi, k - 56);
; #pragma unroll 1
;     for (int k = 120; k < 128; ++k) P11_V(k, cf_hi, vl, e_lo, k - 120);
.Lpv1_evenB:
	s_add_i32 s47, s46, 1
	s_and_b32 s47, s47, 7
	s_lshl_b32 s47, s47, 11
	s_add_i32 s77, s33, s47
	v_add_u32_e32 v4, s77, v70
	s_add_i32 s78, s46, 9
	s_and_b32 s75, s78, 63
	v_readlane_b32 s79, v242, s75
	v_readlane_b32 s47, v113, s75
	s_bitcmp1_b32 s78, 6
	s_cselect_b32 s47, s47, s79
	s_lshr_b32 s47, s47, 8
	s_lshl_b32 s47, s47, 11
	s_bitcmp1_b32 s78, 8
	s_cselect_b32 s78, s98, 0
	s_cselect_b32 s79, s99, 0
	s_add_u32 s78, s78, s47
	s_addc_u32 s79, s79, 0
	s_add_i32 s32, s46, 0
	v_readlane_b32 s74, v125, s32
	s_waitcnt vmcnt(14)
	ds_read_b128 v[126:129], v4
	ds_read_b128 v[130:133], v4 offset:1024
	v_lshl_add_u64 v[2:3], v[72:73], 0, s[78:79]
	v_cvt_scalef32_pk_f32_fp4 v[136:137], v98, 1.0
	v_cvt_scalef32_pk_f32_fp4 v[138:139], v98, 1.0 op_sel:[1,0,0]
	v_cvt_scalef32_pk_f32_fp4 v[140:141], v98, 1.0 op_sel:[0,1,0]
	v_cvt_scalef32_pk_f32_fp4 v[142:143], v98, 1.0 op_sel:[1,1,0]
	v_pk_fma_f32 v[178:179], s[74:75], v[136:137], v[178:179] op_sel_hi:[0,1,1]
	v_pk_fma_f32 v[180:181], s[74:75], v[138:139], v[180:181] op_sel_hi:[0,1,1]
	v_pk_fma_f32 v[182:183], s[74:75], v[140:141], v[182:183] op_sel_hi:[0,1,1]
	v_pk_fma_f32 v[184:185], s[74:75], v[142:143], v[184:185] op_sel_hi:[0,1,1]
	v_cvt_scalef32_pk_f32_fp4 v[136:137], v99, 1.0
	v_cvt_scalef32_pk_f32_fp4 v[138:139], v99, 1.0 op_sel:[1,0,0]
	v_cvt_scalef32_pk_f32_fp4 v[140:141], v99, 1.0 op_sel:[0,1,0]
	v_cvt_scalef32_pk_f32_fp4 v[142:143], v99, 1.0 op_sel:[1,1,0]
	v_pk_fma_f32 v[186:187], s[74:75], v[136:137], v[186:187] op_sel_hi:[0,1,1]
	v_pk_fma_f32 v[188:189], s[74:75], v[138:139], v[188:189] op_sel_hi:[0,1,1]
	v_pk_fma_f32 v[190:191], s[74:75], v[140:141], v[190:191] op_sel_hi:[0,1,1]
	v_pk_fma_f32 v[192:193], s[74:75], v[142:143], v[192:193] op_sel_hi:[0,1,1]
	v_cvt_scalef32_pk_f32_fp4 v[136:137], v100, 1.0
	v_cvt_scalef32_pk_f32_fp4 v[138:139], v100, 1.0 op_sel:[1,0,0]
	v_cvt_scalef32_pk_f32_fp4 v[140:141], v100, 1.0 op_sel:[0,1,0]
	v_cvt_scalef32_pk_f32_fp4 v[142:143], v100, 1.0 op_sel:[1,1,0]
	v_pk_fma_f32 v[194:195], s[74:75], v[136:137], v[194:195] op_sel_hi:[0,1,1]
	v_pk_fma_f32 v[196:197], s[74:75], v[138:139], v[196:197] op_sel_hi:[0,1,1]
	v_pk_fma_f32 v[198:199], s[74:75], v[140:141], v[198:199] op_sel_hi:[0,1,1]
	v_pk_fma_f32 v[200:201], s[74:75], v[142:143], v[200:201] op_sel_hi:[0,1,1]
	s_waitcnt lgkmcnt(0)
	s_mov_b32 m0, s77
	s_nop 0
	global_load_lds_dwordx4 v[2:3], off
	global_load_lds_dwordx4 v[2:3], off offset:1024
	v_cvt_scalef32_pk_f32_fp4 v[136:137], v101, 1.0
	v_cvt_scalef32_pk_f32_fp4 v[138:139], v101, 1.0 op_sel:[1,0,0]
	v_cvt_scalef32_pk_f32_fp4 v[140:141], v101, 1.0 op_sel:[0,1,0]
	v_cvt_scalef32_pk_f32_fp4 v[142:143], v101, 1.0 op_sel:[1,1,0]
	v_pk_fma_f32 v[202:203], s[74:75], v[136:137], v[202:203] op_sel_hi:[0,1,1]
	v_pk_fma_f32 v[204:205], s[74:75], v[138:139], v[204:205] op_sel_hi:[0,1,1]
	v_pk_fma_f32 v[206:207], s[74:75], v[140:141], v[206:207] op_sel_hi:[0,1,1]
	v_pk_fma_f32 v[208:209], s[74:75], v[142:143], v[208:209] op_sel_hi:[0,1,1]
	v_cvt_scalef32_pk_f32_fp4 v[136:137], v102, 1.0
	v_cvt_scalef32_pk_f32_fp4 v[138:139], v102, 1.0 op_sel:[1,0,0]
	v_cvt_scalef32_pk_f32_fp4 v[140:141], v102, 1.0 op_sel:[0,1,0]
	v_cvt_scalef32_pk_f32_fp4 v[142:143], v102, 1.0 op_sel:[1,1,0]
	v_pk_fma_f32 v[210:211], s[74:75], v[136:137], v[210:211] op_sel_hi:[0,1,1]
	v_pk_fma_f32 v[212:213], s[74:75], v[138:139], v[212:213] op_sel_hi:[0,1,1]
	v_pk_fma_f32 v[214:215], s[74:75], v[140:141], v[214:215] op_sel_hi:[0,1,1]
	v_pk_fma_f32 v[216:217], s[74:75], v[142:143], v[216:217] op_sel_hi:[0,1,1]
	v_cvt_scalef32_pk_f32_fp4 v[136:137], v103, 1.0
	v_cvt_scalef32_pk_f32_fp4 v[138:139], v103, 1.0 op_sel:[1,0,0]
	v_cvt_scalef32_pk_f32_fp4 v[140:141], v103, 1.0 op_sel:[0,1,0]
	v_cvt_scalef32_pk_f32_fp4 v[142:143], v103, 1.0 op_sel:[1,1,0]
	v_pk_fma_f32 v[218:219], s[74:75], v[136:137], v[218:219] op_sel_hi:[0,1,1]
	v_pk_fma_f32 v[220:221], s[74:75], v[138:139], v[220:221] op_sel_hi:[0,1,1]
	v_pk_fma_f32 v[222:223], s[74:75], v[140:141], v[222:223] op_sel_hi:[0,1,1]
	v_pk_fma_f32 v[224:225], s[74:75], v[142:143], v[224:225] op_sel_hi:[0,1,1]
	v_cvt_scalef32_pk_f32_fp4 v[136:137], v104, 1.0
	v_cvt_scalef32_pk_f32_fp4 v[138:139], v104, 1.0 op_sel:[1,0,0]
	v_cvt_scalef32_pk_f32_fp4 v[140:141], v104, 1.0 op_sel:[0,1,0]
	v_cvt_scalef32_pk_f32_fp4 v[142:143], v104, 1.0 op_sel:[1,1,0]
	v_pk_fma_f32 v[226:227], s[74:75], v[136:137], v[226:227] op_sel_hi:[0,1,1]
	v_pk_fma_f32 v[228:229], s[74:75], v[138:139], v[228:229] op_sel_hi:[0,1,1]
	v_pk_fma_f32 v[230:231], s[74:75], v[140:141], v[230:231] op_sel_hi:[0,1,1]
	v_pk_fma_f32 v[232:233], s[74:75], v[142:143], v[232:233] op_sel_hi:[0,1,1]
	v_cvt_scalef32_pk_f32_fp4 v[136:137], v105, 1.0
	v_cvt_scalef32_pk_f32_fp4 v[138:139], v105, 1.0 op_sel:[1,0,0]
	v_cvt_scalef32_pk_f32_fp4 v[140:141], v105, 1.0 op_sel:[0,1,0]
	v_cvt_scalef32_pk_f32_fp4 v[142:143], v105, 1.0 op_sel:[1,1,0]
	v_pk_fma_f32 v[234:235], s[74:75], v[136:137], v[234:235] op_sel_hi:[0,1,1]
	v_pk_fma_f32 v[236:237], s[74:75], v[138:139], v[236:237] op_sel_hi:[0,1,1]
	v_pk_fma_f32 v[238:239], s[74:75], v[140:141], v[238:239] op_sel_hi:[0,1,1]
	v_pk_fma_f32 v[240:241], s[74:75], v[142:143], v[240:241] op_sel_hi:[0,1,1]
; DI void peer_token(LAS unsigned char* ring, const bf16* x1row, float inv2, const float* nffn, const int* ex, const float* pg, const unsigned char* U6, const unsigned char* V6,
;                    const float* usc, const float* vsc, float* orow, int lane) {
;     ...
;     for (int k = 0; k < 56; ++k) P11_V(k, cf_lo, vl, e_lo, k + 8);
; #pragma unroll 1
;     for (int k = 56; k < 64; ++k) P11_V(k, cf_lo, vl, e_hi, k - 56);
; #pragma unroll 1
;     for (int k = 64; k < 120; ++k) P11_V(k, cf_hi, vl, e_hi, k - 56);
; #pragma unroll 1
;     for (int k = 120; k < 128; ++k) P11_V(k, cf_hi, vl, e_lo, k - 120);
.Lpv1_odd:
	s_add_i32 s32, s46, 1
	s_bitcmp1_b64 s[50:51], s32
	s_cbranch_scc1 .Lpv1_oddB
	s_add_i32 s47, s46, 2
	s_and_b32 s47, s47, 7
	s_lshl_b32 s47, s47, 11
	s_add_i32 s77, s33, s47
	v_add_u32_e32 v4, s77, v70
	s_add_i32 s78, s46, 10
	s_and_b32 s75, s78, 63
	v_readlane_b32 s79, v242, s75
	v_readlane_b32 s47, v113, s75
	s_bitcmp1_b32 s78, 6
	s_cselect_b32 s47, s47, s79
	s_lshr_b32 s47, s47, 8
	s_lshl_b32 s47, s47, 11
	s_bitcmp1_b32 s78, 8
	s_cselect_b32 s78, s98, 0
	s_cselect_b32 s79, s99, 0
	s_add_u32 s78, s78, s47
	s_addc_u32 s79, s79, 0
	s_add_i32 s32, s46, 1
	v_readlane_b32 s74, v125, s32
	s_waitcnt vmcnt(14)
	ds_read_b128 v[98:101], v4
	ds_read_b128 v[102:105], v4 offset:1024
	v_lshl_add_u64 v[2:3], v[72:73], 0, s[78:79]
	v_cvt_scalef32_pk_f32_fp4 v[136:137], v126, 1.0
	v_cvt_scalef32_pk_f32_fp4 v[138:139], v126, 1.0 op_sel:[1,0,0]
	v_cvt_scalef32_pk_f32_fp4 v[140:141], v126, 1.0 op_sel:[0,1,0]
	v_cvt_scalef32_pk_f32_fp4 v[142:143], v126, 1.0 op_sel:[1,1,0]
	v_pk_fma_f32 v[94:95], s[74:75], v[136:137], v[94:95] op_sel_hi:[0,1,1]
	v_pk_fma_f32 v[96:97], s[74:75], v[138:139], v[96:97] op_sel_hi:[0,1,1]
	v_pk_fma_f32 v[92:93], s[74:75], v[140:141], v[92:93] op_sel_hi:[0,1,1]
	v_pk_fma_f32 v[90:91], s[74:75], v[142:143], v[90:91] op_sel_hi:[0,1,1]
	v_cvt_scalef32_pk_f32_fp4 v[136:137], v127, 1.0
	v_cvt_scalef32_pk_f32_fp4 v[138:139], v127, 1.0 op_sel:[1,0,0]
	v_cvt_scalef32_pk_f32_fp4 v[140:141], v127, 1.0 op_sel:[0,1,0]
	v_cvt_scalef32_pk_f32_fp4 v[142:143], v127, 1.0 op_sel:[1,1,0]
	v_pk_fma_f32 v[88:89], s[74:75], v[136:137], v[88:89] op_sel_hi:[0,1,1]
	v_pk_fma_f32 v[86:87], s[74:75], v[138:139], v[86:87] op_sel_hi:[0,1,1]
	v_pk_fma_f32 v[84:85], s[74:75], v[140:141], v[84:85] op_sel_hi:[0,1,1]
	v_pk_fma_f32 v[82:83], s[74:75], v[142:143], v[82:83] op_sel_hi:[0,1,1]
	v_cvt_scalef32_pk_f32_fp4 v[136:137], v128, 1.0
	v_cvt_scalef32_pk_f32_fp4 v[138:139], v128, 1.0 op_sel:[1,0,0]
	v_cvt_scalef32_pk_f32_fp4 v[140:141], v128, 1.0 op_sel:[0,1,0]
	v_cvt_scalef32_pk_f32_fp4 v[142:143], v128, 1.0 op_sel:[1,1,0]
	v_pk_fma_f32 v[64:65], s[74:75], v[136:137], v[64:65] op_sel_hi:[0,1,1]
	v_pk_fma_f32 v[80:81], s[74:75], v[138:139], v[80:81] op_sel_hi:[0,1,1]
	v_pk_fma_f32 v[62:63], s[74:75], v[140:141], v[62:63] op_sel_hi:[0,1,1]
	v_pk_fma_f32 v[60:61], s[74:75], v[142:143], v[60:61] op_sel_hi:[0,1,1]
	s_waitcnt lgkmcnt(0)
	s_mov_b32 m0, s77
	s_nop 0
	global_load_lds_dwordx4 v[2:3], off
	global_load_lds_dwordx4 v[2:3], off offset:1024
	v_cvt_scalef32_pk_f32_fp4 v[136:137], v129, 1.0
	v_cvt_scalef32_pk_f32_fp4 v[138:139], v129, 1.0 op_sel:[1,0,0]
	v_cvt_scalef32_pk_f32_fp4 v[140:141], v129, 1.0 op_sel:[0,1,0]
	v_cvt_scalef32_pk_f32_fp4 v[142:143], v129, 1.0 op_sel:[1,1,0]
	v_pk_fma_f32 v[58:59], s[74:75], v[136:137], v[58:59] op_sel_hi:[0,1,1]
	v_pk_fma_f32 v[56:57], s[74:75], v[138:139], v[56:57] op_sel_hi:[0,1,1]
	v_pk_fma_f32 v[54:55], s[74:75], v[140:141], v[54:55] op_sel_hi:[0,1,1]
	v_pk_fma_f32 v[52:53], s[74:75], v[142:143], v[52:53] op_sel_hi:[0,1,1]
	v_cvt_scalef32_pk_f32_fp4 v[136:137], v130, 1.0
	v_cvt_scalef32_pk_f32_fp4 v[138:139], v130, 1.0 op_sel:[1,0,0]
	v_cvt_scalef32_pk_f32_fp4 v[140:141], v130, 1.0 op_sel:[0,1,0]
	v_cvt_scalef32_pk_f32_fp4 v[142:143], v130, 1.0 op_sel:[1,1,0]
	v_pk_fma_f32 v[50:51], s[74:75], v[136:137], v[50:51] op_sel_hi:[0,1,1]
	v_pk_fma_f32 v[48:49], s[74:75], v[138:139], v[48:49] op_sel_hi:[0,1,1]
	v_pk_fma_f32 v[46:47], s[74:75], v[140:141], v[46:47] op_sel_hi:[0,1,1]
	v_pk_fma_f32 v[44:45], s[74:75], v[142:143], v[44:45] op_sel_hi:[0,1,1]
	v_cvt_scalef32_pk_f32_fp4 v[136:137], v131, 1.0
	v_cvt_scalef32_pk_f32_fp4 v[138:139], v131, 1.0 op_sel:[1,0,0]
	v_cvt_scalef32_pk_f32_fp4 v[140:141], v131, 1.0 op_sel:[0,1,0]
	v_cvt_scalef32_pk_f32_fp4 v[142:143], v131, 1.0 op_sel:[1,1,0]
	v_pk_fma_f32 v[42:43], s[74:75], v[136:137], v[42:43] op_sel_hi:[0,1,1]
	v_pk_fma_f32 v[40:41], s[74:75], v[138:139], v[40:41] op_sel_hi:[0,1,1]
	v_pk_fma_f32 v[38:39], s[74:75], v[140:141], v[38:39] op_sel_hi:[0,1,1]
	v_pk_fma_f32 v[36:37], s[74:75], v[142:143], v[36:37] op_sel_hi:[0,1,1]
	v_cvt_scalef32_pk_f32_fp4 v[136:137], v132, 1.0
	v_cvt_scalef32_pk_f32_fp4 v[138:139], v132, 1.0 op_sel:[1,0,0]
	v_cvt_scalef32_pk_f32_fp4 v[140:141], v132, 1.0 op_sel:[0,1,0]
	v_cvt_scalef32_pk_f32_fp4 v[142:143], v132, 1.0 op_sel:[1,1,0]
	v_pk_fma_f32 v[32:33], s[74:75], v[136:137], v[32:33] op_sel_hi:[0,1,1]
	v_pk_fma_f32 v[34:35], s[74:75], v[138:139], v[34:35] op_sel_hi:[0,1,1]
	v_pk_fma_f32 v[30:31], s[74:75], v[140:141], v[30:31] op_sel_hi:[0,1,1]
	v_pk_fma_f32 v[28:29], s[74:75], v[142:143], v[28:29] op_sel_hi:[0,1,1]
	v_cvt_scalef32_pk_f32_fp4 v[136:137], v133, 1.0
	v_cvt_scalef32_pk_f32_fp4 v[138:139], v133, 1.0 op_sel:[1,0,0]
	v_cvt_scalef32_pk_f32_fp4 v[140:141], v133, 1.0 op_sel:[0,1,0]
	v_cvt_scalef32_pk_f32_fp4 v[142:143], v133, 1.0 op_sel:[1,1,0]
	v_pk_fma_f32 v[26:27], s[74:75], v[136:137], v[26:27] op_sel_hi:[0,1,1]
	v_pk_fma_f32 v[24:25], s[74:75], v[138:139], v[24:25] op_sel_hi:[0,1,1]
	v_pk_fma_f32 v[20:21], s[74:75], v[140:141], v[20:21] op_sel_hi:[0,1,1]
	v_pk_fma_f32 v[22:23], s[74:75], v[142:143], v[22:23] op_sel_hi:[0,1,1]
	s_branch .Lpv1_next
; DI void peer_token(LAS unsigned char* ring, const bf16* x1row, float inv2, const float* nffn, const int* ex, const float* pg, const unsigned char* U6, const unsigned char* V6,
;                    const float* usc, const float* vsc, float* orow, int lane) {
;     ...
;     for (int k = 0; k < 56; ++k) P11_V(k, cf_lo, vl, e_lo, k + 8);
; #pragma unroll 1
;     for (int k = 56; k < 64; ++k) P11_V(k, cf_lo, vl, e_hi, k - 56);
; #pragma unroll 1
;     for (int k = 64; k < 120; ++k) P11_V(k, cf_hi, vl, e_hi, k - 56);
; #pragma unroll 1
;     for (int k = 120; k < 128; ++k) P11_V(k, cf_hi, vl, e_lo, k - 120);
.Lpv1_oddB:
	s_add_i32 s47, s46, 2
	s_and_b32 s47, s47, 7
	s_lshl_b32 s47, s47, 11
	s_add_i32 s77, s33, s47
	v_add_u32_e32 v4, s77, v70
	s_add_i32 s78, s46, 10
	s_and_b32 s75, s78, 63
	v_readlane_b32 s79, v242, s75
	v_readlane_b32 s47, v113, s75
	s_bitcmp1_b32 s78, 6
	s_cselect_b32 s47, s47, s79
	s_lshr_b32 s47, s47, 8
	s_lshl_b32 s47, s47, 11
	s_bitcmp1_b32 s78, 8
	s_cselect_b32 s78, s98, 0
	s_cselect_b32 s79, s99, 0
	s_add_u32 s78, s78, s47
	s_addc_u32 s79, s79, 0
	s_add_i32 s32, s46, 1
	v_readlane_b32 s74, v125, s32
	s_waitcnt vmcnt(14)
	ds_read_b128 v[98:101], v4
	ds_read_b128 v[102:105], v4 offset:1024
	v_lshl_add_u64 v[2:3], v[72:73], 0, s[78:79]
	v_cvt_scalef32_pk_f32_fp4 v[136:137], v126, 1.0
	v_cvt_scalef32_pk_f32_fp4 v[138:139], v126, 1.0 op_sel:[1,0,0]
	v_cvt_scalef32_pk_f32_fp4 v[140:141], v126, 1.0 op_sel:[0,1,0]
	v_cvt_scalef32_pk_f32_fp4 v[142:143], v126, 1.0 op_sel:[1,1,0]
	v_pk_fma_f32 v[178:179], s[74:75], v[136:137], v[178:179] op_sel_hi:[0,1,1]
	v_pk_fma_f32 v[180:181], s[74:75], v[138:139], v[180:181] op_sel_hi:[0,1,1]
	v_pk_fma_f32 v[182:183], s[74:75], v[140:141], v[182:183] op_sel_hi:[0,1,1]
	v_pk_fma_f32 v[184:185], s[74:75], v[142:143], v[184:185] op_sel_hi:[0,1,1]
	v_cvt_scalef32_pk_f32_fp4 v[136:137], v127, 1.0
	v_cvt_scalef32_pk_f32_fp4 v[138:139], v127, 1.0 op_sel:[1,0,0]
	v_cvt_scalef32_pk_f32_fp4 v[140:141], v127, 1.0 op_sel:[0,1,0]
	v_cvt_scalef32_pk_f32_fp4 v[142:143], v127, 1.0 op_sel:[1,1,0]
	v_pk_fma_f32 v[186:187], s[74:75], v[136:137], v[186:187] op_sel_hi:[0,1,1]
	v_pk_fma_f32 v[188:189], s[74:75], v[138:139], v[188:189] op_sel_hi:[0,1,1]
	v_pk_fma_f32 v[190:191], s[74:75], v[140:141], v[190:191] op_sel_hi:[0,1,1]
	v_pk_fma_f32 v[192:193], s[74:75], v[142:143], v[192:193] op_sel_hi:[0,1,1]
	v_cvt_scalef32_pk_f32_fp4 v[136:137], v128, 1.0
	v_cvt_scalef32_pk_f32_fp4 v[138:139], v128, 1.0 op_sel:[1,0,0]
	v_cvt_scalef32_pk_f32_fp4 v[140:141], v128, 1.0 op_sel:[0,1,0]
	v_cvt_scalef32_pk_f32_fp4 v[142:143], v128, 1.0 op_sel:[1,1,0]
	v_pk_fma_f32 v[194:195], s[74:75], v[136:137], v[194:195] op_sel_hi:[0,1,1]
	v_pk_fma_f32 v[196:197], s[74:75], v[138:139], v[196:197] op_sel_hi:[0,1,1]
	v_pk_fma_f32 v[198:199], s[74:75], v[140:141], v[198:199] op_sel_hi:[0,1,1]
	v_pk_fma_f32 v[200:201], s[74:75], v[142:143], v[200:201] op_sel_hi:[0,1,1]
	s_waitcnt lgkmcnt(0)
	s_mov_b32 m0, s77
	s_nop 0
	global_load_lds_dwordx4 v[2:3], off
	global_load_lds_dwordx4 v[2:3], off offset:1024
	v_cvt_scalef32_pk_f32_fp4 v[136:137], v129, 1.0
	v_cvt_scalef32_pk_f32_fp4 v[138:139], v129, 1.0 op_sel:[1,0,0]
	v_cvt_scalef32_pk_f32_fp4 v[140:141], v129, 1.0 op_sel:[0,1,0]
	v_cvt_scalef32_pk_f32_fp4 v[142:143], v129, 1.0 op_sel:[1,1,0]
	v_pk_fma_f32 v[202:203], s[74:75], v[136:137], v[202:203] op_sel_hi:[0,1,1]
	v_pk_fma_f32 v[204:205], s[74:75], v[138:139], v[204:205] op_sel_hi:[0,1,1]
	v_pk_fma_f32 v[206:207], s[74:75], v[140:141], v[206:207] op_sel_hi:[0,1,1]
	v_pk_fma_f32 v[208:209], s[74:75], v[142:143], v[208:209] op_sel_hi:[0,1,1]
	v_cvt_scalef32_pk_f32_fp4 v[136:137], v130, 1.0
	v_cvt_scalef32_pk_f32_fp4 v[138:139], v130, 1.0 op_sel:[1,0,0]
	v_cvt_scalef32_pk_f32_fp4 v[140:141], v130, 1.0 op_sel:[0,1,0]
	v_cvt_scalef32_pk_f32_fp4 v[142:143], v130, 1.0 op_sel:[1,1,0]
	v_pk_fma_f32 v[210:211], s[74:75], v[136:137], v[210:211] op_sel_hi:[0,1,1]
	v_pk_fma_f32 v[212:213], s[74:75], v[138:139], v[212:213] op_sel_hi:[0,1,1]
	v_pk_fma_f32 v[214:215], s[74:75], v[140:141], v[214:215] op_sel_hi:[0,1,1]
	v_pk_fma_f32 v[216:217], s[74:75], v[142:143], v[216:217] op_sel_hi:[0,1,1]
	v_cvt_scalef32_pk_f32_fp4 v[136:137], v131, 1.0
	v_cvt_scalef32_pk_f32_fp4 v[138:139], v131, 1.0 op_sel:[1,0,0]
	v_cvt_scalef32_pk_f32_fp4 v[140:141], v131, 1.0 op_sel:[0,1,0]
	v_cvt_scalef32_pk_f32_fp4 v[142:143], v131, 1.0 op_sel:[1,1,0]
	v_pk_fma_f32 v[218:219], s[74:75], v[136:137], v[218:219] op_sel_hi:[0,1,1]
	v_pk_fma_f32 v[220:221], s[74:75], v[138:139], v[220:221] op_sel_hi:[0,1,1]
	v_pk_fma_f32 v[222:223], s[74:75], v[140:141], v[222:223] op_sel_hi:[0,1,1]
	v_pk_fma_f32 v[224:225], s[74:75], v[142:143], v[224:225] op_sel_hi:[0,1,1]
	v_cvt_scalef32_pk_f32_fp4 v[136:137], v132, 1.0
	v_cvt_scalef32_pk_f32_fp4 v[138:139], v132, 1.0 op_sel:[1,0,0]
	v_cvt_scalef32_pk_f32_fp4 v[140:141], v132, 1.0 op_sel:[0,1,0]
	v_cvt_scalef32_pk_f32_fp4 v[142:143], v132, 1.0 op_sel:[1,1,0]
	v_pk_fma_f32 v[226:227], s[74:75], v[136:137], v[226:227] op_sel_hi:[0,1,1]
	v_pk_fma_f32 v[228:229], s[74:75], v[138:139], v[228:229] op_sel_hi:[0,1,1]
	v_pk_fma_f32 v[230:231], s[74:75], v[140:141], v[230:231] op_sel_hi:[0,1,1]
	v_pk_fma_f32 v[232:233], s[74:75], v[142:143], v[232:233] op_sel_hi:[0,1,1]
	v_cvt_scalef32_pk_f32_fp4 v[136:137], v133, 1.0
	v_cvt_scalef32_pk_f32_fp4 v[138:139], v133, 1.0 op_sel:[1,0,0]
	v_cvt_scalef32_pk_f32_fp4 v[140:141], v133, 1.0 op_sel:[0,1,0]
	v_cvt_scalef32_pk_f32_fp4 v[142:143], v133, 1.0 op_sel:[1,1,0]
	v_pk_fma_f32 v[234:235], s[74:75], v[136:137], v[234:235] op_sel_hi:[0,1,1]
	v_pk_fma_f32 v[236:237], s[74:75], v[138:139], v[236:237] op_sel_hi:[0,1,1]
	v_pk_fma_f32 v[238:239], s[74:75], v[140:141], v[238:239] op_sel_hi:[0,1,1]
	v_pk_fma_f32 v[240:241], s[74:75], v[142:143], v[240:241] op_sel_hi:[0,1,1]
.Lpv1_next:
	s_add_i32 s46, s46, 2
	s_cmp_lg_u32 s46, 384
	s_cbranch_scc1 .Lpv1_even
; DI void peer_token(LAS unsigned char* ring, const bf16* x1row, float inv2, const float* nffn, const int* ex, const float* pg, const unsigned char* U6, const unsigned char* V6,
;                    const float* usc, const float* vsc, float* orow, int lane) {
;     ...
;     for (int k = 0; k < 56; ++k) P11_V(k, cf_lo, vl, e_lo, k + 8);
; #pragma unroll 1
;     for (int k = 56; k < 64; ++k) P11_V(k, cf_lo, vl, e_hi, k - 56);
; #pragma unroll 1
;     for (int k = 64; k < 120; ++k) P11_V(k, cf_hi, vl, e_hi, k - 56);
; #pragma unroll 1
;     for (int k = 120; k < 128; ++k) P11_V(k, cf_hi, vl, e_lo, k - 120);
.Lpv2_even:
	s_bitcmp1_b64 s[82:83], s46
	s_cbranch_scc1 .Lpv2_evenB
	s_add_i32 s47, s46, 1
	s_and_b32 s47, s47, 7
	s_lshl_b32 s47, s47, 11
	s_add_i32 s77, s33, s47
	v_add_u32_e32 v4, s77, v70
	s_add_i32 s78, s46, 9
	s_and_b32 s75, s78, 63
	v_readlane_b32 s79, v243, s75
	v_readlane_b32 s47, v242, s75
	s_bitcmp1_b32 s78, 6
	s_cselect_b32 s47, s79, s47
	s_lshr_b32 s47, s47, 8
	s_lshl_b32 s47, s47, 11
	s_bitcmp1_b32 s78, 8
	s_cselect_b32 s78, s98, 0
	s_cselect_b32 s79, s99, 0
	s_add_u32 s78, s78, s47
	s_addc_u32 s79, s79, 0
	s_add_i32 s32, s46, 0
	v_readlane_b32 s74, v248, s32
	s_waitcnt vmcnt(14)
	ds_read_b128 v[126:129], v4
	ds_read_b128 v[130:133], v4 offset:1024
	v_lshl_add_u64 v[2:3], v[72:73], 0, s[78:79]
	v_cvt_scalef32_pk_f32_fp4 v[136:137], v98, 1.0
	v_cvt_scalef32_pk_f32_fp4 v[138:139], v98, 1.0 op_sel:[1,0,0]
	v_cvt_scalef32_pk_f32_fp4 v[140:141], v98, 1.0 op_sel:[0,1,0]
	v_cvt_scalef32_pk_f32_fp4 v[142:143], v98, 1.0 op_sel:[1,1,0]
	v_pk_fma_f32 v[94:95], s[74:75], v[136:137], v[94:95] op_sel_hi:[0,1,1]
	v_pk_fma_f32 v[96:97], s[74:75], v[138:139], v[96:97] op_sel_hi:[0,1,1]
	v_pk_fma_f32 v[92:93], s[74:75], v[140:141], v[92:93] op_sel_hi:[0,1,1]
	v_pk_fma_f32 v[90:91], s[74:75], v[142:143], v[90:91] op_sel_hi:[0,1,1]
	v_cvt_scalef32_pk_f32_fp4 v[136:137], v99, 1.0
	v_cvt_scalef32_pk_f32_fp4 v[138:139], v99, 1.0 op_sel:[1,0,0]
	v_cvt_scalef32_pk_f32_fp4 v[140:141], v99, 1.0 op_sel:[0,1,0]
	v_cvt_scalef32_pk_f32_fp4 v[142:143], v99, 1.0 op_sel:[1,1,0]
	v_pk_fma_f32 v[88:89], s[74:75], v[136:137], v[88:89] op_sel_hi:[0,1,1]
	v_pk_fma_f32 v[86:87], s[74:75], v[138:139], v[86:87] op_sel_hi:[0,1,1]
	v_pk_fma_f32 v[84:85], s[74:75], v[140:141], v[84:85] op_sel_hi:[0,1,1]
	v_pk_fma_f32 v[82:83], s[74:75], v[142:143], v[82:83] op_sel_hi:[0,1,1]
	v_cvt_scalef32_pk_f32_fp4 v[136:137], v100, 1.0
	v_cvt_scalef32_pk_f32_fp4 v[138:139], v100, 1.0 op_sel:[1,0,0]
	v_cvt_scalef32_pk_f32_fp4 v[140:141], v100, 1.0 op_sel:[0,1,0]
	v_cvt_scalef32_pk_f32_fp4 v[142:143], v100, 1.0 op_sel:[1,1,0]
	v_pk_fma_f32 v[64:65], s[74:75], v[136:137], v[64:65] op_sel_hi:[0,1,1]
	v_pk_fma_f32 v[80:81], s[74:75], v[138:139], v[80:81] op_sel_hi:[0,1,1]
	v_pk_fma_f32 v[62:63], s[74:75], v[140:141], v[62:63] op_sel_hi:[0,1,1]
	v_pk_fma_f32 v[60:61], s[74:75], v[142:143], v[60:61] op_sel_hi:[0,1,1]
	s_waitcnt lgkmcnt(0)
	s_mov_b32 m0, s77
	s_nop 0
	global_load_lds_dwordx4 v[2:3], off
	global_load_lds_dwordx4 v[2:3], off offset:1024
	v_cvt_scalef32_pk_f32_fp4 v[136:137], v101, 1.0
	v_cvt_scalef32_pk_f32_fp4 v[138:139], v101, 1.0 op_sel:[1,0,0]
	v_cvt_scalef32_pk_f32_fp4 v[140:141], v101, 1.0 op_sel:[0,1,0]
	v_cvt_scalef32_pk_f32_fp4 v[142:143], v101, 1.0 op_sel:[1,1,0]
	v_pk_fma_f32 v[58:59], s[74:75], v[136:137], v[58:59] op_sel_hi:[0,1,1]
	v_pk_fma_f32 v[56:57], s[74:75], v[138:139], v[56:57] op_sel_hi:[0,1,1]
	v_pk_fma_f32 v[54:55], s[74:75], v[140:141], v[54:55] op_sel_hi:[0,1,1]
	v_pk_fma_f32 v[52:53], s[74:75], v[142:143], v[52:53] op_sel_hi:[0,1,1]
	v_cvt_scalef32_pk_f32_fp4 v[136:137], v102, 1.0
	v_cvt_scalef32_pk_f32_fp4 v[138:139], v102, 1.0 op_sel:[1,0,0]
	v_cvt_scalef32_pk_f32_fp4 v[140:141], v102, 1.0 op_sel:[0,1,0]
	v_cvt_scalef32_pk_f32_fp4 v[142:143], v102, 1.0 op_sel:[1,1,0]
	v_pk_fma_f32 v[50:51], s[74:75], v[136:137], v[50:51] op_sel_hi:[0,1,1]
	v_pk_fma_f32 v[48:49], s[74:75], v[138:139], v[48:49] op_sel_hi:[0,1,1]
	v_pk_fma_f32 v[46:47], s[74:75], v[140:141], v[46:47] op_sel_hi:[0,1,1]
	v_pk_fma_f32 v[44:45], s[74:75], v[142:143], v[44:45] op_sel_hi:[0,1,1]
	v_cvt_scalef32_pk_f32_fp4 v[136:137], v103, 1.0
	v_cvt_scalef32_pk_f32_fp4 v[138:139], v103, 1.0 op_sel:[1,0,0]
	v_cvt_scalef32_pk_f32_fp4 v[140:141], v103, 1.0 op_sel:[0,1,0]
	v_cvt_scalef32_pk_f32_fp4 v[142:143], v103, 1.0 op_sel:[1,1,0]
	v_pk_fma_f32 v[42:43], s[74:75], v[136:137], v[42:43] op_sel_hi:[0,1,1]
	v_pk_fma_f32 v[40:41], s[74:75], v[138:139], v[40:41] op_sel_hi:[0,1,1]
	v_pk_fma_f32 v[38:39], s[74:75], v[140:141], v[38:39] op_sel_hi:[0,1,1]
	v_pk_fma_f32 v[36:37], s[74:75], v[142:143], v[36:37] op_sel_hi:[0,1,1]
	v_cvt_scalef32_pk_f32_fp4 v[136:137], v104, 1.0
	v_cvt_scalef32_pk_f32_fp4 v[138:139], v104, 1.0 op_sel:[1,0,0]
	v_cvt_scalef32_pk_f32_fp4 v[140:141], v104, 1.0 op_sel:[0,1,0]
	v_cvt_scalef32_pk_f32_fp4 v[142:143], v104, 1.0 op_sel:[1,1,0]
	v_pk_fma_f32 v[32:33], s[74:75], v[136:137], v[32:33] op_sel_hi:[0,1,1]
	v_pk_fma_f32 v[34:35], s[74:75], v[138:139], v[34:35] op_sel_hi:[0,1,1]
	v_pk_fma_f32 v[30:31], s[74:75], v[140:141], v[30:31] op_sel_hi:[0,1,1]
	v_pk_fma_f32 v[28:29], s[74:75], v[142:143], v[28:29] op_sel_hi:[0,1,1]
	v_cvt_scalef32_pk_f32_fp4 v[136:137], v105, 1.0
	v_cvt_scalef32_pk_f32_fp4 v[138:139], v105, 1.0 op_sel:[1,0,0]
	v_cvt_scalef32_pk_f32_fp4 v[140:141], v105, 1.0 op_sel:[0,1,0]
	v_cvt_scalef32_pk_f32_fp4 v[142:143], v105, 1.0 op_sel:[1,1,0]
	v_pk_fma_f32 v[26:27], s[74:75], v[136:137], v[26:27] op_sel_hi:[0,1,1]
	v_pk_fma_f32 v[24:25], s[74:75], v[138:139], v[24:25] op_sel_hi:[0,1,1]
	v_pk_fma_f32 v[20:21], s[74:75], v[140:141], v[20:21] op_sel_hi:[0,1,1]
	v_pk_fma_f32 v[22:23], s[74:75], v[142:143], v[22:23] op_sel_hi:[0,1,1]
	s_branch .Lpv2_odd
; DI void peer_token(LAS unsigned char* ring, const bf16* x1row, float inv2, const float* nffn, const int* ex, const float* pg, const unsigned char* U6, const unsigned char* V6,
;                    const float* usc, const float* vsc, float* orow, int lane) {
;     ...
;     for (int k = 0; k < 56; ++k) P11_V(k, cf_lo, vl, e_lo, k + 8);
; #pragma unroll 1
;     for (int k = 56; k < 64; ++k) P11_V(k, cf_lo, vl, e_hi, k - 56);
; #pragma unroll 1
;     for (int k = 64; k < 120; ++k) P11_V(k, cf_hi, vl, e_hi, k - 56);
; #pragma unroll 1
;     for (int k = 120; k < 128; ++k) P11_V(k, cf_hi, vl, e_lo, k - 120);
.Lpv2_evenB:
	s_add_i32 s47, s46, 1
	s_and_b32 s47, s47, 7
	s_lshl_b32 s47, s47, 11
	s_add_i32 s77, s33, s47
	v_add_u32_e32 v4, s77, v70
	s_add_i32 s78, s46, 9
	s_and_b32 s75, s78, 63
	v_readlane_b32 s79, v243, s75
	v_readlane_b32 s47, v242, s75
	s_bitcmp1_b32 s78, 6
	s_cselect_b32 s47, s79, s47
	s_lshr_b32 s47, s47, 8
	s_lshl_b32 s47, s47, 11
	s_bitcmp1_b32 s78, 8
	s_cselect_b32 s78, s98, 0
	s_cselect_b32 s79, s99, 0
	s_add_u32 s78, s78, s47
	s_addc_u32 s79, s79, 0
	s_add_i32 s32, s46, 0
	v_readlane_b32 s74, v248, s32
	s_waitcnt vmcnt(14)
	ds_read_b128 v[126:129], v4
	ds_read_b128 v[130:133], v4 offset:1024
	v_lshl_add_u64 v[2:3], v[72:73], 0, s[78:79]
	v_cvt_scalef32_pk_f32_fp4 v[136:137], v98, 1.0
	v_cvt_scalef32_pk_f32_fp4 v[138:139], v98, 1.0 op_sel:[1,0,0]
	v_cvt_scalef32_pk_f32_fp4 v[140:141], v98, 1.0 op_sel:[0,1,0]
	v_cvt_scalef32_pk_f32_fp4 v[142:143], v98, 1.0 op_sel:[1,1,0]
	v_pk_fma_f32 v[178:179], s[74:75], v[136:137], v[178:179] op_sel_hi:[0,1,1]
	v_pk_fma_f32 v[180:181], s[74:75], v[138:139], v[180:181] op_sel_hi:[0,1,1]
	v_pk_fma_f32 v[182:183], s[74:75], v[140:141], v[182:183] op_sel_hi:[0,1,1]
	v_pk_fma_f32 v[184:185], s[74:75], v[142:143], v[184:185] op_sel_hi:[0,1,1]
	v_cvt_scalef32_pk_f32_fp4 v[136:137], v99, 1.0
	v_cvt_scalef32_pk_f32_fp4 v[138:139], v99, 1.0 op_sel:[1,0,0]
	v_cvt_scalef32_pk_f32_fp4 v[140:141], v99, 1.0 op_sel:[0,1,0]
	v_cvt_scalef32_pk_f32_fp4 v[142:143], v99, 1.0 op_sel:[1,1,0]
	v_pk_fma_f32 v[186:187], s[74:75], v[136:137], v[186:187] op_sel_hi:[0,1,1]
	v_pk_fma_f32 v[188:189], s[74:75], v[138:139], v[188:189] op_sel_hi:[0,1,1]
	v_pk_fma_f32 v[190:191], s[74:75], v[140:141], v[190:191] op_sel_hi:[0,1,1]
	v_pk_fma_f32 v[192:193], s[74:75], v[142:143], v[192:193] op_sel_hi:[0,1,1]
	v_cvt_scalef32_pk_f32_fp4 v[136:137], v100, 1.0
	v_cvt_scalef32_pk_f32_fp4 v[138:139], v100, 1.0 op_sel:[1,0,0]
	v_cvt_scalef32_pk_f32_fp4 v[140:141], v100, 1.0 op_sel:[0,1,0]
	v_cvt_scalef32_pk_f32_fp4 v[142:143], v100, 1.0 op_sel:[1,1,0]
	v_pk_fma_f32 v[194:195], s[74:75], v[136:137], v[194:195] op_sel_hi:[0,1,1]
	v_pk_fma_f32 v[196:197], s[74:75], v[138:139], v[196:197] op_sel_hi:[0,1,1]
	v_pk_fma_f32 v[198:199], s[74:75], v[140:141], v[198:199] op_sel_hi:[0,1,1]
	v_pk_fma_f32 v[200:201], s[74:75], v[142:143], v[200:201] op_sel_hi:[0,1,1]
	s_waitcnt lgkmcnt(0)
	s_mov_b32 m0, s77
	s_nop 0
	global_load_lds_dwordx4 v[2:3], off
	global_load_lds_dwordx4 v[2:3], off offset:1024
	v_cvt_scalef32_pk_f32_fp4 v[136:137], v101, 1.0
	v_cvt_scalef32_pk_f32_fp4 v[138:139], v101, 1.0 op_sel:[1,0,0]
	v_cvt_scalef32_pk_f32_fp4 v[140:141], v101, 1.0 op_sel:[0,1,0]
	v_cvt_scalef32_pk_f32_fp4 v[142:143], v101, 1.0 op_sel:[1,1,0]
	v_pk_fma_f32 v[202:203], s[74:75], v[136:137], v[202:203] op_sel_hi:[0,1,1]
	v_pk_fma_f32 v[204:205], s[74:75], v[138:139], v[204:205] op_sel_hi:[0,1,1]
	v_pk_fma_f32 v[206:207], s[74:75], v[140:141], v[206:207] op_sel_hi:[0,1,1]
	v_pk_fma_f32 v[208:209], s[74:75], v[142:143], v[208:209] op_sel_hi:[0,1,1]
	v_cvt_scalef32_pk_f32_fp4 v[136:137], v102, 1.0
	v_cvt_scalef32_pk_f32_fp4 v[138:139], v102, 1.0 op_sel:[1,0,0]
	v_cvt_scalef32_pk_f32_fp4 v[140:141], v102, 1.0 op_sel:[0,1,0]
	v_cvt_scalef32_pk_f32_fp4 v[142:143], v102, 1.0 op_sel:[1,1,0]
	v_pk_fma_f32 v[210:211], s[74:75], v[136:137], v[210:211] op_sel_hi:[0,1,1]
	v_pk_fma_f32 v[212:213], s[74:75], v[138:139], v[212:213] op_sel_hi:[0,1,1]
	v_pk_fma_f32 v[214:215], s[74:75], v[140:141], v[214:215] op_sel_hi:[0,1,1]
	v_pk_fma_f32 v[216:217], s[74:75], v[142:143], v[216:217] op_sel_hi:[0,1,1]
	v_cvt_scalef32_pk_f32_fp4 v[136:137], v103, 1.0
	v_cvt_scalef32_pk_f32_fp4 v[138:139], v103, 1.0 op_sel:[1,0,0]
	v_cvt_scalef32_pk_f32_fp4 v[140:141], v103, 1.0 op_sel:[0,1,0]
	v_cvt_scalef32_pk_f32_fp4 v[142:143], v103, 1.0 op_sel:[1,1,0]
	v_pk_fma_f32 v[218:219], s[74:75], v[136:137], v[218:219] op_sel_hi:[0,1,1]
	v_pk_fma_f32 v[220:221], s[74:75], v[138:139], v[220:221] op_sel_hi:[0,1,1]
	v_pk_fma_f32 v[222:223], s[74:75], v[140:141], v[222:223] op_sel_hi:[0,1,1]
	v_pk_fma_f32 v[224:225], s[74:75], v[142:143], v[224:225] op_sel_hi:[0,1,1]
	v_cvt_scalef32_pk_f32_fp4 v[136:137], v104, 1.0
	v_cvt_scalef32_pk_f32_fp4 v[138:139], v104, 1.0 op_sel:[1,0,0]
	v_cvt_scalef32_pk_f32_fp4 v[140:141], v104, 1.0 op_sel:[0,1,0]
	v_cvt_scalef32_pk_f32_fp4 v[142:143], v104, 1.0 op_sel:[1,1,0]
	v_pk_fma_f32 v[226:227], s[74:75], v[136:137], v[226:227] op_sel_hi:[0,1,1]
	v_pk_fma_f32 v[228:229], s[74:75], v[138:139], v[228:229] op_sel_hi:[0,1,1]
	v_pk_fma_f32 v[230:231], s[74:75], v[140:141], v[230:231] op_sel_hi:[0,1,1]
	v_pk_fma_f32 v[232:233], s[74:75], v[142:143], v[232:233] op_sel_hi:[0,1,1]
	v_cvt_scalef32_pk_f32_fp4 v[136:137], v105, 1.0
	v_cvt_scalef32_pk_f32_fp4 v[138:139], v105, 1.0 op_sel:[1,0,0]
	v_cvt_scalef32_pk_f32_fp4 v[140:141], v105, 1.0 op_sel:[0,1,0]
	v_cvt_scalef32_pk_f32_fp4 v[142:143], v105, 1.0 op_sel:[1,1,0]
	v_pk_fma_f32 v[234:235], s[74:75], v[136:137], v[234:235] op_sel_hi:[0,1,1]
	v_pk_fma_f32 v[236:237], s[74:75], v[138:139], v[236:237] op_sel_hi:[0,1,1]
	v_pk_fma_f32 v[238:239], s[74:75], v[140:141], v[238:239] op_sel_hi:[0,1,1]
	v_pk_fma_f32 v[240:241], s[74:75], v[142:143], v[240:241] op_sel_hi:[0,1,1]
; DI void peer_token(LAS unsigned char* ring, const bf16* x1row, float inv2, const float* nffn, const int* ex, const float* pg, const unsigned char* U6, const unsigned char* V6,
;                    const float* usc, const float* vsc, float* orow, int lane) {
;     ...
;     for (int k = 0; k < 56; ++k) P11_V(k, cf_lo, vl, e_lo, k + 8);
; #pragma unroll 1
;     for (int k = 56; k < 64; ++k) P11_V(k, cf_lo, vl, e_hi, k - 56);
; #pragma unroll 1
;     for (int k = 64; k < 120; ++k) P11_V(k, cf_hi, vl, e_hi, k - 56);
; #pragma unroll 1
;     for (int k = 120; k < 128; ++k) P11_V(k, cf_hi, vl, e_lo, k - 120);
.Lpv2_odd:
	s_add_i32 s32, s46, 1
	s_bitcmp1_b64 s[82:83], s32
	s_cbranch_scc1 .Lpv2_oddB
	s_add_i32 s47, s46, 2
	s_and_b32 s47, s47, 7
	s_lshl_b32 s47, s47, 11
	s_add_i32 s77, s33, s47
	v_add_u32_e32 v4, s77, v70
	s_add_i32 s78, s46, 10
	s_and_b32 s75, s78, 63
	v_readlane_b32 s79, v243, s75
	v_readlane_b32 s47, v242, s75
	s_bitcmp1_b32 s78, 6
	s_cselect_b32 s47, s79, s47
	s_lshr_b32 s47, s47, 8
	s_lshl_b32 s47, s47, 11
	s_bitcmp1_b32 s78, 8
	s_cselect_b32 s78, s98, 0
	s_cselect_b32 s79, s99, 0
	s_add_u32 s78, s78, s47
	s_addc_u32 s79, s79, 0
	s_add_i32 s32, s46, 1
	v_readlane_b32 s74, v248, s32
	s_waitcnt vmcnt(14)
	ds_read_b128 v[98:101], v4
	ds_read_b128 v[102:105], v4 offset:1024
	v_lshl_add_u64 v[2:3], v[72:73], 0, s[78:79]
	v_cvt_scalef32_pk_f32_fp4 v[136:137], v126, 1.0
	v_cvt_scalef32_pk_f32_fp4 v[138:139], v126, 1.0 op_sel:[1,0,0]
	v_cvt_scalef32_pk_f32_fp4 v[140:141], v126, 1.0 op_sel:[0,1,0]
	v_cvt_scalef32_pk_f32_fp4 v[142:143], v126, 1.0 op_sel:[1,1,0]
	v_pk_fma_f32 v[94:95], s[74:75], v[136:137], v[94:95] op_sel_hi:[0,1,1]
	v_pk_fma_f32 v[96:97], s[74:75], v[138:139], v[96:97] op_sel_hi:[0,1,1]
	v_pk_fma_f32 v[92:93], s[74:75], v[140:141], v[92:93] op_sel_hi:[0,1,1]
	v_pk_fma_f32 v[90:91], s[74:75], v[142:143], v[90:91] op_sel_hi:[0,1,1]
	v_cvt_scalef32_pk_f32_fp4 v[136:137], v127, 1.0
	v_cvt_scalef32_pk_f32_fp4 v[138:139], v127, 1.0 op_sel:[1,0,0]
	v_cvt_scalef32_pk_f32_fp4 v[140:141], v127, 1.0 op_sel:[0,1,0]
	v_cvt_scalef32_pk_f32_fp4 v[142:143], v127, 1.0 op_sel:[1,1,0]
	v_pk_fma_f32 v[88:89], s[74:75], v[136:137], v[88:89] op_sel_hi:[0,1,1]
	v_pk_fma_f32 v[86:87], s[74:75], v[138:139], v[86:87] op_sel_hi:[0,1,1]
	v_pk_fma_f32 v[84:85], s[74:75], v[140:141], v[84:85] op_sel_hi:[0,1,1]
	v_pk_fma_f32 v[82:83], s[74:75], v[142:143], v[82:83] op_sel_hi:[0,1,1]
	v_cvt_scalef32_pk_f32_fp4 v[136:137], v128, 1.0
	v_cvt_scalef32_pk_f32_fp4 v[138:139], v128, 1.0 op_sel:[1,0,0]
	v_cvt_scalef32_pk_f32_fp4 v[140:141], v128, 1.0 op_sel:[0,1,0]
	v_cvt_scalef32_pk_f32_fp4 v[142:143], v128, 1.0 op_sel:[1,1,0]
	v_pk_fma_f32 v[64:65], s[74:75], v[136:137], v[64:65] op_sel_hi:[0,1,1]
	v_pk_fma_f32 v[80:81], s[74:75], v[138:139], v[80:81] op_sel_hi:[0,1,1]
	v_pk_fma_f32 v[62:63], s[74:75], v[140:141], v[62:63] op_sel_hi:[0,1,1]
	v_pk_fma_f32 v[60:61], s[74:75], v[142:143], v[60:61] op_sel_hi:[0,1,1]
	s_waitcnt lgkmcnt(0)
	s_mov_b32 m0, s77
	s_nop 0
	global_load_lds_dwordx4 v[2:3], off
	global_load_lds_dwordx4 v[2:3], off offset:1024
	v_cvt_scalef32_pk_f32_fp4 v[136:137], v129, 1.0
	v_cvt_scalef32_pk_f32_fp4 v[138:139], v129, 1.0 op_sel:[1,0,0]
	v_cvt_scalef32_pk_f32_fp4 v[140:141], v129, 1.0 op_sel:[0,1,0]
	v_cvt_scalef32_pk_f32_fp4 v[142:143], v129, 1.0 op_sel:[1,1,0]
	v_pk_fma_f32 v[58:59], s[74:75], v[136:137], v[58:59] op_sel_hi:[0,1,1]
	v_pk_fma_f32 v[56:57], s[74:75], v[138:139], v[56:57] op_sel_hi:[0,1,1]
	v_pk_fma_f32 v[54:55], s[74:75], v[140:141], v[54:55] op_sel_hi:[0,1,1]
	v_pk_fma_f32 v[52:53], s[74:75], v[142:143], v[52:53] op_sel_hi:[0,1,1]
	v_cvt_scalef32_pk_f32_fp4 v[136:137], v130, 1.0
	v_cvt_scalef32_pk_f32_fp4 v[138:139], v130, 1.0 op_sel:[1,0,0]
	v_cvt_scalef32_pk_f32_fp4 v[140:141], v130, 1.0 op_sel:[0,1,0]
	v_cvt_scalef32_pk_f32_fp4 v[142:143], v130, 1.0 op_sel:[1,1,0]
	v_pk_fma_f32 v[50:51], s[74:75], v[136:137], v[50:51] op_sel_hi:[0,1,1]
	v_pk_fma_f32 v[48:49], s[74:75], v[138:139], v[48:49] op_sel_hi:[0,1,1]
	v_pk_fma_f32 v[46:47], s[74:75], v[140:141], v[46:47] op_sel_hi:[0,1,1]
	v_pk_fma_f32 v[44:45], s[74:75], v[142:143], v[44:45] op_sel_hi:[0,1,1]
	v_cvt_scalef32_pk_f32_fp4 v[136:137], v131, 1.0
	v_cvt_scalef32_pk_f32_fp4 v[138:139], v131, 1.0 op_sel:[1,0,0]
	v_cvt_scalef32_pk_f32_fp4 v[140:141], v131, 1.0 op_sel:[0,1,0]
	v_cvt_scalef32_pk_f32_fp4 v[142:143], v131, 1.0 op_sel:[1,1,0]
	v_pk_fma_f32 v[42:43], s[74:75], v[136:137], v[42:43] op_sel_hi:[0,1,1]
	v_pk_fma_f32 v[40:41], s[74:75], v[138:139], v[40:41] op_sel_hi:[0,1,1]
	v_pk_fma_f32 v[38:39], s[74:75], v[140:141], v[38:39] op_sel_hi:[0,1,1]
	v_pk_fma_f32 v[36:37], s[74:75], v[142:143], v[36:37] op_sel_hi:[0,1,1]
	v_cvt_scalef32_pk_f32_fp4 v[136:137], v132, 1.0
	v_cvt_scalef32_pk_f32_fp4 v[138:139], v132, 1.0 op_sel:[1,0,0]
	v_cvt_scalef32_pk_f32_fp4 v[140:141], v132, 1.0 op_sel:[0,1,0]
	v_cvt_scalef32_pk_f32_fp4 v[142:143], v132, 1.0 op_sel:[1,1,0]
	v_pk_fma_f32 v[32:33], s[74:75], v[136:137], v[32:33] op_sel_hi:[0,1,1]
	v_pk_fma_f32 v[34:35], s[74:75], v[138:139], v[34:35] op_sel_hi:[0,1,1]
	v_pk_fma_f32 v[30:31], s[74:75], v[140:141], v[30:31] op_sel_hi:[0,1,1]
	v_pk_fma_f32 v[28:29], s[74:75], v[142:143], v[28:29] op_sel_hi:[0,1,1]
	v_cvt_scalef32_pk_f32_fp4 v[136:137], v133, 1.0
	v_cvt_scalef32_pk_f32_fp4 v[138:139], v133, 1.0 op_sel:[1,0,0]
	v_cvt_scalef32_pk_f32_fp4 v[140:141], v133, 1.0 op_sel:[0,1,0]
	v_cvt_scalef32_pk_f32_fp4 v[142:143], v133, 1.0 op_sel:[1,1,0]
	v_pk_fma_f32 v[26:27], s[74:75], v[136:137], v[26:27] op_sel_hi:[0,1,1]
	v_pk_fma_f32 v[24:25], s[74:75], v[138:139], v[24:25] op_sel_hi:[0,1,1]
	v_pk_fma_f32 v[20:21], s[74:75], v[140:141], v[20:21] op_sel_hi:[0,1,1]
	v_pk_fma_f32 v[22:23], s[74:75], v[142:143], v[22:23] op_sel_hi:[0,1,1]
	s_branch .Lpv2_next
; DI void peer_token(LAS unsigned char* ring, const bf16* x1row, float inv2, const float* nffn, const int* ex, const float* pg, const unsigned char* U6, const unsigned char* V6,
;                    const float* usc, const float* vsc, float* orow, int lane) {
;     ...
;     for (int k = 0; k < 56; ++k) P11_V(k, cf_lo, vl, e_lo, k + 8);
; #pragma unroll 1
;     for (int k = 56; k < 64; ++k) P11_V(k, cf_lo, vl, e_hi, k - 56);
; #pragma unroll 1
;     for (int k = 64; k < 120; ++k) P11_V(k, cf_hi, vl, e_hi, k - 56);
; #pragma unroll 1
;     for (int k = 120; k < 128; ++k) P11_V(k, cf_hi, vl, e_lo, k - 120);
.Lpv2_oddB:
	s_add_i32 s47, s46, 2
	s_and_b32 s47, s47, 7
	s_lshl_b32 s47, s47, 11
	s_add_i32 s77, s33, s47
	v_add_u32_e32 v4, s77, v70
	s_add_i32 s78, s46, 10
	s_and_b32 s75, s78, 63
	v_readlane_b32 s79, v243, s75
	v_readlane_b32 s47, v242, s75
	s_bitcmp1_b32 s78, 6
	s_cselect_b32 s47, s79, s47
	s_lshr_b32 s47, s47, 8
	s_lshl_b32 s47, s47, 11
	s_bitcmp1_b32 s78, 8
	s_cselect_b32 s78, s98, 0
	s_cselect_b32 s79, s99, 0
	s_add_u32 s78, s78, s47
	s_addc_u32 s79, s79, 0
	s_add_i32 s32, s46, 1
	v_readlane_b32 s74, v248, s32
	s_waitcnt vmcnt(14)
	ds_read_b128 v[98:101], v4
	ds_read_b128 v[102:105], v4 offset:1024
	v_lshl_add_u64 v[2:3], v[72:73], 0, s[78:79]
	v_cvt_scalef32_pk_f32_fp4 v[136:137], v126, 1.0
	v_cvt_scalef32_pk_f32_fp4 v[138:139], v126, 1.0 op_sel:[1,0,0]
	v_cvt_scalef32_pk_f32_fp4 v[140:141], v126, 1.0 op_sel:[0,1,0]
	v_cvt_scalef32_pk_f32_fp4 v[142:143], v126, 1.0 op_sel:[1,1,0]
	v_pk_fma_f32 v[178:179], s[74:75], v[136:137], v[178:179] op_sel_hi:[0,1,1]
	v_pk_fma_f32 v[180:181], s[74:75], v[138:139], v[180:181] op_sel_hi:[0,1,1]
	v_pk_fma_f32 v[182:183], s[74:75], v[140:141], v[182:183] op_sel_hi:[0,1,1]
	v_pk_fma_f32 v[184:185], s[74:75], v[142:143], v[184:185] op_sel_hi:[0,1,1]
	v_cvt_scalef32_pk_f32_fp4 v[136:137], v127, 1.0
	v_cvt_scalef32_pk_f32_fp4 v[138:139], v127, 1.0 op_sel:[1,0,0]
	v_cvt_scalef32_pk_f32_fp4 v[140:141], v127, 1.0 op_sel:[0,1,0]
	v_cvt_scalef32_pk_f32_fp4 v[142:143], v127, 1.0 op_sel:[1,1,0]
	v_pk_fma_f32 v[186:187], s[74:75], v[136:137], v[186:187] op_sel_hi:[0,1,1]
	v_pk_fma_f32 v[188:189], s[74:75], v[138:139], v[188:189] op_sel_hi:[0,1,1]
	v_pk_fma_f32 v[190:191], s[74:75], v[140:141], v[190:191] op_sel_hi:[0,1,1]
	v_pk_fma_f32 v[192:193], s[74:75], v[142:143], v[192:193] op_sel_hi:[0,1,1]
	v_cvt_scalef32_pk_f32_fp4 v[136:137], v128, 1.0
	v_cvt_scalef32_pk_f32_fp4 v[138:139], v128, 1.0 op_sel:[1,0,0]
	v_cvt_scalef32_pk_f32_fp4 v[140:141], v128, 1.0 op_sel:[0,1,0]
	v_cvt_scalef32_pk_f32_fp4 v[142:143], v128, 1.0 op_sel:[1,1,0]
	v_pk_fma_f32 v[194:195], s[74:75], v[136:137], v[194:195] op_sel_hi:[0,1,1]
	v_pk_fma_f32 v[196:197], s[74:75], v[138:139], v[196:197] op_sel_hi:[0,1,1]
	v_pk_fma_f32 v[198:199], s[74:75], v[140:141], v[198:199] op_sel_hi:[0,1,1]
	v_pk_fma_f32 v[200:201], s[74:75], v[142:143], v[200:201] op_sel_hi:[0,1,1]
	s_waitcnt lgkmcnt(0)
	s_mov_b32 m0, s77
	s_nop 0
	global_load_lds_dwordx4 v[2:3], off
	global_load_lds_dwordx4 v[2:3], off offset:1024
	v_cvt_scalef32_pk_f32_fp4 v[136:137], v129, 1.0
	v_cvt_scalef32_pk_f32_fp4 v[138:139], v129, 1.0 op_sel:[1,0,0]
	v_cvt_scalef32_pk_f32_fp4 v[140:141], v129, 1.0 op_sel:[0,1,0]
	v_cvt_scalef32_pk_f32_fp4 v[142:143], v129, 1.0 op_sel:[1,1,0]
	v_pk_fma_f32 v[202:203], s[74:75], v[136:137], v[202:203] op_sel_hi:[0,1,1]
	v_pk_fma_f32 v[204:205], s[74:75], v[138:139], v[204:205] op_sel_hi:[0,1,1]
	v_pk_fma_f32 v[206:207], s[74:75], v[140:141], v[206:207] op_sel_hi:[0,1,1]
	v_pk_fma_f32 v[208:209], s[74:75], v[142:143], v[208:209] op_sel_hi:[0,1,1]
	v_cvt_scalef32_pk_f32_fp4 v[136:137], v130, 1.0
	v_cvt_scalef32_pk_f32_fp4 v[138:139], v130, 1.0 op_sel:[1,0,0]
	v_cvt_scalef32_pk_f32_fp4 v[140:141], v130, 1.0 op_sel:[0,1,0]
	v_cvt_scalef32_pk_f32_fp4 v[142:143], v130, 1.0 op_sel:[1,1,0]
	v_pk_fma_f32 v[210:211], s[74:75], v[136:137], v[210:211] op_sel_hi:[0,1,1]
	v_pk_fma_f32 v[212:213], s[74:75], v[138:139], v[212:213] op_sel_hi:[0,1,1]
	v_pk_fma_f32 v[214:215], s[74:75], v[140:141], v[214:215] op_sel_hi:[0,1,1]
	v_pk_fma_f32 v[216:217], s[74:75], v[142:143], v[216:217] op_sel_hi:[0,1,1]
	v_cvt_scalef32_pk_f32_fp4 v[136:137], v131, 1.0
	v_cvt_scalef32_pk_f32_fp4 v[138:139], v131, 1.0 op_sel:[1,0,0]
	v_cvt_scalef32_pk_f32_fp4 v[140:141], v131, 1.0 op_sel:[0,1,0]
	v_cvt_scalef32_pk_f32_fp4 v[142:143], v131, 1.0 op_sel:[1,1,0]
	v_pk_fma_f32 v[218:219], s[74:75], v[136:137], v[218:219] op_sel_hi:[0,1,1]
	v_pk_fma_f32 v[220:221], s[74:75], v[138:139], v[220:221] op_sel_hi:[0,1,1]
	v_pk_fma_f32 v[222:223], s[74:75], v[140:141], v[222:223] op_sel_hi:[0,1,1]
	v_pk_fma_f32 v[224:225], s[74:75], v[142:143], v[224:225] op_sel_hi:[0,1,1]
	v_cvt_scalef32_pk_f32_fp4 v[136:137], v132, 1.0
	v_cvt_scalef32_pk_f32_fp4 v[138:139], v132, 1.0 op_sel:[1,0,0]
	v_cvt_scalef32_pk_f32_fp4 v[140:141], v132, 1.0 op_sel:[0,1,0]
	v_cvt_scalef32_pk_f32_fp4 v[142:143], v132, 1.0 op_sel:[1,1,0]
	v_pk_fma_f32 v[226:227], s[74:75], v[136:137], v[226:227] op_sel_hi:[0,1,1]
	v_pk_fma_f32 v[228:229], s[74:75], v[138:139], v[228:229] op_sel_hi:[0,1,1]
	v_pk_fma_f32 v[230:231], s[74:75], v[140:141], v[230:231] op_sel_hi:[0,1,1]
	v_pk_fma_f32 v[232:233], s[74:75], v[142:143], v[232:233] op_sel_hi:[0,1,1]
	v_cvt_scalef32_pk_f32_fp4 v[136:137], v133, 1.0
	v_cvt_scalef32_pk_f32_fp4 v[138:139], v133, 1.0 op_sel:[1,0,0]
	v_cvt_scalef32_pk_f32_fp4 v[140:141], v133, 1.0 op_sel:[0,1,0]
	v_cvt_scalef32_pk_f32_fp4 v[142:143], v133, 1.0 op_sel:[1,1,0]
	v_pk_fma_f32 v[234:235], s[74:75], v[136:137], v[234:235] op_sel_hi:[0,1,1]
	v_pk_fma_f32 v[236:237], s[74:75], v[138:139], v[236:237] op_sel_hi:[0,1,1]
	v_pk_fma_f32 v[238:239], s[74:75], v[140:141], v[238:239] op_sel_hi:[0,1,1]
	v_pk_fma_f32 v[240:241], s[74:75], v[142:143], v[240:241] op_sel_hi:[0,1,1]
.Lpv2_next:
	s_add_i32 s46, s46, 2
	s_cmp_lg_u32 s46, 448
	s_cbranch_scc1 .Lpv2_even
; DI void peer_token(LAS unsigned char* ring, const bf16* x1row, float inv2, const float* nffn, const int* ex, const float* pg, const unsigned char* U6, const unsigned char* V6,
;                    const float* usc, const float* vsc, float* orow, int lane) {
;     ...
;     for (int k = 0; k < 56; ++k) P11_V(k, cf_lo, vl, e_lo, k + 8);
; #pragma unroll 1
;     for (int k = 56; k < 64; ++k) P11_V(k, cf_lo, vl, e_hi, k - 56);
; #pragma unroll 1
;     for (int k = 64; k < 120; ++k) P11_V(k, cf_hi, vl, e_hi, k - 56);
; #pragma unroll 1
;     for (int k = 120; k < 128; ++k) P11_V(k, cf_hi, vl, e_lo, k - 120);
.Lpv3_even:
	s_bitcmp1_b64 s[70:71], s46
	s_cbranch_scc1 .Lpv3_evenB
	s_add_i32 s47, s46, 1
	s_and_b32 s47, s47, 7
	s_lshl_b32 s47, s47, 11
	s_add_i32 s77, s33, s47
	v_add_u32_e32 v4, s77, v70
	s_add_i32 s78, s46, 9
	s_and_b32 s75, s78, 63
	v_readlane_b32 s79, v112, s75
	v_readlane_b32 s47, v243, s75
	s_bitcmp1_b32 s78, 6
	s_cselect_b32 s47, s47, s79
	s_lshr_b32 s47, s47, 8
	s_lshl_b32 s47, s47, 11
	s_bitcmp1_b32 s78, 8
	s_cselect_b32 s78, s98, 0
	s_cselect_b32 s79, s99, 0
	s_add_u32 s78, s78, s47
	s_addc_u32 s79, s79, 0
	s_add_i32 s32, s46, 0
	v_readlane_b32 s74, v123, s32
	s_waitcnt vmcnt(14)
	ds_read_b128 v[126:129], v4
	ds_read_b128 v[130:133], v4 offset:1024
	v_lshl_add_u64 v[2:3], v[72:73], 0, s[78:79]
	v_cvt_scalef32_pk_f32_fp4 v[136:137], v98, 1.0
	v_cvt_scalef32_pk_f32_fp4 v[138:139], v98, 1.0 op_sel:[1,0,0]
	v_cvt_scalef32_pk_f32_fp4 v[140:141], v98, 1.0 op_sel:[0,1,0]
	v_cvt_scalef32_pk_f32_fp4 v[142:143], v98, 1.0 op_sel:[1,1,0]
	v_pk_fma_f32 v[94:95], s[74:75], v[136:137], v[94:95] op_sel_hi:[0,1,1]
	v_pk_fma_f32 v[96:97], s[74:75], v[138:139], v[96:97] op_sel_hi:[0,1,1]
	v_pk_fma_f32 v[92:93], s[74:75], v[140:141], v[92:93] op_sel_hi:[0,1,1]
	v_pk_fma_f32 v[90:91], s[74:75], v[142:143], v[90:91] op_sel_hi:[0,1,1]
	v_cvt_scalef32_pk_f32_fp4 v[136:137], v99, 1.0
	v_cvt_scalef32_pk_f32_fp4 v[138:139], v99, 1.0 op_sel:[1,0,0]
	v_cvt_scalef32_pk_f32_fp4 v[140:141], v99, 1.0 op_sel:[0,1,0]
	v_cvt_scalef32_pk_f32_fp4 v[142:143], v99, 1.0 op_sel:[1,1,0]
	v_pk_fma_f32 v[88:89], s[74:75], v[136:137], v[88:89] op_sel_hi:[0,1,1]
	v_pk_fma_f32 v[86:87], s[74:75], v[138:139], v[86:87] op_sel_hi:[0,1,1]
	v_pk_fma_f32 v[84:85], s[74:75], v[140:141], v[84:85] op_sel_hi:[0,1,1]
	v_pk_fma_f32 v[82:83], s[74:75], v[142:143], v[82:83] op_sel_hi:[0,1,1]
	v_cvt_scalef32_pk_f32_fp4 v[136:137], v100, 1.0
	v_cvt_scalef32_pk_f32_fp4 v[138:139], v100, 1.0 op_sel:[1,0,0]
	v_cvt_scalef32_pk_f32_fp4 v[140:141], v100, 1.0 op_sel:[0,1,0]
	v_cvt_scalef32_pk_f32_fp4 v[142:143], v100, 1.0 op_sel:[1,1,0]
	v_pk_fma_f32 v[64:65], s[74:75], v[136:137], v[64:65] op_sel_hi:[0,1,1]
	v_pk_fma_f32 v[80:81], s[74:75], v[138:139], v[80:81] op_sel_hi:[0,1,1]
	v_pk_fma_f32 v[62:63], s[74:75], v[140:141], v[62:63] op_sel_hi:[0,1,1]
	v_pk_fma_f32 v[60:61], s[74:75], v[142:143], v[60:61] op_sel_hi:[0,1,1]
	s_waitcnt lgkmcnt(0)
	s_mov_b32 m0, s77
	s_nop 0
	global_load_lds_dwordx4 v[2:3], off
	global_load_lds_dwordx4 v[2:3], off offset:1024
	v_cvt_scalef32_pk_f32_fp4 v[136:137], v101, 1.0
	v_cvt_scalef32_pk_f32_fp4 v[138:139], v101, 1.0 op_sel:[1,0,0]
	v_cvt_scalef32_pk_f32_fp4 v[140:141], v101, 1.0 op_sel:[0,1,0]
	v_cvt_scalef32_pk_f32_fp4 v[142:143], v101, 1.0 op_sel:[1,1,0]
	v_pk_fma_f32 v[58:59], s[74:75], v[136:137], v[58:59] op_sel_hi:[0,1,1]
	v_pk_fma_f32 v[56:57], s[74:75], v[138:139], v[56:57] op_sel_hi:[0,1,1]
	v_pk_fma_f32 v[54:55], s[74:75], v[140:141], v[54:55] op_sel_hi:[0,1,1]
	v_pk_fma_f32 v[52:53], s[74:75], v[142:143], v[52:53] op_sel_hi:[0,1,1]
	v_cvt_scalef32_pk_f32_fp4 v[136:137], v102, 1.0
	v_cvt_scalef32_pk_f32_fp4 v[138:139], v102, 1.0 op_sel:[1,0,0]
	v_cvt_scalef32_pk_f32_fp4 v[140:141], v102, 1.0 op_sel:[0,1,0]
	v_cvt_scalef32_pk_f32_fp4 v[142:143], v102, 1.0 op_sel:[1,1,0]
	v_pk_fma_f32 v[50:51], s[74:75], v[136:137], v[50:51] op_sel_hi:[0,1,1]
	v_pk_fma_f32 v[48:49], s[74:75], v[138:139], v[48:49] op_sel_hi:[0,1,1]
	v_pk_fma_f32 v[46:47], s[74:75], v[140:141], v[46:47] op_sel_hi:[0,1,1]
	v_pk_fma_f32 v[44:45], s[74:75], v[142:143], v[44:45] op_sel_hi:[0,1,1]
	v_cvt_scalef32_pk_f32_fp4 v[136:137], v103, 1.0
	v_cvt_scalef32_pk_f32_fp4 v[138:139], v103, 1.0 op_sel:[1,0,0]
	v_cvt_scalef32_pk_f32_fp4 v[140:141], v103, 1.0 op_sel:[0,1,0]
	v_cvt_scalef32_pk_f32_fp4 v[142:143], v103, 1.0 op_sel:[1,1,0]
	v_pk_fma_f32 v[42:43], s[74:75], v[136:137], v[42:43] op_sel_hi:[0,1,1]
	v_pk_fma_f32 v[40:41], s[74:75], v[138:139], v[40:41] op_sel_hi:[0,1,1]
	v_pk_fma_f32 v[38:39], s[74:75], v[140:141], v[38:39] op_sel_hi:[0,1,1]
	v_pk_fma_f32 v[36:37], s[74:75], v[142:143], v[36:37] op_sel_hi:[0,1,1]
	v_cvt_scalef32_pk_f32_fp4 v[136:137], v104, 1.0
	v_cvt_scalef32_pk_f32_fp4 v[138:139], v104, 1.0 op_sel:[1,0,0]
	v_cvt_scalef32_pk_f32_fp4 v[140:141], v104, 1.0 op_sel:[0,1,0]
	v_cvt_scalef32_pk_f32_fp4 v[142:143], v104, 1.0 op_sel:[1,1,0]
	v_pk_fma_f32 v[32:33], s[74:75], v[136:137], v[32:33] op_sel_hi:[0,1,1]
	v_pk_fma_f32 v[34:35], s[74:75], v[138:139], v[34:35] op_sel_hi:[0,1,1]
	v_pk_fma_f32 v[30:31], s[74:75], v[140:141], v[30:31] op_sel_hi:[0,1,1]
	v_pk_fma_f32 v[28:29], s[74:75], v[142:143], v[28:29] op_sel_hi:[0,1,1]
	v_cvt_scalef32_pk_f32_fp4 v[136:137], v105, 1.0
	v_cvt_scalef32_pk_f32_fp4 v[138:139], v105, 1.0 op_sel:[1,0,0]
	v_cvt_scalef32_pk_f32_fp4 v[140:141], v105, 1.0 op_sel:[0,1,0]
	v_cvt_scalef32_pk_f32_fp4 v[142:143], v105, 1.0 op_sel:[1,1,0]
	v_pk_fma_f32 v[26:27], s[74:75], v[136:137], v[26:27] op_sel_hi:[0,1,1]
	v_pk_fma_f32 v[24:25], s[74:75], v[138:139], v[24:25] op_sel_hi:[0,1,1]
	v_pk_fma_f32 v[20:21], s[74:75], v[140:141], v[20:21] op_sel_hi:[0,1,1]
	v_pk_fma_f32 v[22:23], s[74:75], v[142:143], v[22:23] op_sel_hi:[0,1,1]
	s_branch .Lpv3_odd
; DI void peer_token(LAS unsigned char* ring, const bf16* x1row, float inv2, const float* nffn, const int* ex, const float* pg, const unsigned char* U6, const unsigned char* V6,
;                    const float* usc, const float* vsc, float* orow, int lane) {
;     ...
;     for (int k = 0; k < 56; ++k) P11_V(k, cf_lo, vl, e_lo, k + 8);
; #pragma unroll 1
;     for (int k = 56; k < 64; ++k) P11_V(k, cf_lo, vl, e_hi, k - 56);
; #pragma unroll 1
;     for (int k = 64; k < 120; ++k) P11_V(k, cf_hi, vl, e_hi, k - 56);
; #pragma unroll 1
;     for (int k = 120; k < 128; ++k) P11_V(k, cf_hi, vl, e_lo, k - 120);
.Lpv3_evenB:
	s_add_i32 s47, s46, 1
	s_and_b32 s47, s47, 7
	s_lshl_b32 s47, s47, 11
	s_add_i32 s77, s33, s47
	v_add_u32_e32 v4, s77, v70
	s_add_i32 s78, s46, 9
	s_and_b32 s75, s78, 63
	v_readlane_b32 s79, v112, s75
	v_readlane_b32 s47, v243, s75
	s_bitcmp1_b32 s78, 6
	s_cselect_b32 s47, s47, s79
	s_lshr_b32 s47, s47, 8
	s_lshl_b32 s47, s47, 11
	s_bitcmp1_b32 s78, 8
	s_cselect_b32 s78, s98, 0
	s_cselect_b32 s79, s99, 0
	s_add_u32 s78, s78, s47
	s_addc_u32 s79, s79, 0
	s_add_i32 s32, s46, 0
	v_readlane_b32 s74, v123, s32
	s_waitcnt vmcnt(14)
	ds_read_b128 v[126:129], v4
	ds_read_b128 v[130:133], v4 offset:1024
	v_lshl_add_u64 v[2:3], v[72:73], 0, s[78:79]
	v_cvt_scalef32_pk_f32_fp4 v[136:137], v98, 1.0
	v_cvt_scalef32_pk_f32_fp4 v[138:139], v98, 1.0 op_sel:[1,0,0]
	v_cvt_scalef32_pk_f32_fp4 v[140:141], v98, 1.0 op_sel:[0,1,0]
	v_cvt_scalef32_pk_f32_fp4 v[142:143], v98, 1.0 op_sel:[1,1,0]
	v_pk_fma_f32 v[178:179], s[74:75], v[136:137], v[178:179] op_sel_hi:[0,1,1]
	v_pk_fma_f32 v[180:181], s[74:75], v[138:139], v[180:181] op_sel_hi:[0,1,1]
	v_pk_fma_f32 v[182:183], s[74:75], v[140:141], v[182:183] op_sel_hi:[0,1,1]
	v_pk_fma_f32 v[184:185], s[74:75], v[142:143], v[184:185] op_sel_hi:[0,1,1]
	v_cvt_scalef32_pk_f32_fp4 v[136:137], v99, 1.0
	v_cvt_scalef32_pk_f32_fp4 v[138:139], v99, 1.0 op_sel:[1,0,0]
	v_cvt_scalef32_pk_f32_fp4 v[140:141], v99, 1.0 op_sel:[0,1,0]
	v_cvt_scalef32_pk_f32_fp4 v[142:143], v99, 1.0 op_sel:[1,1,0]
	v_pk_fma_f32 v[186:187], s[74:75], v[136:137], v[186:187] op_sel_hi:[0,1,1]
	v_pk_fma_f32 v[188:189], s[74:75], v[138:139], v[188:189] op_sel_hi:[0,1,1]
	v_pk_fma_f32 v[190:191], s[74:75], v[140:141], v[190:191] op_sel_hi:[0,1,1]
	v_pk_fma_f32 v[192:193], s[74:75], v[142:143], v[192:193] op_sel_hi:[0,1,1]
	v_cvt_scalef32_pk_f32_fp4 v[136:137], v100, 1.0
	v_cvt_scalef32_pk_f32_fp4 v[138:139], v100, 1.0 op_sel:[1,0,0]
	v_cvt_scalef32_pk_f32_fp4 v[140:141], v100, 1.0 op_sel:[0,1,0]
	v_cvt_scalef32_pk_f32_fp4 v[142:143], v100, 1.0 op_sel:[1,1,0]
	v_pk_fma_f32 v[194:195], s[74:75], v[136:137], v[194:195] op_sel_hi:[0,1,1]
	v_pk_fma_f32 v[196:197], s[74:75], v[138:139], v[196:197] op_sel_hi:[0,1,1]
	v_pk_fma_f32 v[198:199], s[74:75], v[140:141], v[198:199] op_sel_hi:[0,1,1]
	v_pk_fma_f32 v[200:201], s[74:75], v[142:143], v[200:201] op_sel_hi:[0,1,1]
	s_waitcnt lgkmcnt(0)
	s_mov_b32 m0, s77
	s_nop 0
	global_load_lds_dwordx4 v[2:3], off
	global_load_lds_dwordx4 v[2:3], off offset:1024
	v_cvt_scalef32_pk_f32_fp4 v[136:137], v101, 1.0
	v_cvt_scalef32_pk_f32_fp4 v[138:139], v101, 1.0 op_sel:[1,0,0]
	v_cvt_scalef32_pk_f32_fp4 v[140:141], v101, 1.0 op_sel:[0,1,0]
	v_cvt_scalef32_pk_f32_fp4 v[142:143], v101, 1.0 op_sel:[1,1,0]
	v_pk_fma_f32 v[202:203], s[74:75], v[136:137], v[202:203] op_sel_hi:[0,1,1]
	v_pk_fma_f32 v[204:205], s[74:75], v[138:139], v[204:205] op_sel_hi:[0,1,1]
	v_pk_fma_f32 v[206:207], s[74:75], v[140:141], v[206:207] op_sel_hi:[0,1,1]
	v_pk_fma_f32 v[208:209], s[74:75], v[142:143], v[208:209] op_sel_hi:[0,1,1]
	v_cvt_scalef32_pk_f32_fp4 v[136:137], v102, 1.0
	v_cvt_scalef32_pk_f32_fp4 v[138:139], v102, 1.0 op_sel:[1,0,0]
	v_cvt_scalef32_pk_f32_fp4 v[140:141], v102, 1.0 op_sel:[0,1,0]
	v_cvt_scalef32_pk_f32_fp4 v[142:143], v102, 1.0 op_sel:[1,1,0]
	v_pk_fma_f32 v[210:211], s[74:75], v[136:137], v[210:211] op_sel_hi:[0,1,1]
	v_pk_fma_f32 v[212:213], s[74:75], v[138:139], v[212:213] op_sel_hi:[0,1,1]
	v_pk_fma_f32 v[214:215], s[74:75], v[140:141], v[214:215] op_sel_hi:[0,1,1]
	v_pk_fma_f32 v[216:217], s[74:75], v[142:143], v[216:217] op_sel_hi:[0,1,1]
	v_cvt_scalef32_pk_f32_fp4 v[136:137], v103, 1.0
	v_cvt_scalef32_pk_f32_fp4 v[138:139], v103, 1.0 op_sel:[1,0,0]
	v_cvt_scalef32_pk_f32_fp4 v[140:141], v103, 1.0 op_sel:[0,1,0]
	v_cvt_scalef32_pk_f32_fp4 v[142:143], v103, 1.0 op_sel:[1,1,0]
	v_pk_fma_f32 v[218:219], s[74:75], v[136:137], v[218:219] op_sel_hi:[0,1,1]
	v_pk_fma_f32 v[220:221], s[74:75], v[138:139], v[220:221] op_sel_hi:[0,1,1]
	v_pk_fma_f32 v[222:223], s[74:75], v[140:141], v[222:223] op_sel_hi:[0,1,1]
	v_pk_fma_f32 v[224:225], s[74:75], v[142:143], v[224:225] op_sel_hi:[0,1,1]
	v_cvt_scalef32_pk_f32_fp4 v[136:137], v104, 1.0
	v_cvt_scalef32_pk_f32_fp4 v[138:139], v104, 1.0 op_sel:[1,0,0]
	v_cvt_scalef32_pk_f32_fp4 v[140:141], v104, 1.0 op_sel:[0,1,0]
	v_cvt_scalef32_pk_f32_fp4 v[142:143], v104, 1.0 op_sel:[1,1,0]
	v_pk_fma_f32 v[226:227], s[74:75], v[136:137], v[226:227] op_sel_hi:[0,1,1]
	v_pk_fma_f32 v[228:229], s[74:75], v[138:139], v[228:229] op_sel_hi:[0,1,1]
	v_pk_fma_f32 v[230:231], s[74:75], v[140:141], v[230:231] op_sel_hi:[0,1,1]
	v_pk_fma_f32 v[232:233], s[74:75], v[142:143], v[232:233] op_sel_hi:[0,1,1]
	v_cvt_scalef32_pk_f32_fp4 v[136:137], v105, 1.0
	v_cvt_scalef32_pk_f32_fp4 v[138:139], v105, 1.0 op_sel:[1,0,0]
	v_cvt_scalef32_pk_f32_fp4 v[140:141], v105, 1.0 op_sel:[0,1,0]
	v_cvt_scalef32_pk_f32_fp4 v[142:143], v105, 1.0 op_sel:[1,1,0]
	v_pk_fma_f32 v[234:235], s[74:75], v[136:137], v[234:235] op_sel_hi:[0,1,1]
	v_pk_fma_f32 v[236:237], s[74:75], v[138:139], v[236:237] op_sel_hi:[0,1,1]
	v_pk_fma_f32 v[238:239], s[74:75], v[140:141], v[238:239] op_sel_hi:[0,1,1]
	v_pk_fma_f32 v[240:241], s[74:75], v[142:143], v[240:241] op_sel_hi:[0,1,1]
; DI void peer_token(LAS unsigned char* ring, const bf16* x1row, float inv2, const float* nffn, const int* ex, const float* pg, const unsigned char* U6, const unsigned char* V6,
;                    const float* usc, const float* vsc, float* orow, int lane) {
;     ...
;     for (int k = 0; k < 56; ++k) P11_V(k, cf_lo, vl, e_lo, k + 8);
; #pragma unroll 1
;     for (int k = 56; k < 64; ++k) P11_V(k, cf_lo, vl, e_hi, k - 56);
; #pragma unroll 1
;     for (int k = 64; k < 120; ++k) P11_V(k, cf_hi, vl, e_hi, k - 56);
; #pragma unroll 1
;     for (int k = 120; k < 128; ++k) P11_V(k, cf_hi, vl, e_lo, k - 120);
.Lpv3_odd:
	s_add_i32 s32, s46, 1
	s_bitcmp1_b64 s[70:71], s32
	s_cbranch_scc1 .Lpv3_oddB
	s_add_i32 s47, s46, 2
	s_and_b32 s47, s47, 7
	s_lshl_b32 s47, s47, 11
	s_add_i32 s77, s33, s47
	v_add_u32_e32 v4, s77, v70
	s_add_i32 s78, s46, 10
	s_and_b32 s75, s78, 63
	v_readlane_b32 s79, v112, s75
	v_readlane_b32 s47, v243, s75
	s_bitcmp1_b32 s78, 6
	s_cselect_b32 s47, s47, s79
	s_lshr_b32 s47, s47, 8
	s_lshl_b32 s47, s47, 11
	s_bitcmp1_b32 s78, 8
	s_cselect_b32 s78, s98, 0
	s_cselect_b32 s79, s99, 0
	s_add_u32 s78, s78, s47
	s_addc_u32 s79, s79, 0
	s_add_i32 s32, s46, 1
	v_readlane_b32 s74, v123, s32
	s_waitcnt vmcnt(14)
	ds_read_b128 v[98:101], v4
	ds_read_b128 v[102:105], v4 offset:1024
	v_lshl_add_u64 v[2:3], v[72:73], 0, s[78:79]
	v_cvt_scalef32_pk_f32_fp4 v[136:137], v126, 1.0
	v_cvt_scalef32_pk_f32_fp4 v[138:139], v126, 1.0 op_sel:[1,0,0]
	v_cvt_scalef32_pk_f32_fp4 v[140:141], v126, 1.0 op_sel:[0,1,0]
	v_cvt_scalef32_pk_f32_fp4 v[142:143], v126, 1.0 op_sel:[1,1,0]
	v_pk_fma_f32 v[94:95], s[74:75], v[136:137], v[94:95] op_sel_hi:[0,1,1]
	v_pk_fma_f32 v[96:97], s[74:75], v[138:139], v[96:97] op_sel_hi:[0,1,1]
	v_pk_fma_f32 v[92:93], s[74:75], v[140:141], v[92:93] op_sel_hi:[0,1,1]
	v_pk_fma_f32 v[90:91], s[74:75], v[142:143], v[90:91] op_sel_hi:[0,1,1]
	v_cvt_scalef32_pk_f32_fp4 v[136:137], v127, 1.0
	v_cvt_scalef32_pk_f32_fp4 v[138:139], v127, 1.0 op_sel:[1,0,0]
	v_cvt_scalef32_pk_f32_fp4 v[140:141], v127, 1.0 op_sel:[0,1,0]
	v_cvt_scalef32_pk_f32_fp4 v[142:143], v127, 1.0 op_sel:[1,1,0]
	v_pk_fma_f32 v[88:89], s[74:75], v[136:137], v[88:89] op_sel_hi:[0,1,1]
	v_pk_fma_f32 v[86:87], s[74:75], v[138:139], v[86:87] op_sel_hi:[0,1,1]
	v_pk_fma_f32 v[84:85], s[74:75], v[140:141], v[84:85] op_sel_hi:[0,1,1]
	v_pk_fma_f32 v[82:83], s[74:75], v[142:143], v[82:83] op_sel_hi:[0,1,1]
	v_cvt_scalef32_pk_f32_fp4 v[136:137], v128, 1.0
	v_cvt_scalef32_pk_f32_fp4 v[138:139], v128, 1.0 op_sel:[1,0,0]
	v_cvt_scalef32_pk_f32_fp4 v[140:141], v128, 1.0 op_sel:[0,1,0]
	v_cvt_scalef32_pk_f32_fp4 v[142:143], v128, 1.0 op_sel:[1,1,0]
	v_pk_fma_f32 v[64:65], s[74:75], v[136:137], v[64:65] op_sel_hi:[0,1,1]
	v_pk_fma_f32 v[80:81], s[74:75], v[138:139], v[80:81] op_sel_hi:[0,1,1]
	v_pk_fma_f32 v[62:63], s[74:75], v[140:141], v[62:63] op_sel_hi:[0,1,1]
	v_pk_fma_f32 v[60:61], s[74:75], v[142:143], v[60:61] op_sel_hi:[0,1,1]
	s_waitcnt lgkmcnt(0)
	s_mov_b32 m0, s77
	s_nop 0
	global_load_lds_dwordx4 v[2:3], off
	global_load_lds_dwordx4 v[2:3], off offset:1024
	v_cvt_scalef32_pk_f32_fp4 v[136:137], v129, 1.0
	v_cvt_scalef32_pk_f32_fp4 v[138:139], v129, 1.0 op_sel:[1,0,0]
	v_cvt_scalef32_pk_f32_fp4 v[140:141], v129, 1.0 op_sel:[0,1,0]
	v_cvt_scalef32_pk_f32_fp4 v[142:143], v129, 1.0 op_sel:[1,1,0]
	v_pk_fma_f32 v[58:59], s[74:75], v[136:137], v[58:59] op_sel_hi:[0,1,1]
	v_pk_fma_f32 v[56:57], s[74:75], v[138:139], v[56:57] op_sel_hi:[0,1,1]
	v_pk_fma_f32 v[54:55], s[74:75], v[140:141], v[54:55] op_sel_hi:[0,1,1]
	v_pk_fma_f32 v[52:53], s[74:75], v[142:143], v[52:53] op_sel_hi:[0,1,1]
	v_cvt_scalef32_pk_f32_fp4 v[136:137], v130, 1.0
	v_cvt_scalef32_pk_f32_fp4 v[138:139], v130, 1.0 op_sel:[1,0,0]
	v_cvt_scalef32_pk_f32_fp4 v[140:141], v130, 1.0 op_sel:[0,1,0]
	v_cvt_scalef32_pk_f32_fp4 v[142:143], v130, 1.0 op_sel:[1,1,0]
	v_pk_fma_f32 v[50:51], s[74:75], v[136:137], v[50:51] op_sel_hi:[0,1,1]
	v_pk_fma_f32 v[48:49], s[74:75], v[138:139], v[48:49] op_sel_hi:[0,1,1]
	v_pk_fma_f32 v[46:47], s[74:75], v[140:141], v[46:47] op_sel_hi:[0,1,1]
	v_pk_fma_f32 v[44:45], s[74:75], v[142:143], v[44:45] op_sel_hi:[0,1,1]
	v_cvt_scalef32_pk_f32_fp4 v[136:137], v131, 1.0
	v_cvt_scalef32_pk_f32_fp4 v[138:139], v131, 1.0 op_sel:[1,0,0]
	v_cvt_scalef32_pk_f32_fp4 v[140:141], v131, 1.0 op_sel:[0,1,0]
	v_cvt_scalef32_pk_f32_fp4 v[142:143], v131, 1.0 op_sel:[1,1,0]
	v_pk_fma_f32 v[42:43], s[74:75], v[136:137], v[42:43] op_sel_hi:[0,1,1]
	v_pk_fma_f32 v[40:41], s[74:75], v[138:139], v[40:41] op_sel_hi:[0,1,1]
	v_pk_fma_f32 v[38:39], s[74:75], v[140:141], v[38:39] op_sel_hi:[0,1,1]
	v_pk_fma_f32 v[36:37], s[74:75], v[142:143], v[36:37] op_sel_hi:[0,1,1]
	v_cvt_scalef32_pk_f32_fp4 v[136:137], v132, 1.0
	v_cvt_scalef32_pk_f32_fp4 v[138:139], v132, 1.0 op_sel:[1,0,0]
	v_cvt_scalef32_pk_f32_fp4 v[140:141], v132, 1.0 op_sel:[0,1,0]
	v_cvt_scalef32_pk_f32_fp4 v[142:143], v132, 1.0 op_sel:[1,1,0]
	v_pk_fma_f32 v[32:33], s[74:75], v[136:137], v[32:33] op_sel_hi:[0,1,1]
	v_pk_fma_f32 v[34:35], s[74:75], v[138:139], v[34:35] op_sel_hi:[0,1,1]
	v_pk_fma_f32 v[30:31], s[74:75], v[140:141], v[30:31] op_sel_hi:[0,1,1]
	v_pk_fma_f32 v[28:29], s[74:75], v[142:143], v[28:29] op_sel_hi:[0,1,1]
	v_cvt_scalef32_pk_f32_fp4 v[136:137], v133, 1.0
	v_cvt_scalef32_pk_f32_fp4 v[138:139], v133, 1.0 op_sel:[1,0,0]
	v_cvt_scalef32_pk_f32_fp4 v[140:141], v133, 1.0 op_sel:[0,1,0]
	v_cvt_scalef32_pk_f32_fp4 v[142:143], v133, 1.0 op_sel:[1,1,0]
	v_pk_fma_f32 v[26:27], s[74:75], v[136:137], v[26:27] op_sel_hi:[0,1,1]
	v_pk_fma_f32 v[24:25], s[74:75], v[138:139], v[24:25] op_sel_hi:[0,1,1]
	v_pk_fma_f32 v[20:21], s[74:75], v[140:141], v[20:21] op_sel_hi:[0,1,1]
	v_pk_fma_f32 v[22:23], s[74:75], v[142:143], v[22:23] op_sel_hi:[0,1,1]
	s_branch .Lpv3_next
; DI void peer_token(LAS unsigned char* ring, const bf16* x1row, float inv2, const float* nffn, const int* ex, const float* pg, const unsigned char* U6, const unsigned char* V6,
;                    const float* usc, const float* vsc, float* orow, int lane) {
;     ...
;     for (int k = 0; k < 56; ++k) P11_V(k, cf_lo, vl, e_lo, k + 8);
; #pragma unroll 1
;     for (int k = 56; k < 64; ++k) P11_V(k, cf_lo, vl, e_hi, k - 56);
; #pragma unroll 1
;     for (int k = 64; k < 120; ++k) P11_V(k, cf_hi, vl, e_hi, k - 56);
; #pragma unroll 1
;     for (int k = 120; k < 128; ++k) P11_V(k, cf_hi, vl, e_lo, k - 120);
.Lpv3_oddB:
	s_add_i32 s47, s46, 2
	s_and_b32 s47, s47, 7
	s_lshl_b32 s47, s47, 11
	s_add_i32 s77, s33, s47
	v_add_u32_e32 v4, s77, v70
	s_add_i32 s78, s46, 10
	s_and_b32 s75, s78, 63
	v_readlane_b32 s79, v112, s75
	v_readlane_b32 s47, v243, s75
	s_bitcmp1_b32 s78, 6
	s_cselect_b32 s47, s47, s79
	s_lshr_b32 s47, s47, 8
	s_lshl_b32 s47, s47, 11
	s_bitcmp1_b32 s78, 8
	s_cselect_b32 s78, s98, 0
	s_cselect_b32 s79, s99, 0
	s_add_u32 s78, s78, s47
	s_addc_u32 s79, s79, 0
	s_add_i32 s32, s46, 1
	v_readlane_b32 s74, v123, s32
	s_waitcnt vmcnt(14)
	ds_read_b128 v[98:101], v4
	ds_read_b128 v[102:105], v4 offset:1024
	v_lshl_add_u64 v[2:3], v[72:73], 0, s[78:79]
	v_cvt_scalef32_pk_f32_fp4 v[136:137], v126, 1.0
	v_cvt_scalef32_pk_f32_fp4 v[138:139], v126, 1.0 op_sel:[1,0,0]
	v_cvt_scalef32_pk_f32_fp4 v[140:141], v126, 1.0 op_sel:[0,1,0]
	v_cvt_scalef32_pk_f32_fp4 v[142:143], v126, 1.0 op_sel:[1,1,0]
	v_pk_fma_f32 v[178:179], s[74:75], v[136:137], v[178:179] op_sel_hi:[0,1,1]
	v_pk_fma_f32 v[180:181], s[74:75], v[138:139], v[180:181] op_sel_hi:[0,1,1]
	v_pk_fma_f32 v[182:183], s[74:75], v[140:141], v[182:183] op_sel_hi:[0,1,1]
	v_pk_fma_f32 v[184:185], s[74:75], v[142:143], v[184:185] op_sel_hi:[0,1,1]
	v_cvt_scalef32_pk_f32_fp4 v[136:137], v127, 1.0
	v_cvt_scalef32_pk_f32_fp4 v[138:139], v127, 1.0 op_sel:[1,0,0]
	v_cvt_scalef32_pk_f32_fp4 v[140:141], v127, 1.0 op_sel:[0,1,0]
	v_cvt_scalef32_pk_f32_fp4 v[142:143], v127, 1.0 op_sel:[1,1,0]
	v_pk_fma_f32 v[186:187], s[74:75], v[136:137], v[186:187] op_sel_hi:[0,1,1]
	v_pk_fma_f32 v[188:189], s[74:75], v[138:139], v[188:189] op_sel_hi:[0,1,1]
	v_pk_fma_f32 v[190:191], s[74:75], v[140:141], v[190:191] op_sel_hi:[0,1,1]
	v_pk_fma_f32 v[192:193], s[74:75], v[142:143], v[192:193] op_sel_hi:[0,1,1]
	v_cvt_scalef32_pk_f32_fp4 v[136:137], v128, 1.0
	v_cvt_scalef32_pk_f32_fp4 v[138:139], v128, 1.0 op_sel:[1,0,0]
	v_cvt_scalef32_pk_f32_fp4 v[140:141], v128, 1.0 op_sel:[0,1,0]
	v_cvt_scalef32_pk_f32_fp4 v[142:143], v128, 1.0 op_sel:[1,1,0]
	v_pk_fma_f32 v[194:195], s[74:75], v[136:137], v[194:195] op_sel_hi:[0,1,1]
	v_pk_fma_f32 v[196:197], s[74:75], v[138:139], v[196:197] op_sel_hi:[0,1,1]
	v_pk_fma_f32 v[198:199], s[74:75], v[140:141], v[198:199] op_sel_hi:[0,1,1]
	v_pk_fma_f32 v[200:201], s[74:75], v[142:143], v[200:201] op_sel_hi:[0,1,1]
	s_waitcnt lgkmcnt(0)
	s_mov_b32 m0, s77
	s_nop 0
	global_load_lds_dwordx4 v[2:3], off
	global_load_lds_dwordx4 v[2:3], off offset:1024
	v_cvt_scalef32_pk_f32_fp4 v[136:137], v129, 1.0
	v_cvt_scalef32_pk_f32_fp4 v[138:139], v129, 1.0 op_sel:[1,0,0]
	v_cvt_scalef32_pk_f32_fp4 v[140:141], v129, 1.0 op_sel:[0,1,0]
	v_cvt_scalef32_pk_f32_fp4 v[142:143], v129, 1.0 op_sel:[1,1,0]
	v_pk_fma_f32 v[202:203], s[74:75], v[136:137], v[202:203] op_sel_hi:[0,1,1]
	v_pk_fma_f32 v[204:205], s[74:75], v[138:139], v[204:205] op_sel_hi:[0,1,1]
	v_pk_fma_f32 v[206:207], s[74:75], v[140:141], v[206:207] op_sel_hi:[0,1,1]
	v_pk_fma_f32 v[208:209], s[74:75], v[142:143], v[208:209] op_sel_hi:[0,1,1]
	v_cvt_scalef32_pk_f32_fp4 v[136:137], v130, 1.0
	v_cvt_scalef32_pk_f32_fp4 v[138:139], v130, 1.0 op_sel:[1,0,0]
	v_cvt_scalef32_pk_f32_fp4 v[140:141], v130, 1.0 op_sel:[0,1,0]
	v_cvt_scalef32_pk_f32_fp4 v[142:143], v130, 1.0 op_sel:[1,1,0]
	v_pk_fma_f32 v[210:211], s[74:75], v[136:137], v[210:211] op_sel_hi:[0,1,1]
	v_pk_fma_f32 v[212:213], s[74:75], v[138:139], v[212:213] op_sel_hi:[0,1,1]
	v_pk_fma_f32 v[214:215], s[74:75], v[140:141], v[214:215] op_sel_hi:[0,1,1]
	v_pk_fma_f32 v[216:217], s[74:75], v[142:143], v[216:217] op_sel_hi:[0,1,1]
	v_cvt_scalef32_pk_f32_fp4 v[136:137], v131, 1.0
	v_cvt_scalef32_pk_f32_fp4 v[138:139], v131, 1.0 op_sel:[1,0,0]
	v_cvt_scalef32_pk_f32_fp4 v[140:141], v131, 1.0 op_sel:[0,1,0]
	v_cvt_scalef32_pk_f32_fp4 v[142:143], v131, 1.0 op_sel:[1,1,0]
	v_pk_fma_f32 v[218:219], s[74:75], v[136:137], v[218:219] op_sel_hi:[0,1,1]
	v_pk_fma_f32 v[220:221], s[74:75], v[138:139], v[220:221] op_sel_hi:[0,1,1]
	v_pk_fma_f32 v[222:223], s[74:75], v[140:141], v[222:223] op_sel_hi:[0,1,1]
	v_pk_fma_f32 v[224:225], s[74:75], v[142:143], v[224:225] op_sel_hi:[0,1,1]
	v_cvt_scalef32_pk_f32_fp4 v[136:137], v132, 1.0
	v_cvt_scalef32_pk_f32_fp4 v[138:139], v132, 1.0 op_sel:[1,0,0]
	v_cvt_scalef32_pk_f32_fp4 v[140:141], v132, 1.0 op_sel:[0,1,0]
	v_cvt_scalef32_pk_f32_fp4 v[142:143], v132, 1.0 op_sel:[1,1,0]
	v_pk_fma_f32 v[226:227], s[74:75], v[136:137], v[226:227] op_sel_hi:[0,1,1]
	v_pk_fma_f32 v[228:229], s[74:75], v[138:139], v[228:229] op_sel_hi:[0,1,1]
	v_pk_fma_f32 v[230:231], s[74:75], v[140:141], v[230:231] op_sel_hi:[0,1,1]
	v_pk_fma_f32 v[232:233], s[74:75], v[142:143], v[232:233] op_sel_hi:[0,1,1]
	v_cvt_scalef32_pk_f32_fp4 v[136:137], v133, 1.0
	v_cvt_scalef32_pk_f32_fp4 v[138:139], v133, 1.0 op_sel:[1,0,0]
	v_cvt_scalef32_pk_f32_fp4 v[140:141], v133, 1.0 op_sel:[0,1,0]
	v_cvt_scalef32_pk_f32_fp4 v[142:143], v133, 1.0 op_sel:[1,1,0]
	v_pk_fma_f32 v[234:235], s[74:75], v[136:137], v[234:235] op_sel_hi:[0,1,1]
	v_pk_fma_f32 v[236:237], s[74:75], v[138:139], v[236:237] op_sel_hi:[0,1,1]
	v_pk_fma_f32 v[238:239], s[74:75], v[140:141], v[238:239] op_sel_hi:[0,1,1]
	v_pk_fma_f32 v[240:241], s[74:75], v[142:143], v[240:241] op_sel_hi:[0,1,1]
; DI void peer_token(LAS unsigned char* ring, const bf16* x1row, float inv2, const float* nffn, const int* ex, const float* pg, const unsigned char* U6, const unsigned char* V6,
;                    const float* usc, const float* vsc, float* orow, int lane) {
;     ...
;     const float ysc = 1.0f;
;     asm volatile("s_waitcnt vmcnt(0)" ::: "memory");
; #pragma unroll
;     for (int i = 0; i < 16; ++i) {
;         const v2u aw = *(const v2u*)(x1row + i * 256 + lane * 4);
;         *(f32x4*)(orow + i * 256 + lane * 4) = (f32x4){bflo(aw.x) + ysc * y[2 * i].x, bfhi(aw.x) + ysc * y[2 * i].y, bflo(aw.y) + ysc * y[2 * i + 1].x, bfhi(aw.y) + ysc * y[2 * i + 1].y};
;     }
; __global__ void __launch_bounds__(NTHREADS, 2) fwd(Args args) {
;     ...
;             for (int j = 0; j < 4; ++j) { const int t = tb * 32 + wave * 4 + j;
;                 peer_token(lds + wave * (4 * RSLOT), XB + (size_t)t * DM, inv2[t], norm_ffn, experts + (size_t)t * 128, pgates + (size_t)t * 128, U8, V8, usc, vsc, out + (size_t)t * DM, lane); }
.Lpv3_next:
	s_add_i32 s46, s46, 2
	s_cmp_lg_u32 s46, 512
	s_cbranch_scc1 .Lpv3_even
	s_waitcnt vmcnt(0)
	s_lshl_b32 s46, s76, 1
	s_add_i32 s46, s46, s97
	s_ashr_i32 s47, s46, 31
	s_lshl_b64 s[46:47], s[46:47], 13
	v_lshl_add_u64 v[2:3], v[68:69], 0, s[46:47]
	s_mov_b64 s[46:47], 0x1000
	v_lshl_add_u64 v[4:5], v[2:3], 0, s[46:47]
	s_mov_b64 s[46:47], 0x2000
	v_lshl_add_u64 v[6:7], v[2:3], 0, s[46:47]
	s_mov_b64 s[46:47], 0x3000
	v_lshl_add_u64 v[16:17], v[2:3], 0, s[46:47]
	global_load_dwordx2 v[146:147], v[2:3], off
	global_load_dwordx2 v[148:149], v[2:3], off offset:512
	global_load_dwordx2 v[150:151], v[2:3], off offset:1024
	global_load_dwordx2 v[152:153], v[2:3], off offset:1536
	global_load_dwordx2 v[154:155], v[2:3], off offset:2048
	global_load_dwordx2 v[156:157], v[2:3], off offset:2560
	global_load_dwordx2 v[158:159], v[2:3], off offset:3072
	global_load_dwordx2 v[160:161], v[2:3], off offset:3584
	global_load_dwordx2 v[162:163], v[4:5], off
	global_load_dwordx2 v[164:165], v[4:5], off offset:512
	global_load_dwordx2 v[166:167], v[4:5], off offset:1024
	global_load_dwordx2 v[168:169], v[4:5], off offset:1536
	global_load_dwordx2 v[170:171], v[4:5], off offset:2048
	global_load_dwordx2 v[172:173], v[4:5], off offset:2560
	global_load_dwordx2 v[174:175], v[4:5], off offset:3072
	global_load_dwordx2 v[176:177], v[4:5], off offset:3584
	global_load_dwordx2 v[98:99], v[6:7], off
	global_load_dwordx2 v[100:101], v[6:7], off offset:512
	global_load_dwordx2 v[102:103], v[6:7], off offset:1024
	global_load_dwordx2 v[104:105], v[6:7], off offset:1536
	global_load_dwordx2 v[126:127], v[6:7], off offset:2048
	global_load_dwordx2 v[128:129], v[6:7], off offset:2560
	global_load_dwordx2 v[130:131], v[6:7], off offset:3072
	global_load_dwordx2 v[132:133], v[6:7], off offset:3584
	global_load_dwordx2 v[136:137], v[16:17], off
	global_load_dwordx2 v[138:139], v[16:17], off offset:512
	global_load_dwordx2 v[140:141], v[16:17], off offset:1024
	global_load_dwordx2 v[142:143], v[16:17], off offset:1536
	global_load_dwordx2 v[8:9], v[16:17], off offset:2048
	global_load_dwordx2 v[10:11], v[16:17], off offset:2560
	global_load_dwordx2 v[12:13], v[16:17], off offset:3072
	global_load_dwordx2 v[14:15], v[16:17], off offset:3584
	v_lshl_add_u64 v[18:19], s[44:45], 2, v[76:77]
	s_mov_b64 s[46:47], 0x2000
	v_lshl_add_u64 v[6:7], v[18:19], 0, s[46:47]
	s_mov_b64 s[46:47], 0x3000
	v_lshl_add_u64 v[16:17], v[18:19], 0, s[46:47]
	s_mov_b64 s[46:47], 0x4000
	v_lshl_add_u64 v[112:113], v[18:19], 0, s[46:47]
	s_mov_b64 s[46:47], 0x6000
	v_lshl_add_u64 v[242:243], v[18:19], 0, s[46:47]
	s_mov_b64 s[46:47], 0x7000
	v_lshl_add_u64 v[124:125], v[18:19], 0, s[46:47]
	s_waitcnt vmcnt(0)
	v_lshlrev_b32_e32 v2, 16, v146
	v_and_b32_e32 v3, 0xffff0000, v146
	v_lshlrev_b32_e32 v4, 16, v147
	v_and_b32_e32 v5, 0xffff0000, v147
	v_pk_add_f32 v[2:3], v[94:95], v[2:3]
	v_pk_add_f32 v[4:5], v[96:97], v[4:5]
	global_store_dwordx4 v[18:19], v[2:5], off
	v_lshlrev_b32_e32 v244, 16, v148
	v_and_b32_e32 v245, 0xffff0000, v148
	v_lshlrev_b32_e32 v246, 16, v149
	v_and_b32_e32 v247, 0xffff0000, v149
	v_pk_add_f32 v[244:245], v[92:93], v[244:245]
	v_pk_add_f32 v[246:247], v[90:91], v[246:247]
	global_store_dwordx4 v[18:19], v[244:247], off offset:1024
	v_lshlrev_b32_e32 v120, 16, v150
	v_and_b32_e32 v121, 0xffff0000, v150
	v_lshlrev_b32_e32 v122, 16, v151
	v_and_b32_e32 v123, 0xffff0000, v151
	v_pk_add_f32 v[120:121], v[88:89], v[120:121]
	v_pk_add_f32 v[122:123], v[86:87], v[122:123]
	global_store_dwordx4 v[18:19], v[120:123], off offset:2048
	v_lshlrev_b32_e32 v2, 16, v152
	v_and_b32_e32 v3, 0xffff0000, v152
	v_lshlrev_b32_e32 v4, 16, v153
	v_and_b32_e32 v5, 0xffff0000, v153
	v_pk_add_f32 v[2:3], v[84:85], v[2:3]
	v_pk_add_f32 v[4:5], v[82:83], v[4:5]
	global_store_dwordx4 v[18:19], v[2:5], off offset:3072
	v_lshlrev_b32_e32 v244, 16, v154
	v_and_b32_e32 v245, 0xffff0000, v154
	v_lshlrev_b32_e32 v246, 16, v155
	v_and_b32_e32 v247, 0xffff0000, v155
	v_pk_add_f32 v[244:245], v[64:65], v[244:245]
	v_pk_add_f32 v[246:247], v[80:81], v[246:247]
	global_store_dwordx4 v[6:7], v[244:247], off offset:-4096
	v_lshlrev_b32_e32 v120, 16, v156
	v_and_b32_e32 v121, 0xffff0000, v156
	v_lshlrev_b32_e32 v122, 16, v157
	v_and_b32_e32 v123, 0xffff0000, v157
	v_pk_add_f32 v[120:121], v[62:63], v[120:121]
	v_pk_add_f32 v[122:123], v[60:61], v[122:123]
	global_store_dwordx4 v[6:7], v[120:123], off offset:-3072
	v_lshlrev_b32_e32 v2, 16, v158
	v_and_b32_e32 v3, 0xffff0000, v158
	v_lshlrev_b32_e32 v4, 16, v159
	v_and_b32_e32 v5, 0xffff0000, v159
	v_pk_add_f32 v[2:3], v[58:59], v[2:3]
	v_pk_add_f32 v[4:5], v[56:57], v[4:5]
	global_store_dwordx4 v[6:7], v[2:5], off offset:-2048
	v_lshlrev_b32_e32 v244, 16, v160
	v_and_b32_e32 v245, 0xffff0000, v160
	v_lshlrev_b32_e32 v246, 16, v161
	v_and_b32_e32 v247, 0xffff0000, v161
	v_pk_add_f32 v[244:245], v[54:55], v[244:245]
	v_pk_add_f32 v[246:247], v[52:53], v[246:247]
	global_store_dwordx4 v[6:7], v[244:247], off offset:-1024
	v_lshlrev_b32_e32 v120, 16, v162
	v_and_b32_e32 v121, 0xffff0000, v162
	v_lshlrev_b32_e32 v122, 16, v163
	v_and_b32_e32 v123, 0xffff0000, v163
	v_pk_add_f32 v[120:121], v[50:51], v[120:121]
	v_pk_add_f32 v[122:123], v[48:49], v[122:123]
	global_store_dwordx4 v[6:7], v[120:123], off
	v_lshlrev_b32_e32 v2, 16, v164
	v_and_b32_e32 v3, 0xffff0000, v164
	v_lshlrev_b32_e32 v4, 16, v165
	v_and_b32_e32 v5, 0xffff0000, v165
	v_pk_add_f32 v[2:3], v[46:47], v[2:3]
	v_pk_add_f32 v[4:5], v[44:45], v[4:5]
	global_store_dwordx4 v[6:7], v[2:5], off offset:1024
	v_lshlrev_b32_e32 v244, 16, v166
	v_and_b32_e32 v245, 0xffff0000, v166
	v_lshlrev_b32_e32 v246, 16, v167
; DI void peer_token(LAS unsigned char* ring, const bf16* x1row, float inv2, const float* nffn, const int* ex, const float* pg, const unsigned char* U6, const unsigned char* V6,
;                    const float* usc, const float* vsc, float* orow, int lane) {
;     ...
;     asm volatile("s_waitcnt vmcnt(0)" ::: "memory");
; #pragma unroll
;     for (int i = 0; i < 16; ++i) {
;         const v2u aw = *(const v2u*)(x1row + i * 256 + lane * 4);
;         *(f32x4*)(orow + i * 256 + lane * 4) = (f32x4){bflo(aw.x) + ysc * y[2 * i].x, bfhi(aw.x) + ysc * y[2 * i].y, bflo(aw.y) + ysc * y[2 * i + 1].x, bfhi(aw.y) + ysc * y[2 * i + 1].y};
;     }
; __global__ void __launch_bounds__(NTHREADS, 2) fwd(Args args) {
;     ...
;         for (int tb = bid; tb < SEQ / 32; tb += G) {
;             routing_block(lds, QB, skb, experts, pgates, tb);
;             asm volatile("s_waitcnt vmcnt(0)" ::: "memory");
;             __syncthreads();
; #pragma unroll 1
;             for (int j = 0; j < 4; ++j) { const int t = tb * 32 + wave * 4 + j;
;                 peer_token(lds + wave * (4 * RSLOT), XB + (size_t)t * DM, inv2[t], norm_ffn, experts + (size_t)t * 128, pgates + (size_t)t * 128, U8, V8, usc, vsc, out + (size_t)t * DM, lane); }
;             __syncthreads();
;         }
	v_and_b32_e32 v247, 0xffff0000, v167
	v_pk_add_f32 v[244:245], v[42:43], v[244:245]
	v_pk_add_f32 v[246:247], v[40:41], v[246:247]
	global_store_dwordx4 v[6:7], v[244:247], off offset:2048
	v_lshlrev_b32_e32 v120, 16, v168
	v_and_b32_e32 v121, 0xffff0000, v168
	v_lshlrev_b32_e32 v122, 16, v169
	v_and_b32_e32 v123, 0xffff0000, v169
	v_pk_add_f32 v[120:121], v[38:39], v[120:121]
	v_pk_add_f32 v[122:123], v[36:37], v[122:123]
	global_store_dwordx4 v[6:7], v[120:123], off offset:3072
	v_lshlrev_b32_e32 v2, 16, v170
	v_and_b32_e32 v3, 0xffff0000, v170
	v_lshlrev_b32_e32 v4, 16, v171
	v_and_b32_e32 v5, 0xffff0000, v171
	v_pk_add_f32 v[2:3], v[32:33], v[2:3]
	v_pk_add_f32 v[4:5], v[34:35], v[4:5]
	global_store_dwordx4 v[16:17], v[2:5], off
	v_lshlrev_b32_e32 v244, 16, v172
	v_and_b32_e32 v245, 0xffff0000, v172
	v_lshlrev_b32_e32 v246, 16, v173
	v_and_b32_e32 v247, 0xffff0000, v173
	v_pk_add_f32 v[244:245], v[30:31], v[244:245]
	v_pk_add_f32 v[246:247], v[28:29], v[246:247]
	global_store_dwordx4 v[16:17], v[244:247], off offset:1024
	v_lshlrev_b32_e32 v120, 16, v174
	v_and_b32_e32 v121, 0xffff0000, v174
	v_lshlrev_b32_e32 v122, 16, v175
	v_and_b32_e32 v123, 0xffff0000, v175
	v_pk_add_f32 v[120:121], v[26:27], v[120:121]
	v_pk_add_f32 v[122:123], v[24:25], v[122:123]
	global_store_dwordx4 v[16:17], v[120:123], off offset:2048
	v_lshlrev_b32_e32 v2, 16, v176
	v_and_b32_e32 v3, 0xffff0000, v176
	v_lshlrev_b32_e32 v4, 16, v177
	v_and_b32_e32 v5, 0xffff0000, v177
	v_pk_add_f32 v[2:3], v[20:21], v[2:3]
	v_pk_add_f32 v[4:5], v[22:23], v[4:5]
	global_store_dwordx4 v[16:17], v[2:5], off offset:3072
	v_lshlrev_b32_e32 v244, 16, v98
	v_and_b32_e32 v245, 0xffff0000, v98
	v_lshlrev_b32_e32 v246, 16, v99
	v_and_b32_e32 v247, 0xffff0000, v99
	v_pk_add_f32 v[244:245], v[178:179], v[244:245]
	v_pk_add_f32 v[246:247], v[180:181], v[246:247]
	global_store_dwordx4 v[112:113], v[244:247], off
	v_lshlrev_b32_e32 v120, 16, v100
	v_and_b32_e32 v121, 0xffff0000, v100
	v_lshlrev_b32_e32 v122, 16, v101
	v_and_b32_e32 v123, 0xffff0000, v101
	v_pk_add_f32 v[120:121], v[182:183], v[120:121]
	v_pk_add_f32 v[122:123], v[184:185], v[122:123]
	global_store_dwordx4 v[112:113], v[120:123], off offset:1024
	v_lshlrev_b32_e32 v2, 16, v102
	v_and_b32_e32 v3, 0xffff0000, v102
	v_lshlrev_b32_e32 v4, 16, v103
	v_and_b32_e32 v5, 0xffff0000, v103
	v_pk_add_f32 v[2:3], v[186:187], v[2:3]
	v_pk_add_f32 v[4:5], v[188:189], v[4:5]
	global_store_dwordx4 v[112:113], v[2:5], off offset:2048
	v_lshlrev_b32_e32 v244, 16, v104
	v_and_b32_e32 v245, 0xffff0000, v104
	v_lshlrev_b32_e32 v246, 16, v105
	v_and_b32_e32 v247, 0xffff0000, v105
	v_pk_add_f32 v[244:245], v[190:191], v[244:245]
	v_pk_add_f32 v[246:247], v[192:193], v[246:247]
	global_store_dwordx4 v[112:113], v[244:247], off offset:3072
	v_lshlrev_b32_e32 v120, 16, v126
	v_and_b32_e32 v121, 0xffff0000, v126
	v_lshlrev_b32_e32 v122, 16, v127
	v_and_b32_e32 v123, 0xffff0000, v127
	v_pk_add_f32 v[120:121], v[194:195], v[120:121]
	v_pk_add_f32 v[122:123], v[196:197], v[122:123]
	global_store_dwordx4 v[242:243], v[120:123], off offset:-4096
	v_lshlrev_b32_e32 v2, 16, v128
	v_and_b32_e32 v3, 0xffff0000, v128
	v_lshlrev_b32_e32 v4, 16, v129
	v_and_b32_e32 v5, 0xffff0000, v129
	v_pk_add_f32 v[2:3], v[198:199], v[2:3]
	v_pk_add_f32 v[4:5], v[200:201], v[4:5]
	global_store_dwordx4 v[242:243], v[2:5], off offset:-3072
	v_lshlrev_b32_e32 v244, 16, v130
	v_and_b32_e32 v245, 0xffff0000, v130
	v_lshlrev_b32_e32 v246, 16, v131
	v_and_b32_e32 v247, 0xffff0000, v131
	v_pk_add_f32 v[244:245], v[202:203], v[244:245]
	v_pk_add_f32 v[246:247], v[204:205], v[246:247]
	global_store_dwordx4 v[242:243], v[244:247], off offset:-2048
	v_lshlrev_b32_e32 v120, 16, v132
	v_and_b32_e32 v121, 0xffff0000, v132
	v_lshlrev_b32_e32 v122, 16, v133
	v_and_b32_e32 v123, 0xffff0000, v133
	v_pk_add_f32 v[120:121], v[206:207], v[120:121]
	v_pk_add_f32 v[122:123], v[208:209], v[122:123]
	global_store_dwordx4 v[242:243], v[120:123], off offset:-1024
	v_lshlrev_b32_e32 v2, 16, v136
	v_and_b32_e32 v3, 0xffff0000, v136
	v_lshlrev_b32_e32 v4, 16, v137
	v_and_b32_e32 v5, 0xffff0000, v137
	v_pk_add_f32 v[2:3], v[210:211], v[2:3]
	v_pk_add_f32 v[4:5], v[212:213], v[4:5]
	global_store_dwordx4 v[242:243], v[2:5], off
	v_lshlrev_b32_e32 v244, 16, v138
	v_and_b32_e32 v245, 0xffff0000, v138
	v_lshlrev_b32_e32 v246, 16, v139
	v_and_b32_e32 v247, 0xffff0000, v139
	v_pk_add_f32 v[244:245], v[214:215], v[244:245]
	v_pk_add_f32 v[246:247], v[216:217], v[246:247]
	global_store_dwordx4 v[242:243], v[244:247], off offset:1024
	v_lshlrev_b32_e32 v120, 16, v140
	v_and_b32_e32 v121, 0xffff0000, v140
	v_lshlrev_b32_e32 v122, 16, v141
	v_and_b32_e32 v123, 0xffff0000, v141
	v_pk_add_f32 v[120:121], v[218:219], v[120:121]
	v_pk_add_f32 v[122:123], v[220:221], v[122:123]
	global_store_dwordx4 v[242:243], v[120:123], off offset:2048
	v_lshlrev_b32_e32 v2, 16, v142
	v_and_b32_e32 v3, 0xffff0000, v142
	v_lshlrev_b32_e32 v4, 16, v143
	v_and_b32_e32 v5, 0xffff0000, v143
	v_pk_add_f32 v[2:3], v[222:223], v[2:3]
	v_pk_add_f32 v[4:5], v[224:225], v[4:5]
	global_store_dwordx4 v[242:243], v[2:5], off offset:3072
	v_lshlrev_b32_e32 v244, 16, v8
	v_and_b32_e32 v245, 0xffff0000, v8
	v_lshlrev_b32_e32 v246, 16, v9
	v_and_b32_e32 v247, 0xffff0000, v9
	v_pk_add_f32 v[244:245], v[226:227], v[244:245]
	v_pk_add_f32 v[246:247], v[228:229], v[246:247]
	global_store_dwordx4 v[124:125], v[244:247], off
	v_lshlrev_b32_e32 v120, 16, v10
	v_and_b32_e32 v121, 0xffff0000, v10
	v_lshlrev_b32_e32 v122, 16, v11
	v_and_b32_e32 v123, 0xffff0000, v11
	v_pk_add_f32 v[120:121], v[230:231], v[120:121]
	v_pk_add_f32 v[122:123], v[232:233], v[122:123]
	global_store_dwordx4 v[124:125], v[120:123], off offset:1024
	v_lshlrev_b32_e32 v2, 16, v12
	v_and_b32_e32 v3, 0xffff0000, v12
	v_lshlrev_b32_e32 v4, 16, v13
	v_and_b32_e32 v5, 0xffff0000, v13
	v_pk_add_f32 v[2:3], v[234:235], v[2:3]
	v_pk_add_f32 v[4:5], v[236:237], v[4:5]
	global_store_dwordx4 v[124:125], v[2:5], off offset:2048
	v_lshlrev_b32_e32 v244, 16, v14
	v_and_b32_e32 v245, 0xffff0000, v14
	v_lshlrev_b32_e32 v246, 16, v15
	v_and_b32_e32 v247, 0xffff0000, v15
	v_pk_add_f32 v[244:245], v[238:239], v[244:245]
	v_pk_add_f32 v[246:247], v[240:241], v[246:247]
	global_store_dwordx4 v[124:125], v[244:247], off offset:3072
	s_add_i32 s76, s76, 1
	s_cmp_eq_u32 s76, 2
	s_cbranch_scc0 .LBB0_901
	s_add_i32 s2, s2, s3
	s_cmpk_gt_i32 s2, 0xff
	s_barrier
	s_cbranch_scc0 .LBB0_892

; #define LAS __attribute__((address_space(3)))
; __global__ void __launch_bounds__(NTHREADS, 2) fwd(Args args) {
;     extern __shared__ __attribute__((aligned(16))) unsigned char lds_raw[];
;     LAS unsigned char* lds = (LAS unsigned char*)lds_raw;
;     volatile LAS unsigned* MISC = (volatile LAS unsigned*)(lds + MISC_OFF);
;     const int tid = threadIdx.x, lane = tid & 63, wave = __builtin_amdgcn_readfirstlane(tid >> 6);
;     const int G = gridDim.x, bid = blockIdx.x;
;     const int gw = bid * NWAVES + wave, NGW = G * NWAVES;
;     unsigned char* ws = args.ws;
	.amdhsa_kernel _Z3fwd4Args
		.amdhsa_group_segment_fixed_size 0
		.amdhsa_private_segment_fixed_size 0
		.amdhsa_kernarg_size 432
		.amdhsa_user_sgpr_count 2
		.amdhsa_user_sgpr_dispatch_ptr 0
		.amdhsa_user_sgpr_queue_ptr 0
		.amdhsa_user_sgpr_kernarg_segment_ptr 1
		.amdhsa_user_sgpr_dispatch_id 0
		.amdhsa_user_sgpr_kernarg_preload_length 0
		.amdhsa_user_sgpr_kernarg_preload_offset 0
		.amdhsa_user_sgpr_private_segment_size 0
		.amdhsa_uses_dynamic_stack 0
		.amdhsa_enable_private_segment 0
		.amdhsa_system_sgpr_workgroup_id_x 1
		.amdhsa_system_sgpr_workgroup_id_y 0
		.amdhsa_system_sgpr_workgroup_id_z 0
		.amdhsa_system_sgpr_workgroup_info 0
		.amdhsa_system_vgpr_workitem_id 0
		.amdhsa_next_free_vgpr 250
		.amdhsa_next_free_sgpr 102
		.amdhsa_accum_offset 252
		.amdhsa_reserve_vcc 1
		.amdhsa_float_round_mode_32 0
		.amdhsa_float_round_mode_16_64 0
		.amdhsa_float_denorm_mode_32 3
		.amdhsa_float_denorm_mode_16_64 3
		.amdhsa_dx10_clamp 1
		.amdhsa_ieee_mode 1
		.amdhsa_fp16_overflow 0
		.amdhsa_tg_split 0
		.amdhsa_exception_fp_ieee_invalid_op 0
		.amdhsa_exception_fp_denorm_src 0
		.amdhsa_exception_fp_ieee_div_zero 0
		.amdhsa_exception_fp_ieee_overflow 0
		.amdhsa_exception_fp_ieee_underflow 0
		.amdhsa_exception_fp_ieee_inexact 0
		.amdhsa_exception_int_div_zero 0
	.end_amdhsa_kernel

; #define LAS __attribute__((address_space(3)))
; __global__ void __launch_bounds__(NTHREADS, 2) fwd(Args args) {
;     extern __shared__ __attribute__((aligned(16))) unsigned char lds_raw[];
;     LAS unsigned char* lds = (LAS unsigned char*)lds_raw;
;     volatile LAS unsigned* MISC = (volatile LAS unsigned*)(lds + MISC_OFF);
;     const int tid = threadIdx.x, lane = tid & 63, wave = __builtin_amdgcn_readfirstlane(tid >> 6);
;     const int G = gridDim.x, bid = blockIdx.x;
;     const int gw = bid * NWAVES + wave, NGW = G * NWAVES;
;     unsigned char* ws = args.ws;
amdhsa.kernels:
  - .agpr_count:     0
    .args:
      - .offset:         0
        .size:           176
        .value_kind:     by_value
      - .offset:         176
        .size:           4
        .value_kind:     hidden_block_count_x
      - .offset:         180
        .size:           4
        .value_kind:     hidden_block_count_y
      - .offset:         184
        .size:           4
        .value_kind:     hidden_block_count_z
      - .offset:         188
        .size:           2
        .value_kind:     hidden_group_size_x
      - .offset:         190
        .size:           2
        .value_kind:     hidden_group_size_y
      - .offset:         192
        .size:           2
        .value_kind:     hidden_group_size_z
      - .offset:         194
        .size:           2
        .value_kind:     hidden_remainder_x
      - .offset:         196
        .size:           2
        .value_kind:     hidden_remainder_y
      - .offset:         198
        .size:           2
        .value_kind:     hidden_remainder_z
      - .offset:         216
        .size:           8
        .value_kind:     hidden_global_offset_x
      - .offset:         224
        .size:           8
        .value_kind:     hidden_global_offset_y
      - .offset:         232
        .size:           8
        .value_kind:     hidden_global_offset_z
      - .offset:         240
        .size:           2
        .value_kind:     hidden_grid_dims
      - .offset:         296
        .size:           4
        .value_kind:     hidden_dynamic_lds_size
    .group_segment_fixed_size: 0
    .kernarg_segment_align: 8
    .kernarg_segment_size: 432
    .language:       OpenCL C
    .language_version:
      - 2
      - 0
    .max_flat_workgroup_size: 512
    .name:           _Z3fwd4Args
    .private_segment_fixed_size: 0
    .sgpr_count:     108
    .sgpr_spill_count: 42
    .symbol:         _Z3fwd4Args.kd
    .uniform_work_group_size: 1
    .uses_dynamic_stack: false
    .vgpr_count:     250
    .vgpr_spill_count: 0
    .wavefront_size: 64
